# v58 + MFMA-segment priority raised from s_setprio 1 to s_setprio 3 in all GEMM K-loops
# baseline (speedup 1.0000x reference)
; #define PG8_STAGE_A(b, h, ptr, NX) do { if constexpr (Sched::GATHER) { unsigned gs_[2]; gs_[0] = ((NX) && last_) ? gN[h][0] : gA[h][0]; gs_[1] = ((NX) && last_) ? gN[h][1] : gA[h][1]; PG8_STAGE(PG8_SA(b, h), ptr, gs_); } \
;         else PG8_STAGE(PG8_SA(b, h), (ptr) + ((h) ? hstep : (size_t)0), voffA); } while (0)
; #define PG8_WAIT_V(n) asm volatile("s_waitcnt vmcnt(" #n ")" ::: "memory")
; #define PG8_WAIT_L(n) asm volatile("s_waitcnt lgkmcnt(" #n ")" ::: "memory")
; #define PG8_BAR __builtin_amdgcn_s_barrier()
; template <class Epi, class Sched, bool ALIGN_EPI = false, bool SP2 = false>
; __device__ __forceinline__ void gemm_phase(PG8_LAS unsigned char* lds, const Gemm g, const Sched& S, const Epi& E, const bool skip_epi = false) {
;     ...
;         const char* nA = has_next ? (const char*)g.A + (size_t)nxt.pm * pmstepA + nxt.ko : cA; const char* nB = has_next ? (const char*)g.Bt + (size_t)nxt.pn * tstep + nxt.ko : cB;
;         for (int t = 0; t < nt; t += 2) {
;             const bool last = (t == nt - 2); last_ = last && has_next;
;             const char* a1 = cA + (size_t)(t + 1) * kstep;
;             const char* a2 = last ? nA : cA + (size_t)(t + 2) * kstep; const char* b2 = last ? nB : cB + (size_t)(t + 2) * kstep;
;             const char* a3 = a2 + kstep; const char* b3 = b2 + kstep;
;             if (last && has_next) S.a_ready(nxt);
;             if constexpr (SP2) {
;             PG8_LDB(B0, 0, 0); PG8_LDB(B1, 0, 1); PG8_SCHED; PG8_LDA(At, 0, 0); PG8_STAGE_A(1, 1, a1, false);
;             PG8_WAIT_V(8); PG8_WAIT_L(0); PG8_BAR; PG8_MMA(0, 0, At, B0); PG8_MMA(0, 1, At, B1); PG8_BAR; PG8_SCHED;
;             PG8_LDA(At, 0, 1); PG8_STAGE(PG8_SB(0, 0), b2, voffB); PG8_STAGE(PG8_SB(0, 1), b2 + hstep, voffB); PG8_STAGE_A(0, 0, a2, true);
;             PG8_WAIT_V(8); PG8_WAIT_L(0); PG8_BAR; PG8_MMA(1, 0, At, B0); PG8_MMA(1, 1, At, B1); PG8_BAR; PG8_SCHED;
;             PG8_LDB(B0, 1, 0); PG8_LDB(B1, 1, 1); PG8_SCHED; PG8_LDA(At, 1, 0); PG8_STAGE_A(0, 1, a2, true);
;             PG8_WAIT_V(8); PG8_WAIT_L(0); PG8_BAR; PG8_MMA(0, 0, At, B0); PG8_MMA(0, 1, At, B1); PG8_BAR; PG8_SCHED;
;             PG8_LDA(At, 1, 1); PG8_STAGE(PG8_SB(1, 0), b3, voffB); PG8_STAGE(PG8_SB(1, 1), b3 + hstep, voffB); PG8_STAGE_A(1, 0, a3, true);
;             PG8_WAIT_V(8); PG8_WAIT_L(0); PG8_BAR; PG8_MMA(1, 0, At, B0); PG8_MMA(1, 1, At, B1); PG8_BAR; PG8_SCHED;
.LBB0_252:
	s_ashr_i32 s17, s16, 31
	s_lshl_b64 s[18:19], s[16:17], 19
	s_add_u32 s18, s86, s18
	s_addc_u32 s19, s87, s19
	s_and_b64 s[20:21], s[4:5], exec
	s_cselect_b32 s17, s19, s25
	s_cselect_b32 s56, s18, s24
	s_ashr_i32 s15, s14, 31
	s_lshl_b64 s[20:21], s[14:15], 19
	v_readlane_b32 s28, v254, 36
	v_readlane_b32 s29, v254, 37
	s_add_u32 s20, s28, s20
	s_addc_u32 s21, s29, s21
	s_and_b64 s[28:29], s[4:5], exec
	s_cselect_b32 s15, s21, s27
	s_cselect_b32 s57, s20, s26
	s_add_u32 s24, s24, 0x40080
	s_addc_u32 s25, s25, 0
	s_add_u32 s58, s26, 0x100
	s_addc_u32 s59, s27, 0
	s_mov_b32 s60, -2
	s_waitcnt vmcnt(0)
	ds_read_b128 v[148:151], v170
	ds_read_b128 v[152:155], v170 offset:1024
	ds_read_b128 v[156:159], v170 offset:2048
	ds_read_b128 v[160:163], v170 offset:3072
	ds_read_b128 v[176:179], v171
	ds_read_b128 v[180:183], v171 offset:1024
	ds_read_b128 v[184:187], v171 offset:2048
	ds_read_b128 v[188:191], v171 offset:3072
	s_add_u32 s26, s24, 0xfffc0080
	s_addc_u32 s27, s25, -1
	s_cmp_eq_u32 s60, 12
	s_cselect_b32 s29, s17, s27
	s_cselect_b32 s28, s56, s26
	s_cselect_b32 s27, s15, s59
	s_cselect_b32 s26, s57, s58
	v_lshl_add_u64 v[164:165], s[24:25], 0, v[140:141]
	s_add_i32 m0, s23, 0xc000
	ds_read_b128 v[192:195], v172
	ds_read_b128 v[196:199], v172 offset:1024
	ds_read_b128 v[200:203], v172 offset:2048
	ds_read_b128 v[204:207], v172 offset:3072
	ds_read_b128 v[208:211], v172 offset:4096
	ds_read_b128 v[212:215], v172 offset:5120
	ds_read_b128 v[216:219], v172 offset:6144
	ds_read_b128 v[220:223], v172 offset:7168
	global_load_lds_dwordx4 v[164:165], off
	v_lshl_add_u64 v[164:165], s[24:25], 0, v[142:143]
	s_add_i32 m0, s23, 0xe000
	s_nop 0
	global_load_lds_dwordx4 v[164:165], off
	s_waitcnt vmcnt(8)
	s_waitcnt lgkmcnt(0)
	s_barrier
	s_setprio 3
	s_waitcnt lgkmcnt(0)
	v_mfma_f32_16x16x32_bf16 v[126:129], v[148:151], v[192:195], 0
	v_mfma_f32_16x16x32_bf16 v[122:125], v[156:159], v[192:195], 0
	v_mfma_f32_16x16x32_bf16 v[114:117], v[148:151], v[200:203], 0
	v_mfma_f32_16x16x32_bf16 v[106:109], v[156:159], v[200:203], 0
	v_mfma_f32_16x16x32_bf16 v[98:101], v[148:151], v[208:211], 0
	v_mfma_f32_16x16x32_bf16 v[90:93], v[156:159], v[208:211], 0
	v_mfma_f32_16x16x32_bf16 v[82:85], v[148:151], v[216:219], 0
	v_mfma_f32_16x16x32_bf16 v[74:77], v[156:159], v[216:219], 0
	v_mfma_f32_16x16x32_bf16 v[126:129], v[152:155], v[196:199], v[126:129]
	v_mfma_f32_16x16x32_bf16 v[122:125], v[160:163], v[196:199], v[122:125]
	v_mfma_f32_16x16x32_bf16 v[114:117], v[152:155], v[204:207], v[114:117]
	v_mfma_f32_16x16x32_bf16 v[106:109], v[160:163], v[204:207], v[106:109]
	v_mfma_f32_16x16x32_bf16 v[98:101], v[152:155], v[212:215], v[98:101]
	v_mfma_f32_16x16x32_bf16 v[90:93], v[160:163], v[212:215], v[90:93]
	v_mfma_f32_16x16x32_bf16 v[82:85], v[152:155], v[220:223], v[82:85]
	v_mfma_f32_16x16x32_bf16 v[74:77], v[160:163], v[220:223], v[74:77]
	s_setprio 0
	s_setprio 3
	v_mfma_f32_16x16x32_bf16 v[118:121], v[176:179], v[192:195], 0
	v_mfma_f32_16x16x32_bf16 v[110:113], v[184:187], v[192:195], 0
	v_mfma_f32_16x16x32_bf16 v[102:105], v[176:179], v[200:203], 0
	v_mfma_f32_16x16x32_bf16 v[94:97], v[184:187], v[200:203], 0
	v_mfma_f32_16x16x32_bf16 v[86:89], v[176:179], v[208:211], 0
	v_mfma_f32_16x16x32_bf16 v[78:81], v[184:187], v[208:211], 0
	v_mfma_f32_16x16x32_bf16 v[70:73], v[176:179], v[216:219], 0
	v_mfma_f32_16x16x32_bf16 v[66:69], v[184:187], v[216:219], 0
	v_mfma_f32_16x16x32_bf16 v[118:121], v[180:183], v[196:199], v[118:121]
	v_mfma_f32_16x16x32_bf16 v[110:113], v[188:191], v[196:199], v[110:113]
	v_mfma_f32_16x16x32_bf16 v[102:105], v[180:183], v[204:207], v[102:105]
	v_mfma_f32_16x16x32_bf16 v[94:97], v[188:191], v[204:207], v[94:97]
	v_mfma_f32_16x16x32_bf16 v[86:89], v[180:183], v[212:215], v[86:89]
	v_mfma_f32_16x16x32_bf16 v[78:81], v[188:191], v[212:215], v[78:81]
	v_mfma_f32_16x16x32_bf16 v[70:73], v[180:183], v[220:223], v[70:73]
	v_mfma_f32_16x16x32_bf16 v[66:69], v[188:191], v[220:223], v[66:69]
	s_setprio 0
	s_barrier
	s_add_i32 s61, s46, s2
	v_lshl_add_u64 v[164:165], s[26:27], 0, v[134:135]
	s_mov_b32 m0, s61
	ds_read_b128 v[192:195], v172 offset:16384
	ds_read_b128 v[196:199], v172 offset:17408
	ds_read_b128 v[200:203], v172 offset:18432
	ds_read_b128 v[204:207], v172 offset:19456
	ds_read_b128 v[208:211], v172 offset:20480
	ds_read_b128 v[212:215], v172 offset:21504
	ds_read_b128 v[216:219], v172 offset:22528
	ds_read_b128 v[220:223], v172 offset:23552
	global_load_lds_dwordx4 v[164:165], off
	s_add_i32 m0, s61, 0x2000
	s_add_u32 s62, s26, 0x40000
	v_lshl_add_u64 v[224:225], s[26:27], 0, v[130:131]
	s_addc_u32 s63, s27, 0
	s_add_i32 s61, s47, s2
	global_load_lds_dwordx4 v[224:225], off
	v_lshl_add_u64 v[226:227], s[62:63], 0, v[134:135]
	s_mov_b32 m0, s61
	v_lshl_add_u64 v[230:231], s[28:29], 0, v[132:133]
	global_load_lds_dwordx4 v[226:227], off
	v_lshl_add_u64 v[226:227], s[62:63], 0, v[130:131]
	s_add_i32 m0, s61, 0x2000
	s_nop 0
	global_load_lds_dwordx4 v[226:227], off
	v_lshl_add_u64 v[226:227], s[28:29], 0, v[136:137]
	s_mov_b32 m0, s23
	s_nop 0
	global_load_lds_dwordx4 v[226:227], off
	s_mov_b32 m0, s31
	s_nop 0
	global_load_lds_dwordx4 v[230:231], off
	s_waitcnt vmcnt(8)
	s_waitcnt lgkmcnt(0)
	s_barrier
; #define PG8_STAGE_A(b, h, ptr, NX) do { if constexpr (Sched::GATHER) { unsigned gs_[2]; gs_[0] = ((NX) && last_) ? gN[h][0] : gA[h][0]; gs_[1] = ((NX) && last_) ? gN[h][1] : gA[h][1]; PG8_STAGE(PG8_SA(b, h), ptr, gs_); } \
;         else PG8_STAGE(PG8_SA(b, h), (ptr) + ((h) ? hstep : (size_t)0), voffA); } while (0)
; #define PG8_STAGE(bufoff, gbase, voff) do { _Pragma("unroll") for (int _i = 0; _i < 2; ++_i) \
;         __builtin_amdgcn_global_load_lds((const unsigned*)((const char*)(gbase) + (voff)[_i]), (PG8_LAS unsigned*)(lds + (bufoff) + ldsw + _i * 8192), 16, 0, 0); } while (0)
; #define PG8_LDA(dst, b, h) do { _Pragma("unroll") for (int m = 0; m < 4; ++m) _Pragma("unroll") for (int k = 0; k < 2; ++k) dst[m][k] = *(const PG8_LAS bf16x8*)(lds + PG8_SA(b, h) + aoff + m * 2048 + k * 1024); } while (0)
; #define PG8_LDB(dst, b, h) do { _Pragma("unroll") for (int n = 0; n < 2; ++n) _Pragma("unroll") for (int k = 0; k < 2; ++k) dst[n][k] = *(const PG8_LAS bf16x8*)(lds + PG8_SB(b, h) + boff + n * 2048 + k * 1024); } while (0)
; #define PG8_WAIT_V(n) asm volatile("s_waitcnt vmcnt(" #n ")" ::: "memory")
; #define PG8_BAR __builtin_amdgcn_s_barrier()
; template <class Epi, class Sched, bool ALIGN_EPI = false, bool SP2 = false>
; __device__ __forceinline__ void gemm_phase(PG8_LAS unsigned char* lds, const Gemm g, const Sched& S, const Epi& E, const bool skip_epi = false) {
;     ...
;             PG8_LDB(B0, 0, 0); PG8_LDB(B1, 0, 1); PG8_SCHED; PG8_LDA(At, 0, 0); PG8_STAGE_A(1, 1, a1, false);
;             PG8_WAIT_V(8); PG8_WAIT_L(0); PG8_BAR; PG8_MMA(0, 0, At, B0); PG8_MMA(0, 1, At, B1); PG8_BAR; PG8_SCHED;
;             PG8_LDA(At, 0, 1); PG8_STAGE(PG8_SB(0, 0), b2, voffB); PG8_STAGE(PG8_SB(0, 1), b2 + hstep, voffB); PG8_STAGE_A(0, 0, a2, true);
;             PG8_WAIT_V(8); PG8_WAIT_L(0); PG8_BAR; PG8_MMA(1, 0, At, B0); PG8_MMA(1, 1, At, B1); PG8_BAR; PG8_SCHED;
;             PG8_LDB(B0, 1, 0); PG8_LDB(B1, 1, 1); PG8_SCHED; PG8_LDA(At, 1, 0); PG8_STAGE_A(0, 1, a2, true);
;             PG8_WAIT_V(8); PG8_WAIT_L(0); PG8_BAR; PG8_MMA(0, 0, At, B0); PG8_MMA(0, 1, At, B1); PG8_BAR; PG8_SCHED;
;             PG8_LDA(At, 1, 1); PG8_STAGE(PG8_SB(1, 0), b3, voffB); PG8_STAGE(PG8_SB(1, 1), b3 + hstep, voffB); PG8_STAGE_A(1, 0, a3, true);
;             PG8_WAIT_V(8); PG8_WAIT_L(0); PG8_BAR; PG8_MMA(1, 0, At, B0); PG8_MMA(1, 1, At, B1); PG8_BAR; PG8_SCHED;
	s_setprio 3
	s_waitcnt lgkmcnt(0)
	v_mfma_f32_16x16x32_bf16 v[62:65], v[148:151], v[192:195], 0
	v_mfma_f32_16x16x32_bf16 v[58:61], v[156:159], v[192:195], 0
	v_mfma_f32_16x16x32_bf16 v[50:53], v[148:151], v[200:203], 0
	v_mfma_f32_16x16x32_bf16 v[42:45], v[156:159], v[200:203], 0
	v_mfma_f32_16x16x32_bf16 v[34:37], v[148:151], v[208:211], 0
	v_mfma_f32_16x16x32_bf16 v[26:29], v[156:159], v[208:211], 0
	v_mfma_f32_16x16x32_bf16 v[18:21], v[148:151], v[216:219], 0
	v_mfma_f32_16x16x32_bf16 v[10:13], v[156:159], v[216:219], 0
	v_mfma_f32_16x16x32_bf16 v[62:65], v[152:155], v[196:199], v[62:65]
	v_mfma_f32_16x16x32_bf16 v[58:61], v[160:163], v[196:199], v[58:61]
	v_mfma_f32_16x16x32_bf16 v[50:53], v[152:155], v[204:207], v[50:53]
	v_mfma_f32_16x16x32_bf16 v[42:45], v[160:163], v[204:207], v[42:45]
	v_mfma_f32_16x16x32_bf16 v[34:37], v[152:155], v[212:215], v[34:37]
	v_mfma_f32_16x16x32_bf16 v[26:29], v[160:163], v[212:215], v[26:29]
	v_mfma_f32_16x16x32_bf16 v[18:21], v[152:155], v[220:223], v[18:21]
	v_mfma_f32_16x16x32_bf16 v[10:13], v[160:163], v[220:223], v[10:13]
	s_setprio 0
	s_setprio 3
	v_mfma_f32_16x16x32_bf16 v[54:57], v[176:179], v[192:195], 0
	v_mfma_f32_16x16x32_bf16 v[46:49], v[184:187], v[192:195], 0
	v_mfma_f32_16x16x32_bf16 v[38:41], v[176:179], v[200:203], 0
	v_mfma_f32_16x16x32_bf16 v[30:33], v[184:187], v[200:203], 0
	v_mfma_f32_16x16x32_bf16 v[22:25], v[176:179], v[208:211], 0
	v_mfma_f32_16x16x32_bf16 v[14:17], v[184:187], v[208:211], 0
	v_mfma_f32_16x16x32_bf16 v[6:9], v[176:179], v[216:219], 0
	v_mfma_f32_16x16x32_bf16 v[2:5], v[184:187], v[216:219], 0
	v_mfma_f32_16x16x32_bf16 v[54:57], v[180:183], v[196:199], v[54:57]
	v_mfma_f32_16x16x32_bf16 v[46:49], v[188:191], v[196:199], v[46:49]
	v_mfma_f32_16x16x32_bf16 v[38:41], v[180:183], v[204:207], v[38:41]
	v_mfma_f32_16x16x32_bf16 v[30:33], v[188:191], v[204:207], v[30:33]
	v_mfma_f32_16x16x32_bf16 v[22:25], v[180:183], v[212:215], v[22:25]
	v_mfma_f32_16x16x32_bf16 v[14:17], v[188:191], v[212:215], v[14:17]
	v_mfma_f32_16x16x32_bf16 v[6:9], v[180:183], v[220:223], v[6:9]
	v_mfma_f32_16x16x32_bf16 v[2:5], v[188:191], v[220:223], v[2:5]
	s_setprio 0
	s_barrier
	s_add_i32 s61, 0, 0x18000
	s_add_i32 s62, 0, 0x1c000
	v_add_u32_e32 v160, s61, v1
	v_add_u32_e32 v188, s62, v1
	ds_read_b128 v[148:151], v160
	ds_read_b128 v[152:155], v160 offset:1024
	ds_read_b128 v[156:159], v160 offset:2048
	ds_read_b128 v[160:163], v160 offset:3072
	ds_read_b128 v[176:179], v188
	ds_read_b128 v[180:183], v188 offset:1024
	ds_read_b128 v[184:187], v188 offset:2048
	ds_read_b128 v[188:191], v188 offset:3072
	s_add_u32 s28, s28, 0x40000
	s_addc_u32 s29, s29, 0
	s_mov_b32 m0, s34
	v_lshl_add_u64 v[232:233], s[28:29], 0, v[136:137]
	ds_read_b128 v[192:195], v172 offset:32768
	ds_read_b128 v[196:199], v172 offset:33792
	ds_read_b128 v[200:203], v172 offset:34816
	ds_read_b128 v[204:207], v172 offset:35840
	ds_read_b128 v[208:211], v172 offset:36864
	ds_read_b128 v[212:215], v172 offset:37888
	ds_read_b128 v[216:219], v172 offset:38912
	ds_read_b128 v[220:223], v172 offset:39936
	global_load_lds_dwordx4 v[232:233], off
	v_lshl_add_u64 v[232:233], s[28:29], 0, v[132:133]
	s_mov_b32 m0, s35
	s_nop 0
	global_load_lds_dwordx4 v[232:233], off
	s_waitcnt vmcnt(8)
	s_waitcnt lgkmcnt(0)
	s_barrier
	s_setprio 3
	s_waitcnt lgkmcnt(0)
	v_mfma_f32_16x16x32_bf16 v[126:129], v[148:151], v[192:195], v[126:129]
	v_mfma_f32_16x16x32_bf16 v[122:125], v[156:159], v[192:195], v[122:125]
	v_mfma_f32_16x16x32_bf16 v[114:117], v[148:151], v[200:203], v[114:117]
	v_mfma_f32_16x16x32_bf16 v[106:109], v[156:159], v[200:203], v[106:109]
	v_mfma_f32_16x16x32_bf16 v[98:101], v[148:151], v[208:211], v[98:101]
	v_mfma_f32_16x16x32_bf16 v[90:93], v[156:159], v[208:211], v[90:93]
	v_mfma_f32_16x16x32_bf16 v[82:85], v[148:151], v[216:219], v[82:85]
	v_mfma_f32_16x16x32_bf16 v[74:77], v[156:159], v[216:219], v[74:77]
	v_mfma_f32_16x16x32_bf16 v[126:129], v[152:155], v[196:199], v[126:129]
	v_mfma_f32_16x16x32_bf16 v[122:125], v[160:163], v[196:199], v[122:125]
	v_mfma_f32_16x16x32_bf16 v[114:117], v[152:155], v[204:207], v[114:117]
	v_mfma_f32_16x16x32_bf16 v[106:109], v[160:163], v[204:207], v[106:109]
	v_mfma_f32_16x16x32_bf16 v[98:101], v[152:155], v[212:215], v[98:101]
	v_mfma_f32_16x16x32_bf16 v[90:93], v[160:163], v[212:215], v[90:93]
	v_mfma_f32_16x16x32_bf16 v[82:85], v[152:155], v[220:223], v[82:85]
	v_mfma_f32_16x16x32_bf16 v[74:77], v[160:163], v[220:223], v[74:77]
	s_setprio 0
	s_setprio 3
	v_mfma_f32_16x16x32_bf16 v[118:121], v[176:179], v[192:195], v[118:121]
	v_mfma_f32_16x16x32_bf16 v[110:113], v[184:187], v[192:195], v[110:113]
	v_mfma_f32_16x16x32_bf16 v[102:105], v[176:179], v[200:203], v[102:105]
	v_mfma_f32_16x16x32_bf16 v[94:97], v[184:187], v[200:203], v[94:97]
	v_mfma_f32_16x16x32_bf16 v[86:89], v[176:179], v[208:211], v[86:89]
	v_mfma_f32_16x16x32_bf16 v[78:81], v[184:187], v[208:211], v[78:81]
	v_mfma_f32_16x16x32_bf16 v[70:73], v[176:179], v[216:219], v[70:73]
	v_mfma_f32_16x16x32_bf16 v[66:69], v[184:187], v[216:219], v[66:69]
	v_mfma_f32_16x16x32_bf16 v[118:121], v[180:183], v[196:199], v[118:121]
	v_mfma_f32_16x16x32_bf16 v[110:113], v[188:191], v[196:199], v[110:113]
	v_mfma_f32_16x16x32_bf16 v[102:105], v[180:183], v[204:207], v[102:105]
	v_mfma_f32_16x16x32_bf16 v[94:97], v[188:191], v[204:207], v[94:97]
	v_mfma_f32_16x16x32_bf16 v[86:89], v[180:183], v[212:215], v[86:89]
	v_mfma_f32_16x16x32_bf16 v[78:81], v[188:191], v[212:215], v[78:81]
	v_mfma_f32_16x16x32_bf16 v[70:73], v[180:183], v[220:223], v[70:73]
	v_mfma_f32_16x16x32_bf16 v[66:69], v[188:191], v[220:223], v[66:69]
	s_setprio 0
	s_barrier
; #define PG8_STAGE_A(b, h, ptr, NX) do { if constexpr (Sched::GATHER) { unsigned gs_[2]; gs_[0] = ((NX) && last_) ? gN[h][0] : gA[h][0]; gs_[1] = ((NX) && last_) ? gN[h][1] : gA[h][1]; PG8_STAGE(PG8_SA(b, h), ptr, gs_); } \
;         else PG8_STAGE(PG8_SA(b, h), (ptr) + ((h) ? hstep : (size_t)0), voffA); } while (0)
; #define PG8_STAGE(bufoff, gbase, voff) do { _Pragma("unroll") for (int _i = 0; _i < 2; ++_i) \
;         __builtin_amdgcn_global_load_lds((const unsigned*)((const char*)(gbase) + (voff)[_i]), (PG8_LAS unsigned*)(lds + (bufoff) + ldsw + _i * 8192), 16, 0, 0); } while (0)
; #define PG8_LDA(dst, b, h) do { _Pragma("unroll") for (int m = 0; m < 4; ++m) _Pragma("unroll") for (int k = 0; k < 2; ++k) dst[m][k] = *(const PG8_LAS bf16x8*)(lds + PG8_SA(b, h) + aoff + m * 2048 + k * 1024); } while (0)
; #define PG8_LDB(dst, b, h) do { _Pragma("unroll") for (int n = 0; n < 2; ++n) _Pragma("unroll") for (int k = 0; k < 2; ++k) dst[n][k] = *(const PG8_LAS bf16x8*)(lds + PG8_SB(b, h) + boff + n * 2048 + k * 1024); } while (0)
; #define PG8_WAIT_V(n) asm volatile("s_waitcnt vmcnt(" #n ")" ::: "memory")
; #define PG8_BAR __builtin_amdgcn_s_barrier()
; template <class Epi, class Sched, bool ALIGN_EPI = false, bool SP2 = false>
; __device__ __forceinline__ void gemm_phase(PG8_LAS unsigned char* lds, const Gemm g, const Sched& S, const Epi& E, const bool skip_epi = false) {
;     ...
;             PG8_LDB(B0, 0, 0); PG8_LDB(B1, 0, 1); PG8_SCHED; PG8_LDA(At, 0, 0); PG8_STAGE_A(1, 1, a1, false);
;             PG8_WAIT_V(8); PG8_WAIT_L(0); PG8_BAR; PG8_MMA(0, 0, At, B0); PG8_MMA(0, 1, At, B1); PG8_BAR; PG8_SCHED;
;             PG8_LDA(At, 0, 1); PG8_STAGE(PG8_SB(0, 0), b2, voffB); PG8_STAGE(PG8_SB(0, 1), b2 + hstep, voffB); PG8_STAGE_A(0, 0, a2, true);
;             PG8_WAIT_V(8); PG8_WAIT_L(0); PG8_BAR; PG8_MMA(1, 0, At, B0); PG8_MMA(1, 1, At, B1); PG8_BAR; PG8_SCHED;
;             PG8_LDB(B0, 1, 0); PG8_LDB(B1, 1, 1); PG8_SCHED; PG8_LDA(At, 1, 0); PG8_STAGE_A(0, 1, a2, true);
;             PG8_WAIT_V(8); PG8_WAIT_L(0); PG8_BAR; PG8_MMA(0, 0, At, B0); PG8_MMA(0, 1, At, B1); PG8_BAR; PG8_SCHED;
;             PG8_LDA(At, 1, 1); PG8_STAGE(PG8_SB(1, 0), b3, voffB); PG8_STAGE(PG8_SB(1, 1), b3 + hstep, voffB); PG8_STAGE_A(1, 0, a3, true);
;             PG8_WAIT_V(8); PG8_WAIT_L(0); PG8_BAR; PG8_MMA(1, 0, At, B0); PG8_MMA(1, 1, At, B1); PG8_BAR; PG8_SCHED;
	s_add_i32 s28, s61, s2
	v_lshl_add_u64 v[164:165], v[164:165], 0, s[10:11]
	s_mov_b32 m0, s28
	ds_read_b128 v[192:195], v172 offset:49152
	ds_read_b128 v[196:199], v172 offset:50176
	ds_read_b128 v[200:203], v172 offset:51200
	ds_read_b128 v[204:207], v172 offset:52224
	ds_read_b128 v[208:211], v172 offset:53248
	ds_read_b128 v[212:215], v172 offset:54272
	ds_read_b128 v[216:219], v172 offset:55296
	ds_read_b128 v[220:223], v172 offset:56320
	global_load_lds_dwordx4 v[164:165], off
	s_add_i32 m0, s28, 0x2000
	s_add_u32 s26, s26, 0x40080
	v_lshl_add_u64 v[164:165], v[224:225], 0, s[10:11]
	s_addc_u32 s27, s27, 0
	s_add_i32 s28, s62, s2
	global_load_lds_dwordx4 v[164:165], off
	v_lshl_add_u64 v[164:165], s[26:27], 0, v[134:135]
	s_mov_b32 m0, s28
	s_nop 0
	global_load_lds_dwordx4 v[164:165], off
	v_lshl_add_u64 v[164:165], s[26:27], 0, v[130:131]
	s_add_i32 m0, s28, 0x2000
	s_nop 0
	global_load_lds_dwordx4 v[164:165], off
	v_lshl_add_u64 v[164:165], v[226:227], 0, s[10:11]
	s_mov_b32 m0, s37
	s_nop 0
	global_load_lds_dwordx4 v[164:165], off
	v_lshl_add_u64 v[164:165], v[230:231], 0, s[10:11]
	s_mov_b32 m0, s38
	s_nop 0
	global_load_lds_dwordx4 v[164:165], off
	s_waitcnt vmcnt(8)
	s_waitcnt lgkmcnt(0)
	s_barrier
	s_setprio 3
	s_waitcnt lgkmcnt(0)
	v_mfma_f32_16x16x32_bf16 v[62:65], v[148:151], v[192:195], v[62:65]
	v_mfma_f32_16x16x32_bf16 v[58:61], v[156:159], v[192:195], v[58:61]
	v_mfma_f32_16x16x32_bf16 v[50:53], v[148:151], v[200:203], v[50:53]
	v_mfma_f32_16x16x32_bf16 v[42:45], v[156:159], v[200:203], v[42:45]
	v_mfma_f32_16x16x32_bf16 v[34:37], v[148:151], v[208:211], v[34:37]
	v_mfma_f32_16x16x32_bf16 v[26:29], v[156:159], v[208:211], v[26:29]
	v_mfma_f32_16x16x32_bf16 v[18:21], v[148:151], v[216:219], v[18:21]
	v_mfma_f32_16x16x32_bf16 v[10:13], v[156:159], v[216:219], v[10:13]
	v_mfma_f32_16x16x32_bf16 v[62:65], v[152:155], v[196:199], v[62:65]
	v_mfma_f32_16x16x32_bf16 v[58:61], v[160:163], v[196:199], v[58:61]
	v_mfma_f32_16x16x32_bf16 v[50:53], v[152:155], v[204:207], v[50:53]
	v_mfma_f32_16x16x32_bf16 v[42:45], v[160:163], v[204:207], v[42:45]
	v_mfma_f32_16x16x32_bf16 v[34:37], v[152:155], v[212:215], v[34:37]
	v_mfma_f32_16x16x32_bf16 v[26:29], v[160:163], v[212:215], v[26:29]
	v_mfma_f32_16x16x32_bf16 v[18:21], v[152:155], v[220:223], v[18:21]
	v_mfma_f32_16x16x32_bf16 v[10:13], v[160:163], v[220:223], v[10:13]
	s_setprio 0
	s_setprio 3
	v_mfma_f32_16x16x32_bf16 v[54:57], v[176:179], v[192:195], v[54:57]
	v_mfma_f32_16x16x32_bf16 v[46:49], v[184:187], v[192:195], v[46:49]
	v_mfma_f32_16x16x32_bf16 v[38:41], v[176:179], v[200:203], v[38:41]
	v_mfma_f32_16x16x32_bf16 v[30:33], v[184:187], v[200:203], v[30:33]
	v_mfma_f32_16x16x32_bf16 v[22:25], v[176:179], v[208:211], v[22:25]
	v_mfma_f32_16x16x32_bf16 v[14:17], v[184:187], v[208:211], v[14:17]
	v_mfma_f32_16x16x32_bf16 v[6:9], v[176:179], v[216:219], v[6:9]
	v_mfma_f32_16x16x32_bf16 v[2:5], v[184:187], v[216:219], v[2:5]
	v_mfma_f32_16x16x32_bf16 v[54:57], v[180:183], v[196:199], v[54:57]
	v_mfma_f32_16x16x32_bf16 v[46:49], v[188:191], v[196:199], v[46:49]
	v_mfma_f32_16x16x32_bf16 v[38:41], v[180:183], v[204:207], v[38:41]
	v_mfma_f32_16x16x32_bf16 v[30:33], v[188:191], v[204:207], v[30:33]
	v_mfma_f32_16x16x32_bf16 v[22:25], v[180:183], v[212:215], v[22:25]
	v_mfma_f32_16x16x32_bf16 v[14:17], v[188:191], v[212:215], v[14:17]
	v_mfma_f32_16x16x32_bf16 v[6:9], v[180:183], v[220:223], v[6:9]
	v_mfma_f32_16x16x32_bf16 v[2:5], v[188:191], v[220:223], v[2:5]
	s_setprio 0
	s_barrier
	s_add_i32 s60, s60, 2
	s_add_u32 s24, s24, 0x100
	s_addc_u32 s25, s25, 0
	s_add_u32 s58, s58, 0x100
	s_addc_u32 s59, s59, 0
	s_cmp_gt_u32 s60, 13
.LBB0_253:
	ds_read_b128 v[148:151], v170
	ds_read_b128 v[152:155], v170 offset:1024
	ds_read_b128 v[156:159], v170 offset:2048
	ds_read_b128 v[160:163], v170 offset:3072
	ds_read_b128 v[176:179], v171
	ds_read_b128 v[180:183], v171 offset:1024
	ds_read_b128 v[184:187], v171 offset:2048
	ds_read_b128 v[188:191], v171 offset:3072
	s_add_u32 s26, s24, 0xfffc0080
	s_addc_u32 s27, s25, -1
	s_cmp_eq_u32 s60, 12
	s_cselect_b32 s29, s17, s27
	s_cselect_b32 s28, s56, s26
	s_cselect_b32 s27, s15, s59
	s_cselect_b32 s26, s57, s58
	v_lshl_add_u64 v[164:165], s[24:25], 0, v[140:141]
	s_add_i32 m0, s23, 0xc000
	ds_read_b128 v[192:195], v172
	ds_read_b128 v[196:199], v172 offset:1024
	ds_read_b128 v[200:203], v172 offset:2048
	ds_read_b128 v[204:207], v172 offset:3072
	ds_read_b128 v[208:211], v172 offset:4096
	ds_read_b128 v[212:215], v172 offset:5120
	ds_read_b128 v[216:219], v172 offset:6144
	ds_read_b128 v[220:223], v172 offset:7168
	global_load_lds_dwordx4 v[164:165], off
	v_lshl_add_u64 v[164:165], s[24:25], 0, v[142:143]
	s_add_i32 m0, s23, 0xe000
	s_nop 0
	global_load_lds_dwordx4 v[164:165], off
	s_waitcnt vmcnt(8)
	s_waitcnt lgkmcnt(0)
	s_barrier
; #define PG8_STAGE_A(b, h, ptr, NX) do { if constexpr (Sched::GATHER) { unsigned gs_[2]; gs_[0] = ((NX) && last_) ? gN[h][0] : gA[h][0]; gs_[1] = ((NX) && last_) ? gN[h][1] : gA[h][1]; PG8_STAGE(PG8_SA(b, h), ptr, gs_); } \
;         else PG8_STAGE(PG8_SA(b, h), (ptr) + ((h) ? hstep : (size_t)0), voffA); } while (0)
; #define PG8_STAGE(bufoff, gbase, voff) do { _Pragma("unroll") for (int _i = 0; _i < 2; ++_i) \
;         __builtin_amdgcn_global_load_lds((const unsigned*)((const char*)(gbase) + (voff)[_i]), (PG8_LAS unsigned*)(lds + (bufoff) + ldsw + _i * 8192), 16, 0, 0); } while (0)
; #define PG8_LDA(dst, b, h) do { _Pragma("unroll") for (int m = 0; m < 4; ++m) _Pragma("unroll") for (int k = 0; k < 2; ++k) dst[m][k] = *(const PG8_LAS bf16x8*)(lds + PG8_SA(b, h) + aoff + m * 2048 + k * 1024); } while (0)
; #define PG8_LDB(dst, b, h) do { _Pragma("unroll") for (int n = 0; n < 2; ++n) _Pragma("unroll") for (int k = 0; k < 2; ++k) dst[n][k] = *(const PG8_LAS bf16x8*)(lds + PG8_SB(b, h) + boff + n * 2048 + k * 1024); } while (0)
; #define PG8_WAIT_V(n) asm volatile("s_waitcnt vmcnt(" #n ")" ::: "memory")
; #define PG8_BAR __builtin_amdgcn_s_barrier()
; template <class Epi, class Sched, bool ALIGN_EPI = false, bool SP2 = false>
; __device__ __forceinline__ void gemm_phase(PG8_LAS unsigned char* lds, const Gemm g, const Sched& S, const Epi& E, const bool skip_epi = false) {
;     ...
;             PG8_LDB(B0, 0, 0); PG8_LDB(B1, 0, 1); PG8_SCHED; PG8_LDA(At, 0, 0); PG8_STAGE_A(1, 1, a1, false);
;             PG8_WAIT_V(8); PG8_WAIT_L(0); PG8_BAR; PG8_MMA(0, 0, At, B0); PG8_MMA(0, 1, At, B1); PG8_BAR; PG8_SCHED;
;             PG8_LDA(At, 0, 1); PG8_STAGE(PG8_SB(0, 0), b2, voffB); PG8_STAGE(PG8_SB(0, 1), b2 + hstep, voffB); PG8_STAGE_A(0, 0, a2, true);
;             PG8_WAIT_V(8); PG8_WAIT_L(0); PG8_BAR; PG8_MMA(1, 0, At, B0); PG8_MMA(1, 1, At, B1); PG8_BAR; PG8_SCHED;
;             PG8_LDB(B0, 1, 0); PG8_LDB(B1, 1, 1); PG8_SCHED; PG8_LDA(At, 1, 0); PG8_STAGE_A(0, 1, a2, true);
;             PG8_WAIT_V(8); PG8_WAIT_L(0); PG8_BAR; PG8_MMA(0, 0, At, B0); PG8_MMA(0, 1, At, B1); PG8_BAR; PG8_SCHED;
;             PG8_LDA(At, 1, 1); PG8_STAGE(PG8_SB(1, 0), b3, voffB); PG8_STAGE(PG8_SB(1, 1), b3 + hstep, voffB); PG8_STAGE_A(1, 0, a3, true);
;             PG8_WAIT_V(8); PG8_WAIT_L(0); PG8_BAR; PG8_MMA(1, 0, At, B0); PG8_MMA(1, 1, At, B1); PG8_BAR; PG8_SCHED;
	s_setprio 3
	s_waitcnt lgkmcnt(0)
	v_mfma_f32_16x16x32_bf16 v[126:129], v[148:151], v[192:195], v[126:129]
	v_mfma_f32_16x16x32_bf16 v[122:125], v[156:159], v[192:195], v[122:125]
	v_mfma_f32_16x16x32_bf16 v[114:117], v[148:151], v[200:203], v[114:117]
	v_mfma_f32_16x16x32_bf16 v[106:109], v[156:159], v[200:203], v[106:109]
	v_mfma_f32_16x16x32_bf16 v[98:101], v[148:151], v[208:211], v[98:101]
	v_mfma_f32_16x16x32_bf16 v[90:93], v[156:159], v[208:211], v[90:93]
	v_mfma_f32_16x16x32_bf16 v[82:85], v[148:151], v[216:219], v[82:85]
	v_mfma_f32_16x16x32_bf16 v[74:77], v[156:159], v[216:219], v[74:77]
	v_mfma_f32_16x16x32_bf16 v[126:129], v[152:155], v[196:199], v[126:129]
	v_mfma_f32_16x16x32_bf16 v[122:125], v[160:163], v[196:199], v[122:125]
	v_mfma_f32_16x16x32_bf16 v[114:117], v[152:155], v[204:207], v[114:117]
	v_mfma_f32_16x16x32_bf16 v[106:109], v[160:163], v[204:207], v[106:109]
	v_mfma_f32_16x16x32_bf16 v[98:101], v[152:155], v[212:215], v[98:101]
	v_mfma_f32_16x16x32_bf16 v[90:93], v[160:163], v[212:215], v[90:93]
	v_mfma_f32_16x16x32_bf16 v[82:85], v[152:155], v[220:223], v[82:85]
	v_mfma_f32_16x16x32_bf16 v[74:77], v[160:163], v[220:223], v[74:77]
	s_setprio 0
	s_setprio 3
	v_mfma_f32_16x16x32_bf16 v[118:121], v[176:179], v[192:195], v[118:121]
	v_mfma_f32_16x16x32_bf16 v[110:113], v[184:187], v[192:195], v[110:113]
	v_mfma_f32_16x16x32_bf16 v[102:105], v[176:179], v[200:203], v[102:105]
	v_mfma_f32_16x16x32_bf16 v[94:97], v[184:187], v[200:203], v[94:97]
	v_mfma_f32_16x16x32_bf16 v[86:89], v[176:179], v[208:211], v[86:89]
	v_mfma_f32_16x16x32_bf16 v[78:81], v[184:187], v[208:211], v[78:81]
	v_mfma_f32_16x16x32_bf16 v[70:73], v[176:179], v[216:219], v[70:73]
	v_mfma_f32_16x16x32_bf16 v[66:69], v[184:187], v[216:219], v[66:69]
	v_mfma_f32_16x16x32_bf16 v[118:121], v[180:183], v[196:199], v[118:121]
	v_mfma_f32_16x16x32_bf16 v[110:113], v[188:191], v[196:199], v[110:113]
	v_mfma_f32_16x16x32_bf16 v[102:105], v[180:183], v[204:207], v[102:105]
	v_mfma_f32_16x16x32_bf16 v[94:97], v[188:191], v[204:207], v[94:97]
	v_mfma_f32_16x16x32_bf16 v[86:89], v[180:183], v[212:215], v[86:89]
	v_mfma_f32_16x16x32_bf16 v[78:81], v[188:191], v[212:215], v[78:81]
	v_mfma_f32_16x16x32_bf16 v[70:73], v[180:183], v[220:223], v[70:73]
	v_mfma_f32_16x16x32_bf16 v[66:69], v[188:191], v[220:223], v[66:69]
	s_setprio 0
	s_barrier
	s_add_i32 s61, s46, s2
	v_lshl_add_u64 v[164:165], s[26:27], 0, v[134:135]
	s_mov_b32 m0, s61
	ds_read_b128 v[192:195], v172 offset:16384
	ds_read_b128 v[196:199], v172 offset:17408
	ds_read_b128 v[200:203], v172 offset:18432
	ds_read_b128 v[204:207], v172 offset:19456
	ds_read_b128 v[208:211], v172 offset:20480
	ds_read_b128 v[212:215], v172 offset:21504
	ds_read_b128 v[216:219], v172 offset:22528
	ds_read_b128 v[220:223], v172 offset:23552
	global_load_lds_dwordx4 v[164:165], off
	s_add_i32 m0, s61, 0x2000
	s_add_u32 s62, s26, 0x40000
	v_lshl_add_u64 v[224:225], s[26:27], 0, v[130:131]
	s_addc_u32 s63, s27, 0
	s_add_i32 s61, s47, s2
	global_load_lds_dwordx4 v[224:225], off
	v_lshl_add_u64 v[226:227], s[62:63], 0, v[134:135]
	s_mov_b32 m0, s61
	v_lshl_add_u64 v[230:231], s[28:29], 0, v[132:133]
	global_load_lds_dwordx4 v[226:227], off
	v_lshl_add_u64 v[226:227], s[62:63], 0, v[130:131]
	s_add_i32 m0, s61, 0x2000
	s_nop 0
	global_load_lds_dwordx4 v[226:227], off
	v_lshl_add_u64 v[226:227], s[28:29], 0, v[136:137]
	s_mov_b32 m0, s23
	s_nop 0
	global_load_lds_dwordx4 v[226:227], off
	s_mov_b32 m0, s31
	s_nop 0
	global_load_lds_dwordx4 v[230:231], off
	s_waitcnt vmcnt(8)
	s_waitcnt lgkmcnt(0)
	s_barrier
	s_setprio 3
	s_waitcnt lgkmcnt(0)
	v_mfma_f32_16x16x32_bf16 v[62:65], v[148:151], v[192:195], v[62:65]
	v_mfma_f32_16x16x32_bf16 v[58:61], v[156:159], v[192:195], v[58:61]
	v_mfma_f32_16x16x32_bf16 v[50:53], v[148:151], v[200:203], v[50:53]
	v_mfma_f32_16x16x32_bf16 v[42:45], v[156:159], v[200:203], v[42:45]
	v_mfma_f32_16x16x32_bf16 v[34:37], v[148:151], v[208:211], v[34:37]
	v_mfma_f32_16x16x32_bf16 v[26:29], v[156:159], v[208:211], v[26:29]
	v_mfma_f32_16x16x32_bf16 v[18:21], v[148:151], v[216:219], v[18:21]
	v_mfma_f32_16x16x32_bf16 v[10:13], v[156:159], v[216:219], v[10:13]
	v_mfma_f32_16x16x32_bf16 v[62:65], v[152:155], v[196:199], v[62:65]
	v_mfma_f32_16x16x32_bf16 v[58:61], v[160:163], v[196:199], v[58:61]
	v_mfma_f32_16x16x32_bf16 v[50:53], v[152:155], v[204:207], v[50:53]
	v_mfma_f32_16x16x32_bf16 v[42:45], v[160:163], v[204:207], v[42:45]
	v_mfma_f32_16x16x32_bf16 v[34:37], v[152:155], v[212:215], v[34:37]
	v_mfma_f32_16x16x32_bf16 v[26:29], v[160:163], v[212:215], v[26:29]
	v_mfma_f32_16x16x32_bf16 v[18:21], v[152:155], v[220:223], v[18:21]
	v_mfma_f32_16x16x32_bf16 v[10:13], v[160:163], v[220:223], v[10:13]
	s_setprio 0
	s_setprio 3
	v_mfma_f32_16x16x32_bf16 v[54:57], v[176:179], v[192:195], v[54:57]
	v_mfma_f32_16x16x32_bf16 v[46:49], v[184:187], v[192:195], v[46:49]
	v_mfma_f32_16x16x32_bf16 v[38:41], v[176:179], v[200:203], v[38:41]
	v_mfma_f32_16x16x32_bf16 v[30:33], v[184:187], v[200:203], v[30:33]
	v_mfma_f32_16x16x32_bf16 v[22:25], v[176:179], v[208:211], v[22:25]
	v_mfma_f32_16x16x32_bf16 v[14:17], v[184:187], v[208:211], v[14:17]
	v_mfma_f32_16x16x32_bf16 v[6:9], v[176:179], v[216:219], v[6:9]
	v_mfma_f32_16x16x32_bf16 v[2:5], v[184:187], v[216:219], v[2:5]
	v_mfma_f32_16x16x32_bf16 v[54:57], v[180:183], v[196:199], v[54:57]
	v_mfma_f32_16x16x32_bf16 v[46:49], v[188:191], v[196:199], v[46:49]
	v_mfma_f32_16x16x32_bf16 v[38:41], v[180:183], v[204:207], v[38:41]
	v_mfma_f32_16x16x32_bf16 v[30:33], v[188:191], v[204:207], v[30:33]
	v_mfma_f32_16x16x32_bf16 v[22:25], v[180:183], v[212:215], v[22:25]
	v_mfma_f32_16x16x32_bf16 v[14:17], v[188:191], v[212:215], v[14:17]
	v_mfma_f32_16x16x32_bf16 v[6:9], v[180:183], v[220:223], v[6:9]
	v_mfma_f32_16x16x32_bf16 v[2:5], v[188:191], v[220:223], v[2:5]
	s_setprio 0
	s_barrier
; #define PG8_STAGE_A(b, h, ptr, NX) do { if constexpr (Sched::GATHER) { unsigned gs_[2]; gs_[0] = ((NX) && last_) ? gN[h][0] : gA[h][0]; gs_[1] = ((NX) && last_) ? gN[h][1] : gA[h][1]; PG8_STAGE(PG8_SA(b, h), ptr, gs_); } \
;         else PG8_STAGE(PG8_SA(b, h), (ptr) + ((h) ? hstep : (size_t)0), voffA); } while (0)
; #define PG8_STAGE(bufoff, gbase, voff) do { _Pragma("unroll") for (int _i = 0; _i < 2; ++_i) \
;         __builtin_amdgcn_global_load_lds((const unsigned*)((const char*)(gbase) + (voff)[_i]), (PG8_LAS unsigned*)(lds + (bufoff) + ldsw + _i * 8192), 16, 0, 0); } while (0)
; #define PG8_LDA(dst, b, h) do { _Pragma("unroll") for (int m = 0; m < 4; ++m) _Pragma("unroll") for (int k = 0; k < 2; ++k) dst[m][k] = *(const PG8_LAS bf16x8*)(lds + PG8_SA(b, h) + aoff + m * 2048 + k * 1024); } while (0)
; #define PG8_LDB(dst, b, h) do { _Pragma("unroll") for (int n = 0; n < 2; ++n) _Pragma("unroll") for (int k = 0; k < 2; ++k) dst[n][k] = *(const PG8_LAS bf16x8*)(lds + PG8_SB(b, h) + boff + n * 2048 + k * 1024); } while (0)
; #define PG8_WAIT_V(n) asm volatile("s_waitcnt vmcnt(" #n ")" ::: "memory")
; #define PG8_BAR __builtin_amdgcn_s_barrier()
; template <class Epi, class Sched, bool ALIGN_EPI = false, bool SP2 = false>
; __device__ __forceinline__ void gemm_phase(PG8_LAS unsigned char* lds, const Gemm g, const Sched& S, const Epi& E, const bool skip_epi = false) {
;     ...
;             PG8_LDB(B0, 0, 0); PG8_LDB(B1, 0, 1); PG8_SCHED; PG8_LDA(At, 0, 0); PG8_STAGE_A(1, 1, a1, false);
;             PG8_WAIT_V(8); PG8_WAIT_L(0); PG8_BAR; PG8_MMA(0, 0, At, B0); PG8_MMA(0, 1, At, B1); PG8_BAR; PG8_SCHED;
;             PG8_LDA(At, 0, 1); PG8_STAGE(PG8_SB(0, 0), b2, voffB); PG8_STAGE(PG8_SB(0, 1), b2 + hstep, voffB); PG8_STAGE_A(0, 0, a2, true);
;             PG8_WAIT_V(8); PG8_WAIT_L(0); PG8_BAR; PG8_MMA(1, 0, At, B0); PG8_MMA(1, 1, At, B1); PG8_BAR; PG8_SCHED;
;             PG8_LDB(B0, 1, 0); PG8_LDB(B1, 1, 1); PG8_SCHED; PG8_LDA(At, 1, 0); PG8_STAGE_A(0, 1, a2, true);
;             PG8_WAIT_V(8); PG8_WAIT_L(0); PG8_BAR; PG8_MMA(0, 0, At, B0); PG8_MMA(0, 1, At, B1); PG8_BAR; PG8_SCHED;
;             PG8_LDA(At, 1, 1); PG8_STAGE(PG8_SB(1, 0), b3, voffB); PG8_STAGE(PG8_SB(1, 1), b3 + hstep, voffB); PG8_STAGE_A(1, 0, a3, true);
;             PG8_WAIT_V(8); PG8_WAIT_L(0); PG8_BAR; PG8_MMA(1, 0, At, B0); PG8_MMA(1, 1, At, B1); PG8_BAR; PG8_SCHED;
	s_add_i32 s61, 0, 0x18000
	s_add_i32 s62, 0, 0x1c000
	v_add_u32_e32 v160, s61, v1
	v_add_u32_e32 v188, s62, v1
	ds_read_b128 v[148:151], v160
	ds_read_b128 v[152:155], v160 offset:1024
	ds_read_b128 v[156:159], v160 offset:2048
	ds_read_b128 v[160:163], v160 offset:3072
	ds_read_b128 v[176:179], v188
	ds_read_b128 v[180:183], v188 offset:1024
	ds_read_b128 v[184:187], v188 offset:2048
	ds_read_b128 v[188:191], v188 offset:3072
	s_add_u32 s28, s28, 0x40000
	s_addc_u32 s29, s29, 0
	s_mov_b32 m0, s34
	v_lshl_add_u64 v[232:233], s[28:29], 0, v[136:137]
	ds_read_b128 v[192:195], v172 offset:32768
	ds_read_b128 v[196:199], v172 offset:33792
	ds_read_b128 v[200:203], v172 offset:34816
	ds_read_b128 v[204:207], v172 offset:35840
	ds_read_b128 v[208:211], v172 offset:36864
	ds_read_b128 v[212:215], v172 offset:37888
	ds_read_b128 v[216:219], v172 offset:38912
	ds_read_b128 v[220:223], v172 offset:39936
	global_load_lds_dwordx4 v[232:233], off
	v_lshl_add_u64 v[232:233], s[28:29], 0, v[132:133]
	s_mov_b32 m0, s35
	s_nop 0
	global_load_lds_dwordx4 v[232:233], off
	s_waitcnt vmcnt(8)
	s_waitcnt lgkmcnt(0)
	s_barrier
	s_setprio 3
	s_waitcnt lgkmcnt(0)
	v_mfma_f32_16x16x32_bf16 v[126:129], v[148:151], v[192:195], v[126:129]
	v_mfma_f32_16x16x32_bf16 v[122:125], v[156:159], v[192:195], v[122:125]
	v_mfma_f32_16x16x32_bf16 v[114:117], v[148:151], v[200:203], v[114:117]
	v_mfma_f32_16x16x32_bf16 v[106:109], v[156:159], v[200:203], v[106:109]
	v_mfma_f32_16x16x32_bf16 v[98:101], v[148:151], v[208:211], v[98:101]
	v_mfma_f32_16x16x32_bf16 v[90:93], v[156:159], v[208:211], v[90:93]
	v_mfma_f32_16x16x32_bf16 v[82:85], v[148:151], v[216:219], v[82:85]
	v_mfma_f32_16x16x32_bf16 v[74:77], v[156:159], v[216:219], v[74:77]
	v_mfma_f32_16x16x32_bf16 v[126:129], v[152:155], v[196:199], v[126:129]
	v_mfma_f32_16x16x32_bf16 v[122:125], v[160:163], v[196:199], v[122:125]
	v_mfma_f32_16x16x32_bf16 v[114:117], v[152:155], v[204:207], v[114:117]
	v_mfma_f32_16x16x32_bf16 v[106:109], v[160:163], v[204:207], v[106:109]
	v_mfma_f32_16x16x32_bf16 v[98:101], v[152:155], v[212:215], v[98:101]
	v_mfma_f32_16x16x32_bf16 v[90:93], v[160:163], v[212:215], v[90:93]
	v_mfma_f32_16x16x32_bf16 v[82:85], v[152:155], v[220:223], v[82:85]
	v_mfma_f32_16x16x32_bf16 v[74:77], v[160:163], v[220:223], v[74:77]
	s_setprio 0
	s_setprio 3
	v_mfma_f32_16x16x32_bf16 v[118:121], v[176:179], v[192:195], v[118:121]
	v_mfma_f32_16x16x32_bf16 v[110:113], v[184:187], v[192:195], v[110:113]
	v_mfma_f32_16x16x32_bf16 v[102:105], v[176:179], v[200:203], v[102:105]
	v_mfma_f32_16x16x32_bf16 v[94:97], v[184:187], v[200:203], v[94:97]
	v_mfma_f32_16x16x32_bf16 v[86:89], v[176:179], v[208:211], v[86:89]
	v_mfma_f32_16x16x32_bf16 v[78:81], v[184:187], v[208:211], v[78:81]
	v_mfma_f32_16x16x32_bf16 v[70:73], v[176:179], v[216:219], v[70:73]
	v_mfma_f32_16x16x32_bf16 v[66:69], v[184:187], v[216:219], v[66:69]
	v_mfma_f32_16x16x32_bf16 v[118:121], v[180:183], v[196:199], v[118:121]
	v_mfma_f32_16x16x32_bf16 v[110:113], v[188:191], v[196:199], v[110:113]
	v_mfma_f32_16x16x32_bf16 v[102:105], v[180:183], v[204:207], v[102:105]
	v_mfma_f32_16x16x32_bf16 v[94:97], v[188:191], v[204:207], v[94:97]
	v_mfma_f32_16x16x32_bf16 v[86:89], v[180:183], v[212:215], v[86:89]
	v_mfma_f32_16x16x32_bf16 v[78:81], v[188:191], v[212:215], v[78:81]
	v_mfma_f32_16x16x32_bf16 v[70:73], v[180:183], v[220:223], v[70:73]
	v_mfma_f32_16x16x32_bf16 v[66:69], v[188:191], v[220:223], v[66:69]
	s_setprio 0
	s_barrier
; #define PG8_STAGE_A(b, h, ptr, NX) do { if constexpr (Sched::GATHER) { unsigned gs_[2]; gs_[0] = ((NX) && last_) ? gN[h][0] : gA[h][0]; gs_[1] = ((NX) && last_) ? gN[h][1] : gA[h][1]; PG8_STAGE(PG8_SA(b, h), ptr, gs_); } \
;         else PG8_STAGE(PG8_SA(b, h), (ptr) + ((h) ? hstep : (size_t)0), voffA); } while (0)
; #define PG8_STAGE(bufoff, gbase, voff) do { _Pragma("unroll") for (int _i = 0; _i < 2; ++_i) \
;         __builtin_amdgcn_global_load_lds((const unsigned*)((const char*)(gbase) + (voff)[_i]), (PG8_LAS unsigned*)(lds + (bufoff) + ldsw + _i * 8192), 16, 0, 0); } while (0)
; #define PG8_WAIT_V(n) asm volatile("s_waitcnt vmcnt(" #n ")" ::: "memory")
; __device__ __forceinline__ void rstd8(const float* SS, int rowb, int lane, float (&rs)[2][4]) {
;     f32x4 p[2][4];
; #pragma unroll
;     for (int ai = 0; ai < 2; ++ai)
; #pragma unroll
;         for (int m = 0; m < 4; ++m) p[ai][m] = *(const f32x4*)(SS + (size_t)(rowb + HALF * ai + 16 * m + (lane >> 2)) * 16 + 4 * (lane & 3));
;     asm volatile("" : "+v"(p[0][0]), "+v"(p[0][1]), "+v"(p[0][2]), "+v"(p[0][3]), "+v"(p[1][0]), "+v"(p[1][1]), "+v"(p[1][2]), "+v"(p[1][3]));
; template <class Epi, class Sched, bool ALIGN_EPI = false, bool SP2 = false>
; __device__ __forceinline__ void gemm_phase(PG8_LAS unsigned char* lds, const Gemm g, const Sched& S, const Epi& E, const bool skip_epi = false) {
;     ...
;             PG8_LDB(B0, 0, 0); PG8_LDB(B1, 0, 1); PG8_SCHED; PG8_LDA(At, 0, 0); PG8_STAGE_A(1, 1, a1, false);
;             PG8_WAIT_V(8); PG8_WAIT_L(0); PG8_BAR; PG8_MMA(0, 0, At, B0); PG8_MMA(0, 1, At, B1); PG8_BAR; PG8_SCHED;
;             PG8_LDA(At, 0, 1); PG8_STAGE(PG8_SB(0, 0), b2, voffB); PG8_STAGE(PG8_SB(0, 1), b2 + hstep, voffB); PG8_STAGE_A(0, 0, a2, true);
;             PG8_WAIT_V(8); PG8_WAIT_L(0); PG8_BAR; PG8_MMA(1, 0, At, B0); PG8_MMA(1, 1, At, B1); PG8_BAR; PG8_SCHED;
;             PG8_LDB(B0, 1, 0); PG8_LDB(B1, 1, 1); PG8_SCHED; PG8_LDA(At, 1, 0); PG8_STAGE_A(0, 1, a2, true);
;             PG8_WAIT_V(8); PG8_WAIT_L(0); PG8_BAR; PG8_MMA(0, 0, At, B0); PG8_MMA(0, 1, At, B1); PG8_BAR; PG8_SCHED;
;             PG8_LDA(At, 1, 1); PG8_STAGE(PG8_SB(1, 0), b3, voffB); PG8_STAGE(PG8_SB(1, 1), b3 + hstep, voffB); PG8_STAGE_A(1, 0, a3, true);
;             PG8_WAIT_V(8); PG8_WAIT_L(0); PG8_BAR; PG8_MMA(1, 0, At, B0); PG8_MMA(1, 1, At, B1); PG8_BAR; PG8_SCHED;
	s_add_i32 s28, s61, s2
	v_lshl_add_u64 v[164:165], v[164:165], 0, s[10:11]
	s_mov_b32 m0, s28
	ds_read_b128 v[192:195], v172 offset:49152
	ds_read_b128 v[196:199], v172 offset:50176
	ds_read_b128 v[200:203], v172 offset:51200
	ds_read_b128 v[204:207], v172 offset:52224
	ds_read_b128 v[208:211], v172 offset:53248
	ds_read_b128 v[212:215], v172 offset:54272
	ds_read_b128 v[216:219], v172 offset:55296
	ds_read_b128 v[220:223], v172 offset:56320
	global_load_lds_dwordx4 v[164:165], off
	s_add_i32 m0, s28, 0x2000
	s_add_u32 s26, s26, 0x40080
	v_lshl_add_u64 v[164:165], v[224:225], 0, s[10:11]
	s_addc_u32 s27, s27, 0
	s_add_i32 s28, s62, s2
	global_load_lds_dwordx4 v[164:165], off
	v_lshl_add_u64 v[164:165], s[26:27], 0, v[134:135]
	s_mov_b32 m0, s28
	s_nop 0
	global_load_lds_dwordx4 v[164:165], off
	v_lshl_add_u64 v[164:165], s[26:27], 0, v[130:131]
	s_add_i32 m0, s28, 0x2000
	s_nop 0
	global_load_lds_dwordx4 v[164:165], off
	v_lshl_add_u64 v[164:165], v[226:227], 0, s[10:11]
	s_mov_b32 m0, s37
	s_nop 0
	global_load_lds_dwordx4 v[164:165], off
	v_lshl_add_u64 v[164:165], v[230:231], 0, s[10:11]
	s_mov_b32 m0, s38
	s_nop 0
	global_load_lds_dwordx4 v[164:165], off
	s_waitcnt vmcnt(8)
	s_waitcnt lgkmcnt(0)
	s_barrier
	s_setprio 3
	s_waitcnt lgkmcnt(0)
	v_mfma_f32_16x16x32_bf16 v[62:65], v[148:151], v[192:195], v[62:65]
	v_mfma_f32_16x16x32_bf16 v[58:61], v[156:159], v[192:195], v[58:61]
	v_mfma_f32_16x16x32_bf16 v[50:53], v[148:151], v[200:203], v[50:53]
	v_mfma_f32_16x16x32_bf16 v[42:45], v[156:159], v[200:203], v[42:45]
	v_mfma_f32_16x16x32_bf16 v[34:37], v[148:151], v[208:211], v[34:37]
	v_mfma_f32_16x16x32_bf16 v[26:29], v[156:159], v[208:211], v[26:29]
	v_mfma_f32_16x16x32_bf16 v[18:21], v[148:151], v[216:219], v[18:21]
	v_mfma_f32_16x16x32_bf16 v[10:13], v[156:159], v[216:219], v[10:13]
	v_mfma_f32_16x16x32_bf16 v[62:65], v[152:155], v[196:199], v[62:65]
	v_mfma_f32_16x16x32_bf16 v[58:61], v[160:163], v[196:199], v[58:61]
	v_mfma_f32_16x16x32_bf16 v[50:53], v[152:155], v[204:207], v[50:53]
	v_mfma_f32_16x16x32_bf16 v[42:45], v[160:163], v[204:207], v[42:45]
	v_mfma_f32_16x16x32_bf16 v[34:37], v[152:155], v[212:215], v[34:37]
	v_mfma_f32_16x16x32_bf16 v[26:29], v[160:163], v[212:215], v[26:29]
	v_mfma_f32_16x16x32_bf16 v[18:21], v[152:155], v[220:223], v[18:21]
	v_mfma_f32_16x16x32_bf16 v[10:13], v[160:163], v[220:223], v[10:13]
	s_setprio 0
	s_setprio 3
	v_mfma_f32_16x16x32_bf16 v[54:57], v[176:179], v[192:195], v[54:57]
	v_mfma_f32_16x16x32_bf16 v[46:49], v[184:187], v[192:195], v[46:49]
	v_mfma_f32_16x16x32_bf16 v[38:41], v[176:179], v[200:203], v[38:41]
	v_mfma_f32_16x16x32_bf16 v[30:33], v[184:187], v[200:203], v[30:33]
	v_mfma_f32_16x16x32_bf16 v[22:25], v[176:179], v[208:211], v[22:25]
	v_mfma_f32_16x16x32_bf16 v[14:17], v[184:187], v[208:211], v[14:17]
	v_mfma_f32_16x16x32_bf16 v[6:9], v[176:179], v[216:219], v[6:9]
	v_mfma_f32_16x16x32_bf16 v[2:5], v[184:187], v[216:219], v[2:5]
	v_mfma_f32_16x16x32_bf16 v[54:57], v[180:183], v[196:199], v[54:57]
	v_mfma_f32_16x16x32_bf16 v[46:49], v[188:191], v[196:199], v[46:49]
	v_mfma_f32_16x16x32_bf16 v[38:41], v[180:183], v[204:207], v[38:41]
	v_mfma_f32_16x16x32_bf16 v[30:33], v[188:191], v[204:207], v[30:33]
	v_mfma_f32_16x16x32_bf16 v[22:25], v[180:183], v[212:215], v[22:25]
	v_mfma_f32_16x16x32_bf16 v[14:17], v[188:191], v[212:215], v[14:17]
	v_mfma_f32_16x16x32_bf16 v[6:9], v[180:183], v[220:223], v[6:9]
	v_mfma_f32_16x16x32_bf16 v[2:5], v[188:191], v[220:223], v[2:5]
	s_setprio 0
	s_barrier
	s_add_i32 s60, s60, 2
	s_add_u32 s24, s24, 0x100
	s_addc_u32 s25, s25, 0
	s_add_u32 s58, s58, 0x100
	s_addc_u32 s59, s59, 0
	s_cmp_gt_u32 s60, 13
	s_cbranch_scc0 .LBB0_253
	v_lshl_add_u32 v164, s22, 8, v167
	v_ashrrev_i32_e32 v165, 31, v164
	v_lshlrev_b64 v[148:149], 6, v[164:165]
	v_lshl_add_u64 v[148:149], v[138:139], 0, v[148:149]
	v_add_co_u32_e32 v150, vcc, 0x2000, v148
	v_addc_co_u32_e32 v151, vcc, 0, v149, vcc
	global_load_dwordx4 v[176:179], v[148:149], off
	global_load_dwordx4 v[180:183], v[148:149], off offset:1024
	global_load_dwordx4 v[184:187], v[148:149], off offset:2048
	global_load_dwordx4 v[188:191], v[148:149], off offset:3072
	global_load_dwordx4 v[192:195], v[150:151], off
	global_load_dwordx4 v[196:199], v[150:151], off offset:1024
	global_load_dwordx4 v[200:203], v[150:151], off offset:2048
	global_load_dwordx4 v[204:207], v[150:151], off offset:3072
	s_and_b64 vcc, exec, s[12:13]
	s_cbranch_vccz .LBB0_256
	s_barrier

; #define PG8_STAGE_A(b, h, ptr, NX) do { if constexpr (Sched::GATHER) { unsigned gs_[2]; gs_[0] = ((NX) && last_) ? gN[h][0] : gA[h][0]; gs_[1] = ((NX) && last_) ? gN[h][1] : gA[h][1]; PG8_STAGE(PG8_SA(b, h), ptr, gs_); } \
;         else PG8_STAGE(PG8_SA(b, h), (ptr) + ((h) ? hstep : (size_t)0), voffA); } while (0)
; #define PG8_WAIT_V(n) asm volatile("s_waitcnt vmcnt(" #n ")" ::: "memory")
; #define PG8_WAIT_L(n) asm volatile("s_waitcnt lgkmcnt(" #n ")" ::: "memory")
; #define PG8_BAR __builtin_amdgcn_s_barrier()
; template <class Epi, class Sched, bool ALIGN_EPI = false, bool SP2 = false>
; __device__ __forceinline__ void gemm_phase(PG8_LAS unsigned char* lds, const Gemm g, const Sched& S, const Epi& E, const bool skip_epi = false) {
;     ...
;         const char* nA = has_next ? (const char*)g.A + (size_t)nxt.pm * pmstepA + nxt.ko : cA; const char* nB = has_next ? (const char*)g.Bt + (size_t)nxt.pn * tstep + nxt.ko : cB;
;         for (int t = 0; t < nt; t += 2) {
;             const bool last = (t == nt - 2); last_ = last && has_next;
;             const char* a1 = cA + (size_t)(t + 1) * kstep;
;             const char* a2 = last ? nA : cA + (size_t)(t + 2) * kstep; const char* b2 = last ? nB : cB + (size_t)(t + 2) * kstep;
;             const char* a3 = a2 + kstep; const char* b3 = b2 + kstep;
;             if (last && has_next) S.a_ready(nxt);
;             if constexpr (SP2) {
;             PG8_LDB(B0, 0, 0); PG8_LDB(B1, 0, 1); PG8_SCHED; PG8_LDA(At, 0, 0); PG8_STAGE_A(1, 1, a1, false);
;             PG8_WAIT_V(8); PG8_WAIT_L(0); PG8_BAR; PG8_MMA(0, 0, At, B0); PG8_MMA(0, 1, At, B1); PG8_BAR; PG8_SCHED;
;             PG8_LDA(At, 0, 1); PG8_STAGE(PG8_SB(0, 0), b2, voffB); PG8_STAGE(PG8_SB(0, 1), b2 + hstep, voffB); PG8_STAGE_A(0, 0, a2, true);
;             PG8_WAIT_V(8); PG8_WAIT_L(0); PG8_BAR; PG8_MMA(1, 0, At, B0); PG8_MMA(1, 1, At, B1); PG8_BAR; PG8_SCHED;
;             PG8_LDB(B0, 1, 0); PG8_LDB(B1, 1, 1); PG8_SCHED; PG8_LDA(At, 1, 0); PG8_STAGE_A(0, 1, a2, true);
;             PG8_WAIT_V(8); PG8_WAIT_L(0); PG8_BAR; PG8_MMA(0, 0, At, B0); PG8_MMA(0, 1, At, B1); PG8_BAR; PG8_SCHED;
;             PG8_LDA(At, 1, 1); PG8_STAGE(PG8_SB(1, 0), b3, voffB); PG8_STAGE(PG8_SB(1, 1), b3 + hstep, voffB); PG8_STAGE_A(1, 0, a3, true);
;             PG8_WAIT_V(8); PG8_WAIT_L(0); PG8_BAR; PG8_MMA(1, 0, At, B0); PG8_MMA(1, 1, At, B1); PG8_BAR; PG8_SCHED;
.LBB0_633:
	s_ashr_i32 s19, s18, 31
	s_lshl_b64 s[20:21], s[18:19], 19
	s_add_u32 s20, s46, s20
	s_addc_u32 s21, s47, s21
	s_and_b64 s[22:23], s[6:7], exec
	s_cselect_b32 s19, s21, s27
	s_cselect_b32 s25, s20, s26
	s_ashr_i32 s17, s16, 31
	s_lshl_b64 s[22:23], s[16:17], 19
	v_readlane_b32 s17, v254, 40
	s_add_u32 s22, s17, s22
	v_readlane_b32 s17, v254, 41
	s_addc_u32 s23, s17, s23
	s_and_b64 s[30:31], s[6:7], exec
	s_cselect_b32 s17, s23, s29
	s_cselect_b32 s60, s22, s28
	s_add_u32 s26, s26, 0x40080
	s_addc_u32 s27, s27, 0
	s_add_u32 s61, s28, 0x100
	s_addc_u32 s62, s29, 0
	s_mov_b32 s63, -2
	s_waitcnt lgkmcnt(0)
	ds_read_b128 v[98:101], v234
	ds_read_b128 v[110:113], v234 offset:1024
	ds_read_b128 v[122:125], v234 offset:2048
	ds_read_b128 v[126:129], v234 offset:3072
	ds_read_b128 v[138:141], v235
	ds_read_b128 v[142:145], v235 offset:1024
	ds_read_b128 v[146:149], v235 offset:2048
	ds_read_b128 v[150:153], v235 offset:3072
	s_add_u32 s28, s26, 0xfffc0080
	s_addc_u32 s29, s27, -1
	s_cmp_eq_u32 s63, 12
	s_cselect_b32 s31, s19, s29
	s_cselect_b32 s30, s25, s28
	s_cselect_b32 s29, s17, s62
	s_cselect_b32 s28, s60, s61
	v_lshl_add_u64 v[210:211], s[26:27], 0, v[198:199]
	s_add_i32 m0, s3, 0xc000
	ds_read_b128 v[154:157], v236
	ds_read_b128 v[166:169], v236 offset:1024
	ds_read_b128 v[170:173], v236 offset:2048
	ds_read_b128 v[174:177], v236 offset:3072
	ds_read_b128 v[178:181], v236 offset:4096
	ds_read_b128 v[182:185], v236 offset:5120
	ds_read_b128 v[186:189], v236 offset:6144
	ds_read_b128 v[206:209], v236 offset:7168
	global_load_lds_dwordx4 v[210:211], off
	v_lshl_add_u64 v[210:211], s[26:27], 0, v[200:201]
	s_add_i32 m0, s3, 0xe000
	s_nop 0
	global_load_lds_dwordx4 v[210:211], off
	s_waitcnt vmcnt(8)
	s_waitcnt lgkmcnt(0)
	s_barrier
	s_setprio 3
	s_waitcnt lgkmcnt(0)
	v_mfma_f32_16x16x32_bf16 v[162:165], v[98:101], v[154:157], 0
	v_mfma_f32_16x16x32_bf16 v[158:161], v[122:125], v[154:157], 0
	v_mfma_f32_16x16x32_bf16 v[118:121], v[98:101], v[170:173], 0
	v_mfma_f32_16x16x32_bf16 v[114:117], v[122:125], v[170:173], 0
	v_mfma_f32_16x16x32_bf16 v[94:97], v[98:101], v[178:181], 0
	v_mfma_f32_16x16x32_bf16 v[90:93], v[122:125], v[178:181], 0
	v_mfma_f32_16x16x32_bf16 v[78:81], v[98:101], v[186:189], 0
	v_mfma_f32_16x16x32_bf16 v[74:77], v[122:125], v[186:189], 0
	v_mfma_f32_16x16x32_bf16 v[162:165], v[110:113], v[166:169], v[162:165]
	v_mfma_f32_16x16x32_bf16 v[158:161], v[126:129], v[166:169], v[158:161]
	v_mfma_f32_16x16x32_bf16 v[118:121], v[110:113], v[174:177], v[118:121]
	v_mfma_f32_16x16x32_bf16 v[114:117], v[126:129], v[174:177], v[114:117]
	v_mfma_f32_16x16x32_bf16 v[94:97], v[110:113], v[182:185], v[94:97]
	v_mfma_f32_16x16x32_bf16 v[90:93], v[126:129], v[182:185], v[90:93]
	v_mfma_f32_16x16x32_bf16 v[78:81], v[110:113], v[206:209], v[78:81]
	v_mfma_f32_16x16x32_bf16 v[74:77], v[126:129], v[206:209], v[74:77]
	s_setprio 0
	s_setprio 3
	v_mfma_f32_16x16x32_bf16 v[134:137], v[138:141], v[154:157], 0
	v_mfma_f32_16x16x32_bf16 v[130:133], v[146:149], v[154:157], 0
	v_mfma_f32_16x16x32_bf16 v[106:109], v[138:141], v[170:173], 0
	v_mfma_f32_16x16x32_bf16 v[102:105], v[146:149], v[170:173], 0
	v_mfma_f32_16x16x32_bf16 v[86:89], v[138:141], v[178:181], 0
	v_mfma_f32_16x16x32_bf16 v[82:85], v[146:149], v[178:181], 0
	v_mfma_f32_16x16x32_bf16 v[70:73], v[138:141], v[186:189], 0
	v_mfma_f32_16x16x32_bf16 v[66:69], v[146:149], v[186:189], 0
	v_mfma_f32_16x16x32_bf16 v[134:137], v[142:145], v[166:169], v[134:137]
	v_mfma_f32_16x16x32_bf16 v[130:133], v[150:153], v[166:169], v[130:133]
	v_mfma_f32_16x16x32_bf16 v[106:109], v[142:145], v[174:177], v[106:109]
	v_mfma_f32_16x16x32_bf16 v[102:105], v[150:153], v[174:177], v[102:105]
	v_mfma_f32_16x16x32_bf16 v[86:89], v[142:145], v[182:185], v[86:89]
	v_mfma_f32_16x16x32_bf16 v[82:85], v[150:153], v[182:185], v[82:85]
	v_mfma_f32_16x16x32_bf16 v[70:73], v[142:145], v[206:209], v[70:73]
	v_mfma_f32_16x16x32_bf16 v[66:69], v[150:153], v[206:209], v[66:69]
	s_setprio 0
	s_barrier
	s_add_i32 s64, s57, s2
	v_lshl_add_u64 v[210:211], s[28:29], 0, v[192:193]
	s_mov_b32 m0, s64
	ds_read_b128 v[154:157], v236 offset:16384
	ds_read_b128 v[166:169], v236 offset:17408
	ds_read_b128 v[170:173], v236 offset:18432
	ds_read_b128 v[174:177], v236 offset:19456
	ds_read_b128 v[178:181], v236 offset:20480
	ds_read_b128 v[182:185], v236 offset:21504
	ds_read_b128 v[186:189], v236 offset:22528
	ds_read_b128 v[206:209], v236 offset:23552
	global_load_lds_dwordx4 v[210:211], off
	s_add_i32 m0, s64, 0x2000
	s_add_u32 s64, s28, 0x40000
	v_lshl_add_u64 v[212:213], s[28:29], 0, v[196:197]
	s_addc_u32 s65, s29, 0
	s_add_i32 s66, s58, s2
	global_load_lds_dwordx4 v[212:213], off
	v_lshl_add_u64 v[214:215], s[64:65], 0, v[192:193]
	s_mov_b32 m0, s66
	v_lshl_add_u64 v[216:217], s[30:31], 0, v[194:195]
	global_load_lds_dwordx4 v[214:215], off
	v_lshl_add_u64 v[214:215], s[64:65], 0, v[196:197]
	s_add_i32 m0, s66, 0x2000
	s_nop 0
	global_load_lds_dwordx4 v[214:215], off
	v_lshl_add_u64 v[214:215], s[30:31], 0, v[190:191]
	s_mov_b32 m0, s3
	s_nop 0
	global_load_lds_dwordx4 v[214:215], off
	s_mov_b32 m0, s34
	s_nop 0
	global_load_lds_dwordx4 v[216:217], off
	s_waitcnt vmcnt(8)
	s_waitcnt lgkmcnt(0)
	s_barrier
; #define PG8_STAGE_A(b, h, ptr, NX) do { if constexpr (Sched::GATHER) { unsigned gs_[2]; gs_[0] = ((NX) && last_) ? gN[h][0] : gA[h][0]; gs_[1] = ((NX) && last_) ? gN[h][1] : gA[h][1]; PG8_STAGE(PG8_SA(b, h), ptr, gs_); } \
;         else PG8_STAGE(PG8_SA(b, h), (ptr) + ((h) ? hstep : (size_t)0), voffA); } while (0)
; #define PG8_STAGE(bufoff, gbase, voff) do { _Pragma("unroll") for (int _i = 0; _i < 2; ++_i) \
;         __builtin_amdgcn_global_load_lds((const unsigned*)((const char*)(gbase) + (voff)[_i]), (PG8_LAS unsigned*)(lds + (bufoff) + ldsw + _i * 8192), 16, 0, 0); } while (0)
; #define PG8_LDA(dst, b, h) do { _Pragma("unroll") for (int m = 0; m < 4; ++m) _Pragma("unroll") for (int k = 0; k < 2; ++k) dst[m][k] = *(const PG8_LAS bf16x8*)(lds + PG8_SA(b, h) + aoff + m * 2048 + k * 1024); } while (0)
; #define PG8_LDB(dst, b, h) do { _Pragma("unroll") for (int n = 0; n < 2; ++n) _Pragma("unroll") for (int k = 0; k < 2; ++k) dst[n][k] = *(const PG8_LAS bf16x8*)(lds + PG8_SB(b, h) + boff + n * 2048 + k * 1024); } while (0)
; #define PG8_WAIT_V(n) asm volatile("s_waitcnt vmcnt(" #n ")" ::: "memory")
; #define PG8_BAR __builtin_amdgcn_s_barrier()
; template <class Epi, class Sched, bool ALIGN_EPI = false, bool SP2 = false>
; __device__ __forceinline__ void gemm_phase(PG8_LAS unsigned char* lds, const Gemm g, const Sched& S, const Epi& E, const bool skip_epi = false) {
;     ...
;             PG8_LDB(B0, 0, 0); PG8_LDB(B1, 0, 1); PG8_SCHED; PG8_LDA(At, 0, 0); PG8_STAGE_A(1, 1, a1, false);
;             PG8_WAIT_V(8); PG8_WAIT_L(0); PG8_BAR; PG8_MMA(0, 0, At, B0); PG8_MMA(0, 1, At, B1); PG8_BAR; PG8_SCHED;
;             PG8_LDA(At, 0, 1); PG8_STAGE(PG8_SB(0, 0), b2, voffB); PG8_STAGE(PG8_SB(0, 1), b2 + hstep, voffB); PG8_STAGE_A(0, 0, a2, true);
;             PG8_WAIT_V(8); PG8_WAIT_L(0); PG8_BAR; PG8_MMA(1, 0, At, B0); PG8_MMA(1, 1, At, B1); PG8_BAR; PG8_SCHED;
;             PG8_LDB(B0, 1, 0); PG8_LDB(B1, 1, 1); PG8_SCHED; PG8_LDA(At, 1, 0); PG8_STAGE_A(0, 1, a2, true);
;             PG8_WAIT_V(8); PG8_WAIT_L(0); PG8_BAR; PG8_MMA(0, 0, At, B0); PG8_MMA(0, 1, At, B1); PG8_BAR; PG8_SCHED;
;             PG8_LDA(At, 1, 1); PG8_STAGE(PG8_SB(1, 0), b3, voffB); PG8_STAGE(PG8_SB(1, 1), b3 + hstep, voffB); PG8_STAGE_A(1, 0, a3, true);
;             PG8_WAIT_V(8); PG8_WAIT_L(0); PG8_BAR; PG8_MMA(1, 0, At, B0); PG8_MMA(1, 1, At, B1); PG8_BAR; PG8_SCHED;
	s_setprio 3
	s_waitcnt lgkmcnt(0)
	v_mfma_f32_16x16x32_bf16 v[62:65], v[98:101], v[154:157], 0
	v_mfma_f32_16x16x32_bf16 v[58:61], v[122:125], v[154:157], 0
	v_mfma_f32_16x16x32_bf16 v[46:49], v[98:101], v[170:173], 0
	v_mfma_f32_16x16x32_bf16 v[42:45], v[122:125], v[170:173], 0
	v_mfma_f32_16x16x32_bf16 v[30:33], v[98:101], v[178:181], 0
	v_mfma_f32_16x16x32_bf16 v[26:29], v[122:125], v[178:181], 0
	v_mfma_f32_16x16x32_bf16 v[14:17], v[98:101], v[186:189], 0
	v_mfma_f32_16x16x32_bf16 v[10:13], v[122:125], v[186:189], 0
	v_mfma_f32_16x16x32_bf16 v[62:65], v[110:113], v[166:169], v[62:65]
	v_mfma_f32_16x16x32_bf16 v[58:61], v[126:129], v[166:169], v[58:61]
	v_mfma_f32_16x16x32_bf16 v[46:49], v[110:113], v[174:177], v[46:49]
	v_mfma_f32_16x16x32_bf16 v[42:45], v[126:129], v[174:177], v[42:45]
	v_mfma_f32_16x16x32_bf16 v[30:33], v[110:113], v[182:185], v[30:33]
	v_mfma_f32_16x16x32_bf16 v[26:29], v[126:129], v[182:185], v[26:29]
	v_mfma_f32_16x16x32_bf16 v[14:17], v[110:113], v[206:209], v[14:17]
	v_mfma_f32_16x16x32_bf16 v[10:13], v[126:129], v[206:209], v[10:13]
	s_setprio 0
	s_setprio 3
	v_mfma_f32_16x16x32_bf16 v[54:57], v[138:141], v[154:157], 0
	v_mfma_f32_16x16x32_bf16 v[50:53], v[146:149], v[154:157], 0
	v_mfma_f32_16x16x32_bf16 v[38:41], v[138:141], v[170:173], 0
	v_mfma_f32_16x16x32_bf16 v[34:37], v[146:149], v[170:173], 0
	v_mfma_f32_16x16x32_bf16 v[22:25], v[138:141], v[178:181], 0
	v_mfma_f32_16x16x32_bf16 v[18:21], v[146:149], v[178:181], 0
	v_mfma_f32_16x16x32_bf16 v[6:9], v[138:141], v[186:189], 0
	v_mfma_f32_16x16x32_bf16 v[2:5], v[146:149], v[186:189], 0
	v_mfma_f32_16x16x32_bf16 v[54:57], v[142:145], v[166:169], v[54:57]
	v_mfma_f32_16x16x32_bf16 v[50:53], v[150:153], v[166:169], v[50:53]
	v_mfma_f32_16x16x32_bf16 v[38:41], v[142:145], v[174:177], v[38:41]
	v_mfma_f32_16x16x32_bf16 v[34:37], v[150:153], v[174:177], v[34:37]
	v_mfma_f32_16x16x32_bf16 v[22:25], v[142:145], v[182:185], v[22:25]
	v_mfma_f32_16x16x32_bf16 v[18:21], v[150:153], v[182:185], v[18:21]
	v_mfma_f32_16x16x32_bf16 v[6:9], v[142:145], v[206:209], v[6:9]
	v_mfma_f32_16x16x32_bf16 v[2:5], v[150:153], v[206:209], v[2:5]
	s_setprio 0
	s_barrier
	s_add_i32 s64, 0, 0x18000
	s_add_i32 s65, 0, 0x1c000
	v_add_u32_e32 v126, s64, v229
	v_add_u32_e32 v150, s65, v229
	ds_read_b128 v[98:101], v126
	ds_read_b128 v[110:113], v126 offset:1024
	ds_read_b128 v[122:125], v126 offset:2048
	ds_read_b128 v[126:129], v126 offset:3072
	ds_read_b128 v[138:141], v150
	ds_read_b128 v[142:145], v150 offset:1024
	ds_read_b128 v[146:149], v150 offset:2048
	ds_read_b128 v[150:153], v150 offset:3072
	s_add_u32 s30, s30, 0x40000
	s_addc_u32 s31, s31, 0
	s_mov_b32 m0, s35
	v_lshl_add_u64 v[218:219], s[30:31], 0, v[190:191]
	ds_read_b128 v[154:157], v236 offset:32768
	ds_read_b128 v[166:169], v236 offset:33792
	ds_read_b128 v[170:173], v236 offset:34816
	ds_read_b128 v[174:177], v236 offset:35840
	ds_read_b128 v[178:181], v236 offset:36864
	ds_read_b128 v[182:185], v236 offset:37888
	ds_read_b128 v[186:189], v236 offset:38912
	ds_read_b128 v[206:209], v236 offset:39936
	global_load_lds_dwordx4 v[218:219], off
	v_lshl_add_u64 v[218:219], s[30:31], 0, v[194:195]
	s_mov_b32 m0, s36
	s_nop 0
	global_load_lds_dwordx4 v[218:219], off
	s_waitcnt vmcnt(8)
	s_waitcnt lgkmcnt(0)
	s_barrier
	s_setprio 3
	s_waitcnt lgkmcnt(0)
	v_mfma_f32_16x16x32_bf16 v[162:165], v[98:101], v[154:157], v[162:165]
	v_mfma_f32_16x16x32_bf16 v[158:161], v[122:125], v[154:157], v[158:161]
	v_mfma_f32_16x16x32_bf16 v[118:121], v[98:101], v[170:173], v[118:121]
	v_mfma_f32_16x16x32_bf16 v[114:117], v[122:125], v[170:173], v[114:117]
	v_mfma_f32_16x16x32_bf16 v[94:97], v[98:101], v[178:181], v[94:97]
	v_mfma_f32_16x16x32_bf16 v[90:93], v[122:125], v[178:181], v[90:93]
	v_mfma_f32_16x16x32_bf16 v[78:81], v[98:101], v[186:189], v[78:81]
	v_mfma_f32_16x16x32_bf16 v[74:77], v[122:125], v[186:189], v[74:77]
	v_mfma_f32_16x16x32_bf16 v[162:165], v[110:113], v[166:169], v[162:165]
	v_mfma_f32_16x16x32_bf16 v[158:161], v[126:129], v[166:169], v[158:161]
	v_mfma_f32_16x16x32_bf16 v[118:121], v[110:113], v[174:177], v[118:121]
	v_mfma_f32_16x16x32_bf16 v[114:117], v[126:129], v[174:177], v[114:117]
	v_mfma_f32_16x16x32_bf16 v[94:97], v[110:113], v[182:185], v[94:97]
	v_mfma_f32_16x16x32_bf16 v[90:93], v[126:129], v[182:185], v[90:93]
	v_mfma_f32_16x16x32_bf16 v[78:81], v[110:113], v[206:209], v[78:81]
	v_mfma_f32_16x16x32_bf16 v[74:77], v[126:129], v[206:209], v[74:77]
	s_setprio 0
	s_setprio 3
	v_mfma_f32_16x16x32_bf16 v[134:137], v[138:141], v[154:157], v[134:137]
	v_mfma_f32_16x16x32_bf16 v[130:133], v[146:149], v[154:157], v[130:133]
	v_mfma_f32_16x16x32_bf16 v[106:109], v[138:141], v[170:173], v[106:109]
	v_mfma_f32_16x16x32_bf16 v[102:105], v[146:149], v[170:173], v[102:105]
	v_mfma_f32_16x16x32_bf16 v[86:89], v[138:141], v[178:181], v[86:89]
	v_mfma_f32_16x16x32_bf16 v[82:85], v[146:149], v[178:181], v[82:85]
	v_mfma_f32_16x16x32_bf16 v[70:73], v[138:141], v[186:189], v[70:73]
	v_mfma_f32_16x16x32_bf16 v[66:69], v[146:149], v[186:189], v[66:69]
	v_mfma_f32_16x16x32_bf16 v[134:137], v[142:145], v[166:169], v[134:137]
	v_mfma_f32_16x16x32_bf16 v[130:133], v[150:153], v[166:169], v[130:133]
	v_mfma_f32_16x16x32_bf16 v[106:109], v[142:145], v[174:177], v[106:109]
	v_mfma_f32_16x16x32_bf16 v[102:105], v[150:153], v[174:177], v[102:105]
	v_mfma_f32_16x16x32_bf16 v[86:89], v[142:145], v[182:185], v[86:89]
	v_mfma_f32_16x16x32_bf16 v[82:85], v[150:153], v[182:185], v[82:85]
	v_mfma_f32_16x16x32_bf16 v[70:73], v[142:145], v[206:209], v[70:73]
	v_mfma_f32_16x16x32_bf16 v[66:69], v[150:153], v[206:209], v[66:69]
	s_setprio 0
	s_barrier
; #define PG8_STAGE_A(b, h, ptr, NX) do { if constexpr (Sched::GATHER) { unsigned gs_[2]; gs_[0] = ((NX) && last_) ? gN[h][0] : gA[h][0]; gs_[1] = ((NX) && last_) ? gN[h][1] : gA[h][1]; PG8_STAGE(PG8_SA(b, h), ptr, gs_); } \
;         else PG8_STAGE(PG8_SA(b, h), (ptr) + ((h) ? hstep : (size_t)0), voffA); } while (0)
; #define PG8_STAGE(bufoff, gbase, voff) do { _Pragma("unroll") for (int _i = 0; _i < 2; ++_i) \
;         __builtin_amdgcn_global_load_lds((const unsigned*)((const char*)(gbase) + (voff)[_i]), (PG8_LAS unsigned*)(lds + (bufoff) + ldsw + _i * 8192), 16, 0, 0); } while (0)
; #define PG8_LDA(dst, b, h) do { _Pragma("unroll") for (int m = 0; m < 4; ++m) _Pragma("unroll") for (int k = 0; k < 2; ++k) dst[m][k] = *(const PG8_LAS bf16x8*)(lds + PG8_SA(b, h) + aoff + m * 2048 + k * 1024); } while (0)
; #define PG8_LDB(dst, b, h) do { _Pragma("unroll") for (int n = 0; n < 2; ++n) _Pragma("unroll") for (int k = 0; k < 2; ++k) dst[n][k] = *(const PG8_LAS bf16x8*)(lds + PG8_SB(b, h) + boff + n * 2048 + k * 1024); } while (0)
; #define PG8_WAIT_V(n) asm volatile("s_waitcnt vmcnt(" #n ")" ::: "memory")
; #define PG8_BAR __builtin_amdgcn_s_barrier()
; template <class Epi, class Sched, bool ALIGN_EPI = false, bool SP2 = false>
; __device__ __forceinline__ void gemm_phase(PG8_LAS unsigned char* lds, const Gemm g, const Sched& S, const Epi& E, const bool skip_epi = false) {
;     ...
;             PG8_LDB(B0, 0, 0); PG8_LDB(B1, 0, 1); PG8_SCHED; PG8_LDA(At, 0, 0); PG8_STAGE_A(1, 1, a1, false);
;             PG8_WAIT_V(8); PG8_WAIT_L(0); PG8_BAR; PG8_MMA(0, 0, At, B0); PG8_MMA(0, 1, At, B1); PG8_BAR; PG8_SCHED;
;             PG8_LDA(At, 0, 1); PG8_STAGE(PG8_SB(0, 0), b2, voffB); PG8_STAGE(PG8_SB(0, 1), b2 + hstep, voffB); PG8_STAGE_A(0, 0, a2, true);
;             PG8_WAIT_V(8); PG8_WAIT_L(0); PG8_BAR; PG8_MMA(1, 0, At, B0); PG8_MMA(1, 1, At, B1); PG8_BAR; PG8_SCHED;
;             PG8_LDB(B0, 1, 0); PG8_LDB(B1, 1, 1); PG8_SCHED; PG8_LDA(At, 1, 0); PG8_STAGE_A(0, 1, a2, true);
;             PG8_WAIT_V(8); PG8_WAIT_L(0); PG8_BAR; PG8_MMA(0, 0, At, B0); PG8_MMA(0, 1, At, B1); PG8_BAR; PG8_SCHED;
;             PG8_LDA(At, 1, 1); PG8_STAGE(PG8_SB(1, 0), b3, voffB); PG8_STAGE(PG8_SB(1, 1), b3 + hstep, voffB); PG8_STAGE_A(1, 0, a3, true);
;             PG8_WAIT_V(8); PG8_WAIT_L(0); PG8_BAR; PG8_MMA(1, 0, At, B0); PG8_MMA(1, 1, At, B1); PG8_BAR; PG8_SCHED;
	s_add_i32 s30, s64, s2
	v_lshl_add_u64 v[210:211], v[210:211], 0, s[12:13]
	s_mov_b32 m0, s30
	ds_read_b128 v[154:157], v236 offset:49152
	ds_read_b128 v[166:169], v236 offset:50176
	ds_read_b128 v[170:173], v236 offset:51200
	ds_read_b128 v[174:177], v236 offset:52224
	ds_read_b128 v[178:181], v236 offset:53248
	ds_read_b128 v[182:185], v236 offset:54272
	ds_read_b128 v[186:189], v236 offset:55296
	ds_read_b128 v[206:209], v236 offset:56320
	global_load_lds_dwordx4 v[210:211], off
	s_add_i32 m0, s30, 0x2000
	s_add_u32 s28, s28, 0x40080
	v_lshl_add_u64 v[210:211], v[212:213], 0, s[12:13]
	s_addc_u32 s29, s29, 0
	s_add_i32 s30, s65, s2
	global_load_lds_dwordx4 v[210:211], off
	v_lshl_add_u64 v[210:211], s[28:29], 0, v[192:193]
	s_mov_b32 m0, s30
	s_nop 0
	global_load_lds_dwordx4 v[210:211], off
	v_lshl_add_u64 v[210:211], s[28:29], 0, v[196:197]
	s_add_i32 m0, s30, 0x2000
	s_nop 0
	global_load_lds_dwordx4 v[210:211], off
	v_lshl_add_u64 v[210:211], v[214:215], 0, s[12:13]
	s_mov_b32 m0, s39
	s_nop 0
	global_load_lds_dwordx4 v[210:211], off
	v_lshl_add_u64 v[210:211], v[216:217], 0, s[12:13]
	s_mov_b32 m0, s48
	s_nop 0
	global_load_lds_dwordx4 v[210:211], off
	s_waitcnt vmcnt(8)
	s_waitcnt lgkmcnt(0)
	s_barrier
	s_setprio 3
	s_waitcnt lgkmcnt(0)
	v_mfma_f32_16x16x32_bf16 v[62:65], v[98:101], v[154:157], v[62:65]
	v_mfma_f32_16x16x32_bf16 v[58:61], v[122:125], v[154:157], v[58:61]
	v_mfma_f32_16x16x32_bf16 v[46:49], v[98:101], v[170:173], v[46:49]
	v_mfma_f32_16x16x32_bf16 v[42:45], v[122:125], v[170:173], v[42:45]
	v_mfma_f32_16x16x32_bf16 v[30:33], v[98:101], v[178:181], v[30:33]
	v_mfma_f32_16x16x32_bf16 v[26:29], v[122:125], v[178:181], v[26:29]
	v_mfma_f32_16x16x32_bf16 v[14:17], v[98:101], v[186:189], v[14:17]
	v_mfma_f32_16x16x32_bf16 v[10:13], v[122:125], v[186:189], v[10:13]
	v_mfma_f32_16x16x32_bf16 v[62:65], v[110:113], v[166:169], v[62:65]
	v_mfma_f32_16x16x32_bf16 v[58:61], v[126:129], v[166:169], v[58:61]
	v_mfma_f32_16x16x32_bf16 v[46:49], v[110:113], v[174:177], v[46:49]
	v_mfma_f32_16x16x32_bf16 v[42:45], v[126:129], v[174:177], v[42:45]
	v_mfma_f32_16x16x32_bf16 v[30:33], v[110:113], v[182:185], v[30:33]
	v_mfma_f32_16x16x32_bf16 v[26:29], v[126:129], v[182:185], v[26:29]
	v_mfma_f32_16x16x32_bf16 v[14:17], v[110:113], v[206:209], v[14:17]
	v_mfma_f32_16x16x32_bf16 v[10:13], v[126:129], v[206:209], v[10:13]
	s_setprio 0
	s_setprio 3
	v_mfma_f32_16x16x32_bf16 v[54:57], v[138:141], v[154:157], v[54:57]
	v_mfma_f32_16x16x32_bf16 v[50:53], v[146:149], v[154:157], v[50:53]
	v_mfma_f32_16x16x32_bf16 v[38:41], v[138:141], v[170:173], v[38:41]
	v_mfma_f32_16x16x32_bf16 v[34:37], v[146:149], v[170:173], v[34:37]
	v_mfma_f32_16x16x32_bf16 v[22:25], v[138:141], v[178:181], v[22:25]
	v_mfma_f32_16x16x32_bf16 v[18:21], v[146:149], v[178:181], v[18:21]
	v_mfma_f32_16x16x32_bf16 v[6:9], v[138:141], v[186:189], v[6:9]
	v_mfma_f32_16x16x32_bf16 v[2:5], v[146:149], v[186:189], v[2:5]
	v_mfma_f32_16x16x32_bf16 v[54:57], v[142:145], v[166:169], v[54:57]
	v_mfma_f32_16x16x32_bf16 v[50:53], v[150:153], v[166:169], v[50:53]
	v_mfma_f32_16x16x32_bf16 v[38:41], v[142:145], v[174:177], v[38:41]
	v_mfma_f32_16x16x32_bf16 v[34:37], v[150:153], v[174:177], v[34:37]
	v_mfma_f32_16x16x32_bf16 v[22:25], v[142:145], v[182:185], v[22:25]
	v_mfma_f32_16x16x32_bf16 v[18:21], v[150:153], v[182:185], v[18:21]
	v_mfma_f32_16x16x32_bf16 v[6:9], v[142:145], v[206:209], v[6:9]
	v_mfma_f32_16x16x32_bf16 v[2:5], v[150:153], v[206:209], v[2:5]
	s_setprio 0
	s_barrier
	s_add_i32 s63, s63, 2
	s_add_u32 s26, s26, 0x100
	s_addc_u32 s27, s27, 0
	s_add_u32 s61, s61, 0x100
	s_addc_u32 s62, s62, 0
	s_cmp_gt_u32 s63, 13
.LBB0_634:
	ds_read_b128 v[98:101], v234
	ds_read_b128 v[110:113], v234 offset:1024
	ds_read_b128 v[122:125], v234 offset:2048
	ds_read_b128 v[126:129], v234 offset:3072
	ds_read_b128 v[138:141], v235
	ds_read_b128 v[142:145], v235 offset:1024
	ds_read_b128 v[146:149], v235 offset:2048
	ds_read_b128 v[150:153], v235 offset:3072
	s_add_u32 s28, s26, 0xfffc0080
	s_addc_u32 s29, s27, -1
	s_cmp_eq_u32 s63, 12
	s_cselect_b32 s31, s19, s29
	s_cselect_b32 s30, s25, s28
	s_cselect_b32 s29, s17, s62
	s_cselect_b32 s28, s60, s61
	v_lshl_add_u64 v[210:211], s[26:27], 0, v[198:199]
	s_add_i32 m0, s3, 0xc000
	ds_read_b128 v[154:157], v236
	ds_read_b128 v[166:169], v236 offset:1024
	ds_read_b128 v[170:173], v236 offset:2048
	ds_read_b128 v[174:177], v236 offset:3072
	ds_read_b128 v[178:181], v236 offset:4096
	ds_read_b128 v[182:185], v236 offset:5120
	ds_read_b128 v[186:189], v236 offset:6144
	ds_read_b128 v[206:209], v236 offset:7168
	global_load_lds_dwordx4 v[210:211], off
	v_lshl_add_u64 v[210:211], s[26:27], 0, v[200:201]
	s_add_i32 m0, s3, 0xe000
	s_nop 0
	global_load_lds_dwordx4 v[210:211], off
	s_waitcnt vmcnt(8)
	s_waitcnt lgkmcnt(0)
	s_barrier
; #define PG8_STAGE_A(b, h, ptr, NX) do { if constexpr (Sched::GATHER) { unsigned gs_[2]; gs_[0] = ((NX) && last_) ? gN[h][0] : gA[h][0]; gs_[1] = ((NX) && last_) ? gN[h][1] : gA[h][1]; PG8_STAGE(PG8_SA(b, h), ptr, gs_); } \
;         else PG8_STAGE(PG8_SA(b, h), (ptr) + ((h) ? hstep : (size_t)0), voffA); } while (0)
; #define PG8_STAGE(bufoff, gbase, voff) do { _Pragma("unroll") for (int _i = 0; _i < 2; ++_i) \
;         __builtin_amdgcn_global_load_lds((const unsigned*)((const char*)(gbase) + (voff)[_i]), (PG8_LAS unsigned*)(lds + (bufoff) + ldsw + _i * 8192), 16, 0, 0); } while (0)
; #define PG8_LDA(dst, b, h) do { _Pragma("unroll") for (int m = 0; m < 4; ++m) _Pragma("unroll") for (int k = 0; k < 2; ++k) dst[m][k] = *(const PG8_LAS bf16x8*)(lds + PG8_SA(b, h) + aoff + m * 2048 + k * 1024); } while (0)
; #define PG8_LDB(dst, b, h) do { _Pragma("unroll") for (int n = 0; n < 2; ++n) _Pragma("unroll") for (int k = 0; k < 2; ++k) dst[n][k] = *(const PG8_LAS bf16x8*)(lds + PG8_SB(b, h) + boff + n * 2048 + k * 1024); } while (0)
; #define PG8_WAIT_V(n) asm volatile("s_waitcnt vmcnt(" #n ")" ::: "memory")
; #define PG8_BAR __builtin_amdgcn_s_barrier()
; template <class Epi, class Sched, bool ALIGN_EPI = false, bool SP2 = false>
; __device__ __forceinline__ void gemm_phase(PG8_LAS unsigned char* lds, const Gemm g, const Sched& S, const Epi& E, const bool skip_epi = false) {
;     ...
;             PG8_LDB(B0, 0, 0); PG8_LDB(B1, 0, 1); PG8_SCHED; PG8_LDA(At, 0, 0); PG8_STAGE_A(1, 1, a1, false);
;             PG8_WAIT_V(8); PG8_WAIT_L(0); PG8_BAR; PG8_MMA(0, 0, At, B0); PG8_MMA(0, 1, At, B1); PG8_BAR; PG8_SCHED;
;             PG8_LDA(At, 0, 1); PG8_STAGE(PG8_SB(0, 0), b2, voffB); PG8_STAGE(PG8_SB(0, 1), b2 + hstep, voffB); PG8_STAGE_A(0, 0, a2, true);
;             PG8_WAIT_V(8); PG8_WAIT_L(0); PG8_BAR; PG8_MMA(1, 0, At, B0); PG8_MMA(1, 1, At, B1); PG8_BAR; PG8_SCHED;
;             PG8_LDB(B0, 1, 0); PG8_LDB(B1, 1, 1); PG8_SCHED; PG8_LDA(At, 1, 0); PG8_STAGE_A(0, 1, a2, true);
;             PG8_WAIT_V(8); PG8_WAIT_L(0); PG8_BAR; PG8_MMA(0, 0, At, B0); PG8_MMA(0, 1, At, B1); PG8_BAR; PG8_SCHED;
;             PG8_LDA(At, 1, 1); PG8_STAGE(PG8_SB(1, 0), b3, voffB); PG8_STAGE(PG8_SB(1, 1), b3 + hstep, voffB); PG8_STAGE_A(1, 0, a3, true);
;             PG8_WAIT_V(8); PG8_WAIT_L(0); PG8_BAR; PG8_MMA(1, 0, At, B0); PG8_MMA(1, 1, At, B1); PG8_BAR; PG8_SCHED;
	s_setprio 3
	s_waitcnt lgkmcnt(0)
	v_mfma_f32_16x16x32_bf16 v[162:165], v[98:101], v[154:157], v[162:165]
	v_mfma_f32_16x16x32_bf16 v[158:161], v[122:125], v[154:157], v[158:161]
	v_mfma_f32_16x16x32_bf16 v[118:121], v[98:101], v[170:173], v[118:121]
	v_mfma_f32_16x16x32_bf16 v[114:117], v[122:125], v[170:173], v[114:117]
	v_mfma_f32_16x16x32_bf16 v[94:97], v[98:101], v[178:181], v[94:97]
	v_mfma_f32_16x16x32_bf16 v[90:93], v[122:125], v[178:181], v[90:93]
	v_mfma_f32_16x16x32_bf16 v[78:81], v[98:101], v[186:189], v[78:81]
	v_mfma_f32_16x16x32_bf16 v[74:77], v[122:125], v[186:189], v[74:77]
	v_mfma_f32_16x16x32_bf16 v[162:165], v[110:113], v[166:169], v[162:165]
	v_mfma_f32_16x16x32_bf16 v[158:161], v[126:129], v[166:169], v[158:161]
	v_mfma_f32_16x16x32_bf16 v[118:121], v[110:113], v[174:177], v[118:121]
	v_mfma_f32_16x16x32_bf16 v[114:117], v[126:129], v[174:177], v[114:117]
	v_mfma_f32_16x16x32_bf16 v[94:97], v[110:113], v[182:185], v[94:97]
	v_mfma_f32_16x16x32_bf16 v[90:93], v[126:129], v[182:185], v[90:93]
	v_mfma_f32_16x16x32_bf16 v[78:81], v[110:113], v[206:209], v[78:81]
	v_mfma_f32_16x16x32_bf16 v[74:77], v[126:129], v[206:209], v[74:77]
	s_setprio 0
	s_setprio 3
	v_mfma_f32_16x16x32_bf16 v[134:137], v[138:141], v[154:157], v[134:137]
	v_mfma_f32_16x16x32_bf16 v[130:133], v[146:149], v[154:157], v[130:133]
	v_mfma_f32_16x16x32_bf16 v[106:109], v[138:141], v[170:173], v[106:109]
	v_mfma_f32_16x16x32_bf16 v[102:105], v[146:149], v[170:173], v[102:105]
	v_mfma_f32_16x16x32_bf16 v[86:89], v[138:141], v[178:181], v[86:89]
	v_mfma_f32_16x16x32_bf16 v[82:85], v[146:149], v[178:181], v[82:85]
	v_mfma_f32_16x16x32_bf16 v[70:73], v[138:141], v[186:189], v[70:73]
	v_mfma_f32_16x16x32_bf16 v[66:69], v[146:149], v[186:189], v[66:69]
	v_mfma_f32_16x16x32_bf16 v[134:137], v[142:145], v[166:169], v[134:137]
	v_mfma_f32_16x16x32_bf16 v[130:133], v[150:153], v[166:169], v[130:133]
	v_mfma_f32_16x16x32_bf16 v[106:109], v[142:145], v[174:177], v[106:109]
	v_mfma_f32_16x16x32_bf16 v[102:105], v[150:153], v[174:177], v[102:105]
	v_mfma_f32_16x16x32_bf16 v[86:89], v[142:145], v[182:185], v[86:89]
	v_mfma_f32_16x16x32_bf16 v[82:85], v[150:153], v[182:185], v[82:85]
	v_mfma_f32_16x16x32_bf16 v[70:73], v[142:145], v[206:209], v[70:73]
	v_mfma_f32_16x16x32_bf16 v[66:69], v[150:153], v[206:209], v[66:69]
	s_setprio 0
	s_barrier
	s_add_i32 s64, s57, s2
	v_lshl_add_u64 v[210:211], s[28:29], 0, v[192:193]
	s_mov_b32 m0, s64
	ds_read_b128 v[154:157], v236 offset:16384
	ds_read_b128 v[166:169], v236 offset:17408
	ds_read_b128 v[170:173], v236 offset:18432
	ds_read_b128 v[174:177], v236 offset:19456
	ds_read_b128 v[178:181], v236 offset:20480
	ds_read_b128 v[182:185], v236 offset:21504
	ds_read_b128 v[186:189], v236 offset:22528
	ds_read_b128 v[206:209], v236 offset:23552
	global_load_lds_dwordx4 v[210:211], off
	s_add_i32 m0, s64, 0x2000
	s_add_u32 s64, s28, 0x40000
	v_lshl_add_u64 v[212:213], s[28:29], 0, v[196:197]
	s_addc_u32 s65, s29, 0
	s_add_i32 s66, s58, s2
	global_load_lds_dwordx4 v[212:213], off
	v_lshl_add_u64 v[214:215], s[64:65], 0, v[192:193]
	s_mov_b32 m0, s66
	v_lshl_add_u64 v[216:217], s[30:31], 0, v[194:195]
	global_load_lds_dwordx4 v[214:215], off
	v_lshl_add_u64 v[214:215], s[64:65], 0, v[196:197]
	s_add_i32 m0, s66, 0x2000
	s_nop 0
	global_load_lds_dwordx4 v[214:215], off
	v_lshl_add_u64 v[214:215], s[30:31], 0, v[190:191]
	s_mov_b32 m0, s3
	s_nop 0
	global_load_lds_dwordx4 v[214:215], off
	s_mov_b32 m0, s34
	s_nop 0
	global_load_lds_dwordx4 v[216:217], off
	s_waitcnt vmcnt(8)
	s_waitcnt lgkmcnt(0)
	s_barrier
	s_setprio 3
	s_waitcnt lgkmcnt(0)
	v_mfma_f32_16x16x32_bf16 v[62:65], v[98:101], v[154:157], v[62:65]
	v_mfma_f32_16x16x32_bf16 v[58:61], v[122:125], v[154:157], v[58:61]
	v_mfma_f32_16x16x32_bf16 v[46:49], v[98:101], v[170:173], v[46:49]
	v_mfma_f32_16x16x32_bf16 v[42:45], v[122:125], v[170:173], v[42:45]
	v_mfma_f32_16x16x32_bf16 v[30:33], v[98:101], v[178:181], v[30:33]
	v_mfma_f32_16x16x32_bf16 v[26:29], v[122:125], v[178:181], v[26:29]
	v_mfma_f32_16x16x32_bf16 v[14:17], v[98:101], v[186:189], v[14:17]
	v_mfma_f32_16x16x32_bf16 v[10:13], v[122:125], v[186:189], v[10:13]
	v_mfma_f32_16x16x32_bf16 v[62:65], v[110:113], v[166:169], v[62:65]
	v_mfma_f32_16x16x32_bf16 v[58:61], v[126:129], v[166:169], v[58:61]
	v_mfma_f32_16x16x32_bf16 v[46:49], v[110:113], v[174:177], v[46:49]
	v_mfma_f32_16x16x32_bf16 v[42:45], v[126:129], v[174:177], v[42:45]
	v_mfma_f32_16x16x32_bf16 v[30:33], v[110:113], v[182:185], v[30:33]
	v_mfma_f32_16x16x32_bf16 v[26:29], v[126:129], v[182:185], v[26:29]
	v_mfma_f32_16x16x32_bf16 v[14:17], v[110:113], v[206:209], v[14:17]
	v_mfma_f32_16x16x32_bf16 v[10:13], v[126:129], v[206:209], v[10:13]
	s_setprio 0
	s_setprio 3
	v_mfma_f32_16x16x32_bf16 v[54:57], v[138:141], v[154:157], v[54:57]
	v_mfma_f32_16x16x32_bf16 v[50:53], v[146:149], v[154:157], v[50:53]
	v_mfma_f32_16x16x32_bf16 v[38:41], v[138:141], v[170:173], v[38:41]
	v_mfma_f32_16x16x32_bf16 v[34:37], v[146:149], v[170:173], v[34:37]
	v_mfma_f32_16x16x32_bf16 v[22:25], v[138:141], v[178:181], v[22:25]
	v_mfma_f32_16x16x32_bf16 v[18:21], v[146:149], v[178:181], v[18:21]
	v_mfma_f32_16x16x32_bf16 v[6:9], v[138:141], v[186:189], v[6:9]
	v_mfma_f32_16x16x32_bf16 v[2:5], v[146:149], v[186:189], v[2:5]
	v_mfma_f32_16x16x32_bf16 v[54:57], v[142:145], v[166:169], v[54:57]
	v_mfma_f32_16x16x32_bf16 v[50:53], v[150:153], v[166:169], v[50:53]
	v_mfma_f32_16x16x32_bf16 v[38:41], v[142:145], v[174:177], v[38:41]
	v_mfma_f32_16x16x32_bf16 v[34:37], v[150:153], v[174:177], v[34:37]
	v_mfma_f32_16x16x32_bf16 v[22:25], v[142:145], v[182:185], v[22:25]
	v_mfma_f32_16x16x32_bf16 v[18:21], v[150:153], v[182:185], v[18:21]
	v_mfma_f32_16x16x32_bf16 v[6:9], v[142:145], v[206:209], v[6:9]
	v_mfma_f32_16x16x32_bf16 v[2:5], v[150:153], v[206:209], v[2:5]
	s_setprio 0
	s_barrier
; #define PG8_STAGE_A(b, h, ptr, NX) do { if constexpr (Sched::GATHER) { unsigned gs_[2]; gs_[0] = ((NX) && last_) ? gN[h][0] : gA[h][0]; gs_[1] = ((NX) && last_) ? gN[h][1] : gA[h][1]; PG8_STAGE(PG8_SA(b, h), ptr, gs_); } \
;         else PG8_STAGE(PG8_SA(b, h), (ptr) + ((h) ? hstep : (size_t)0), voffA); } while (0)
; #define PG8_STAGE(bufoff, gbase, voff) do { _Pragma("unroll") for (int _i = 0; _i < 2; ++_i) \
;         __builtin_amdgcn_global_load_lds((const unsigned*)((const char*)(gbase) + (voff)[_i]), (PG8_LAS unsigned*)(lds + (bufoff) + ldsw + _i * 8192), 16, 0, 0); } while (0)
; #define PG8_LDA(dst, b, h) do { _Pragma("unroll") for (int m = 0; m < 4; ++m) _Pragma("unroll") for (int k = 0; k < 2; ++k) dst[m][k] = *(const PG8_LAS bf16x8*)(lds + PG8_SA(b, h) + aoff + m * 2048 + k * 1024); } while (0)
; #define PG8_LDB(dst, b, h) do { _Pragma("unroll") for (int n = 0; n < 2; ++n) _Pragma("unroll") for (int k = 0; k < 2; ++k) dst[n][k] = *(const PG8_LAS bf16x8*)(lds + PG8_SB(b, h) + boff + n * 2048 + k * 1024); } while (0)
; #define PG8_WAIT_V(n) asm volatile("s_waitcnt vmcnt(" #n ")" ::: "memory")
; #define PG8_BAR __builtin_amdgcn_s_barrier()
; template <class Epi, class Sched, bool ALIGN_EPI = false, bool SP2 = false>
; __device__ __forceinline__ void gemm_phase(PG8_LAS unsigned char* lds, const Gemm g, const Sched& S, const Epi& E, const bool skip_epi = false) {
;     ...
;             PG8_LDB(B0, 0, 0); PG8_LDB(B1, 0, 1); PG8_SCHED; PG8_LDA(At, 0, 0); PG8_STAGE_A(1, 1, a1, false);
;             PG8_WAIT_V(8); PG8_WAIT_L(0); PG8_BAR; PG8_MMA(0, 0, At, B0); PG8_MMA(0, 1, At, B1); PG8_BAR; PG8_SCHED;
;             PG8_LDA(At, 0, 1); PG8_STAGE(PG8_SB(0, 0), b2, voffB); PG8_STAGE(PG8_SB(0, 1), b2 + hstep, voffB); PG8_STAGE_A(0, 0, a2, true);
;             PG8_WAIT_V(8); PG8_WAIT_L(0); PG8_BAR; PG8_MMA(1, 0, At, B0); PG8_MMA(1, 1, At, B1); PG8_BAR; PG8_SCHED;
;             PG8_LDB(B0, 1, 0); PG8_LDB(B1, 1, 1); PG8_SCHED; PG8_LDA(At, 1, 0); PG8_STAGE_A(0, 1, a2, true);
;             PG8_WAIT_V(8); PG8_WAIT_L(0); PG8_BAR; PG8_MMA(0, 0, At, B0); PG8_MMA(0, 1, At, B1); PG8_BAR; PG8_SCHED;
;             PG8_LDA(At, 1, 1); PG8_STAGE(PG8_SB(1, 0), b3, voffB); PG8_STAGE(PG8_SB(1, 1), b3 + hstep, voffB); PG8_STAGE_A(1, 0, a3, true);
;             PG8_WAIT_V(8); PG8_WAIT_L(0); PG8_BAR; PG8_MMA(1, 0, At, B0); PG8_MMA(1, 1, At, B1); PG8_BAR; PG8_SCHED;
	s_add_i32 s64, 0, 0x18000
	s_add_i32 s65, 0, 0x1c000
	v_add_u32_e32 v126, s64, v229
	v_add_u32_e32 v150, s65, v229
	ds_read_b128 v[98:101], v126
	ds_read_b128 v[110:113], v126 offset:1024
	ds_read_b128 v[122:125], v126 offset:2048
	ds_read_b128 v[126:129], v126 offset:3072
	ds_read_b128 v[138:141], v150
	ds_read_b128 v[142:145], v150 offset:1024
	ds_read_b128 v[146:149], v150 offset:2048
	ds_read_b128 v[150:153], v150 offset:3072
	s_add_u32 s30, s30, 0x40000
	s_addc_u32 s31, s31, 0
	s_mov_b32 m0, s35
	v_lshl_add_u64 v[218:219], s[30:31], 0, v[190:191]
	ds_read_b128 v[154:157], v236 offset:32768
	ds_read_b128 v[166:169], v236 offset:33792
	ds_read_b128 v[170:173], v236 offset:34816
	ds_read_b128 v[174:177], v236 offset:35840
	ds_read_b128 v[178:181], v236 offset:36864
	ds_read_b128 v[182:185], v236 offset:37888
	ds_read_b128 v[186:189], v236 offset:38912
	ds_read_b128 v[206:209], v236 offset:39936
	global_load_lds_dwordx4 v[218:219], off
	v_lshl_add_u64 v[218:219], s[30:31], 0, v[194:195]
	s_mov_b32 m0, s36
	s_nop 0
	global_load_lds_dwordx4 v[218:219], off
	s_waitcnt vmcnt(8)
	s_waitcnt lgkmcnt(0)
	s_barrier
	s_setprio 3
	s_waitcnt lgkmcnt(0)
	v_mfma_f32_16x16x32_bf16 v[162:165], v[98:101], v[154:157], v[162:165]
	v_mfma_f32_16x16x32_bf16 v[158:161], v[122:125], v[154:157], v[158:161]
	v_mfma_f32_16x16x32_bf16 v[118:121], v[98:101], v[170:173], v[118:121]
	v_mfma_f32_16x16x32_bf16 v[114:117], v[122:125], v[170:173], v[114:117]
	v_mfma_f32_16x16x32_bf16 v[94:97], v[98:101], v[178:181], v[94:97]
	v_mfma_f32_16x16x32_bf16 v[90:93], v[122:125], v[178:181], v[90:93]
	v_mfma_f32_16x16x32_bf16 v[78:81], v[98:101], v[186:189], v[78:81]
	v_mfma_f32_16x16x32_bf16 v[74:77], v[122:125], v[186:189], v[74:77]
	v_mfma_f32_16x16x32_bf16 v[162:165], v[110:113], v[166:169], v[162:165]
	v_mfma_f32_16x16x32_bf16 v[158:161], v[126:129], v[166:169], v[158:161]
	v_mfma_f32_16x16x32_bf16 v[118:121], v[110:113], v[174:177], v[118:121]
	v_mfma_f32_16x16x32_bf16 v[114:117], v[126:129], v[174:177], v[114:117]
	v_mfma_f32_16x16x32_bf16 v[94:97], v[110:113], v[182:185], v[94:97]
	v_mfma_f32_16x16x32_bf16 v[90:93], v[126:129], v[182:185], v[90:93]
	v_mfma_f32_16x16x32_bf16 v[78:81], v[110:113], v[206:209], v[78:81]
	v_mfma_f32_16x16x32_bf16 v[74:77], v[126:129], v[206:209], v[74:77]
	s_setprio 0
	s_setprio 3
	v_mfma_f32_16x16x32_bf16 v[134:137], v[138:141], v[154:157], v[134:137]
	v_mfma_f32_16x16x32_bf16 v[130:133], v[146:149], v[154:157], v[130:133]
	v_mfma_f32_16x16x32_bf16 v[106:109], v[138:141], v[170:173], v[106:109]
	v_mfma_f32_16x16x32_bf16 v[102:105], v[146:149], v[170:173], v[102:105]
	v_mfma_f32_16x16x32_bf16 v[86:89], v[138:141], v[178:181], v[86:89]
	v_mfma_f32_16x16x32_bf16 v[82:85], v[146:149], v[178:181], v[82:85]
	v_mfma_f32_16x16x32_bf16 v[70:73], v[138:141], v[186:189], v[70:73]
	v_mfma_f32_16x16x32_bf16 v[66:69], v[146:149], v[186:189], v[66:69]
	v_mfma_f32_16x16x32_bf16 v[134:137], v[142:145], v[166:169], v[134:137]
	v_mfma_f32_16x16x32_bf16 v[130:133], v[150:153], v[166:169], v[130:133]
	v_mfma_f32_16x16x32_bf16 v[106:109], v[142:145], v[174:177], v[106:109]
	v_mfma_f32_16x16x32_bf16 v[102:105], v[150:153], v[174:177], v[102:105]
	v_mfma_f32_16x16x32_bf16 v[86:89], v[142:145], v[182:185], v[86:89]
	v_mfma_f32_16x16x32_bf16 v[82:85], v[150:153], v[182:185], v[82:85]
	v_mfma_f32_16x16x32_bf16 v[70:73], v[142:145], v[206:209], v[70:73]
	v_mfma_f32_16x16x32_bf16 v[66:69], v[150:153], v[206:209], v[66:69]
	s_setprio 0
	s_barrier
; #define PG8_STAGE_A(b, h, ptr, NX) do { if constexpr (Sched::GATHER) { unsigned gs_[2]; gs_[0] = ((NX) && last_) ? gN[h][0] : gA[h][0]; gs_[1] = ((NX) && last_) ? gN[h][1] : gA[h][1]; PG8_STAGE(PG8_SA(b, h), ptr, gs_); } \
;         else PG8_STAGE(PG8_SA(b, h), (ptr) + ((h) ? hstep : (size_t)0), voffA); } while (0)
; #define PG8_STAGE(bufoff, gbase, voff) do { _Pragma("unroll") for (int _i = 0; _i < 2; ++_i) \
;         __builtin_amdgcn_global_load_lds((const unsigned*)((const char*)(gbase) + (voff)[_i]), (PG8_LAS unsigned*)(lds + (bufoff) + ldsw + _i * 8192), 16, 0, 0); } while (0)
; #define PG8_LDA(dst, b, h) do { _Pragma("unroll") for (int m = 0; m < 4; ++m) _Pragma("unroll") for (int k = 0; k < 2; ++k) dst[m][k] = *(const PG8_LAS bf16x8*)(lds + PG8_SA(b, h) + aoff + m * 2048 + k * 1024); } while (0)
; #define PG8_LDB(dst, b, h) do { _Pragma("unroll") for (int n = 0; n < 2; ++n) _Pragma("unroll") for (int k = 0; k < 2; ++k) dst[n][k] = *(const PG8_LAS bf16x8*)(lds + PG8_SB(b, h) + boff + n * 2048 + k * 1024); } while (0)
; #define PG8_WAIT_V(n) asm volatile("s_waitcnt vmcnt(" #n ")" ::: "memory")
; #define PG8_BAR __builtin_amdgcn_s_barrier()
; template <class Epi, class Sched, bool ALIGN_EPI = false, bool SP2 = false>
; __device__ __forceinline__ void gemm_phase(PG8_LAS unsigned char* lds, const Gemm g, const Sched& S, const Epi& E, const bool skip_epi = false) {
;     ...
;             PG8_LDB(B0, 0, 0); PG8_LDB(B1, 0, 1); PG8_SCHED; PG8_LDA(At, 0, 0); PG8_STAGE_A(1, 1, a1, false);
;             PG8_WAIT_V(8); PG8_WAIT_L(0); PG8_BAR; PG8_MMA(0, 0, At, B0); PG8_MMA(0, 1, At, B1); PG8_BAR; PG8_SCHED;
;             PG8_LDA(At, 0, 1); PG8_STAGE(PG8_SB(0, 0), b2, voffB); PG8_STAGE(PG8_SB(0, 1), b2 + hstep, voffB); PG8_STAGE_A(0, 0, a2, true);
;             PG8_WAIT_V(8); PG8_WAIT_L(0); PG8_BAR; PG8_MMA(1, 0, At, B0); PG8_MMA(1, 1, At, B1); PG8_BAR; PG8_SCHED;
;             PG8_LDB(B0, 1, 0); PG8_LDB(B1, 1, 1); PG8_SCHED; PG8_LDA(At, 1, 0); PG8_STAGE_A(0, 1, a2, true);
;             PG8_WAIT_V(8); PG8_WAIT_L(0); PG8_BAR; PG8_MMA(0, 0, At, B0); PG8_MMA(0, 1, At, B1); PG8_BAR; PG8_SCHED;
;             PG8_LDA(At, 1, 1); PG8_STAGE(PG8_SB(1, 0), b3, voffB); PG8_STAGE(PG8_SB(1, 1), b3 + hstep, voffB); PG8_STAGE_A(1, 0, a3, true);
;             PG8_WAIT_V(8); PG8_WAIT_L(0); PG8_BAR; PG8_MMA(1, 0, At, B0); PG8_MMA(1, 1, At, B1); PG8_BAR; PG8_SCHED;
	s_add_i32 s30, s64, s2
	v_lshl_add_u64 v[210:211], v[210:211], 0, s[12:13]
	s_mov_b32 m0, s30
	ds_read_b128 v[154:157], v236 offset:49152
	ds_read_b128 v[166:169], v236 offset:50176
	ds_read_b128 v[170:173], v236 offset:51200
	ds_read_b128 v[174:177], v236 offset:52224
	ds_read_b128 v[178:181], v236 offset:53248
	ds_read_b128 v[182:185], v236 offset:54272
	ds_read_b128 v[186:189], v236 offset:55296
	ds_read_b128 v[206:209], v236 offset:56320
	global_load_lds_dwordx4 v[210:211], off
	s_add_i32 m0, s30, 0x2000
	s_add_u32 s28, s28, 0x40080
	v_lshl_add_u64 v[210:211], v[212:213], 0, s[12:13]
	s_addc_u32 s29, s29, 0
	s_add_i32 s30, s65, s2
	global_load_lds_dwordx4 v[210:211], off
	v_lshl_add_u64 v[210:211], s[28:29], 0, v[192:193]
	s_mov_b32 m0, s30
	s_nop 0
	global_load_lds_dwordx4 v[210:211], off
	v_lshl_add_u64 v[210:211], s[28:29], 0, v[196:197]
	s_add_i32 m0, s30, 0x2000
	s_nop 0
	global_load_lds_dwordx4 v[210:211], off
	v_lshl_add_u64 v[210:211], v[214:215], 0, s[12:13]
	s_mov_b32 m0, s39
	s_nop 0
	global_load_lds_dwordx4 v[210:211], off
	v_lshl_add_u64 v[210:211], v[216:217], 0, s[12:13]
	s_mov_b32 m0, s48
	s_nop 0
	global_load_lds_dwordx4 v[210:211], off
	s_waitcnt vmcnt(8)
	s_waitcnt lgkmcnt(0)
	s_barrier
	s_setprio 3
	s_waitcnt lgkmcnt(0)
	v_mfma_f32_16x16x32_bf16 v[62:65], v[98:101], v[154:157], v[62:65]
	v_mfma_f32_16x16x32_bf16 v[58:61], v[122:125], v[154:157], v[58:61]
	v_mfma_f32_16x16x32_bf16 v[46:49], v[98:101], v[170:173], v[46:49]
	v_mfma_f32_16x16x32_bf16 v[42:45], v[122:125], v[170:173], v[42:45]
	v_mfma_f32_16x16x32_bf16 v[30:33], v[98:101], v[178:181], v[30:33]
	v_mfma_f32_16x16x32_bf16 v[26:29], v[122:125], v[178:181], v[26:29]
	v_mfma_f32_16x16x32_bf16 v[14:17], v[98:101], v[186:189], v[14:17]
	v_mfma_f32_16x16x32_bf16 v[10:13], v[122:125], v[186:189], v[10:13]
	v_mfma_f32_16x16x32_bf16 v[62:65], v[110:113], v[166:169], v[62:65]
	v_mfma_f32_16x16x32_bf16 v[58:61], v[126:129], v[166:169], v[58:61]
	v_mfma_f32_16x16x32_bf16 v[46:49], v[110:113], v[174:177], v[46:49]
	v_mfma_f32_16x16x32_bf16 v[42:45], v[126:129], v[174:177], v[42:45]
	v_mfma_f32_16x16x32_bf16 v[30:33], v[110:113], v[182:185], v[30:33]
	v_mfma_f32_16x16x32_bf16 v[26:29], v[126:129], v[182:185], v[26:29]
	v_mfma_f32_16x16x32_bf16 v[14:17], v[110:113], v[206:209], v[14:17]
	v_mfma_f32_16x16x32_bf16 v[10:13], v[126:129], v[206:209], v[10:13]
	s_setprio 0
	s_setprio 3
	v_mfma_f32_16x16x32_bf16 v[54:57], v[138:141], v[154:157], v[54:57]
	v_mfma_f32_16x16x32_bf16 v[50:53], v[146:149], v[154:157], v[50:53]
	v_mfma_f32_16x16x32_bf16 v[38:41], v[138:141], v[170:173], v[38:41]
	v_mfma_f32_16x16x32_bf16 v[34:37], v[146:149], v[170:173], v[34:37]
	v_mfma_f32_16x16x32_bf16 v[22:25], v[138:141], v[178:181], v[22:25]
	v_mfma_f32_16x16x32_bf16 v[18:21], v[146:149], v[178:181], v[18:21]
	v_mfma_f32_16x16x32_bf16 v[6:9], v[138:141], v[186:189], v[6:9]
	v_mfma_f32_16x16x32_bf16 v[2:5], v[146:149], v[186:189], v[2:5]
	v_mfma_f32_16x16x32_bf16 v[54:57], v[142:145], v[166:169], v[54:57]
	v_mfma_f32_16x16x32_bf16 v[50:53], v[150:153], v[166:169], v[50:53]
	v_mfma_f32_16x16x32_bf16 v[38:41], v[142:145], v[174:177], v[38:41]
	v_mfma_f32_16x16x32_bf16 v[34:37], v[150:153], v[174:177], v[34:37]
	v_mfma_f32_16x16x32_bf16 v[22:25], v[142:145], v[182:185], v[22:25]
	v_mfma_f32_16x16x32_bf16 v[18:21], v[150:153], v[182:185], v[18:21]
	v_mfma_f32_16x16x32_bf16 v[6:9], v[142:145], v[206:209], v[6:9]
	v_mfma_f32_16x16x32_bf16 v[2:5], v[150:153], v[206:209], v[2:5]
	s_setprio 0
	s_barrier
	s_add_i32 s63, s63, 2
	s_add_u32 s26, s26, 0x100
	s_addc_u32 s27, s27, 0
	s_add_u32 s61, s61, 0x100
	s_addc_u32 s62, s62, 0
	s_cmp_gt_u32 s63, 13
	s_cbranch_scc0 .LBB0_634
	s_and_b64 vcc, exec, s[14:15]
	s_cbranch_vccz .LBB0_637
	s_barrier

; #define PG8_STAGE_A(b, h, ptr, NX) do { if constexpr (Sched::GATHER) { unsigned gs_[2]; gs_[0] = ((NX) && last_) ? gN[h][0] : gA[h][0]; gs_[1] = ((NX) && last_) ? gN[h][1] : gA[h][1]; PG8_STAGE(PG8_SA(b, h), ptr, gs_); } \
;         else PG8_STAGE(PG8_SA(b, h), (ptr) + ((h) ? hstep : (size_t)0), voffA); } while (0)
; #define PG8_WAIT_V(n) asm volatile("s_waitcnt vmcnt(" #n ")" ::: "memory")
; #define PG8_WAIT_L(n) asm volatile("s_waitcnt lgkmcnt(" #n ")" ::: "memory")
; #define PG8_BAR __builtin_amdgcn_s_barrier()
; template <class Epi, class Sched, bool ALIGN_EPI = false, bool SP2 = false>
; __device__ __forceinline__ void gemm_phase(PG8_LAS unsigned char* lds, const Gemm g, const Sched& S, const Epi& E, const bool skip_epi = false) {
;     ...
;         const char* nA = has_next ? (const char*)g.A + (size_t)nxt.pm * pmstepA + nxt.ko : cA; const char* nB = has_next ? (const char*)g.Bt + (size_t)nxt.pn * tstep + nxt.ko : cB;
;         for (int t = 0; t < nt; t += 2) {
;             const bool last = (t == nt - 2); last_ = last && has_next;
;             const char* a1 = cA + (size_t)(t + 1) * kstep;
;             const char* a2 = last ? nA : cA + (size_t)(t + 2) * kstep; const char* b2 = last ? nB : cB + (size_t)(t + 2) * kstep;
;             const char* a3 = a2 + kstep; const char* b3 = b2 + kstep;
;             if (last && has_next) S.a_ready(nxt);
;             if constexpr (SP2) {
;             PG8_LDB(B0, 0, 0); PG8_LDB(B1, 0, 1); PG8_SCHED; PG8_LDA(At, 0, 0); PG8_STAGE_A(1, 1, a1, false);
;             PG8_WAIT_V(8); PG8_WAIT_L(0); PG8_BAR; PG8_MMA(0, 0, At, B0); PG8_MMA(0, 1, At, B1); PG8_BAR; PG8_SCHED;
;             PG8_LDA(At, 0, 1); PG8_STAGE(PG8_SB(0, 0), b2, voffB); PG8_STAGE(PG8_SB(0, 1), b2 + hstep, voffB); PG8_STAGE_A(0, 0, a2, true);
;             PG8_WAIT_V(8); PG8_WAIT_L(0); PG8_BAR; PG8_MMA(1, 0, At, B0); PG8_MMA(1, 1, At, B1); PG8_BAR; PG8_SCHED;
;             PG8_LDB(B0, 1, 0); PG8_LDB(B1, 1, 1); PG8_SCHED; PG8_LDA(At, 1, 0); PG8_STAGE_A(0, 1, a2, true);
;             PG8_WAIT_V(8); PG8_WAIT_L(0); PG8_BAR; PG8_MMA(0, 0, At, B0); PG8_MMA(0, 1, At, B1); PG8_BAR; PG8_SCHED;
;             PG8_LDA(At, 1, 1); PG8_STAGE(PG8_SB(1, 0), b3, voffB); PG8_STAGE(PG8_SB(1, 1), b3 + hstep, voffB); PG8_STAGE_A(1, 0, a3, true);
;             PG8_WAIT_V(8); PG8_WAIT_L(0); PG8_BAR; PG8_MMA(1, 0, At, B0); PG8_MMA(1, 1, At, B1); PG8_BAR; PG8_SCHED;
.LBB0_720:
	s_ashr_i32 s15, s14, 31
	s_lshl_b64 s[16:17], s[14:15], 19
	s_add_u32 s16, s86, s16
	s_addc_u32 s17, s87, s17
	s_and_b64 s[18:19], s[4:5], exec
	s_cselect_b32 s15, s17, s23
	s_cselect_b32 s56, s16, s22
	s_ashr_i32 s13, s12, 31
	s_lshl_b64 s[18:19], s[12:13], 19
	v_readlane_b32 s26, v254, 15
	v_readlane_b32 s27, v254, 16
	s_add_u32 s18, s26, s18
	s_addc_u32 s19, s27, s19
	s_and_b64 s[26:27], s[4:5], exec
	s_cselect_b32 s13, s19, s25
	s_cselect_b32 s57, s18, s24
	s_add_u32 s22, s22, 0x40080
	s_addc_u32 s23, s23, 0
	s_add_u32 s58, s24, 0x100
	s_addc_u32 s59, s25, 0
	s_mov_b32 s60, -2
	s_waitcnt vmcnt(0)
	v_lshl_add_u32 v130, s20, 8, v175
	v_ashrrev_i32_e32 v131, 31, v130
	v_lshlrev_b64 v[130:131], 6, v[130:131]
	v_lshl_add_u64 v[130:131], v[150:151], 0, v[130:131]
	global_load_dwordx4 v[238:241], v[130:131], off
	global_load_dwordx4 v[242:245], v[130:131], off offset:1024
	global_load_dwordx4 v[246:249], v[130:131], off offset:2048
	global_load_dwordx4 v[250:253], v[130:131], off offset:3072
	ds_read_b128 v[130:133], v187
	ds_read_b128 v[134:137], v187 offset:1024
	ds_read_b128 v[138:141], v187 offset:2048
	ds_read_b128 v[160:163], v187 offset:3072
	ds_read_b128 v[164:167], v188
	ds_read_b128 v[182:185], v188 offset:1024
	ds_read_b128 v[192:195], v188 offset:2048
	ds_read_b128 v[196:199], v188 offset:3072
	s_add_u32 s24, s22, 0xfffc0080
	s_addc_u32 s25, s23, -1
	s_cmp_eq_u32 s60, 12
	s_cselect_b32 s27, s15, s25
	s_cselect_b32 s26, s56, s24
	s_cselect_b32 s25, s13, s59
	s_cselect_b32 s24, s57, s58
	v_lshl_add_u64 v[168:169], s[22:23], 0, v[152:153]
	s_add_i32 m0, s29, 0xc000
	ds_read_b128 v[200:203], v189
	ds_read_b128 v[204:207], v189 offset:1024
	ds_read_b128 v[208:211], v189 offset:2048
	ds_read_b128 v[212:215], v189 offset:3072
	ds_read_b128 v[216:219], v189 offset:4096
	ds_read_b128 v[220:223], v189 offset:5120
	ds_read_b128 v[224:227], v189 offset:6144
	ds_read_b128 v[230:233], v189 offset:7168
	global_load_lds_dwordx4 v[168:169], off
	v_lshl_add_u64 v[168:169], s[22:23], 0, v[154:155]
	s_add_i32 m0, s29, 0xe000
	s_nop 0
	global_load_lds_dwordx4 v[168:169], off
	s_waitcnt vmcnt(8)
	s_waitcnt lgkmcnt(0)
	s_barrier
	s_setprio 3
	s_waitcnt lgkmcnt(0)
	v_mfma_f32_16x16x32_bf16 v[126:129], v[130:133], v[200:203], 0
	v_mfma_f32_16x16x32_bf16 v[122:125], v[138:141], v[200:203], 0
	v_mfma_f32_16x16x32_bf16 v[110:113], v[130:133], v[208:211], 0
	v_mfma_f32_16x16x32_bf16 v[106:109], v[138:141], v[208:211], 0
	v_mfma_f32_16x16x32_bf16 v[94:97], v[130:133], v[216:219], 0
	v_mfma_f32_16x16x32_bf16 v[90:93], v[138:141], v[216:219], 0
	v_mfma_f32_16x16x32_bf16 v[78:81], v[130:133], v[224:227], 0
	v_mfma_f32_16x16x32_bf16 v[74:77], v[138:141], v[224:227], 0
	v_mfma_f32_16x16x32_bf16 v[126:129], v[134:137], v[204:207], v[126:129]
	v_mfma_f32_16x16x32_bf16 v[122:125], v[160:163], v[204:207], v[122:125]
	v_mfma_f32_16x16x32_bf16 v[110:113], v[134:137], v[212:215], v[110:113]
	v_mfma_f32_16x16x32_bf16 v[106:109], v[160:163], v[212:215], v[106:109]
	v_mfma_f32_16x16x32_bf16 v[94:97], v[134:137], v[220:223], v[94:97]
	v_mfma_f32_16x16x32_bf16 v[90:93], v[160:163], v[220:223], v[90:93]
	v_mfma_f32_16x16x32_bf16 v[78:81], v[134:137], v[230:233], v[78:81]
	v_mfma_f32_16x16x32_bf16 v[74:77], v[160:163], v[230:233], v[74:77]
	s_setprio 0
	s_setprio 3
	v_mfma_f32_16x16x32_bf16 v[118:121], v[164:167], v[200:203], 0
	v_mfma_f32_16x16x32_bf16 v[114:117], v[192:195], v[200:203], 0
	v_mfma_f32_16x16x32_bf16 v[102:105], v[164:167], v[208:211], 0
	v_mfma_f32_16x16x32_bf16 v[98:101], v[192:195], v[208:211], 0
	v_mfma_f32_16x16x32_bf16 v[86:89], v[164:167], v[216:219], 0
	v_mfma_f32_16x16x32_bf16 v[82:85], v[192:195], v[216:219], 0
	v_mfma_f32_16x16x32_bf16 v[70:73], v[164:167], v[224:227], 0
	v_mfma_f32_16x16x32_bf16 v[66:69], v[192:195], v[224:227], 0
	v_mfma_f32_16x16x32_bf16 v[118:121], v[182:185], v[204:207], v[118:121]
	v_mfma_f32_16x16x32_bf16 v[114:117], v[196:199], v[204:207], v[114:117]
	v_mfma_f32_16x16x32_bf16 v[102:105], v[182:185], v[212:215], v[102:105]
	v_mfma_f32_16x16x32_bf16 v[98:101], v[196:199], v[212:215], v[98:101]
	v_mfma_f32_16x16x32_bf16 v[86:89], v[182:185], v[220:223], v[86:89]
	v_mfma_f32_16x16x32_bf16 v[82:85], v[196:199], v[220:223], v[82:85]
	v_mfma_f32_16x16x32_bf16 v[70:73], v[182:185], v[230:233], v[70:73]
	v_mfma_f32_16x16x32_bf16 v[66:69], v[196:199], v[230:233], v[66:69]
	s_setprio 0
	s_barrier
	s_add_i32 s61, s39, s2
	v_lshl_add_u64 v[168:169], s[24:25], 0, v[146:147]
	s_mov_b32 m0, s61
	ds_read_b128 v[200:203], v189 offset:16384
	ds_read_b128 v[204:207], v189 offset:17408
	ds_read_b128 v[208:211], v189 offset:18432
	ds_read_b128 v[212:215], v189 offset:19456
	ds_read_b128 v[216:219], v189 offset:20480
	ds_read_b128 v[220:223], v189 offset:21504
	ds_read_b128 v[224:227], v189 offset:22528
	ds_read_b128 v[230:233], v189 offset:23552
	global_load_lds_dwordx4 v[168:169], off
	s_add_i32 m0, s61, 0x2000
	s_add_u32 s62, s24, 0x40000
	v_lshl_add_u64 v[172:173], s[24:25], 0, v[142:143]
	s_addc_u32 s63, s25, 0
	s_add_i32 s61, s48, s2
	global_load_lds_dwordx4 v[172:173], off
	v_lshl_add_u64 v[176:177], s[62:63], 0, v[146:147]
	s_mov_b32 m0, s61
	v_lshl_add_u64 v[234:235], s[26:27], 0, v[144:145]
	global_load_lds_dwordx4 v[176:177], off
	v_lshl_add_u64 v[176:177], s[62:63], 0, v[142:143]
	s_add_i32 m0, s61, 0x2000
	s_nop 0
	global_load_lds_dwordx4 v[176:177], off
	v_lshl_add_u64 v[176:177], s[26:27], 0, v[148:149]
	s_mov_b32 m0, s29
	s_nop 0
	global_load_lds_dwordx4 v[176:177], off
	s_mov_b32 m0, s30
	s_nop 0
	global_load_lds_dwordx4 v[234:235], off
	s_waitcnt vmcnt(8)
	s_waitcnt lgkmcnt(0)
	s_barrier
; #define PG8_STAGE_A(b, h, ptr, NX) do { if constexpr (Sched::GATHER) { unsigned gs_[2]; gs_[0] = ((NX) && last_) ? gN[h][0] : gA[h][0]; gs_[1] = ((NX) && last_) ? gN[h][1] : gA[h][1]; PG8_STAGE(PG8_SA(b, h), ptr, gs_); } \
;         else PG8_STAGE(PG8_SA(b, h), (ptr) + ((h) ? hstep : (size_t)0), voffA); } while (0)
; #define PG8_STAGE(bufoff, gbase, voff) do { _Pragma("unroll") for (int _i = 0; _i < 2; ++_i) \
;         __builtin_amdgcn_global_load_lds((const unsigned*)((const char*)(gbase) + (voff)[_i]), (PG8_LAS unsigned*)(lds + (bufoff) + ldsw + _i * 8192), 16, 0, 0); } while (0)
; #define PG8_LDA(dst, b, h) do { _Pragma("unroll") for (int m = 0; m < 4; ++m) _Pragma("unroll") for (int k = 0; k < 2; ++k) dst[m][k] = *(const PG8_LAS bf16x8*)(lds + PG8_SA(b, h) + aoff + m * 2048 + k * 1024); } while (0)
; #define PG8_LDB(dst, b, h) do { _Pragma("unroll") for (int n = 0; n < 2; ++n) _Pragma("unroll") for (int k = 0; k < 2; ++k) dst[n][k] = *(const PG8_LAS bf16x8*)(lds + PG8_SB(b, h) + boff + n * 2048 + k * 1024); } while (0)
; #define PG8_WAIT_V(n) asm volatile("s_waitcnt vmcnt(" #n ")" ::: "memory")
; #define PG8_BAR __builtin_amdgcn_s_barrier()
; template <class Epi, class Sched, bool ALIGN_EPI = false, bool SP2 = false>
; __device__ __forceinline__ void gemm_phase(PG8_LAS unsigned char* lds, const Gemm g, const Sched& S, const Epi& E, const bool skip_epi = false) {
;     ...
;             PG8_LDB(B0, 0, 0); PG8_LDB(B1, 0, 1); PG8_SCHED; PG8_LDA(At, 0, 0); PG8_STAGE_A(1, 1, a1, false);
;             PG8_WAIT_V(8); PG8_WAIT_L(0); PG8_BAR; PG8_MMA(0, 0, At, B0); PG8_MMA(0, 1, At, B1); PG8_BAR; PG8_SCHED;
;             PG8_LDA(At, 0, 1); PG8_STAGE(PG8_SB(0, 0), b2, voffB); PG8_STAGE(PG8_SB(0, 1), b2 + hstep, voffB); PG8_STAGE_A(0, 0, a2, true);
;             PG8_WAIT_V(8); PG8_WAIT_L(0); PG8_BAR; PG8_MMA(1, 0, At, B0); PG8_MMA(1, 1, At, B1); PG8_BAR; PG8_SCHED;
;             PG8_LDB(B0, 1, 0); PG8_LDB(B1, 1, 1); PG8_SCHED; PG8_LDA(At, 1, 0); PG8_STAGE_A(0, 1, a2, true);
;             PG8_WAIT_V(8); PG8_WAIT_L(0); PG8_BAR; PG8_MMA(0, 0, At, B0); PG8_MMA(0, 1, At, B1); PG8_BAR; PG8_SCHED;
;             PG8_LDA(At, 1, 1); PG8_STAGE(PG8_SB(1, 0), b3, voffB); PG8_STAGE(PG8_SB(1, 1), b3 + hstep, voffB); PG8_STAGE_A(1, 0, a3, true);
;             PG8_WAIT_V(8); PG8_WAIT_L(0); PG8_BAR; PG8_MMA(1, 0, At, B0); PG8_MMA(1, 1, At, B1); PG8_BAR; PG8_SCHED;
	s_setprio 3
	s_waitcnt lgkmcnt(0)
	v_mfma_f32_16x16x32_bf16 v[62:65], v[130:133], v[200:203], 0
	v_mfma_f32_16x16x32_bf16 v[58:61], v[138:141], v[200:203], 0
	v_mfma_f32_16x16x32_bf16 v[46:49], v[130:133], v[208:211], 0
	v_mfma_f32_16x16x32_bf16 v[42:45], v[138:141], v[208:211], 0
	v_mfma_f32_16x16x32_bf16 v[30:33], v[130:133], v[216:219], 0
	v_mfma_f32_16x16x32_bf16 v[26:29], v[138:141], v[216:219], 0
	v_mfma_f32_16x16x32_bf16 v[14:17], v[130:133], v[224:227], 0
	v_mfma_f32_16x16x32_bf16 v[10:13], v[138:141], v[224:227], 0
	v_mfma_f32_16x16x32_bf16 v[62:65], v[134:137], v[204:207], v[62:65]
	v_mfma_f32_16x16x32_bf16 v[58:61], v[160:163], v[204:207], v[58:61]
	v_mfma_f32_16x16x32_bf16 v[46:49], v[134:137], v[212:215], v[46:49]
	v_mfma_f32_16x16x32_bf16 v[42:45], v[160:163], v[212:215], v[42:45]
	v_mfma_f32_16x16x32_bf16 v[30:33], v[134:137], v[220:223], v[30:33]
	v_mfma_f32_16x16x32_bf16 v[26:29], v[160:163], v[220:223], v[26:29]
	v_mfma_f32_16x16x32_bf16 v[14:17], v[134:137], v[230:233], v[14:17]
	v_mfma_f32_16x16x32_bf16 v[10:13], v[160:163], v[230:233], v[10:13]
	s_setprio 0
	s_setprio 3
	v_mfma_f32_16x16x32_bf16 v[54:57], v[164:167], v[200:203], 0
	v_mfma_f32_16x16x32_bf16 v[50:53], v[192:195], v[200:203], 0
	v_mfma_f32_16x16x32_bf16 v[38:41], v[164:167], v[208:211], 0
	v_mfma_f32_16x16x32_bf16 v[34:37], v[192:195], v[208:211], 0
	v_mfma_f32_16x16x32_bf16 v[22:25], v[164:167], v[216:219], 0
	v_mfma_f32_16x16x32_bf16 v[18:21], v[192:195], v[216:219], 0
	v_mfma_f32_16x16x32_bf16 v[6:9], v[164:167], v[224:227], 0
	v_mfma_f32_16x16x32_bf16 v[2:5], v[192:195], v[224:227], 0
	v_mfma_f32_16x16x32_bf16 v[54:57], v[182:185], v[204:207], v[54:57]
	v_mfma_f32_16x16x32_bf16 v[50:53], v[196:199], v[204:207], v[50:53]
	v_mfma_f32_16x16x32_bf16 v[38:41], v[182:185], v[212:215], v[38:41]
	v_mfma_f32_16x16x32_bf16 v[34:37], v[196:199], v[212:215], v[34:37]
	v_mfma_f32_16x16x32_bf16 v[22:25], v[182:185], v[220:223], v[22:25]
	v_mfma_f32_16x16x32_bf16 v[18:21], v[196:199], v[220:223], v[18:21]
	v_mfma_f32_16x16x32_bf16 v[6:9], v[182:185], v[230:233], v[6:9]
	v_mfma_f32_16x16x32_bf16 v[2:5], v[196:199], v[230:233], v[2:5]
	s_setprio 0
	s_barrier
	s_add_i32 s61, 0, 0x18000
	s_add_i32 s62, 0, 0x1c000
	v_add_u32_e32 v160, s61, v1
	v_add_u32_e32 v170, s62, v1
	ds_read_b128 v[130:133], v160
	ds_read_b128 v[134:137], v160 offset:1024
	ds_read_b128 v[138:141], v160 offset:2048
	ds_read_b128 v[160:163], v160 offset:3072
	ds_read_b128 v[164:167], v170
	ds_read_b128 v[182:185], v170 offset:1024
	ds_read_b128 v[192:195], v170 offset:2048
	ds_read_b128 v[196:199], v170 offset:3072
	s_add_u32 s26, s26, 0x40000
	s_addc_u32 s27, s27, 0
	s_mov_b32 m0, s31
	v_lshl_add_u64 v[236:237], s[26:27], 0, v[148:149]
	ds_read_b128 v[200:203], v189 offset:32768
	ds_read_b128 v[204:207], v189 offset:33792
	ds_read_b128 v[208:211], v189 offset:34816
	ds_read_b128 v[212:215], v189 offset:35840
	ds_read_b128 v[216:219], v189 offset:36864
	ds_read_b128 v[220:223], v189 offset:37888
	ds_read_b128 v[224:227], v189 offset:38912
	ds_read_b128 v[230:233], v189 offset:39936
	global_load_lds_dwordx4 v[236:237], off
	v_lshl_add_u64 v[236:237], s[26:27], 0, v[144:145]
	s_mov_b32 m0, s34
	s_nop 0
	global_load_lds_dwordx4 v[236:237], off
	s_waitcnt vmcnt(8)
	s_waitcnt lgkmcnt(0)
	s_barrier
	s_setprio 3
	s_waitcnt lgkmcnt(0)
	v_mfma_f32_16x16x32_bf16 v[126:129], v[130:133], v[200:203], v[126:129]
	v_mfma_f32_16x16x32_bf16 v[122:125], v[138:141], v[200:203], v[122:125]
	v_mfma_f32_16x16x32_bf16 v[110:113], v[130:133], v[208:211], v[110:113]
	v_mfma_f32_16x16x32_bf16 v[106:109], v[138:141], v[208:211], v[106:109]
	v_mfma_f32_16x16x32_bf16 v[94:97], v[130:133], v[216:219], v[94:97]
	v_mfma_f32_16x16x32_bf16 v[90:93], v[138:141], v[216:219], v[90:93]
	v_mfma_f32_16x16x32_bf16 v[78:81], v[130:133], v[224:227], v[78:81]
	v_mfma_f32_16x16x32_bf16 v[74:77], v[138:141], v[224:227], v[74:77]
	v_mfma_f32_16x16x32_bf16 v[126:129], v[134:137], v[204:207], v[126:129]
	v_mfma_f32_16x16x32_bf16 v[122:125], v[160:163], v[204:207], v[122:125]
	v_mfma_f32_16x16x32_bf16 v[110:113], v[134:137], v[212:215], v[110:113]
	v_mfma_f32_16x16x32_bf16 v[106:109], v[160:163], v[212:215], v[106:109]
	v_mfma_f32_16x16x32_bf16 v[94:97], v[134:137], v[220:223], v[94:97]
	v_mfma_f32_16x16x32_bf16 v[90:93], v[160:163], v[220:223], v[90:93]
	v_mfma_f32_16x16x32_bf16 v[78:81], v[134:137], v[230:233], v[78:81]
	v_mfma_f32_16x16x32_bf16 v[74:77], v[160:163], v[230:233], v[74:77]
	s_setprio 0
	s_setprio 3
	v_mfma_f32_16x16x32_bf16 v[118:121], v[164:167], v[200:203], v[118:121]
	v_mfma_f32_16x16x32_bf16 v[114:117], v[192:195], v[200:203], v[114:117]
	v_mfma_f32_16x16x32_bf16 v[102:105], v[164:167], v[208:211], v[102:105]
	v_mfma_f32_16x16x32_bf16 v[98:101], v[192:195], v[208:211], v[98:101]
	v_mfma_f32_16x16x32_bf16 v[86:89], v[164:167], v[216:219], v[86:89]
	v_mfma_f32_16x16x32_bf16 v[82:85], v[192:195], v[216:219], v[82:85]
	v_mfma_f32_16x16x32_bf16 v[70:73], v[164:167], v[224:227], v[70:73]
	v_mfma_f32_16x16x32_bf16 v[66:69], v[192:195], v[224:227], v[66:69]
	v_mfma_f32_16x16x32_bf16 v[118:121], v[182:185], v[204:207], v[118:121]
	v_mfma_f32_16x16x32_bf16 v[114:117], v[196:199], v[204:207], v[114:117]
	v_mfma_f32_16x16x32_bf16 v[102:105], v[182:185], v[212:215], v[102:105]
	v_mfma_f32_16x16x32_bf16 v[98:101], v[196:199], v[212:215], v[98:101]
	v_mfma_f32_16x16x32_bf16 v[86:89], v[182:185], v[220:223], v[86:89]
	v_mfma_f32_16x16x32_bf16 v[82:85], v[196:199], v[220:223], v[82:85]
	v_mfma_f32_16x16x32_bf16 v[70:73], v[182:185], v[230:233], v[70:73]
	v_mfma_f32_16x16x32_bf16 v[66:69], v[196:199], v[230:233], v[66:69]
	s_setprio 0
	s_barrier
; #define PG8_STAGE_A(b, h, ptr, NX) do { if constexpr (Sched::GATHER) { unsigned gs_[2]; gs_[0] = ((NX) && last_) ? gN[h][0] : gA[h][0]; gs_[1] = ((NX) && last_) ? gN[h][1] : gA[h][1]; PG8_STAGE(PG8_SA(b, h), ptr, gs_); } \
;         else PG8_STAGE(PG8_SA(b, h), (ptr) + ((h) ? hstep : (size_t)0), voffA); } while (0)
; #define PG8_STAGE(bufoff, gbase, voff) do { _Pragma("unroll") for (int _i = 0; _i < 2; ++_i) \
;         __builtin_amdgcn_global_load_lds((const unsigned*)((const char*)(gbase) + (voff)[_i]), (PG8_LAS unsigned*)(lds + (bufoff) + ldsw + _i * 8192), 16, 0, 0); } while (0)
; #define PG8_LDA(dst, b, h) do { _Pragma("unroll") for (int m = 0; m < 4; ++m) _Pragma("unroll") for (int k = 0; k < 2; ++k) dst[m][k] = *(const PG8_LAS bf16x8*)(lds + PG8_SA(b, h) + aoff + m * 2048 + k * 1024); } while (0)
; #define PG8_LDB(dst, b, h) do { _Pragma("unroll") for (int n = 0; n < 2; ++n) _Pragma("unroll") for (int k = 0; k < 2; ++k) dst[n][k] = *(const PG8_LAS bf16x8*)(lds + PG8_SB(b, h) + boff + n * 2048 + k * 1024); } while (0)
; #define PG8_WAIT_V(n) asm volatile("s_waitcnt vmcnt(" #n ")" ::: "memory")
; #define PG8_BAR __builtin_amdgcn_s_barrier()
; template <class Epi, class Sched, bool ALIGN_EPI = false, bool SP2 = false>
; __device__ __forceinline__ void gemm_phase(PG8_LAS unsigned char* lds, const Gemm g, const Sched& S, const Epi& E, const bool skip_epi = false) {
;     ...
;             PG8_LDB(B0, 0, 0); PG8_LDB(B1, 0, 1); PG8_SCHED; PG8_LDA(At, 0, 0); PG8_STAGE_A(1, 1, a1, false);
;             PG8_WAIT_V(8); PG8_WAIT_L(0); PG8_BAR; PG8_MMA(0, 0, At, B0); PG8_MMA(0, 1, At, B1); PG8_BAR; PG8_SCHED;
;             PG8_LDA(At, 0, 1); PG8_STAGE(PG8_SB(0, 0), b2, voffB); PG8_STAGE(PG8_SB(0, 1), b2 + hstep, voffB); PG8_STAGE_A(0, 0, a2, true);
;             PG8_WAIT_V(8); PG8_WAIT_L(0); PG8_BAR; PG8_MMA(1, 0, At, B0); PG8_MMA(1, 1, At, B1); PG8_BAR; PG8_SCHED;
;             PG8_LDB(B0, 1, 0); PG8_LDB(B1, 1, 1); PG8_SCHED; PG8_LDA(At, 1, 0); PG8_STAGE_A(0, 1, a2, true);
;             PG8_WAIT_V(8); PG8_WAIT_L(0); PG8_BAR; PG8_MMA(0, 0, At, B0); PG8_MMA(0, 1, At, B1); PG8_BAR; PG8_SCHED;
;             PG8_LDA(At, 1, 1); PG8_STAGE(PG8_SB(1, 0), b3, voffB); PG8_STAGE(PG8_SB(1, 1), b3 + hstep, voffB); PG8_STAGE_A(1, 0, a3, true);
;             PG8_WAIT_V(8); PG8_WAIT_L(0); PG8_BAR; PG8_MMA(1, 0, At, B0); PG8_MMA(1, 1, At, B1); PG8_BAR; PG8_SCHED;
	s_add_i32 s26, s61, s2
	v_lshl_add_u64 v[168:169], v[168:169], 0, s[8:9]
	s_mov_b32 m0, s26
	ds_read_b128 v[200:203], v189 offset:49152
	ds_read_b128 v[204:207], v189 offset:50176
	ds_read_b128 v[208:211], v189 offset:51200
	ds_read_b128 v[212:215], v189 offset:52224
	ds_read_b128 v[216:219], v189 offset:53248
	ds_read_b128 v[220:223], v189 offset:54272
	ds_read_b128 v[224:227], v189 offset:55296
	ds_read_b128 v[230:233], v189 offset:56320
	global_load_lds_dwordx4 v[168:169], off
	s_add_i32 m0, s26, 0x2000
	s_add_u32 s24, s24, 0x40080
	v_lshl_add_u64 v[168:169], v[172:173], 0, s[8:9]
	s_addc_u32 s25, s25, 0
	s_add_i32 s26, s62, s2
	global_load_lds_dwordx4 v[168:169], off
	v_lshl_add_u64 v[168:169], s[24:25], 0, v[146:147]
	s_mov_b32 m0, s26
	s_nop 0
	global_load_lds_dwordx4 v[168:169], off
	v_lshl_add_u64 v[168:169], s[24:25], 0, v[142:143]
	s_add_i32 m0, s26, 0x2000
	s_nop 0
	global_load_lds_dwordx4 v[168:169], off
	v_lshl_add_u64 v[168:169], v[176:177], 0, s[8:9]
	s_mov_b32 m0, s36
	s_nop 0
	global_load_lds_dwordx4 v[168:169], off
	v_lshl_add_u64 v[168:169], v[234:235], 0, s[8:9]
	s_mov_b32 m0, s37
	s_nop 0
	global_load_lds_dwordx4 v[168:169], off
	s_waitcnt vmcnt(8)
	s_waitcnt lgkmcnt(0)
	s_barrier
	s_setprio 3
	s_waitcnt lgkmcnt(0)
	v_mfma_f32_16x16x32_bf16 v[62:65], v[130:133], v[200:203], v[62:65]
	v_mfma_f32_16x16x32_bf16 v[58:61], v[138:141], v[200:203], v[58:61]
	v_mfma_f32_16x16x32_bf16 v[46:49], v[130:133], v[208:211], v[46:49]
	v_mfma_f32_16x16x32_bf16 v[42:45], v[138:141], v[208:211], v[42:45]
	v_mfma_f32_16x16x32_bf16 v[30:33], v[130:133], v[216:219], v[30:33]
	v_mfma_f32_16x16x32_bf16 v[26:29], v[138:141], v[216:219], v[26:29]
	v_mfma_f32_16x16x32_bf16 v[14:17], v[130:133], v[224:227], v[14:17]
	v_mfma_f32_16x16x32_bf16 v[10:13], v[138:141], v[224:227], v[10:13]
	v_mfma_f32_16x16x32_bf16 v[62:65], v[134:137], v[204:207], v[62:65]
	v_mfma_f32_16x16x32_bf16 v[58:61], v[160:163], v[204:207], v[58:61]
	v_mfma_f32_16x16x32_bf16 v[46:49], v[134:137], v[212:215], v[46:49]
	v_mfma_f32_16x16x32_bf16 v[42:45], v[160:163], v[212:215], v[42:45]
	v_mfma_f32_16x16x32_bf16 v[30:33], v[134:137], v[220:223], v[30:33]
	v_mfma_f32_16x16x32_bf16 v[26:29], v[160:163], v[220:223], v[26:29]
	v_mfma_f32_16x16x32_bf16 v[14:17], v[134:137], v[230:233], v[14:17]
	v_mfma_f32_16x16x32_bf16 v[10:13], v[160:163], v[230:233], v[10:13]
	s_setprio 0
	s_setprio 3
	v_mfma_f32_16x16x32_bf16 v[54:57], v[164:167], v[200:203], v[54:57]
	v_mfma_f32_16x16x32_bf16 v[50:53], v[192:195], v[200:203], v[50:53]
	v_mfma_f32_16x16x32_bf16 v[38:41], v[164:167], v[208:211], v[38:41]
	v_mfma_f32_16x16x32_bf16 v[34:37], v[192:195], v[208:211], v[34:37]
	v_mfma_f32_16x16x32_bf16 v[22:25], v[164:167], v[216:219], v[22:25]
	v_mfma_f32_16x16x32_bf16 v[18:21], v[192:195], v[216:219], v[18:21]
	v_mfma_f32_16x16x32_bf16 v[6:9], v[164:167], v[224:227], v[6:9]
	v_mfma_f32_16x16x32_bf16 v[2:5], v[192:195], v[224:227], v[2:5]
	v_mfma_f32_16x16x32_bf16 v[54:57], v[182:185], v[204:207], v[54:57]
	v_mfma_f32_16x16x32_bf16 v[50:53], v[196:199], v[204:207], v[50:53]
	v_mfma_f32_16x16x32_bf16 v[38:41], v[182:185], v[212:215], v[38:41]
	v_mfma_f32_16x16x32_bf16 v[34:37], v[196:199], v[212:215], v[34:37]
	v_mfma_f32_16x16x32_bf16 v[22:25], v[182:185], v[220:223], v[22:25]
	v_mfma_f32_16x16x32_bf16 v[18:21], v[196:199], v[220:223], v[18:21]
	v_mfma_f32_16x16x32_bf16 v[6:9], v[182:185], v[230:233], v[6:9]
	v_mfma_f32_16x16x32_bf16 v[2:5], v[196:199], v[230:233], v[2:5]
	s_setprio 0
	s_barrier
	s_add_i32 s60, s60, 2
	s_add_u32 s22, s22, 0x100
	s_addc_u32 s23, s23, 0
	s_add_u32 s58, s58, 0x100
	s_addc_u32 s59, s59, 0
	s_cmp_gt_u32 s60, 13
.LBB0_721:
	ds_read_b128 v[130:133], v187
	ds_read_b128 v[134:137], v187 offset:1024
	ds_read_b128 v[138:141], v187 offset:2048
	ds_read_b128 v[160:163], v187 offset:3072
	ds_read_b128 v[164:167], v188
	ds_read_b128 v[182:185], v188 offset:1024
	ds_read_b128 v[192:195], v188 offset:2048
	ds_read_b128 v[196:199], v188 offset:3072
	s_add_u32 s24, s22, 0xfffc0080
	s_addc_u32 s25, s23, -1
	s_cmp_eq_u32 s60, 12
	s_cselect_b32 s27, s15, s25
	s_cselect_b32 s26, s56, s24
	s_cselect_b32 s25, s13, s59
	s_cselect_b32 s24, s57, s58
	v_lshl_add_u64 v[168:169], s[22:23], 0, v[152:153]
	s_add_i32 m0, s29, 0xc000
	ds_read_b128 v[200:203], v189
	ds_read_b128 v[204:207], v189 offset:1024
	ds_read_b128 v[208:211], v189 offset:2048
	ds_read_b128 v[212:215], v189 offset:3072
	ds_read_b128 v[216:219], v189 offset:4096
	ds_read_b128 v[220:223], v189 offset:5120
	ds_read_b128 v[224:227], v189 offset:6144
	ds_read_b128 v[230:233], v189 offset:7168
	global_load_lds_dwordx4 v[168:169], off
	v_lshl_add_u64 v[168:169], s[22:23], 0, v[154:155]
	s_add_i32 m0, s29, 0xe000
	s_nop 0
	global_load_lds_dwordx4 v[168:169], off
	s_waitcnt vmcnt(8)
	s_waitcnt lgkmcnt(0)
	s_barrier
; #define PG8_STAGE_A(b, h, ptr, NX) do { if constexpr (Sched::GATHER) { unsigned gs_[2]; gs_[0] = ((NX) && last_) ? gN[h][0] : gA[h][0]; gs_[1] = ((NX) && last_) ? gN[h][1] : gA[h][1]; PG8_STAGE(PG8_SA(b, h), ptr, gs_); } \
;         else PG8_STAGE(PG8_SA(b, h), (ptr) + ((h) ? hstep : (size_t)0), voffA); } while (0)
; #define PG8_STAGE(bufoff, gbase, voff) do { _Pragma("unroll") for (int _i = 0; _i < 2; ++_i) \
;         __builtin_amdgcn_global_load_lds((const unsigned*)((const char*)(gbase) + (voff)[_i]), (PG8_LAS unsigned*)(lds + (bufoff) + ldsw + _i * 8192), 16, 0, 0); } while (0)
; #define PG8_LDA(dst, b, h) do { _Pragma("unroll") for (int m = 0; m < 4; ++m) _Pragma("unroll") for (int k = 0; k < 2; ++k) dst[m][k] = *(const PG8_LAS bf16x8*)(lds + PG8_SA(b, h) + aoff + m * 2048 + k * 1024); } while (0)
; #define PG8_LDB(dst, b, h) do { _Pragma("unroll") for (int n = 0; n < 2; ++n) _Pragma("unroll") for (int k = 0; k < 2; ++k) dst[n][k] = *(const PG8_LAS bf16x8*)(lds + PG8_SB(b, h) + boff + n * 2048 + k * 1024); } while (0)
; #define PG8_WAIT_V(n) asm volatile("s_waitcnt vmcnt(" #n ")" ::: "memory")
; #define PG8_BAR __builtin_amdgcn_s_barrier()
; template <class Epi, class Sched, bool ALIGN_EPI = false, bool SP2 = false>
; __device__ __forceinline__ void gemm_phase(PG8_LAS unsigned char* lds, const Gemm g, const Sched& S, const Epi& E, const bool skip_epi = false) {
;     ...
;             PG8_LDB(B0, 0, 0); PG8_LDB(B1, 0, 1); PG8_SCHED; PG8_LDA(At, 0, 0); PG8_STAGE_A(1, 1, a1, false);
;             PG8_WAIT_V(8); PG8_WAIT_L(0); PG8_BAR; PG8_MMA(0, 0, At, B0); PG8_MMA(0, 1, At, B1); PG8_BAR; PG8_SCHED;
;             PG8_LDA(At, 0, 1); PG8_STAGE(PG8_SB(0, 0), b2, voffB); PG8_STAGE(PG8_SB(0, 1), b2 + hstep, voffB); PG8_STAGE_A(0, 0, a2, true);
;             PG8_WAIT_V(8); PG8_WAIT_L(0); PG8_BAR; PG8_MMA(1, 0, At, B0); PG8_MMA(1, 1, At, B1); PG8_BAR; PG8_SCHED;
;             PG8_LDB(B0, 1, 0); PG8_LDB(B1, 1, 1); PG8_SCHED; PG8_LDA(At, 1, 0); PG8_STAGE_A(0, 1, a2, true);
;             PG8_WAIT_V(8); PG8_WAIT_L(0); PG8_BAR; PG8_MMA(0, 0, At, B0); PG8_MMA(0, 1, At, B1); PG8_BAR; PG8_SCHED;
;             PG8_LDA(At, 1, 1); PG8_STAGE(PG8_SB(1, 0), b3, voffB); PG8_STAGE(PG8_SB(1, 1), b3 + hstep, voffB); PG8_STAGE_A(1, 0, a3, true);
;             PG8_WAIT_V(8); PG8_WAIT_L(0); PG8_BAR; PG8_MMA(1, 0, At, B0); PG8_MMA(1, 1, At, B1); PG8_BAR; PG8_SCHED;
	s_setprio 3
	s_waitcnt lgkmcnt(0)
	v_mfma_f32_16x16x32_bf16 v[126:129], v[130:133], v[200:203], v[126:129]
	v_mfma_f32_16x16x32_bf16 v[122:125], v[138:141], v[200:203], v[122:125]
	v_mfma_f32_16x16x32_bf16 v[110:113], v[130:133], v[208:211], v[110:113]
	v_mfma_f32_16x16x32_bf16 v[106:109], v[138:141], v[208:211], v[106:109]
	v_mfma_f32_16x16x32_bf16 v[94:97], v[130:133], v[216:219], v[94:97]
	v_mfma_f32_16x16x32_bf16 v[90:93], v[138:141], v[216:219], v[90:93]
	v_mfma_f32_16x16x32_bf16 v[78:81], v[130:133], v[224:227], v[78:81]
	v_mfma_f32_16x16x32_bf16 v[74:77], v[138:141], v[224:227], v[74:77]
	v_mfma_f32_16x16x32_bf16 v[126:129], v[134:137], v[204:207], v[126:129]
	v_mfma_f32_16x16x32_bf16 v[122:125], v[160:163], v[204:207], v[122:125]
	v_mfma_f32_16x16x32_bf16 v[110:113], v[134:137], v[212:215], v[110:113]
	v_mfma_f32_16x16x32_bf16 v[106:109], v[160:163], v[212:215], v[106:109]
	v_mfma_f32_16x16x32_bf16 v[94:97], v[134:137], v[220:223], v[94:97]
	v_mfma_f32_16x16x32_bf16 v[90:93], v[160:163], v[220:223], v[90:93]
	v_mfma_f32_16x16x32_bf16 v[78:81], v[134:137], v[230:233], v[78:81]
	v_mfma_f32_16x16x32_bf16 v[74:77], v[160:163], v[230:233], v[74:77]
	s_setprio 0
	s_setprio 3
	v_mfma_f32_16x16x32_bf16 v[118:121], v[164:167], v[200:203], v[118:121]
	v_mfma_f32_16x16x32_bf16 v[114:117], v[192:195], v[200:203], v[114:117]
	v_mfma_f32_16x16x32_bf16 v[102:105], v[164:167], v[208:211], v[102:105]
	v_mfma_f32_16x16x32_bf16 v[98:101], v[192:195], v[208:211], v[98:101]
	v_mfma_f32_16x16x32_bf16 v[86:89], v[164:167], v[216:219], v[86:89]
	v_mfma_f32_16x16x32_bf16 v[82:85], v[192:195], v[216:219], v[82:85]
	v_mfma_f32_16x16x32_bf16 v[70:73], v[164:167], v[224:227], v[70:73]
	v_mfma_f32_16x16x32_bf16 v[66:69], v[192:195], v[224:227], v[66:69]
	v_mfma_f32_16x16x32_bf16 v[118:121], v[182:185], v[204:207], v[118:121]
	v_mfma_f32_16x16x32_bf16 v[114:117], v[196:199], v[204:207], v[114:117]
	v_mfma_f32_16x16x32_bf16 v[102:105], v[182:185], v[212:215], v[102:105]
	v_mfma_f32_16x16x32_bf16 v[98:101], v[196:199], v[212:215], v[98:101]
	v_mfma_f32_16x16x32_bf16 v[86:89], v[182:185], v[220:223], v[86:89]
	v_mfma_f32_16x16x32_bf16 v[82:85], v[196:199], v[220:223], v[82:85]
	v_mfma_f32_16x16x32_bf16 v[70:73], v[182:185], v[230:233], v[70:73]
	v_mfma_f32_16x16x32_bf16 v[66:69], v[196:199], v[230:233], v[66:69]
	s_setprio 0
	s_barrier
	s_add_i32 s61, s39, s2
	v_lshl_add_u64 v[168:169], s[24:25], 0, v[146:147]
	s_mov_b32 m0, s61
	ds_read_b128 v[200:203], v189 offset:16384
	ds_read_b128 v[204:207], v189 offset:17408
	ds_read_b128 v[208:211], v189 offset:18432
	ds_read_b128 v[212:215], v189 offset:19456
	ds_read_b128 v[216:219], v189 offset:20480
	ds_read_b128 v[220:223], v189 offset:21504
	ds_read_b128 v[224:227], v189 offset:22528
	ds_read_b128 v[230:233], v189 offset:23552
	global_load_lds_dwordx4 v[168:169], off
	s_add_i32 m0, s61, 0x2000
	s_add_u32 s62, s24, 0x40000
	v_lshl_add_u64 v[172:173], s[24:25], 0, v[142:143]
	s_addc_u32 s63, s25, 0
	s_add_i32 s61, s48, s2
	global_load_lds_dwordx4 v[172:173], off
	v_lshl_add_u64 v[176:177], s[62:63], 0, v[146:147]
	s_mov_b32 m0, s61
	v_lshl_add_u64 v[234:235], s[26:27], 0, v[144:145]
	global_load_lds_dwordx4 v[176:177], off
	v_lshl_add_u64 v[176:177], s[62:63], 0, v[142:143]
	s_add_i32 m0, s61, 0x2000
	s_nop 0
	global_load_lds_dwordx4 v[176:177], off
	v_lshl_add_u64 v[176:177], s[26:27], 0, v[148:149]
	s_mov_b32 m0, s29
	s_nop 0
	global_load_lds_dwordx4 v[176:177], off
	s_mov_b32 m0, s30
	s_nop 0
	global_load_lds_dwordx4 v[234:235], off
	s_waitcnt vmcnt(8)
	s_waitcnt lgkmcnt(0)
	s_barrier
	s_setprio 3
	s_waitcnt lgkmcnt(0)
	v_mfma_f32_16x16x32_bf16 v[62:65], v[130:133], v[200:203], v[62:65]
	v_mfma_f32_16x16x32_bf16 v[58:61], v[138:141], v[200:203], v[58:61]
	v_mfma_f32_16x16x32_bf16 v[46:49], v[130:133], v[208:211], v[46:49]
	v_mfma_f32_16x16x32_bf16 v[42:45], v[138:141], v[208:211], v[42:45]
	v_mfma_f32_16x16x32_bf16 v[30:33], v[130:133], v[216:219], v[30:33]
	v_mfma_f32_16x16x32_bf16 v[26:29], v[138:141], v[216:219], v[26:29]
	v_mfma_f32_16x16x32_bf16 v[14:17], v[130:133], v[224:227], v[14:17]
	v_mfma_f32_16x16x32_bf16 v[10:13], v[138:141], v[224:227], v[10:13]
	v_mfma_f32_16x16x32_bf16 v[62:65], v[134:137], v[204:207], v[62:65]
	v_mfma_f32_16x16x32_bf16 v[58:61], v[160:163], v[204:207], v[58:61]
	v_mfma_f32_16x16x32_bf16 v[46:49], v[134:137], v[212:215], v[46:49]
	v_mfma_f32_16x16x32_bf16 v[42:45], v[160:163], v[212:215], v[42:45]
	v_mfma_f32_16x16x32_bf16 v[30:33], v[134:137], v[220:223], v[30:33]
	v_mfma_f32_16x16x32_bf16 v[26:29], v[160:163], v[220:223], v[26:29]
	v_mfma_f32_16x16x32_bf16 v[14:17], v[134:137], v[230:233], v[14:17]
	v_mfma_f32_16x16x32_bf16 v[10:13], v[160:163], v[230:233], v[10:13]
	s_setprio 0
	s_setprio 3
	v_mfma_f32_16x16x32_bf16 v[54:57], v[164:167], v[200:203], v[54:57]
	v_mfma_f32_16x16x32_bf16 v[50:53], v[192:195], v[200:203], v[50:53]
	v_mfma_f32_16x16x32_bf16 v[38:41], v[164:167], v[208:211], v[38:41]
	v_mfma_f32_16x16x32_bf16 v[34:37], v[192:195], v[208:211], v[34:37]
	v_mfma_f32_16x16x32_bf16 v[22:25], v[164:167], v[216:219], v[22:25]
	v_mfma_f32_16x16x32_bf16 v[18:21], v[192:195], v[216:219], v[18:21]
	v_mfma_f32_16x16x32_bf16 v[6:9], v[164:167], v[224:227], v[6:9]
	v_mfma_f32_16x16x32_bf16 v[2:5], v[192:195], v[224:227], v[2:5]
	v_mfma_f32_16x16x32_bf16 v[54:57], v[182:185], v[204:207], v[54:57]
	v_mfma_f32_16x16x32_bf16 v[50:53], v[196:199], v[204:207], v[50:53]
	v_mfma_f32_16x16x32_bf16 v[38:41], v[182:185], v[212:215], v[38:41]
	v_mfma_f32_16x16x32_bf16 v[34:37], v[196:199], v[212:215], v[34:37]
	v_mfma_f32_16x16x32_bf16 v[22:25], v[182:185], v[220:223], v[22:25]
	v_mfma_f32_16x16x32_bf16 v[18:21], v[196:199], v[220:223], v[18:21]
	v_mfma_f32_16x16x32_bf16 v[6:9], v[182:185], v[230:233], v[6:9]
	v_mfma_f32_16x16x32_bf16 v[2:5], v[196:199], v[230:233], v[2:5]
	s_setprio 0
	s_barrier
; #define PG8_STAGE_A(b, h, ptr, NX) do { if constexpr (Sched::GATHER) { unsigned gs_[2]; gs_[0] = ((NX) && last_) ? gN[h][0] : gA[h][0]; gs_[1] = ((NX) && last_) ? gN[h][1] : gA[h][1]; PG8_STAGE(PG8_SA(b, h), ptr, gs_); } \
;         else PG8_STAGE(PG8_SA(b, h), (ptr) + ((h) ? hstep : (size_t)0), voffA); } while (0)
; #define PG8_STAGE(bufoff, gbase, voff) do { _Pragma("unroll") for (int _i = 0; _i < 2; ++_i) \
;         __builtin_amdgcn_global_load_lds((const unsigned*)((const char*)(gbase) + (voff)[_i]), (PG8_LAS unsigned*)(lds + (bufoff) + ldsw + _i * 8192), 16, 0, 0); } while (0)
; #define PG8_LDA(dst, b, h) do { _Pragma("unroll") for (int m = 0; m < 4; ++m) _Pragma("unroll") for (int k = 0; k < 2; ++k) dst[m][k] = *(const PG8_LAS bf16x8*)(lds + PG8_SA(b, h) + aoff + m * 2048 + k * 1024); } while (0)
; #define PG8_LDB(dst, b, h) do { _Pragma("unroll") for (int n = 0; n < 2; ++n) _Pragma("unroll") for (int k = 0; k < 2; ++k) dst[n][k] = *(const PG8_LAS bf16x8*)(lds + PG8_SB(b, h) + boff + n * 2048 + k * 1024); } while (0)
; #define PG8_WAIT_V(n) asm volatile("s_waitcnt vmcnt(" #n ")" ::: "memory")
; #define PG8_BAR __builtin_amdgcn_s_barrier()
; template <class Epi, class Sched, bool ALIGN_EPI = false, bool SP2 = false>
; __device__ __forceinline__ void gemm_phase(PG8_LAS unsigned char* lds, const Gemm g, const Sched& S, const Epi& E, const bool skip_epi = false) {
;     ...
;             PG8_LDB(B0, 0, 0); PG8_LDB(B1, 0, 1); PG8_SCHED; PG8_LDA(At, 0, 0); PG8_STAGE_A(1, 1, a1, false);
;             PG8_WAIT_V(8); PG8_WAIT_L(0); PG8_BAR; PG8_MMA(0, 0, At, B0); PG8_MMA(0, 1, At, B1); PG8_BAR; PG8_SCHED;
;             PG8_LDA(At, 0, 1); PG8_STAGE(PG8_SB(0, 0), b2, voffB); PG8_STAGE(PG8_SB(0, 1), b2 + hstep, voffB); PG8_STAGE_A(0, 0, a2, true);
;             PG8_WAIT_V(8); PG8_WAIT_L(0); PG8_BAR; PG8_MMA(1, 0, At, B0); PG8_MMA(1, 1, At, B1); PG8_BAR; PG8_SCHED;
;             PG8_LDB(B0, 1, 0); PG8_LDB(B1, 1, 1); PG8_SCHED; PG8_LDA(At, 1, 0); PG8_STAGE_A(0, 1, a2, true);
;             PG8_WAIT_V(8); PG8_WAIT_L(0); PG8_BAR; PG8_MMA(0, 0, At, B0); PG8_MMA(0, 1, At, B1); PG8_BAR; PG8_SCHED;
;             PG8_LDA(At, 1, 1); PG8_STAGE(PG8_SB(1, 0), b3, voffB); PG8_STAGE(PG8_SB(1, 1), b3 + hstep, voffB); PG8_STAGE_A(1, 0, a3, true);
;             PG8_WAIT_V(8); PG8_WAIT_L(0); PG8_BAR; PG8_MMA(1, 0, At, B0); PG8_MMA(1, 1, At, B1); PG8_BAR; PG8_SCHED;
	s_add_i32 s61, 0, 0x18000
	s_add_i32 s62, 0, 0x1c000
	v_add_u32_e32 v160, s61, v1
	v_add_u32_e32 v170, s62, v1
	ds_read_b128 v[130:133], v160
	ds_read_b128 v[134:137], v160 offset:1024
	ds_read_b128 v[138:141], v160 offset:2048
	ds_read_b128 v[160:163], v160 offset:3072
	ds_read_b128 v[164:167], v170
	ds_read_b128 v[182:185], v170 offset:1024
	ds_read_b128 v[192:195], v170 offset:2048
	ds_read_b128 v[196:199], v170 offset:3072
	s_add_u32 s26, s26, 0x40000
	s_addc_u32 s27, s27, 0
	s_mov_b32 m0, s31
	v_lshl_add_u64 v[236:237], s[26:27], 0, v[148:149]
	ds_read_b128 v[200:203], v189 offset:32768
	ds_read_b128 v[204:207], v189 offset:33792
	ds_read_b128 v[208:211], v189 offset:34816
	ds_read_b128 v[212:215], v189 offset:35840
	ds_read_b128 v[216:219], v189 offset:36864
	ds_read_b128 v[220:223], v189 offset:37888
	ds_read_b128 v[224:227], v189 offset:38912
	ds_read_b128 v[230:233], v189 offset:39936
	global_load_lds_dwordx4 v[236:237], off
	v_lshl_add_u64 v[236:237], s[26:27], 0, v[144:145]
	s_mov_b32 m0, s34
	s_nop 0
	global_load_lds_dwordx4 v[236:237], off
	s_waitcnt vmcnt(8)
	s_waitcnt lgkmcnt(0)
	s_barrier
	s_setprio 3
	s_waitcnt lgkmcnt(0)
	v_mfma_f32_16x16x32_bf16 v[126:129], v[130:133], v[200:203], v[126:129]
	v_mfma_f32_16x16x32_bf16 v[122:125], v[138:141], v[200:203], v[122:125]
	v_mfma_f32_16x16x32_bf16 v[110:113], v[130:133], v[208:211], v[110:113]
	v_mfma_f32_16x16x32_bf16 v[106:109], v[138:141], v[208:211], v[106:109]
	v_mfma_f32_16x16x32_bf16 v[94:97], v[130:133], v[216:219], v[94:97]
	v_mfma_f32_16x16x32_bf16 v[90:93], v[138:141], v[216:219], v[90:93]
	v_mfma_f32_16x16x32_bf16 v[78:81], v[130:133], v[224:227], v[78:81]
	v_mfma_f32_16x16x32_bf16 v[74:77], v[138:141], v[224:227], v[74:77]
	v_mfma_f32_16x16x32_bf16 v[126:129], v[134:137], v[204:207], v[126:129]
	v_mfma_f32_16x16x32_bf16 v[122:125], v[160:163], v[204:207], v[122:125]
	v_mfma_f32_16x16x32_bf16 v[110:113], v[134:137], v[212:215], v[110:113]
	v_mfma_f32_16x16x32_bf16 v[106:109], v[160:163], v[212:215], v[106:109]
	v_mfma_f32_16x16x32_bf16 v[94:97], v[134:137], v[220:223], v[94:97]
	v_mfma_f32_16x16x32_bf16 v[90:93], v[160:163], v[220:223], v[90:93]
	v_mfma_f32_16x16x32_bf16 v[78:81], v[134:137], v[230:233], v[78:81]
	v_mfma_f32_16x16x32_bf16 v[74:77], v[160:163], v[230:233], v[74:77]
	s_setprio 0
	s_setprio 3
	v_mfma_f32_16x16x32_bf16 v[118:121], v[164:167], v[200:203], v[118:121]
	v_mfma_f32_16x16x32_bf16 v[114:117], v[192:195], v[200:203], v[114:117]
	v_mfma_f32_16x16x32_bf16 v[102:105], v[164:167], v[208:211], v[102:105]
	v_mfma_f32_16x16x32_bf16 v[98:101], v[192:195], v[208:211], v[98:101]
	v_mfma_f32_16x16x32_bf16 v[86:89], v[164:167], v[216:219], v[86:89]
	v_mfma_f32_16x16x32_bf16 v[82:85], v[192:195], v[216:219], v[82:85]
	v_mfma_f32_16x16x32_bf16 v[70:73], v[164:167], v[224:227], v[70:73]
	v_mfma_f32_16x16x32_bf16 v[66:69], v[192:195], v[224:227], v[66:69]
	v_mfma_f32_16x16x32_bf16 v[118:121], v[182:185], v[204:207], v[118:121]
	v_mfma_f32_16x16x32_bf16 v[114:117], v[196:199], v[204:207], v[114:117]
	v_mfma_f32_16x16x32_bf16 v[102:105], v[182:185], v[212:215], v[102:105]
	v_mfma_f32_16x16x32_bf16 v[98:101], v[196:199], v[212:215], v[98:101]
	v_mfma_f32_16x16x32_bf16 v[86:89], v[182:185], v[220:223], v[86:89]
	v_mfma_f32_16x16x32_bf16 v[82:85], v[196:199], v[220:223], v[82:85]
	v_mfma_f32_16x16x32_bf16 v[70:73], v[182:185], v[230:233], v[70:73]
	v_mfma_f32_16x16x32_bf16 v[66:69], v[196:199], v[230:233], v[66:69]
	s_setprio 0
	s_barrier
; #define PG8_STAGE_A(b, h, ptr, NX) do { if constexpr (Sched::GATHER) { unsigned gs_[2]; gs_[0] = ((NX) && last_) ? gN[h][0] : gA[h][0]; gs_[1] = ((NX) && last_) ? gN[h][1] : gA[h][1]; PG8_STAGE(PG8_SA(b, h), ptr, gs_); } \
;         else PG8_STAGE(PG8_SA(b, h), (ptr) + ((h) ? hstep : (size_t)0), voffA); } while (0)
; #define PG8_STAGE(bufoff, gbase, voff) do { _Pragma("unroll") for (int _i = 0; _i < 2; ++_i) \
;         __builtin_amdgcn_global_load_lds((const unsigned*)((const char*)(gbase) + (voff)[_i]), (PG8_LAS unsigned*)(lds + (bufoff) + ldsw + _i * 8192), 16, 0, 0); } while (0)
; #define PG8_LDA(dst, b, h) do { _Pragma("unroll") for (int m = 0; m < 4; ++m) _Pragma("unroll") for (int k = 0; k < 2; ++k) dst[m][k] = *(const PG8_LAS bf16x8*)(lds + PG8_SA(b, h) + aoff + m * 2048 + k * 1024); } while (0)
; #define PG8_LDB(dst, b, h) do { _Pragma("unroll") for (int n = 0; n < 2; ++n) _Pragma("unroll") for (int k = 0; k < 2; ++k) dst[n][k] = *(const PG8_LAS bf16x8*)(lds + PG8_SB(b, h) + boff + n * 2048 + k * 1024); } while (0)
; #define PG8_WAIT_V(n) asm volatile("s_waitcnt vmcnt(" #n ")" ::: "memory")
; #define PG8_BAR __builtin_amdgcn_s_barrier()
; template <class Epi, class Sched, bool ALIGN_EPI = false, bool SP2 = false>
; __device__ __forceinline__ void gemm_phase(PG8_LAS unsigned char* lds, const Gemm g, const Sched& S, const Epi& E, const bool skip_epi = false) {
;     ...
;             PG8_LDB(B0, 0, 0); PG8_LDB(B1, 0, 1); PG8_SCHED; PG8_LDA(At, 0, 0); PG8_STAGE_A(1, 1, a1, false);
;             PG8_WAIT_V(8); PG8_WAIT_L(0); PG8_BAR; PG8_MMA(0, 0, At, B0); PG8_MMA(0, 1, At, B1); PG8_BAR; PG8_SCHED;
;             PG8_LDA(At, 0, 1); PG8_STAGE(PG8_SB(0, 0), b2, voffB); PG8_STAGE(PG8_SB(0, 1), b2 + hstep, voffB); PG8_STAGE_A(0, 0, a2, true);
;             PG8_WAIT_V(8); PG8_WAIT_L(0); PG8_BAR; PG8_MMA(1, 0, At, B0); PG8_MMA(1, 1, At, B1); PG8_BAR; PG8_SCHED;
;             PG8_LDB(B0, 1, 0); PG8_LDB(B1, 1, 1); PG8_SCHED; PG8_LDA(At, 1, 0); PG8_STAGE_A(0, 1, a2, true);
;             PG8_WAIT_V(8); PG8_WAIT_L(0); PG8_BAR; PG8_MMA(0, 0, At, B0); PG8_MMA(0, 1, At, B1); PG8_BAR; PG8_SCHED;
;             PG8_LDA(At, 1, 1); PG8_STAGE(PG8_SB(1, 0), b3, voffB); PG8_STAGE(PG8_SB(1, 1), b3 + hstep, voffB); PG8_STAGE_A(1, 0, a3, true);
;             PG8_WAIT_V(8); PG8_WAIT_L(0); PG8_BAR; PG8_MMA(1, 0, At, B0); PG8_MMA(1, 1, At, B1); PG8_BAR; PG8_SCHED;
	s_add_i32 s26, s61, s2
	v_lshl_add_u64 v[168:169], v[168:169], 0, s[8:9]
	s_mov_b32 m0, s26
	ds_read_b128 v[200:203], v189 offset:49152
	ds_read_b128 v[204:207], v189 offset:50176
	ds_read_b128 v[208:211], v189 offset:51200
	ds_read_b128 v[212:215], v189 offset:52224
	ds_read_b128 v[216:219], v189 offset:53248
	ds_read_b128 v[220:223], v189 offset:54272
	ds_read_b128 v[224:227], v189 offset:55296
	ds_read_b128 v[230:233], v189 offset:56320
	global_load_lds_dwordx4 v[168:169], off
	s_add_i32 m0, s26, 0x2000
	s_add_u32 s24, s24, 0x40080
	v_lshl_add_u64 v[168:169], v[172:173], 0, s[8:9]
	s_addc_u32 s25, s25, 0
	s_add_i32 s26, s62, s2
	global_load_lds_dwordx4 v[168:169], off
	v_lshl_add_u64 v[168:169], s[24:25], 0, v[146:147]
	s_mov_b32 m0, s26
	s_nop 0
	global_load_lds_dwordx4 v[168:169], off
	v_lshl_add_u64 v[168:169], s[24:25], 0, v[142:143]
	s_add_i32 m0, s26, 0x2000
	s_nop 0
	global_load_lds_dwordx4 v[168:169], off
	v_lshl_add_u64 v[168:169], v[176:177], 0, s[8:9]
	s_mov_b32 m0, s36
	s_nop 0
	global_load_lds_dwordx4 v[168:169], off
	v_lshl_add_u64 v[168:169], v[234:235], 0, s[8:9]
	s_mov_b32 m0, s37
	s_nop 0
	global_load_lds_dwordx4 v[168:169], off
	s_waitcnt vmcnt(8)
	s_waitcnt lgkmcnt(0)
	s_barrier
	s_setprio 3
	s_waitcnt lgkmcnt(0)
	v_mfma_f32_16x16x32_bf16 v[62:65], v[130:133], v[200:203], v[62:65]
	v_mfma_f32_16x16x32_bf16 v[58:61], v[138:141], v[200:203], v[58:61]
	v_mfma_f32_16x16x32_bf16 v[46:49], v[130:133], v[208:211], v[46:49]
	v_mfma_f32_16x16x32_bf16 v[42:45], v[138:141], v[208:211], v[42:45]
	v_mfma_f32_16x16x32_bf16 v[30:33], v[130:133], v[216:219], v[30:33]
	v_mfma_f32_16x16x32_bf16 v[26:29], v[138:141], v[216:219], v[26:29]
	v_mfma_f32_16x16x32_bf16 v[14:17], v[130:133], v[224:227], v[14:17]
	v_mfma_f32_16x16x32_bf16 v[10:13], v[138:141], v[224:227], v[10:13]
	v_mfma_f32_16x16x32_bf16 v[62:65], v[134:137], v[204:207], v[62:65]
	v_mfma_f32_16x16x32_bf16 v[58:61], v[160:163], v[204:207], v[58:61]
	v_mfma_f32_16x16x32_bf16 v[46:49], v[134:137], v[212:215], v[46:49]
	v_mfma_f32_16x16x32_bf16 v[42:45], v[160:163], v[212:215], v[42:45]
	v_mfma_f32_16x16x32_bf16 v[30:33], v[134:137], v[220:223], v[30:33]
	v_mfma_f32_16x16x32_bf16 v[26:29], v[160:163], v[220:223], v[26:29]
	v_mfma_f32_16x16x32_bf16 v[14:17], v[134:137], v[230:233], v[14:17]
	v_mfma_f32_16x16x32_bf16 v[10:13], v[160:163], v[230:233], v[10:13]
	s_setprio 0
	s_setprio 3
	v_mfma_f32_16x16x32_bf16 v[54:57], v[164:167], v[200:203], v[54:57]
	v_mfma_f32_16x16x32_bf16 v[50:53], v[192:195], v[200:203], v[50:53]
	v_mfma_f32_16x16x32_bf16 v[38:41], v[164:167], v[208:211], v[38:41]
	v_mfma_f32_16x16x32_bf16 v[34:37], v[192:195], v[208:211], v[34:37]
	v_mfma_f32_16x16x32_bf16 v[22:25], v[164:167], v[216:219], v[22:25]
	v_mfma_f32_16x16x32_bf16 v[18:21], v[192:195], v[216:219], v[18:21]
	v_mfma_f32_16x16x32_bf16 v[6:9], v[164:167], v[224:227], v[6:9]
	v_mfma_f32_16x16x32_bf16 v[2:5], v[192:195], v[224:227], v[2:5]
	v_mfma_f32_16x16x32_bf16 v[54:57], v[182:185], v[204:207], v[54:57]
	v_mfma_f32_16x16x32_bf16 v[50:53], v[196:199], v[204:207], v[50:53]
	v_mfma_f32_16x16x32_bf16 v[38:41], v[182:185], v[212:215], v[38:41]
	v_mfma_f32_16x16x32_bf16 v[34:37], v[196:199], v[212:215], v[34:37]
	v_mfma_f32_16x16x32_bf16 v[22:25], v[182:185], v[220:223], v[22:25]
	v_mfma_f32_16x16x32_bf16 v[18:21], v[196:199], v[220:223], v[18:21]
	v_mfma_f32_16x16x32_bf16 v[6:9], v[182:185], v[230:233], v[6:9]
	v_mfma_f32_16x16x32_bf16 v[2:5], v[196:199], v[230:233], v[2:5]
	s_setprio 0
	s_barrier
	s_add_i32 s60, s60, 2
	s_add_u32 s22, s22, 0x100
	s_addc_u32 s23, s23, 0
	s_add_u32 s58, s58, 0x100
	s_addc_u32 s59, s59, 0
	s_cmp_gt_u32 s60, 13
	s_cbranch_scc0 .LBB0_721
	s_and_b64 vcc, exec, s[10:11]
	s_cbranch_vccz .LBB0_724
	s_barrier

; #define PG8_STAGE_A(b, h, ptr, NX) do { if constexpr (Sched::GATHER) { unsigned gs_[2]; gs_[0] = ((NX) && last_) ? gN[h][0] : gA[h][0]; gs_[1] = ((NX) && last_) ? gN[h][1] : gA[h][1]; PG8_STAGE(PG8_SA(b, h), ptr, gs_); } \
;         else PG8_STAGE(PG8_SA(b, h), (ptr) + ((h) ? hstep : (size_t)0), voffA); } while (0)
; #define PG8_WAIT_V(n) asm volatile("s_waitcnt vmcnt(" #n ")" ::: "memory")
; #define PG8_WAIT_L(n) asm volatile("s_waitcnt lgkmcnt(" #n ")" ::: "memory")
; #define PG8_BAR __builtin_amdgcn_s_barrier()
; template <class Epi, class Sched, bool ALIGN_EPI = false, bool SP2 = false>
; __device__ __forceinline__ void gemm_phase(PG8_LAS unsigned char* lds, const Gemm g, const Sched& S, const Epi& E, const bool skip_epi = false) {
;     ...
;         const char* nA = has_next ? (const char*)g.A + (size_t)nxt.pm * pmstepA + nxt.ko : cA; const char* nB = has_next ? (const char*)g.Bt + (size_t)nxt.pn * tstep + nxt.ko : cB;
;         for (int t = 0; t < nt; t += 2) {
;             const bool last = (t == nt - 2); last_ = last && has_next;
;             const char* a1 = cA + (size_t)(t + 1) * kstep;
;             const char* a2 = last ? nA : cA + (size_t)(t + 2) * kstep; const char* b2 = last ? nB : cB + (size_t)(t + 2) * kstep;
;             const char* a3 = a2 + kstep; const char* b3 = b2 + kstep;
;             if (last && has_next) S.a_ready(nxt);
;             if constexpr (SP2) {
;             PG8_LDB(B0, 0, 0); PG8_LDB(B1, 0, 1); PG8_SCHED; PG8_LDA(At, 0, 0); PG8_STAGE_A(1, 1, a1, false);
;             PG8_WAIT_V(8); PG8_WAIT_L(0); PG8_BAR; PG8_MMA(0, 0, At, B0); PG8_MMA(0, 1, At, B1); PG8_BAR; PG8_SCHED;
;             PG8_LDA(At, 0, 1); PG8_STAGE(PG8_SB(0, 0), b2, voffB); PG8_STAGE(PG8_SB(0, 1), b2 + hstep, voffB); PG8_STAGE_A(0, 0, a2, true);
;             PG8_WAIT_V(8); PG8_WAIT_L(0); PG8_BAR; PG8_MMA(1, 0, At, B0); PG8_MMA(1, 1, At, B1); PG8_BAR; PG8_SCHED;
;             PG8_LDB(B0, 1, 0); PG8_LDB(B1, 1, 1); PG8_SCHED; PG8_LDA(At, 1, 0); PG8_STAGE_A(0, 1, a2, true);
;             PG8_WAIT_V(8); PG8_WAIT_L(0); PG8_BAR; PG8_MMA(0, 0, At, B0); PG8_MMA(0, 1, At, B1); PG8_BAR; PG8_SCHED;
;             PG8_LDA(At, 1, 1); PG8_STAGE(PG8_SB(1, 0), b3, voffB); PG8_STAGE(PG8_SB(1, 1), b3 + hstep, voffB); PG8_STAGE_A(1, 0, a3, true);
;             PG8_WAIT_V(8); PG8_WAIT_L(0); PG8_BAR; PG8_MMA(1, 0, At, B0); PG8_MMA(1, 1, At, B1); PG8_BAR; PG8_SCHED;
.LBB0_856:
	s_add_u32 s55, s22, 0x100
	s_addc_u32 s56, s23, 0
	s_mov_b32 s57, -2
	s_waitcnt vmcnt(0)
	s_waitcnt lgkmcnt(0)
	ds_read_b128 v[98:101], v234
	ds_read_b128 v[110:113], v234 offset:1024
	ds_read_b128 v[122:125], v234 offset:2048
	ds_read_b128 v[126:129], v234 offset:3072
	ds_read_b128 v[138:141], v235
	ds_read_b128 v[142:145], v235 offset:1024
	ds_read_b128 v[146:149], v235 offset:2048
	ds_read_b128 v[150:153], v235 offset:3072
	s_add_u32 s22, s20, 0x100
	s_addc_u32 s23, s21, 0
	s_cmp_eq_u32 s57, 40
	s_cselect_b32 s27, s9, s23
	s_cselect_b32 s26, s8, s22
	s_cselect_b32 s25, s19, s56
	s_cselect_b32 s24, s18, s55
	v_lshl_add_u64 v[210:211], s[20:21], 0, v[198:199]
	s_add_i32 m0, s3, 0xc000
	ds_read_b128 v[154:157], v236
	ds_read_b128 v[166:169], v236 offset:1024
	ds_read_b128 v[170:173], v236 offset:2048
	ds_read_b128 v[174:177], v236 offset:3072
	ds_read_b128 v[178:181], v236 offset:4096
	ds_read_b128 v[182:185], v236 offset:5120
	ds_read_b128 v[186:189], v236 offset:6144
	ds_read_b128 v[206:209], v236 offset:7168
	global_load_lds_dwordx4 v[210:211], off
	v_lshl_add_u64 v[210:211], s[20:21], 0, v[200:201]
	s_add_i32 m0, s3, 0xe000
	s_nop 0
	global_load_lds_dwordx4 v[210:211], off
	s_waitcnt vmcnt(8)
	s_waitcnt lgkmcnt(0)
	s_barrier
	s_setprio 3
	s_waitcnt lgkmcnt(0)
	v_mfma_f32_16x16x32_bf16 v[162:165], v[98:101], v[154:157], 0
	v_mfma_f32_16x16x32_bf16 v[158:161], v[122:125], v[154:157], 0
	v_mfma_f32_16x16x32_bf16 v[118:121], v[98:101], v[170:173], 0
	v_mfma_f32_16x16x32_bf16 v[114:117], v[122:125], v[170:173], 0
	v_mfma_f32_16x16x32_bf16 v[94:97], v[98:101], v[178:181], 0
	v_mfma_f32_16x16x32_bf16 v[90:93], v[122:125], v[178:181], 0
	v_mfma_f32_16x16x32_bf16 v[78:81], v[98:101], v[186:189], 0
	v_mfma_f32_16x16x32_bf16 v[74:77], v[122:125], v[186:189], 0
	v_mfma_f32_16x16x32_bf16 v[162:165], v[110:113], v[166:169], v[162:165]
	v_mfma_f32_16x16x32_bf16 v[158:161], v[126:129], v[166:169], v[158:161]
	v_mfma_f32_16x16x32_bf16 v[118:121], v[110:113], v[174:177], v[118:121]
	v_mfma_f32_16x16x32_bf16 v[114:117], v[126:129], v[174:177], v[114:117]
	v_mfma_f32_16x16x32_bf16 v[94:97], v[110:113], v[182:185], v[94:97]
	v_mfma_f32_16x16x32_bf16 v[90:93], v[126:129], v[182:185], v[90:93]
	v_mfma_f32_16x16x32_bf16 v[78:81], v[110:113], v[206:209], v[78:81]
	v_mfma_f32_16x16x32_bf16 v[74:77], v[126:129], v[206:209], v[74:77]
	s_setprio 0
	s_setprio 3
	v_mfma_f32_16x16x32_bf16 v[134:137], v[138:141], v[154:157], 0
	v_mfma_f32_16x16x32_bf16 v[130:133], v[146:149], v[154:157], 0
	v_mfma_f32_16x16x32_bf16 v[106:109], v[138:141], v[170:173], 0
	v_mfma_f32_16x16x32_bf16 v[102:105], v[146:149], v[170:173], 0
	v_mfma_f32_16x16x32_bf16 v[86:89], v[138:141], v[178:181], 0
	v_mfma_f32_16x16x32_bf16 v[82:85], v[146:149], v[178:181], 0
	v_mfma_f32_16x16x32_bf16 v[70:73], v[138:141], v[186:189], 0
	v_mfma_f32_16x16x32_bf16 v[66:69], v[146:149], v[186:189], 0
	v_mfma_f32_16x16x32_bf16 v[134:137], v[142:145], v[166:169], v[134:137]
	v_mfma_f32_16x16x32_bf16 v[130:133], v[150:153], v[166:169], v[130:133]
	v_mfma_f32_16x16x32_bf16 v[106:109], v[142:145], v[174:177], v[106:109]
	v_mfma_f32_16x16x32_bf16 v[102:105], v[150:153], v[174:177], v[102:105]
	v_mfma_f32_16x16x32_bf16 v[86:89], v[142:145], v[182:185], v[86:89]
	v_mfma_f32_16x16x32_bf16 v[82:85], v[150:153], v[182:185], v[82:85]
	v_mfma_f32_16x16x32_bf16 v[70:73], v[142:145], v[206:209], v[70:73]
	v_mfma_f32_16x16x32_bf16 v[66:69], v[150:153], v[206:209], v[66:69]
	s_setprio 0
	s_barrier
	s_add_i32 s20, s39, s2
	v_lshl_add_u64 v[210:211], s[24:25], 0, v[192:193]
	s_mov_b32 m0, s20
	ds_read_b128 v[154:157], v236 offset:16384
	ds_read_b128 v[166:169], v236 offset:17408
	ds_read_b128 v[170:173], v236 offset:18432
	ds_read_b128 v[174:177], v236 offset:19456
	ds_read_b128 v[178:181], v236 offset:20480
	ds_read_b128 v[182:185], v236 offset:21504
	ds_read_b128 v[186:189], v236 offset:22528
	ds_read_b128 v[206:209], v236 offset:23552
	global_load_lds_dwordx4 v[210:211], off
	s_add_i32 m0, s20, 0x2000
	s_add_u32 s20, s24, 0xb0000
	v_lshl_add_u64 v[212:213], s[24:25], 0, v[196:197]
	s_addc_u32 s21, s25, 0
	s_add_i32 s58, s48, s2
	global_load_lds_dwordx4 v[212:213], off
	v_lshl_add_u64 v[214:215], s[20:21], 0, v[192:193]
	s_mov_b32 m0, s58
	v_lshl_add_u64 v[216:217], s[26:27], 0, v[194:195]
	global_load_lds_dwordx4 v[214:215], off
	v_lshl_add_u64 v[214:215], s[20:21], 0, v[196:197]
	s_add_i32 m0, s58, 0x2000
	s_nop 0
	global_load_lds_dwordx4 v[214:215], off
	v_lshl_add_u64 v[214:215], s[26:27], 0, v[190:191]
	s_mov_b32 m0, s3
	s_nop 0
	global_load_lds_dwordx4 v[214:215], off
	s_mov_b32 m0, s28
	s_nop 0
	global_load_lds_dwordx4 v[216:217], off
	s_waitcnt vmcnt(8)
	s_waitcnt lgkmcnt(0)
	s_barrier
; #define PG8_STAGE_A(b, h, ptr, NX) do { if constexpr (Sched::GATHER) { unsigned gs_[2]; gs_[0] = ((NX) && last_) ? gN[h][0] : gA[h][0]; gs_[1] = ((NX) && last_) ? gN[h][1] : gA[h][1]; PG8_STAGE(PG8_SA(b, h), ptr, gs_); } \
;         else PG8_STAGE(PG8_SA(b, h), (ptr) + ((h) ? hstep : (size_t)0), voffA); } while (0)
; #define PG8_STAGE(bufoff, gbase, voff) do { _Pragma("unroll") for (int _i = 0; _i < 2; ++_i) \
;         __builtin_amdgcn_global_load_lds((const unsigned*)((const char*)(gbase) + (voff)[_i]), (PG8_LAS unsigned*)(lds + (bufoff) + ldsw + _i * 8192), 16, 0, 0); } while (0)
; #define PG8_LDA(dst, b, h) do { _Pragma("unroll") for (int m = 0; m < 4; ++m) _Pragma("unroll") for (int k = 0; k < 2; ++k) dst[m][k] = *(const PG8_LAS bf16x8*)(lds + PG8_SA(b, h) + aoff + m * 2048 + k * 1024); } while (0)
; #define PG8_LDB(dst, b, h) do { _Pragma("unroll") for (int n = 0; n < 2; ++n) _Pragma("unroll") for (int k = 0; k < 2; ++k) dst[n][k] = *(const PG8_LAS bf16x8*)(lds + PG8_SB(b, h) + boff + n * 2048 + k * 1024); } while (0)
; #define PG8_WAIT_V(n) asm volatile("s_waitcnt vmcnt(" #n ")" ::: "memory")
; #define PG8_BAR __builtin_amdgcn_s_barrier()
; template <class Epi, class Sched, bool ALIGN_EPI = false, bool SP2 = false>
; __device__ __forceinline__ void gemm_phase(PG8_LAS unsigned char* lds, const Gemm g, const Sched& S, const Epi& E, const bool skip_epi = false) {
;     ...
;             PG8_LDB(B0, 0, 0); PG8_LDB(B1, 0, 1); PG8_SCHED; PG8_LDA(At, 0, 0); PG8_STAGE_A(1, 1, a1, false);
;             PG8_WAIT_V(8); PG8_WAIT_L(0); PG8_BAR; PG8_MMA(0, 0, At, B0); PG8_MMA(0, 1, At, B1); PG8_BAR; PG8_SCHED;
;             PG8_LDA(At, 0, 1); PG8_STAGE(PG8_SB(0, 0), b2, voffB); PG8_STAGE(PG8_SB(0, 1), b2 + hstep, voffB); PG8_STAGE_A(0, 0, a2, true);
;             PG8_WAIT_V(8); PG8_WAIT_L(0); PG8_BAR; PG8_MMA(1, 0, At, B0); PG8_MMA(1, 1, At, B1); PG8_BAR; PG8_SCHED;
;             PG8_LDB(B0, 1, 0); PG8_LDB(B1, 1, 1); PG8_SCHED; PG8_LDA(At, 1, 0); PG8_STAGE_A(0, 1, a2, true);
;             PG8_WAIT_V(8); PG8_WAIT_L(0); PG8_BAR; PG8_MMA(0, 0, At, B0); PG8_MMA(0, 1, At, B1); PG8_BAR; PG8_SCHED;
;             PG8_LDA(At, 1, 1); PG8_STAGE(PG8_SB(1, 0), b3, voffB); PG8_STAGE(PG8_SB(1, 1), b3 + hstep, voffB); PG8_STAGE_A(1, 0, a3, true);
;             PG8_WAIT_V(8); PG8_WAIT_L(0); PG8_BAR; PG8_MMA(1, 0, At, B0); PG8_MMA(1, 1, At, B1); PG8_BAR; PG8_SCHED;
	s_setprio 3
	s_waitcnt lgkmcnt(0)
	v_mfma_f32_16x16x32_bf16 v[62:65], v[98:101], v[154:157], 0
	v_mfma_f32_16x16x32_bf16 v[58:61], v[122:125], v[154:157], 0
	v_mfma_f32_16x16x32_bf16 v[46:49], v[98:101], v[170:173], 0
	v_mfma_f32_16x16x32_bf16 v[42:45], v[122:125], v[170:173], 0
	v_mfma_f32_16x16x32_bf16 v[30:33], v[98:101], v[178:181], 0
	v_mfma_f32_16x16x32_bf16 v[26:29], v[122:125], v[178:181], 0
	v_mfma_f32_16x16x32_bf16 v[14:17], v[98:101], v[186:189], 0
	v_mfma_f32_16x16x32_bf16 v[10:13], v[122:125], v[186:189], 0
	v_mfma_f32_16x16x32_bf16 v[62:65], v[110:113], v[166:169], v[62:65]
	v_mfma_f32_16x16x32_bf16 v[58:61], v[126:129], v[166:169], v[58:61]
	v_mfma_f32_16x16x32_bf16 v[46:49], v[110:113], v[174:177], v[46:49]
	v_mfma_f32_16x16x32_bf16 v[42:45], v[126:129], v[174:177], v[42:45]
	v_mfma_f32_16x16x32_bf16 v[30:33], v[110:113], v[182:185], v[30:33]
	v_mfma_f32_16x16x32_bf16 v[26:29], v[126:129], v[182:185], v[26:29]
	v_mfma_f32_16x16x32_bf16 v[14:17], v[110:113], v[206:209], v[14:17]
	v_mfma_f32_16x16x32_bf16 v[10:13], v[126:129], v[206:209], v[10:13]
	s_setprio 0
	s_setprio 3
	v_mfma_f32_16x16x32_bf16 v[54:57], v[138:141], v[154:157], 0
	v_mfma_f32_16x16x32_bf16 v[50:53], v[146:149], v[154:157], 0
	v_mfma_f32_16x16x32_bf16 v[38:41], v[138:141], v[170:173], 0
	v_mfma_f32_16x16x32_bf16 v[34:37], v[146:149], v[170:173], 0
	v_mfma_f32_16x16x32_bf16 v[22:25], v[138:141], v[178:181], 0
	v_mfma_f32_16x16x32_bf16 v[18:21], v[146:149], v[178:181], 0
	v_mfma_f32_16x16x32_bf16 v[6:9], v[138:141], v[186:189], 0
	v_mfma_f32_16x16x32_bf16 v[2:5], v[146:149], v[186:189], 0
	v_mfma_f32_16x16x32_bf16 v[54:57], v[142:145], v[166:169], v[54:57]
	v_mfma_f32_16x16x32_bf16 v[50:53], v[150:153], v[166:169], v[50:53]
	v_mfma_f32_16x16x32_bf16 v[38:41], v[142:145], v[174:177], v[38:41]
	v_mfma_f32_16x16x32_bf16 v[34:37], v[150:153], v[174:177], v[34:37]
	v_mfma_f32_16x16x32_bf16 v[22:25], v[142:145], v[182:185], v[22:25]
	v_mfma_f32_16x16x32_bf16 v[18:21], v[150:153], v[182:185], v[18:21]
	v_mfma_f32_16x16x32_bf16 v[6:9], v[142:145], v[206:209], v[6:9]
	v_mfma_f32_16x16x32_bf16 v[2:5], v[150:153], v[206:209], v[2:5]
	s_setprio 0
	s_barrier
	s_add_i32 s58, 0, 0x18000
	s_add_i32 s59, 0, 0x1c000
	v_add_u32_e32 v126, s58, v229
	v_add_u32_e32 v150, s59, v229
	ds_read_b128 v[98:101], v126
	ds_read_b128 v[110:113], v126 offset:1024
	ds_read_b128 v[122:125], v126 offset:2048
	ds_read_b128 v[126:129], v126 offset:3072
	ds_read_b128 v[138:141], v150
	ds_read_b128 v[142:145], v150 offset:1024
	ds_read_b128 v[146:149], v150 offset:2048
	ds_read_b128 v[150:153], v150 offset:3072
	s_add_u32 s20, s26, 0xb0000
	s_addc_u32 s21, s27, 0
	s_mov_b32 m0, s29
	v_lshl_add_u64 v[218:219], s[20:21], 0, v[190:191]
	ds_read_b128 v[154:157], v236 offset:32768
	ds_read_b128 v[166:169], v236 offset:33792
	ds_read_b128 v[170:173], v236 offset:34816
	ds_read_b128 v[174:177], v236 offset:35840
	ds_read_b128 v[178:181], v236 offset:36864
	ds_read_b128 v[182:185], v236 offset:37888
	ds_read_b128 v[186:189], v236 offset:38912
	ds_read_b128 v[206:209], v236 offset:39936
	global_load_lds_dwordx4 v[218:219], off
	v_lshl_add_u64 v[218:219], s[20:21], 0, v[194:195]
	s_mov_b32 m0, s30
	s_nop 0
	global_load_lds_dwordx4 v[218:219], off
	s_waitcnt vmcnt(8)
	s_waitcnt lgkmcnt(0)
	s_barrier
	s_setprio 3
	s_waitcnt lgkmcnt(0)
	v_mfma_f32_16x16x32_bf16 v[162:165], v[98:101], v[154:157], v[162:165]
	v_mfma_f32_16x16x32_bf16 v[158:161], v[122:125], v[154:157], v[158:161]
	v_mfma_f32_16x16x32_bf16 v[118:121], v[98:101], v[170:173], v[118:121]
	v_mfma_f32_16x16x32_bf16 v[114:117], v[122:125], v[170:173], v[114:117]
	v_mfma_f32_16x16x32_bf16 v[94:97], v[98:101], v[178:181], v[94:97]
	v_mfma_f32_16x16x32_bf16 v[90:93], v[122:125], v[178:181], v[90:93]
	v_mfma_f32_16x16x32_bf16 v[78:81], v[98:101], v[186:189], v[78:81]
	v_mfma_f32_16x16x32_bf16 v[74:77], v[122:125], v[186:189], v[74:77]
	v_mfma_f32_16x16x32_bf16 v[162:165], v[110:113], v[166:169], v[162:165]
	v_mfma_f32_16x16x32_bf16 v[158:161], v[126:129], v[166:169], v[158:161]
	v_mfma_f32_16x16x32_bf16 v[118:121], v[110:113], v[174:177], v[118:121]
	v_mfma_f32_16x16x32_bf16 v[114:117], v[126:129], v[174:177], v[114:117]
	v_mfma_f32_16x16x32_bf16 v[94:97], v[110:113], v[182:185], v[94:97]
	v_mfma_f32_16x16x32_bf16 v[90:93], v[126:129], v[182:185], v[90:93]
	v_mfma_f32_16x16x32_bf16 v[78:81], v[110:113], v[206:209], v[78:81]
	v_mfma_f32_16x16x32_bf16 v[74:77], v[126:129], v[206:209], v[74:77]
	s_setprio 0
	s_setprio 3
	v_mfma_f32_16x16x32_bf16 v[134:137], v[138:141], v[154:157], v[134:137]
	v_mfma_f32_16x16x32_bf16 v[130:133], v[146:149], v[154:157], v[130:133]
	v_mfma_f32_16x16x32_bf16 v[106:109], v[138:141], v[170:173], v[106:109]
	v_mfma_f32_16x16x32_bf16 v[102:105], v[146:149], v[170:173], v[102:105]
	v_mfma_f32_16x16x32_bf16 v[86:89], v[138:141], v[178:181], v[86:89]
	v_mfma_f32_16x16x32_bf16 v[82:85], v[146:149], v[178:181], v[82:85]
	v_mfma_f32_16x16x32_bf16 v[70:73], v[138:141], v[186:189], v[70:73]
	v_mfma_f32_16x16x32_bf16 v[66:69], v[146:149], v[186:189], v[66:69]
	v_mfma_f32_16x16x32_bf16 v[134:137], v[142:145], v[166:169], v[134:137]
	v_mfma_f32_16x16x32_bf16 v[130:133], v[150:153], v[166:169], v[130:133]
	v_mfma_f32_16x16x32_bf16 v[106:109], v[142:145], v[174:177], v[106:109]
	v_mfma_f32_16x16x32_bf16 v[102:105], v[150:153], v[174:177], v[102:105]
	v_mfma_f32_16x16x32_bf16 v[86:89], v[142:145], v[182:185], v[86:89]
	v_mfma_f32_16x16x32_bf16 v[82:85], v[150:153], v[182:185], v[82:85]
	v_mfma_f32_16x16x32_bf16 v[70:73], v[142:145], v[206:209], v[70:73]
	v_mfma_f32_16x16x32_bf16 v[66:69], v[150:153], v[206:209], v[66:69]
	s_setprio 0
	s_barrier
; #define PG8_STAGE_A(b, h, ptr, NX) do { if constexpr (Sched::GATHER) { unsigned gs_[2]; gs_[0] = ((NX) && last_) ? gN[h][0] : gA[h][0]; gs_[1] = ((NX) && last_) ? gN[h][1] : gA[h][1]; PG8_STAGE(PG8_SA(b, h), ptr, gs_); } \
;         else PG8_STAGE(PG8_SA(b, h), (ptr) + ((h) ? hstep : (size_t)0), voffA); } while (0)
; #define PG8_STAGE(bufoff, gbase, voff) do { _Pragma("unroll") for (int _i = 0; _i < 2; ++_i) \
;         __builtin_amdgcn_global_load_lds((const unsigned*)((const char*)(gbase) + (voff)[_i]), (PG8_LAS unsigned*)(lds + (bufoff) + ldsw + _i * 8192), 16, 0, 0); } while (0)
; #define PG8_WAIT_V(n) asm volatile("s_waitcnt vmcnt(" #n ")" ::: "memory")
; #define PG8_BAR __builtin_amdgcn_s_barrier()
; template <class Epi, class Sched, bool ALIGN_EPI = false, bool SP2 = false>
; __device__ __forceinline__ void gemm_phase(PG8_LAS unsigned char* lds, const Gemm g, const Sched& S, const Epi& E, const bool skip_epi = false) {
;     ...
;         for (int t = 0; t < nt; t += 2) {
;             const bool last = (t == nt - 2); last_ = last && has_next;
;             const char* a1 = cA + (size_t)(t + 1) * kstep;
;             const char* a2 = last ? nA : cA + (size_t)(t + 2) * kstep; const char* b2 = last ? nB : cB + (size_t)(t + 2) * kstep;
;             const char* a3 = a2 + kstep; const char* b3 = b2 + kstep;
;             if (last && has_next) S.a_ready(nxt);
;             if constexpr (SP2) {
;             PG8_LDB(B0, 0, 0); PG8_LDB(B1, 0, 1); PG8_SCHED; PG8_LDA(At, 0, 0); PG8_STAGE_A(1, 1, a1, false);
;             PG8_WAIT_V(8); PG8_WAIT_L(0); PG8_BAR; PG8_MMA(0, 0, At, B0); PG8_MMA(0, 1, At, B1); PG8_BAR; PG8_SCHED;
;             PG8_LDA(At, 0, 1); PG8_STAGE(PG8_SB(0, 0), b2, voffB); PG8_STAGE(PG8_SB(0, 1), b2 + hstep, voffB); PG8_STAGE_A(0, 0, a2, true);
;             PG8_WAIT_V(8); PG8_WAIT_L(0); PG8_BAR; PG8_MMA(1, 0, At, B0); PG8_MMA(1, 1, At, B1); PG8_BAR; PG8_SCHED;
;             PG8_LDB(B0, 1, 0); PG8_LDB(B1, 1, 1); PG8_SCHED; PG8_LDA(At, 1, 0); PG8_STAGE_A(0, 1, a2, true);
;             PG8_WAIT_V(8); PG8_WAIT_L(0); PG8_BAR; PG8_MMA(0, 0, At, B0); PG8_MMA(0, 1, At, B1); PG8_BAR; PG8_SCHED;
;             PG8_LDA(At, 1, 1); PG8_STAGE(PG8_SB(1, 0), b3, voffB); PG8_STAGE(PG8_SB(1, 1), b3 + hstep, voffB); PG8_STAGE_A(1, 0, a3, true);
;             PG8_WAIT_V(8); PG8_WAIT_L(0); PG8_BAR; PG8_MMA(1, 0, At, B0); PG8_MMA(1, 1, At, B1); PG8_BAR; PG8_SCHED;
	s_add_i32 s20, s58, s2
	v_lshl_add_u64 v[210:211], v[210:211], 0, s[14:15]
	s_mov_b32 m0, s20
	ds_read_b128 v[154:157], v236 offset:49152
	ds_read_b128 v[166:169], v236 offset:50176
	ds_read_b128 v[170:173], v236 offset:51200
	ds_read_b128 v[174:177], v236 offset:52224
	ds_read_b128 v[178:181], v236 offset:53248
	ds_read_b128 v[182:185], v236 offset:54272
	ds_read_b128 v[186:189], v236 offset:55296
	ds_read_b128 v[206:209], v236 offset:56320
	global_load_lds_dwordx4 v[210:211], off
	s_add_i32 m0, s20, 0x2000
	s_add_u32 s20, s24, 0xb0080
	v_lshl_add_u64 v[210:211], v[212:213], 0, s[14:15]
	s_addc_u32 s21, s25, 0
	s_add_i32 s24, s59, s2
	global_load_lds_dwordx4 v[210:211], off
	v_lshl_add_u64 v[210:211], s[20:21], 0, v[192:193]
	s_mov_b32 m0, s24
	s_nop 0
	global_load_lds_dwordx4 v[210:211], off
	v_lshl_add_u64 v[210:211], s[20:21], 0, v[196:197]
	s_add_i32 m0, s24, 0x2000
	s_nop 0
	global_load_lds_dwordx4 v[210:211], off
	v_lshl_add_u64 v[210:211], v[214:215], 0, s[14:15]
	s_mov_b32 m0, s35
	s_nop 0
	global_load_lds_dwordx4 v[210:211], off
	v_lshl_add_u64 v[210:211], v[216:217], 0, s[14:15]
	s_mov_b32 m0, s36
	s_nop 0
	global_load_lds_dwordx4 v[210:211], off
	s_waitcnt vmcnt(8)
	s_waitcnt lgkmcnt(0)
	s_barrier
	s_setprio 3
	s_waitcnt lgkmcnt(0)
	v_mfma_f32_16x16x32_bf16 v[62:65], v[98:101], v[154:157], v[62:65]
	v_mfma_f32_16x16x32_bf16 v[58:61], v[122:125], v[154:157], v[58:61]
	v_mfma_f32_16x16x32_bf16 v[46:49], v[98:101], v[170:173], v[46:49]
	v_mfma_f32_16x16x32_bf16 v[42:45], v[122:125], v[170:173], v[42:45]
	v_mfma_f32_16x16x32_bf16 v[30:33], v[98:101], v[178:181], v[30:33]
	v_mfma_f32_16x16x32_bf16 v[26:29], v[122:125], v[178:181], v[26:29]
	v_mfma_f32_16x16x32_bf16 v[14:17], v[98:101], v[186:189], v[14:17]
	v_mfma_f32_16x16x32_bf16 v[10:13], v[122:125], v[186:189], v[10:13]
	v_mfma_f32_16x16x32_bf16 v[62:65], v[110:113], v[166:169], v[62:65]
	v_mfma_f32_16x16x32_bf16 v[58:61], v[126:129], v[166:169], v[58:61]
	v_mfma_f32_16x16x32_bf16 v[46:49], v[110:113], v[174:177], v[46:49]
	v_mfma_f32_16x16x32_bf16 v[42:45], v[126:129], v[174:177], v[42:45]
	v_mfma_f32_16x16x32_bf16 v[30:33], v[110:113], v[182:185], v[30:33]
	v_mfma_f32_16x16x32_bf16 v[26:29], v[126:129], v[182:185], v[26:29]
	v_mfma_f32_16x16x32_bf16 v[14:17], v[110:113], v[206:209], v[14:17]
	v_mfma_f32_16x16x32_bf16 v[10:13], v[126:129], v[206:209], v[10:13]
	s_setprio 0
	s_setprio 3
	v_mfma_f32_16x16x32_bf16 v[54:57], v[138:141], v[154:157], v[54:57]
	v_mfma_f32_16x16x32_bf16 v[50:53], v[146:149], v[154:157], v[50:53]
	v_mfma_f32_16x16x32_bf16 v[38:41], v[138:141], v[170:173], v[38:41]
	v_mfma_f32_16x16x32_bf16 v[34:37], v[146:149], v[170:173], v[34:37]
	v_mfma_f32_16x16x32_bf16 v[22:25], v[138:141], v[178:181], v[22:25]
	v_mfma_f32_16x16x32_bf16 v[18:21], v[146:149], v[178:181], v[18:21]
	v_mfma_f32_16x16x32_bf16 v[6:9], v[138:141], v[186:189], v[6:9]
	v_mfma_f32_16x16x32_bf16 v[2:5], v[146:149], v[186:189], v[2:5]
	v_mfma_f32_16x16x32_bf16 v[54:57], v[142:145], v[166:169], v[54:57]
	v_mfma_f32_16x16x32_bf16 v[50:53], v[150:153], v[166:169], v[50:53]
	v_mfma_f32_16x16x32_bf16 v[38:41], v[142:145], v[174:177], v[38:41]
	v_mfma_f32_16x16x32_bf16 v[34:37], v[150:153], v[174:177], v[34:37]
	v_mfma_f32_16x16x32_bf16 v[22:25], v[142:145], v[182:185], v[22:25]
	v_mfma_f32_16x16x32_bf16 v[18:21], v[150:153], v[182:185], v[18:21]
	v_mfma_f32_16x16x32_bf16 v[6:9], v[142:145], v[206:209], v[6:9]
	v_mfma_f32_16x16x32_bf16 v[2:5], v[150:153], v[206:209], v[2:5]
	s_setprio 0
	s_barrier
	s_add_i32 s57, s57, 2
	s_add_u32 s55, s55, 0x100
	s_addc_u32 s56, s56, 0
	s_cmp_gt_u32 s57, 41
	s_mov_b64 s[20:21], s[22:23]
.LBB0_857:
	ds_read_b128 v[98:101], v234
	ds_read_b128 v[110:113], v234 offset:1024
	ds_read_b128 v[122:125], v234 offset:2048
	ds_read_b128 v[126:129], v234 offset:3072
	ds_read_b128 v[138:141], v235
	ds_read_b128 v[142:145], v235 offset:1024
	ds_read_b128 v[146:149], v235 offset:2048
	ds_read_b128 v[150:153], v235 offset:3072
	s_add_u32 s22, s20, 0x100
	s_addc_u32 s23, s21, 0
	s_cmp_eq_u32 s57, 40
	s_cselect_b32 s27, s9, s23
	s_cselect_b32 s26, s8, s22
	s_cselect_b32 s25, s19, s56
	s_cselect_b32 s24, s18, s55
	v_lshl_add_u64 v[210:211], s[20:21], 0, v[198:199]
	s_add_i32 m0, s3, 0xc000
	ds_read_b128 v[154:157], v236
	ds_read_b128 v[166:169], v236 offset:1024
	ds_read_b128 v[170:173], v236 offset:2048
	ds_read_b128 v[174:177], v236 offset:3072
	ds_read_b128 v[178:181], v236 offset:4096
	ds_read_b128 v[182:185], v236 offset:5120
	ds_read_b128 v[186:189], v236 offset:6144
	ds_read_b128 v[206:209], v236 offset:7168
	global_load_lds_dwordx4 v[210:211], off
	v_lshl_add_u64 v[210:211], s[20:21], 0, v[200:201]
	s_add_i32 m0, s3, 0xe000
	s_nop 0
	global_load_lds_dwordx4 v[210:211], off
	s_waitcnt vmcnt(8)
	s_waitcnt lgkmcnt(0)
	s_barrier
; #define PG8_STAGE_A(b, h, ptr, NX) do { if constexpr (Sched::GATHER) { unsigned gs_[2]; gs_[0] = ((NX) && last_) ? gN[h][0] : gA[h][0]; gs_[1] = ((NX) && last_) ? gN[h][1] : gA[h][1]; PG8_STAGE(PG8_SA(b, h), ptr, gs_); } \
;         else PG8_STAGE(PG8_SA(b, h), (ptr) + ((h) ? hstep : (size_t)0), voffA); } while (0)
; #define PG8_STAGE(bufoff, gbase, voff) do { _Pragma("unroll") for (int _i = 0; _i < 2; ++_i) \
;         __builtin_amdgcn_global_load_lds((const unsigned*)((const char*)(gbase) + (voff)[_i]), (PG8_LAS unsigned*)(lds + (bufoff) + ldsw + _i * 8192), 16, 0, 0); } while (0)
; #define PG8_LDA(dst, b, h) do { _Pragma("unroll") for (int m = 0; m < 4; ++m) _Pragma("unroll") for (int k = 0; k < 2; ++k) dst[m][k] = *(const PG8_LAS bf16x8*)(lds + PG8_SA(b, h) + aoff + m * 2048 + k * 1024); } while (0)
; #define PG8_LDB(dst, b, h) do { _Pragma("unroll") for (int n = 0; n < 2; ++n) _Pragma("unroll") for (int k = 0; k < 2; ++k) dst[n][k] = *(const PG8_LAS bf16x8*)(lds + PG8_SB(b, h) + boff + n * 2048 + k * 1024); } while (0)
; #define PG8_MMA(ai, bj, At, Bt) do { __builtin_amdgcn_s_setprio(1); _Pragma("unroll") for (int m = 0; m < 4; ++m) _Pragma("unroll") for (int n = 0; n < 2; ++n) _Pragma("unroll") for (int k = 0; k < 2; ++k) \
;         acc[ai][bj][m][n] = __builtin_amdgcn_mfma_f32_16x16x32_bf16(Bt[n][k], At[m][k], acc[ai][bj][m][n], 0, 0, 0); __builtin_amdgcn_s_setprio(0); } while (0)
; #define PG8_WAIT_V(n) asm volatile("s_waitcnt vmcnt(" #n ")" ::: "memory")
; #define PG8_WAIT_L(n) asm volatile("s_waitcnt lgkmcnt(" #n ")" ::: "memory")
; #define PG8_BAR __builtin_amdgcn_s_barrier()
; #define PG8_SCHED __builtin_amdgcn_sched_barrier(0)
; template <class Epi, class Sched, bool ALIGN_EPI = false, bool SP2 = false>
; __device__ __forceinline__ void gemm_phase(PG8_LAS unsigned char* lds, const Gemm g, const Sched& S, const Epi& E, const bool skip_epi = false) {
;     ...
;             PG8_LDB(B0, 0, 0); PG8_LDB(B1, 0, 1); PG8_SCHED; PG8_LDA(At, 0, 0); PG8_STAGE_A(1, 1, a1, false);
;             PG8_WAIT_V(8); PG8_WAIT_L(0); PG8_BAR; PG8_MMA(0, 0, At, B0); PG8_MMA(0, 1, At, B1); PG8_BAR; PG8_SCHED;
;             PG8_LDA(At, 0, 1); PG8_STAGE(PG8_SB(0, 0), b2, voffB); PG8_STAGE(PG8_SB(0, 1), b2 + hstep, voffB); PG8_STAGE_A(0, 0, a2, true);
;             PG8_WAIT_V(8); PG8_WAIT_L(0); PG8_BAR; PG8_MMA(1, 0, At, B0); PG8_MMA(1, 1, At, B1); PG8_BAR; PG8_SCHED;
	s_setprio 3
	s_waitcnt lgkmcnt(0)
	v_mfma_f32_16x16x32_bf16 v[162:165], v[98:101], v[154:157], v[162:165]
	v_mfma_f32_16x16x32_bf16 v[158:161], v[122:125], v[154:157], v[158:161]
	v_mfma_f32_16x16x32_bf16 v[118:121], v[98:101], v[170:173], v[118:121]
	v_mfma_f32_16x16x32_bf16 v[114:117], v[122:125], v[170:173], v[114:117]
	v_mfma_f32_16x16x32_bf16 v[94:97], v[98:101], v[178:181], v[94:97]
	v_mfma_f32_16x16x32_bf16 v[90:93], v[122:125], v[178:181], v[90:93]
	v_mfma_f32_16x16x32_bf16 v[78:81], v[98:101], v[186:189], v[78:81]
	v_mfma_f32_16x16x32_bf16 v[74:77], v[122:125], v[186:189], v[74:77]
	v_mfma_f32_16x16x32_bf16 v[162:165], v[110:113], v[166:169], v[162:165]
	v_mfma_f32_16x16x32_bf16 v[158:161], v[126:129], v[166:169], v[158:161]
	v_mfma_f32_16x16x32_bf16 v[118:121], v[110:113], v[174:177], v[118:121]
	v_mfma_f32_16x16x32_bf16 v[114:117], v[126:129], v[174:177], v[114:117]
	v_mfma_f32_16x16x32_bf16 v[94:97], v[110:113], v[182:185], v[94:97]
	v_mfma_f32_16x16x32_bf16 v[90:93], v[126:129], v[182:185], v[90:93]
	v_mfma_f32_16x16x32_bf16 v[78:81], v[110:113], v[206:209], v[78:81]
	v_mfma_f32_16x16x32_bf16 v[74:77], v[126:129], v[206:209], v[74:77]
	s_setprio 0
	s_setprio 3
	v_mfma_f32_16x16x32_bf16 v[134:137], v[138:141], v[154:157], v[134:137]
	v_mfma_f32_16x16x32_bf16 v[130:133], v[146:149], v[154:157], v[130:133]
	v_mfma_f32_16x16x32_bf16 v[106:109], v[138:141], v[170:173], v[106:109]
	v_mfma_f32_16x16x32_bf16 v[102:105], v[146:149], v[170:173], v[102:105]
	v_mfma_f32_16x16x32_bf16 v[86:89], v[138:141], v[178:181], v[86:89]
	v_mfma_f32_16x16x32_bf16 v[82:85], v[146:149], v[178:181], v[82:85]
	v_mfma_f32_16x16x32_bf16 v[70:73], v[138:141], v[186:189], v[70:73]
	v_mfma_f32_16x16x32_bf16 v[66:69], v[146:149], v[186:189], v[66:69]
	v_mfma_f32_16x16x32_bf16 v[134:137], v[142:145], v[166:169], v[134:137]
	v_mfma_f32_16x16x32_bf16 v[130:133], v[150:153], v[166:169], v[130:133]
	v_mfma_f32_16x16x32_bf16 v[106:109], v[142:145], v[174:177], v[106:109]
	v_mfma_f32_16x16x32_bf16 v[102:105], v[150:153], v[174:177], v[102:105]
	v_mfma_f32_16x16x32_bf16 v[86:89], v[142:145], v[182:185], v[86:89]
	v_mfma_f32_16x16x32_bf16 v[82:85], v[150:153], v[182:185], v[82:85]
	v_mfma_f32_16x16x32_bf16 v[70:73], v[142:145], v[206:209], v[70:73]
	v_mfma_f32_16x16x32_bf16 v[66:69], v[150:153], v[206:209], v[66:69]
	s_setprio 0
	s_barrier
	s_add_i32 s20, s39, s2
	v_lshl_add_u64 v[210:211], s[24:25], 0, v[192:193]
	s_mov_b32 m0, s20
	ds_read_b128 v[154:157], v236 offset:16384
	ds_read_b128 v[166:169], v236 offset:17408
	ds_read_b128 v[170:173], v236 offset:18432
	ds_read_b128 v[174:177], v236 offset:19456
	ds_read_b128 v[178:181], v236 offset:20480
	ds_read_b128 v[182:185], v236 offset:21504
	ds_read_b128 v[186:189], v236 offset:22528
	ds_read_b128 v[206:209], v236 offset:23552
	global_load_lds_dwordx4 v[210:211], off
	s_add_i32 m0, s20, 0x2000
	s_add_u32 s20, s24, 0xb0000
	v_lshl_add_u64 v[212:213], s[24:25], 0, v[196:197]
	s_addc_u32 s21, s25, 0
	s_add_i32 s58, s48, s2
	global_load_lds_dwordx4 v[212:213], off
	v_lshl_add_u64 v[214:215], s[20:21], 0, v[192:193]
	s_mov_b32 m0, s58
	v_lshl_add_u64 v[216:217], s[26:27], 0, v[194:195]
	global_load_lds_dwordx4 v[214:215], off
	v_lshl_add_u64 v[214:215], s[20:21], 0, v[196:197]
	s_add_i32 m0, s58, 0x2000
	s_nop 0
	global_load_lds_dwordx4 v[214:215], off
	v_lshl_add_u64 v[214:215], s[26:27], 0, v[190:191]
	s_mov_b32 m0, s3
	s_nop 0
	global_load_lds_dwordx4 v[214:215], off
	s_mov_b32 m0, s28
	s_nop 0
	global_load_lds_dwordx4 v[216:217], off
	s_waitcnt vmcnt(8)
	s_waitcnt lgkmcnt(0)
	s_barrier
	s_setprio 3
	s_waitcnt lgkmcnt(0)
	v_mfma_f32_16x16x32_bf16 v[62:65], v[98:101], v[154:157], v[62:65]
	v_mfma_f32_16x16x32_bf16 v[58:61], v[122:125], v[154:157], v[58:61]
	v_mfma_f32_16x16x32_bf16 v[46:49], v[98:101], v[170:173], v[46:49]
	v_mfma_f32_16x16x32_bf16 v[42:45], v[122:125], v[170:173], v[42:45]
	v_mfma_f32_16x16x32_bf16 v[30:33], v[98:101], v[178:181], v[30:33]
	v_mfma_f32_16x16x32_bf16 v[26:29], v[122:125], v[178:181], v[26:29]
	v_mfma_f32_16x16x32_bf16 v[14:17], v[98:101], v[186:189], v[14:17]
	v_mfma_f32_16x16x32_bf16 v[10:13], v[122:125], v[186:189], v[10:13]
	v_mfma_f32_16x16x32_bf16 v[62:65], v[110:113], v[166:169], v[62:65]
	v_mfma_f32_16x16x32_bf16 v[58:61], v[126:129], v[166:169], v[58:61]
	v_mfma_f32_16x16x32_bf16 v[46:49], v[110:113], v[174:177], v[46:49]
	v_mfma_f32_16x16x32_bf16 v[42:45], v[126:129], v[174:177], v[42:45]
	v_mfma_f32_16x16x32_bf16 v[30:33], v[110:113], v[182:185], v[30:33]
	v_mfma_f32_16x16x32_bf16 v[26:29], v[126:129], v[182:185], v[26:29]
	v_mfma_f32_16x16x32_bf16 v[14:17], v[110:113], v[206:209], v[14:17]
	v_mfma_f32_16x16x32_bf16 v[10:13], v[126:129], v[206:209], v[10:13]
	s_setprio 0
	s_setprio 3
	v_mfma_f32_16x16x32_bf16 v[54:57], v[138:141], v[154:157], v[54:57]
	v_mfma_f32_16x16x32_bf16 v[50:53], v[146:149], v[154:157], v[50:53]
	v_mfma_f32_16x16x32_bf16 v[38:41], v[138:141], v[170:173], v[38:41]
	v_mfma_f32_16x16x32_bf16 v[34:37], v[146:149], v[170:173], v[34:37]
	v_mfma_f32_16x16x32_bf16 v[22:25], v[138:141], v[178:181], v[22:25]
	v_mfma_f32_16x16x32_bf16 v[18:21], v[146:149], v[178:181], v[18:21]
	v_mfma_f32_16x16x32_bf16 v[6:9], v[138:141], v[186:189], v[6:9]
	v_mfma_f32_16x16x32_bf16 v[2:5], v[146:149], v[186:189], v[2:5]
	v_mfma_f32_16x16x32_bf16 v[54:57], v[142:145], v[166:169], v[54:57]
	v_mfma_f32_16x16x32_bf16 v[50:53], v[150:153], v[166:169], v[50:53]
	v_mfma_f32_16x16x32_bf16 v[38:41], v[142:145], v[174:177], v[38:41]
	v_mfma_f32_16x16x32_bf16 v[34:37], v[150:153], v[174:177], v[34:37]
	v_mfma_f32_16x16x32_bf16 v[22:25], v[142:145], v[182:185], v[22:25]
	v_mfma_f32_16x16x32_bf16 v[18:21], v[150:153], v[182:185], v[18:21]
	v_mfma_f32_16x16x32_bf16 v[6:9], v[142:145], v[206:209], v[6:9]
	v_mfma_f32_16x16x32_bf16 v[2:5], v[150:153], v[206:209], v[2:5]
	s_setprio 0
	s_barrier
; #define PG8_STAGE_A(b, h, ptr, NX) do { if constexpr (Sched::GATHER) { unsigned gs_[2]; gs_[0] = ((NX) && last_) ? gN[h][0] : gA[h][0]; gs_[1] = ((NX) && last_) ? gN[h][1] : gA[h][1]; PG8_STAGE(PG8_SA(b, h), ptr, gs_); } \
;         else PG8_STAGE(PG8_SA(b, h), (ptr) + ((h) ? hstep : (size_t)0), voffA); } while (0)
; #define PG8_LDA(dst, b, h) do { _Pragma("unroll") for (int m = 0; m < 4; ++m) _Pragma("unroll") for (int k = 0; k < 2; ++k) dst[m][k] = *(const PG8_LAS bf16x8*)(lds + PG8_SA(b, h) + aoff + m * 2048 + k * 1024); } while (0)
; #define PG8_LDB(dst, b, h) do { _Pragma("unroll") for (int n = 0; n < 2; ++n) _Pragma("unroll") for (int k = 0; k < 2; ++k) dst[n][k] = *(const PG8_LAS bf16x8*)(lds + PG8_SB(b, h) + boff + n * 2048 + k * 1024); } while (0)
; #define PG8_MMA(ai, bj, At, Bt) do { __builtin_amdgcn_s_setprio(1); _Pragma("unroll") for (int m = 0; m < 4; ++m) _Pragma("unroll") for (int n = 0; n < 2; ++n) _Pragma("unroll") for (int k = 0; k < 2; ++k) \
;         acc[ai][bj][m][n] = __builtin_amdgcn_mfma_f32_16x16x32_bf16(Bt[n][k], At[m][k], acc[ai][bj][m][n], 0, 0, 0); __builtin_amdgcn_s_setprio(0); } while (0)
; #define PG8_WAIT_V(n) asm volatile("s_waitcnt vmcnt(" #n ")" ::: "memory")
; #define PG8_WAIT_L(n) asm volatile("s_waitcnt lgkmcnt(" #n ")" ::: "memory")
; #define PG8_BAR __builtin_amdgcn_s_barrier()
; #define PG8_SCHED __builtin_amdgcn_sched_barrier(0)
; template <class Epi, class Sched, bool ALIGN_EPI = false, bool SP2 = false>
; __device__ __forceinline__ void gemm_phase(PG8_LAS unsigned char* lds, const Gemm g, const Sched& S, const Epi& E, const bool skip_epi = false) {
;     ...
;             PG8_LDB(B0, 1, 0); PG8_LDB(B1, 1, 1); PG8_SCHED; PG8_LDA(At, 1, 0); PG8_STAGE_A(0, 1, a2, true);
;             PG8_WAIT_V(8); PG8_WAIT_L(0); PG8_BAR; PG8_MMA(0, 0, At, B0); PG8_MMA(0, 1, At, B1); PG8_BAR; PG8_SCHED;
	s_add_i32 s58, 0, 0x18000
	s_add_i32 s59, 0, 0x1c000
	v_add_u32_e32 v126, s58, v229
	v_add_u32_e32 v150, s59, v229
	ds_read_b128 v[98:101], v126
	ds_read_b128 v[110:113], v126 offset:1024
	ds_read_b128 v[122:125], v126 offset:2048
	ds_read_b128 v[126:129], v126 offset:3072
	ds_read_b128 v[138:141], v150
	ds_read_b128 v[142:145], v150 offset:1024
	ds_read_b128 v[146:149], v150 offset:2048
	ds_read_b128 v[150:153], v150 offset:3072
	s_add_u32 s20, s26, 0xb0000
	s_addc_u32 s21, s27, 0
	s_mov_b32 m0, s29
	v_lshl_add_u64 v[218:219], s[20:21], 0, v[190:191]
	ds_read_b128 v[154:157], v236 offset:32768
	ds_read_b128 v[166:169], v236 offset:33792
	ds_read_b128 v[170:173], v236 offset:34816
	ds_read_b128 v[174:177], v236 offset:35840
	ds_read_b128 v[178:181], v236 offset:36864
	ds_read_b128 v[182:185], v236 offset:37888
	ds_read_b128 v[186:189], v236 offset:38912
	ds_read_b128 v[206:209], v236 offset:39936
	global_load_lds_dwordx4 v[218:219], off
	v_lshl_add_u64 v[218:219], s[20:21], 0, v[194:195]
	s_mov_b32 m0, s30
	s_nop 0
	global_load_lds_dwordx4 v[218:219], off
	s_waitcnt vmcnt(8)
	s_waitcnt lgkmcnt(0)
	s_barrier
	s_setprio 3
	s_waitcnt lgkmcnt(0)
	v_mfma_f32_16x16x32_bf16 v[162:165], v[98:101], v[154:157], v[162:165]
	v_mfma_f32_16x16x32_bf16 v[158:161], v[122:125], v[154:157], v[158:161]
	v_mfma_f32_16x16x32_bf16 v[118:121], v[98:101], v[170:173], v[118:121]
	v_mfma_f32_16x16x32_bf16 v[114:117], v[122:125], v[170:173], v[114:117]
	v_mfma_f32_16x16x32_bf16 v[94:97], v[98:101], v[178:181], v[94:97]
	v_mfma_f32_16x16x32_bf16 v[90:93], v[122:125], v[178:181], v[90:93]
	v_mfma_f32_16x16x32_bf16 v[78:81], v[98:101], v[186:189], v[78:81]
	v_mfma_f32_16x16x32_bf16 v[74:77], v[122:125], v[186:189], v[74:77]
	v_mfma_f32_16x16x32_bf16 v[162:165], v[110:113], v[166:169], v[162:165]
	v_mfma_f32_16x16x32_bf16 v[158:161], v[126:129], v[166:169], v[158:161]
	v_mfma_f32_16x16x32_bf16 v[118:121], v[110:113], v[174:177], v[118:121]
	v_mfma_f32_16x16x32_bf16 v[114:117], v[126:129], v[174:177], v[114:117]
	v_mfma_f32_16x16x32_bf16 v[94:97], v[110:113], v[182:185], v[94:97]
	v_mfma_f32_16x16x32_bf16 v[90:93], v[126:129], v[182:185], v[90:93]
	v_mfma_f32_16x16x32_bf16 v[78:81], v[110:113], v[206:209], v[78:81]
	v_mfma_f32_16x16x32_bf16 v[74:77], v[126:129], v[206:209], v[74:77]
	s_setprio 0
	s_setprio 3
	v_mfma_f32_16x16x32_bf16 v[134:137], v[138:141], v[154:157], v[134:137]
	v_mfma_f32_16x16x32_bf16 v[130:133], v[146:149], v[154:157], v[130:133]
	v_mfma_f32_16x16x32_bf16 v[106:109], v[138:141], v[170:173], v[106:109]
	v_mfma_f32_16x16x32_bf16 v[102:105], v[146:149], v[170:173], v[102:105]
	v_mfma_f32_16x16x32_bf16 v[86:89], v[138:141], v[178:181], v[86:89]
	v_mfma_f32_16x16x32_bf16 v[82:85], v[146:149], v[178:181], v[82:85]
	v_mfma_f32_16x16x32_bf16 v[70:73], v[138:141], v[186:189], v[70:73]
	v_mfma_f32_16x16x32_bf16 v[66:69], v[146:149], v[186:189], v[66:69]
	v_mfma_f32_16x16x32_bf16 v[134:137], v[142:145], v[166:169], v[134:137]
	v_mfma_f32_16x16x32_bf16 v[130:133], v[150:153], v[166:169], v[130:133]
	v_mfma_f32_16x16x32_bf16 v[106:109], v[142:145], v[174:177], v[106:109]
	v_mfma_f32_16x16x32_bf16 v[102:105], v[150:153], v[174:177], v[102:105]
	v_mfma_f32_16x16x32_bf16 v[86:89], v[142:145], v[182:185], v[86:89]
	v_mfma_f32_16x16x32_bf16 v[82:85], v[150:153], v[182:185], v[82:85]
	v_mfma_f32_16x16x32_bf16 v[70:73], v[142:145], v[206:209], v[70:73]
	v_mfma_f32_16x16x32_bf16 v[66:69], v[150:153], v[206:209], v[66:69]
	s_setprio 0
	s_barrier
; #define PG8_STAGE_A(b, h, ptr, NX) do { if constexpr (Sched::GATHER) { unsigned gs_[2]; gs_[0] = ((NX) && last_) ? gN[h][0] : gA[h][0]; gs_[1] = ((NX) && last_) ? gN[h][1] : gA[h][1]; PG8_STAGE(PG8_SA(b, h), ptr, gs_); } \
;         else PG8_STAGE(PG8_SA(b, h), (ptr) + ((h) ? hstep : (size_t)0), voffA); } while (0)
; #define PG8_STAGE(bufoff, gbase, voff) do { _Pragma("unroll") for (int _i = 0; _i < 2; ++_i) \
;         __builtin_amdgcn_global_load_lds((const unsigned*)((const char*)(gbase) + (voff)[_i]), (PG8_LAS unsigned*)(lds + (bufoff) + ldsw + _i * 8192), 16, 0, 0); } while (0)
; #define PG8_LDA(dst, b, h) do { _Pragma("unroll") for (int m = 0; m < 4; ++m) _Pragma("unroll") for (int k = 0; k < 2; ++k) dst[m][k] = *(const PG8_LAS bf16x8*)(lds + PG8_SA(b, h) + aoff + m * 2048 + k * 1024); } while (0)
; #define PG8_MMA(ai, bj, At, Bt) do { __builtin_amdgcn_s_setprio(1); _Pragma("unroll") for (int m = 0; m < 4; ++m) _Pragma("unroll") for (int n = 0; n < 2; ++n) _Pragma("unroll") for (int k = 0; k < 2; ++k) \
;         acc[ai][bj][m][n] = __builtin_amdgcn_mfma_f32_16x16x32_bf16(Bt[n][k], At[m][k], acc[ai][bj][m][n], 0, 0, 0); __builtin_amdgcn_s_setprio(0); } while (0)
; #define PG8_WAIT_V(n) asm volatile("s_waitcnt vmcnt(" #n ")" ::: "memory")
; #define PG8_WAIT_L(n) asm volatile("s_waitcnt lgkmcnt(" #n ")" ::: "memory")
; #define PG8_BAR __builtin_amdgcn_s_barrier()
; #define PG8_SCHED __builtin_amdgcn_sched_barrier(0)
; template <class Epi, class Sched, bool ALIGN_EPI = false, bool SP2 = false>
; __device__ __forceinline__ void gemm_phase(PG8_LAS unsigned char* lds, const Gemm g, const Sched& S, const Epi& E, const bool skip_epi = false) {
;     ...
;             PG8_LDA(At, 1, 1); PG8_STAGE(PG8_SB(1, 0), b3, voffB); PG8_STAGE(PG8_SB(1, 1), b3 + hstep, voffB); PG8_STAGE_A(1, 0, a3, true);
;             PG8_WAIT_V(8); PG8_WAIT_L(0); PG8_BAR; PG8_MMA(1, 0, At, B0); PG8_MMA(1, 1, At, B1); PG8_BAR; PG8_SCHED;
;     ...
;         if constexpr (ALIGN_EPI) { if (wr == 0) PG8_BAR; }
	s_add_i32 s20, s58, s2
	v_lshl_add_u64 v[210:211], v[210:211], 0, s[14:15]
	s_mov_b32 m0, s20
	ds_read_b128 v[154:157], v236 offset:49152
	ds_read_b128 v[166:169], v236 offset:50176
	ds_read_b128 v[170:173], v236 offset:51200
	ds_read_b128 v[174:177], v236 offset:52224
	ds_read_b128 v[178:181], v236 offset:53248
	ds_read_b128 v[182:185], v236 offset:54272
	ds_read_b128 v[186:189], v236 offset:55296
	ds_read_b128 v[206:209], v236 offset:56320
	global_load_lds_dwordx4 v[210:211], off
	s_add_i32 m0, s20, 0x2000
	s_add_u32 s20, s24, 0xb0080
	v_lshl_add_u64 v[210:211], v[212:213], 0, s[14:15]
	s_addc_u32 s21, s25, 0
	s_add_i32 s24, s59, s2
	global_load_lds_dwordx4 v[210:211], off
	v_lshl_add_u64 v[210:211], s[20:21], 0, v[192:193]
	s_mov_b32 m0, s24
	s_nop 0
	global_load_lds_dwordx4 v[210:211], off
	v_lshl_add_u64 v[210:211], s[20:21], 0, v[196:197]
	s_add_i32 m0, s24, 0x2000
	s_nop 0
	global_load_lds_dwordx4 v[210:211], off
	v_lshl_add_u64 v[210:211], v[214:215], 0, s[14:15]
	s_mov_b32 m0, s35
	s_nop 0
	global_load_lds_dwordx4 v[210:211], off
	v_lshl_add_u64 v[210:211], v[216:217], 0, s[14:15]
	s_mov_b32 m0, s36
	s_nop 0
	global_load_lds_dwordx4 v[210:211], off
	s_waitcnt vmcnt(8)
	s_waitcnt lgkmcnt(0)
	s_barrier
	s_setprio 3
	s_waitcnt lgkmcnt(0)
	v_mfma_f32_16x16x32_bf16 v[62:65], v[98:101], v[154:157], v[62:65]
	v_mfma_f32_16x16x32_bf16 v[58:61], v[122:125], v[154:157], v[58:61]
	v_mfma_f32_16x16x32_bf16 v[46:49], v[98:101], v[170:173], v[46:49]
	v_mfma_f32_16x16x32_bf16 v[42:45], v[122:125], v[170:173], v[42:45]
	v_mfma_f32_16x16x32_bf16 v[30:33], v[98:101], v[178:181], v[30:33]
	v_mfma_f32_16x16x32_bf16 v[26:29], v[122:125], v[178:181], v[26:29]
	v_mfma_f32_16x16x32_bf16 v[14:17], v[98:101], v[186:189], v[14:17]
	v_mfma_f32_16x16x32_bf16 v[10:13], v[122:125], v[186:189], v[10:13]
	v_mfma_f32_16x16x32_bf16 v[62:65], v[110:113], v[166:169], v[62:65]
	v_mfma_f32_16x16x32_bf16 v[58:61], v[126:129], v[166:169], v[58:61]
	v_mfma_f32_16x16x32_bf16 v[46:49], v[110:113], v[174:177], v[46:49]
	v_mfma_f32_16x16x32_bf16 v[42:45], v[126:129], v[174:177], v[42:45]
	v_mfma_f32_16x16x32_bf16 v[30:33], v[110:113], v[182:185], v[30:33]
	v_mfma_f32_16x16x32_bf16 v[26:29], v[126:129], v[182:185], v[26:29]
	v_mfma_f32_16x16x32_bf16 v[14:17], v[110:113], v[206:209], v[14:17]
	v_mfma_f32_16x16x32_bf16 v[10:13], v[126:129], v[206:209], v[10:13]
	s_setprio 0
	s_setprio 3
	v_mfma_f32_16x16x32_bf16 v[54:57], v[138:141], v[154:157], v[54:57]
	v_mfma_f32_16x16x32_bf16 v[50:53], v[146:149], v[154:157], v[50:53]
	v_mfma_f32_16x16x32_bf16 v[38:41], v[138:141], v[170:173], v[38:41]
	v_mfma_f32_16x16x32_bf16 v[34:37], v[146:149], v[170:173], v[34:37]
	v_mfma_f32_16x16x32_bf16 v[22:25], v[138:141], v[178:181], v[22:25]
	v_mfma_f32_16x16x32_bf16 v[18:21], v[146:149], v[178:181], v[18:21]
	v_mfma_f32_16x16x32_bf16 v[6:9], v[138:141], v[186:189], v[6:9]
	v_mfma_f32_16x16x32_bf16 v[2:5], v[146:149], v[186:189], v[2:5]
	v_mfma_f32_16x16x32_bf16 v[54:57], v[142:145], v[166:169], v[54:57]
	v_mfma_f32_16x16x32_bf16 v[50:53], v[150:153], v[166:169], v[50:53]
	v_mfma_f32_16x16x32_bf16 v[38:41], v[142:145], v[174:177], v[38:41]
	v_mfma_f32_16x16x32_bf16 v[34:37], v[150:153], v[174:177], v[34:37]
	v_mfma_f32_16x16x32_bf16 v[22:25], v[142:145], v[182:185], v[22:25]
	v_mfma_f32_16x16x32_bf16 v[18:21], v[150:153], v[182:185], v[18:21]
	v_mfma_f32_16x16x32_bf16 v[6:9], v[142:145], v[206:209], v[6:9]
	v_mfma_f32_16x16x32_bf16 v[2:5], v[150:153], v[206:209], v[2:5]
	s_setprio 0
	s_barrier
	s_add_i32 s57, s57, 2
	s_add_u32 s55, s55, 0x100
	s_addc_u32 s56, s56, 0
	s_cmp_gt_u32 s57, 41
	s_mov_b64 s[20:21], s[22:23]
	s_cbranch_scc0 .LBB0_857
	s_and_b64 vcc, exec, s[16:17]
	s_cbranch_vccz .LBB0_860
	s_barrier

; #define PG8_GIDX(G_, PM_) do { if constexpr (Sched::GATHER) { _Pragma("unroll") for (int h_ = 0; h_ < 2; ++h_) _Pragma("unroll") for (int i_ = 0; i_ < 2; ++i_) { int R_, C_; stage_rc(tid * 16 + i_ * 8192, R_, C_); \
;         const int src_ = S.rowsrc[(PM_) * BM + h_ * HALF + R_]; G_[h_][i_] = (unsigned)(src_ * K + C_) * 2u; } } } while (0)
; #define PG8_STAGE_A(b, h, ptr, NX) do { if constexpr (Sched::GATHER) { unsigned gs_[2]; gs_[0] = ((NX) && last_) ? gN[h][0] : gA[h][0]; gs_[1] = ((NX) && last_) ? gN[h][1] : gA[h][1]; PG8_STAGE(PG8_SA(b, h), ptr, gs_); } \
;         else PG8_STAGE(PG8_SA(b, h), (ptr) + ((h) ? hstep : (size_t)0), voffA); } while (0)
; #define PG8_LDA(dst, b, h) do { _Pragma("unroll") for (int m = 0; m < 4; ++m) _Pragma("unroll") for (int k = 0; k < 2; ++k) dst[m][k] = *(const PG8_LAS bf16x8*)(lds + PG8_SA(b, h) + aoff + m * 2048 + k * 1024); } while (0)
; template <class Epi, class Sched, bool ALIGN_EPI = false, bool SP2 = false>
; __device__ __forceinline__ void gemm_phase(PG8_LAS unsigned char* lds, const Gemm g, const Sched& S, const Epi& E, const bool skip_epi = false) {
;     ...
;         const bool has_next = S.next(ui + 1, nxt);
;         if (has_next) PG8_GIDX(gN, nxt.pm);
;         const char* nA = has_next ? (const char*)g.A + (size_t)nxt.pm * pmstepA + nxt.ko : cA; const char* nB = has_next ? (const char*)g.Bt + (size_t)nxt.pn * tstep + nxt.ko : cB;
;         for (int t = 0; t < nt; t += 2) {
;             const bool last = (t == nt - 2); last_ = last && has_next;
;             const char* a1 = cA + (size_t)(t + 1) * kstep;
;             const char* a2 = last ? nA : cA + (size_t)(t + 2) * kstep; const char* b2 = last ? nB : cB + (size_t)(t + 2) * kstep;
;             const char* a3 = a2 + kstep; const char* b3 = b2 + kstep;
;             if (last && has_next) S.a_ready(nxt);
;             if constexpr (SP2) {
;             PG8_LDB(B0, 0, 0); PG8_LDB(B1, 0, 1); PG8_SCHED; PG8_LDA(At, 0, 0); PG8_STAGE_A(1, 1, a1, false);
;             PG8_WAIT_V(8); PG8_WAIT_L(0); PG8_BAR; PG8_MMA(0, 0, At, B0); PG8_MMA(0, 1, At, B1); PG8_BAR; PG8_SCHED;
;             PG8_LDA(At, 0, 1); PG8_STAGE(PG8_SB(0, 0), b2, voffB); PG8_STAGE(PG8_SB(0, 1), b2 + hstep, voffB); PG8_STAGE_A(0, 0, a2, true);
;             PG8_WAIT_V(8); PG8_WAIT_L(0); PG8_BAR; PG8_MMA(1, 0, At, B0); PG8_MMA(1, 1, At, B1); PG8_BAR; PG8_SCHED;
.LBB0_943:
	s_ashr_i32 s15, s14, 31
	s_lshl_b64 s[16:17], s[14:15], 19
	s_add_u32 s16, s86, s16
	s_addc_u32 s17, s87, s17
	s_and_b64 s[18:19], s[4:5], exec
	s_cselect_b32 s15, s17, s23
	s_cselect_b32 s54, s16, s22
	s_ashr_i32 s13, s12, 31
	s_lshl_b64 s[18:19], s[12:13], 19
	s_add_u32 s18, s2, s18
	s_addc_u32 s19, s3, s19
	s_and_b64 s[26:27], s[4:5], exec
	s_cselect_b32 s13, s19, s25
	s_cselect_b32 s55, s18, s24
	s_add_u32 s22, s22, 0x40080
	s_addc_u32 s23, s23, 0
	s_add_u32 s56, s24, 0x100
	s_addc_u32 s57, s25, 0
	s_mov_b32 s58, -2
	s_waitcnt vmcnt(0)
	ds_read_b128 v[148:151], v170
	ds_read_b128 v[152:155], v170 offset:1024
	ds_read_b128 v[156:159], v170 offset:2048
	ds_read_b128 v[160:163], v170 offset:3072
	ds_read_b128 v[176:179], v171
	ds_read_b128 v[180:183], v171 offset:1024
	ds_read_b128 v[184:187], v171 offset:2048
	ds_read_b128 v[188:191], v171 offset:3072
	s_add_u32 s24, s22, 0xfffc0080
	s_addc_u32 s25, s23, -1
	s_cmp_eq_u32 s58, 12
	s_cselect_b32 s27, s15, s25
	s_cselect_b32 s26, s54, s24
	s_cselect_b32 s25, s13, s57
	s_cselect_b32 s24, s55, s56
	v_lshl_add_u64 v[164:165], s[22:23], 0, v[140:141]
	s_add_i32 m0, s21, 0xc000
	ds_read_b128 v[192:195], v172
	ds_read_b128 v[196:199], v172 offset:1024
	ds_read_b128 v[200:203], v172 offset:2048
	ds_read_b128 v[204:207], v172 offset:3072
	ds_read_b128 v[208:211], v172 offset:4096
	ds_read_b128 v[212:215], v172 offset:5120
	ds_read_b128 v[216:219], v172 offset:6144
	ds_read_b128 v[220:223], v172 offset:7168
	global_load_lds_dwordx4 v[164:165], off
	v_lshl_add_u64 v[164:165], s[22:23], 0, v[142:143]
	s_add_i32 m0, s21, 0xe000
	s_nop 0
	global_load_lds_dwordx4 v[164:165], off
	s_waitcnt vmcnt(8)
	s_waitcnt lgkmcnt(0)
	s_barrier
	s_setprio 3
	s_waitcnt lgkmcnt(0)
	v_mfma_f32_16x16x32_bf16 v[126:129], v[148:151], v[192:195], 0
	v_mfma_f32_16x16x32_bf16 v[122:125], v[156:159], v[192:195], 0
	v_mfma_f32_16x16x32_bf16 v[114:117], v[148:151], v[200:203], 0
	v_mfma_f32_16x16x32_bf16 v[106:109], v[156:159], v[200:203], 0
	v_mfma_f32_16x16x32_bf16 v[98:101], v[148:151], v[208:211], 0
	v_mfma_f32_16x16x32_bf16 v[90:93], v[156:159], v[208:211], 0
	v_mfma_f32_16x16x32_bf16 v[82:85], v[148:151], v[216:219], 0
	v_mfma_f32_16x16x32_bf16 v[74:77], v[156:159], v[216:219], 0
	v_mfma_f32_16x16x32_bf16 v[126:129], v[152:155], v[196:199], v[126:129]
	v_mfma_f32_16x16x32_bf16 v[122:125], v[160:163], v[196:199], v[122:125]
	v_mfma_f32_16x16x32_bf16 v[114:117], v[152:155], v[204:207], v[114:117]
	v_mfma_f32_16x16x32_bf16 v[106:109], v[160:163], v[204:207], v[106:109]
	v_mfma_f32_16x16x32_bf16 v[98:101], v[152:155], v[212:215], v[98:101]
	v_mfma_f32_16x16x32_bf16 v[90:93], v[160:163], v[212:215], v[90:93]
	v_mfma_f32_16x16x32_bf16 v[82:85], v[152:155], v[220:223], v[82:85]
	v_mfma_f32_16x16x32_bf16 v[74:77], v[160:163], v[220:223], v[74:77]
	s_setprio 0
	s_setprio 3
	v_mfma_f32_16x16x32_bf16 v[118:121], v[176:179], v[192:195], 0
	v_mfma_f32_16x16x32_bf16 v[110:113], v[184:187], v[192:195], 0
	v_mfma_f32_16x16x32_bf16 v[102:105], v[176:179], v[200:203], 0
	v_mfma_f32_16x16x32_bf16 v[94:97], v[184:187], v[200:203], 0
	v_mfma_f32_16x16x32_bf16 v[86:89], v[176:179], v[208:211], 0
	v_mfma_f32_16x16x32_bf16 v[78:81], v[184:187], v[208:211], 0
	v_mfma_f32_16x16x32_bf16 v[70:73], v[176:179], v[216:219], 0
	v_mfma_f32_16x16x32_bf16 v[66:69], v[184:187], v[216:219], 0
	v_mfma_f32_16x16x32_bf16 v[118:121], v[180:183], v[196:199], v[118:121]
	v_mfma_f32_16x16x32_bf16 v[110:113], v[188:191], v[196:199], v[110:113]
	v_mfma_f32_16x16x32_bf16 v[102:105], v[180:183], v[204:207], v[102:105]
	v_mfma_f32_16x16x32_bf16 v[94:97], v[188:191], v[204:207], v[94:97]
	v_mfma_f32_16x16x32_bf16 v[86:89], v[180:183], v[212:215], v[86:89]
	v_mfma_f32_16x16x32_bf16 v[78:81], v[188:191], v[212:215], v[78:81]
	v_mfma_f32_16x16x32_bf16 v[70:73], v[180:183], v[220:223], v[70:73]
	v_mfma_f32_16x16x32_bf16 v[66:69], v[188:191], v[220:223], v[66:69]
	s_setprio 0
	s_barrier
	s_add_i32 s59, s48, s28
	v_lshl_add_u64 v[164:165], s[24:25], 0, v[134:135]
	s_mov_b32 m0, s59
	ds_read_b128 v[192:195], v172 offset:16384
	ds_read_b128 v[196:199], v172 offset:17408
	ds_read_b128 v[200:203], v172 offset:18432
	ds_read_b128 v[204:207], v172 offset:19456
	ds_read_b128 v[208:211], v172 offset:20480
	ds_read_b128 v[212:215], v172 offset:21504
	ds_read_b128 v[216:219], v172 offset:22528
	ds_read_b128 v[220:223], v172 offset:23552
	global_load_lds_dwordx4 v[164:165], off
	s_add_i32 m0, s59, 0x2000
	s_add_u32 s60, s24, 0x40000
	v_lshl_add_u64 v[224:225], s[24:25], 0, v[130:131]
	s_addc_u32 s61, s25, 0
	s_add_i32 s59, s49, s28
	global_load_lds_dwordx4 v[224:225], off
	v_lshl_add_u64 v[226:227], s[60:61], 0, v[134:135]
	s_mov_b32 m0, s59
	v_lshl_add_u64 v[230:231], s[26:27], 0, v[132:133]
	global_load_lds_dwordx4 v[226:227], off
	v_lshl_add_u64 v[226:227], s[60:61], 0, v[130:131]
	s_add_i32 m0, s59, 0x2000
	s_nop 0
	global_load_lds_dwordx4 v[226:227], off
	v_lshl_add_u64 v[226:227], s[26:27], 0, v[136:137]
	s_mov_b32 m0, s21
	s_nop 0
	global_load_lds_dwordx4 v[226:227], off
	s_mov_b32 m0, s31
	s_nop 0
	global_load_lds_dwordx4 v[230:231], off
	s_waitcnt vmcnt(8)
	s_waitcnt lgkmcnt(0)
	s_barrier
; #define PG8_STAGE_A(b, h, ptr, NX) do { if constexpr (Sched::GATHER) { unsigned gs_[2]; gs_[0] = ((NX) && last_) ? gN[h][0] : gA[h][0]; gs_[1] = ((NX) && last_) ? gN[h][1] : gA[h][1]; PG8_STAGE(PG8_SA(b, h), ptr, gs_); } \
;         else PG8_STAGE(PG8_SA(b, h), (ptr) + ((h) ? hstep : (size_t)0), voffA); } while (0)
; #define PG8_LDA(dst, b, h) do { _Pragma("unroll") for (int m = 0; m < 4; ++m) _Pragma("unroll") for (int k = 0; k < 2; ++k) dst[m][k] = *(const PG8_LAS bf16x8*)(lds + PG8_SA(b, h) + aoff + m * 2048 + k * 1024); } while (0)
; #define PG8_LDB(dst, b, h) do { _Pragma("unroll") for (int n = 0; n < 2; ++n) _Pragma("unroll") for (int k = 0; k < 2; ++k) dst[n][k] = *(const PG8_LAS bf16x8*)(lds + PG8_SB(b, h) + boff + n * 2048 + k * 1024); } while (0)
; #define PG8_MMA(ai, bj, At, Bt) do { __builtin_amdgcn_s_setprio(1); _Pragma("unroll") for (int m = 0; m < 4; ++m) _Pragma("unroll") for (int n = 0; n < 2; ++n) _Pragma("unroll") for (int k = 0; k < 2; ++k) \
;         acc[ai][bj][m][n] = __builtin_amdgcn_mfma_f32_16x16x32_bf16(Bt[n][k], At[m][k], acc[ai][bj][m][n], 0, 0, 0); __builtin_amdgcn_s_setprio(0); } while (0)
; #define PG8_WAIT_V(n) asm volatile("s_waitcnt vmcnt(" #n ")" ::: "memory")
; #define PG8_WAIT_L(n) asm volatile("s_waitcnt lgkmcnt(" #n ")" ::: "memory")
; #define PG8_BAR __builtin_amdgcn_s_barrier()
; #define PG8_SCHED __builtin_amdgcn_sched_barrier(0)
; template <class Epi, class Sched, bool ALIGN_EPI = false, bool SP2 = false>
; __device__ __forceinline__ void gemm_phase(PG8_LAS unsigned char* lds, const Gemm g, const Sched& S, const Epi& E, const bool skip_epi = false) {
;     ...
;             PG8_WAIT_V(8); PG8_WAIT_L(0); PG8_BAR; PG8_MMA(1, 0, At, B0); PG8_MMA(1, 1, At, B1); PG8_BAR; PG8_SCHED;
;             PG8_LDB(B0, 1, 0); PG8_LDB(B1, 1, 1); PG8_SCHED; PG8_LDA(At, 1, 0); PG8_STAGE_A(0, 1, a2, true);
;             PG8_WAIT_V(8); PG8_WAIT_L(0); PG8_BAR; PG8_MMA(0, 0, At, B0); PG8_MMA(0, 1, At, B1); PG8_BAR; PG8_SCHED;
	s_setprio 3
	s_waitcnt lgkmcnt(0)
	v_mfma_f32_16x16x32_bf16 v[62:65], v[148:151], v[192:195], 0
	v_mfma_f32_16x16x32_bf16 v[58:61], v[156:159], v[192:195], 0
	v_mfma_f32_16x16x32_bf16 v[50:53], v[148:151], v[200:203], 0
	v_mfma_f32_16x16x32_bf16 v[42:45], v[156:159], v[200:203], 0
	v_mfma_f32_16x16x32_bf16 v[34:37], v[148:151], v[208:211], 0
	v_mfma_f32_16x16x32_bf16 v[26:29], v[156:159], v[208:211], 0
	v_mfma_f32_16x16x32_bf16 v[18:21], v[148:151], v[216:219], 0
	v_mfma_f32_16x16x32_bf16 v[10:13], v[156:159], v[216:219], 0
	v_mfma_f32_16x16x32_bf16 v[62:65], v[152:155], v[196:199], v[62:65]
	v_mfma_f32_16x16x32_bf16 v[58:61], v[160:163], v[196:199], v[58:61]
	v_mfma_f32_16x16x32_bf16 v[50:53], v[152:155], v[204:207], v[50:53]
	v_mfma_f32_16x16x32_bf16 v[42:45], v[160:163], v[204:207], v[42:45]
	v_mfma_f32_16x16x32_bf16 v[34:37], v[152:155], v[212:215], v[34:37]
	v_mfma_f32_16x16x32_bf16 v[26:29], v[160:163], v[212:215], v[26:29]
	v_mfma_f32_16x16x32_bf16 v[18:21], v[152:155], v[220:223], v[18:21]
	v_mfma_f32_16x16x32_bf16 v[10:13], v[160:163], v[220:223], v[10:13]
	s_setprio 0
	s_setprio 3
	v_mfma_f32_16x16x32_bf16 v[54:57], v[176:179], v[192:195], 0
	v_mfma_f32_16x16x32_bf16 v[46:49], v[184:187], v[192:195], 0
	v_mfma_f32_16x16x32_bf16 v[38:41], v[176:179], v[200:203], 0
	v_mfma_f32_16x16x32_bf16 v[30:33], v[184:187], v[200:203], 0
	v_mfma_f32_16x16x32_bf16 v[22:25], v[176:179], v[208:211], 0
	v_mfma_f32_16x16x32_bf16 v[14:17], v[184:187], v[208:211], 0
	v_mfma_f32_16x16x32_bf16 v[6:9], v[176:179], v[216:219], 0
	v_mfma_f32_16x16x32_bf16 v[2:5], v[184:187], v[216:219], 0
	v_mfma_f32_16x16x32_bf16 v[54:57], v[180:183], v[196:199], v[54:57]
	v_mfma_f32_16x16x32_bf16 v[46:49], v[188:191], v[196:199], v[46:49]
	v_mfma_f32_16x16x32_bf16 v[38:41], v[180:183], v[204:207], v[38:41]
	v_mfma_f32_16x16x32_bf16 v[30:33], v[188:191], v[204:207], v[30:33]
	v_mfma_f32_16x16x32_bf16 v[22:25], v[180:183], v[212:215], v[22:25]
	v_mfma_f32_16x16x32_bf16 v[14:17], v[188:191], v[212:215], v[14:17]
	v_mfma_f32_16x16x32_bf16 v[6:9], v[180:183], v[220:223], v[6:9]
	v_mfma_f32_16x16x32_bf16 v[2:5], v[188:191], v[220:223], v[2:5]
	s_setprio 0
	s_barrier
	s_add_i32 s59, 0, 0x18000
	s_add_i32 s60, 0, 0x1c000
	v_add_u32_e32 v160, s59, v1
	v_add_u32_e32 v188, s60, v1
	ds_read_b128 v[148:151], v160
	ds_read_b128 v[152:155], v160 offset:1024
	ds_read_b128 v[156:159], v160 offset:2048
	ds_read_b128 v[160:163], v160 offset:3072
	ds_read_b128 v[176:179], v188
	ds_read_b128 v[180:183], v188 offset:1024
	ds_read_b128 v[184:187], v188 offset:2048
	ds_read_b128 v[188:191], v188 offset:3072
	s_add_u32 s26, s26, 0x40000
	s_addc_u32 s27, s27, 0
	s_mov_b32 m0, s34
	v_lshl_add_u64 v[232:233], s[26:27], 0, v[136:137]
	ds_read_b128 v[192:195], v172 offset:32768
	ds_read_b128 v[196:199], v172 offset:33792
	ds_read_b128 v[200:203], v172 offset:34816
	ds_read_b128 v[204:207], v172 offset:35840
	ds_read_b128 v[208:211], v172 offset:36864
	ds_read_b128 v[212:215], v172 offset:37888
	ds_read_b128 v[216:219], v172 offset:38912
	ds_read_b128 v[220:223], v172 offset:39936
	global_load_lds_dwordx4 v[232:233], off
	v_lshl_add_u64 v[232:233], s[26:27], 0, v[132:133]
	s_mov_b32 m0, s35
	s_nop 0
	global_load_lds_dwordx4 v[232:233], off
	s_waitcnt vmcnt(8)
	s_waitcnt lgkmcnt(0)
	s_barrier
	s_setprio 3
	s_waitcnt lgkmcnt(0)
	v_mfma_f32_16x16x32_bf16 v[126:129], v[148:151], v[192:195], v[126:129]
	v_mfma_f32_16x16x32_bf16 v[122:125], v[156:159], v[192:195], v[122:125]
	v_mfma_f32_16x16x32_bf16 v[114:117], v[148:151], v[200:203], v[114:117]
	v_mfma_f32_16x16x32_bf16 v[106:109], v[156:159], v[200:203], v[106:109]
	v_mfma_f32_16x16x32_bf16 v[98:101], v[148:151], v[208:211], v[98:101]
	v_mfma_f32_16x16x32_bf16 v[90:93], v[156:159], v[208:211], v[90:93]
	v_mfma_f32_16x16x32_bf16 v[82:85], v[148:151], v[216:219], v[82:85]
	v_mfma_f32_16x16x32_bf16 v[74:77], v[156:159], v[216:219], v[74:77]
	v_mfma_f32_16x16x32_bf16 v[126:129], v[152:155], v[196:199], v[126:129]
	v_mfma_f32_16x16x32_bf16 v[122:125], v[160:163], v[196:199], v[122:125]
	v_mfma_f32_16x16x32_bf16 v[114:117], v[152:155], v[204:207], v[114:117]
	v_mfma_f32_16x16x32_bf16 v[106:109], v[160:163], v[204:207], v[106:109]
	v_mfma_f32_16x16x32_bf16 v[98:101], v[152:155], v[212:215], v[98:101]
	v_mfma_f32_16x16x32_bf16 v[90:93], v[160:163], v[212:215], v[90:93]
	v_mfma_f32_16x16x32_bf16 v[82:85], v[152:155], v[220:223], v[82:85]
	v_mfma_f32_16x16x32_bf16 v[74:77], v[160:163], v[220:223], v[74:77]
	s_setprio 0
	s_setprio 3
	v_mfma_f32_16x16x32_bf16 v[118:121], v[176:179], v[192:195], v[118:121]
	v_mfma_f32_16x16x32_bf16 v[110:113], v[184:187], v[192:195], v[110:113]
	v_mfma_f32_16x16x32_bf16 v[102:105], v[176:179], v[200:203], v[102:105]
	v_mfma_f32_16x16x32_bf16 v[94:97], v[184:187], v[200:203], v[94:97]
	v_mfma_f32_16x16x32_bf16 v[86:89], v[176:179], v[208:211], v[86:89]
	v_mfma_f32_16x16x32_bf16 v[78:81], v[184:187], v[208:211], v[78:81]
	v_mfma_f32_16x16x32_bf16 v[70:73], v[176:179], v[216:219], v[70:73]
	v_mfma_f32_16x16x32_bf16 v[66:69], v[184:187], v[216:219], v[66:69]
	v_mfma_f32_16x16x32_bf16 v[118:121], v[180:183], v[196:199], v[118:121]
	v_mfma_f32_16x16x32_bf16 v[110:113], v[188:191], v[196:199], v[110:113]
	v_mfma_f32_16x16x32_bf16 v[102:105], v[180:183], v[204:207], v[102:105]
	v_mfma_f32_16x16x32_bf16 v[94:97], v[188:191], v[204:207], v[94:97]
	v_mfma_f32_16x16x32_bf16 v[86:89], v[180:183], v[212:215], v[86:89]
	v_mfma_f32_16x16x32_bf16 v[78:81], v[188:191], v[212:215], v[78:81]
	v_mfma_f32_16x16x32_bf16 v[70:73], v[180:183], v[220:223], v[70:73]
	v_mfma_f32_16x16x32_bf16 v[66:69], v[188:191], v[220:223], v[66:69]
	s_setprio 0
	s_barrier
; #define PG8_STAGE_A(b, h, ptr, NX) do { if constexpr (Sched::GATHER) { unsigned gs_[2]; gs_[0] = ((NX) && last_) ? gN[h][0] : gA[h][0]; gs_[1] = ((NX) && last_) ? gN[h][1] : gA[h][1]; PG8_STAGE(PG8_SA(b, h), ptr, gs_); } \
;         else PG8_STAGE(PG8_SA(b, h), (ptr) + ((h) ? hstep : (size_t)0), voffA); } while (0)
; #define PG8_STAGE(bufoff, gbase, voff) do { _Pragma("unroll") for (int _i = 0; _i < 2; ++_i) \
;         __builtin_amdgcn_global_load_lds((const unsigned*)((const char*)(gbase) + (voff)[_i]), (PG8_LAS unsigned*)(lds + (bufoff) + ldsw + _i * 8192), 16, 0, 0); } while (0)
; #define PG8_LDA(dst, b, h) do { _Pragma("unroll") for (int m = 0; m < 4; ++m) _Pragma("unroll") for (int k = 0; k < 2; ++k) dst[m][k] = *(const PG8_LAS bf16x8*)(lds + PG8_SA(b, h) + aoff + m * 2048 + k * 1024); } while (0)
; #define PG8_LDB(dst, b, h) do { _Pragma("unroll") for (int n = 0; n < 2; ++n) _Pragma("unroll") for (int k = 0; k < 2; ++k) dst[n][k] = *(const PG8_LAS bf16x8*)(lds + PG8_SB(b, h) + boff + n * 2048 + k * 1024); } while (0)
; #define PG8_WAIT_V(n) asm volatile("s_waitcnt vmcnt(" #n ")" ::: "memory")
; #define PG8_BAR __builtin_amdgcn_s_barrier()
; template <class Epi, class Sched, bool ALIGN_EPI = false, bool SP2 = false>
; __device__ __forceinline__ void gemm_phase(PG8_LAS unsigned char* lds, const Gemm g, const Sched& S, const Epi& E, const bool skip_epi = false) {
;     ...
;             PG8_LDB(B0, 0, 0); PG8_LDB(B1, 0, 1); PG8_SCHED; PG8_LDA(At, 0, 0); PG8_STAGE_A(1, 1, a1, false);
;             PG8_WAIT_V(8); PG8_WAIT_L(0); PG8_BAR; PG8_MMA(0, 0, At, B0); PG8_MMA(0, 1, At, B1); PG8_BAR; PG8_SCHED;
;             PG8_LDA(At, 0, 1); PG8_STAGE(PG8_SB(0, 0), b2, voffB); PG8_STAGE(PG8_SB(0, 1), b2 + hstep, voffB); PG8_STAGE_A(0, 0, a2, true);
;             PG8_WAIT_V(8); PG8_WAIT_L(0); PG8_BAR; PG8_MMA(1, 0, At, B0); PG8_MMA(1, 1, At, B1); PG8_BAR; PG8_SCHED;
;             PG8_LDB(B0, 1, 0); PG8_LDB(B1, 1, 1); PG8_SCHED; PG8_LDA(At, 1, 0); PG8_STAGE_A(0, 1, a2, true);
;             PG8_WAIT_V(8); PG8_WAIT_L(0); PG8_BAR; PG8_MMA(0, 0, At, B0); PG8_MMA(0, 1, At, B1); PG8_BAR; PG8_SCHED;
;             PG8_LDA(At, 1, 1); PG8_STAGE(PG8_SB(1, 0), b3, voffB); PG8_STAGE(PG8_SB(1, 1), b3 + hstep, voffB); PG8_STAGE_A(1, 0, a3, true);
;             PG8_WAIT_V(8); PG8_WAIT_L(0); PG8_BAR; PG8_MMA(1, 0, At, B0); PG8_MMA(1, 1, At, B1); PG8_BAR; PG8_SCHED;
	s_add_i32 s26, s59, s28
	v_lshl_add_u64 v[164:165], v[164:165], 0, s[8:9]
	s_mov_b32 m0, s26
	ds_read_b128 v[192:195], v172 offset:49152
	ds_read_b128 v[196:199], v172 offset:50176
	ds_read_b128 v[200:203], v172 offset:51200
	ds_read_b128 v[204:207], v172 offset:52224
	ds_read_b128 v[208:211], v172 offset:53248
	ds_read_b128 v[212:215], v172 offset:54272
	ds_read_b128 v[216:219], v172 offset:55296
	ds_read_b128 v[220:223], v172 offset:56320
	global_load_lds_dwordx4 v[164:165], off
	s_add_i32 m0, s26, 0x2000
	s_add_u32 s24, s24, 0x40080
	v_lshl_add_u64 v[164:165], v[224:225], 0, s[8:9]
	s_addc_u32 s25, s25, 0
	s_add_i32 s26, s60, s28
	global_load_lds_dwordx4 v[164:165], off
	v_lshl_add_u64 v[164:165], s[24:25], 0, v[134:135]
	s_mov_b32 m0, s26
	s_nop 0
	global_load_lds_dwordx4 v[164:165], off
	v_lshl_add_u64 v[164:165], s[24:25], 0, v[130:131]
	s_add_i32 m0, s26, 0x2000
	s_nop 0
	global_load_lds_dwordx4 v[164:165], off
	v_lshl_add_u64 v[164:165], v[226:227], 0, s[8:9]
	s_mov_b32 m0, s37
	s_nop 0
	global_load_lds_dwordx4 v[164:165], off
	v_lshl_add_u64 v[164:165], v[230:231], 0, s[8:9]
	s_mov_b32 m0, s38
	s_nop 0
	global_load_lds_dwordx4 v[164:165], off
	s_waitcnt vmcnt(8)
	s_waitcnt lgkmcnt(0)
	s_barrier
	s_setprio 3
	s_waitcnt lgkmcnt(0)
	v_mfma_f32_16x16x32_bf16 v[62:65], v[148:151], v[192:195], v[62:65]
	v_mfma_f32_16x16x32_bf16 v[58:61], v[156:159], v[192:195], v[58:61]
	v_mfma_f32_16x16x32_bf16 v[50:53], v[148:151], v[200:203], v[50:53]
	v_mfma_f32_16x16x32_bf16 v[42:45], v[156:159], v[200:203], v[42:45]
	v_mfma_f32_16x16x32_bf16 v[34:37], v[148:151], v[208:211], v[34:37]
	v_mfma_f32_16x16x32_bf16 v[26:29], v[156:159], v[208:211], v[26:29]
	v_mfma_f32_16x16x32_bf16 v[18:21], v[148:151], v[216:219], v[18:21]
	v_mfma_f32_16x16x32_bf16 v[10:13], v[156:159], v[216:219], v[10:13]
	v_mfma_f32_16x16x32_bf16 v[62:65], v[152:155], v[196:199], v[62:65]
	v_mfma_f32_16x16x32_bf16 v[58:61], v[160:163], v[196:199], v[58:61]
	v_mfma_f32_16x16x32_bf16 v[50:53], v[152:155], v[204:207], v[50:53]
	v_mfma_f32_16x16x32_bf16 v[42:45], v[160:163], v[204:207], v[42:45]
	v_mfma_f32_16x16x32_bf16 v[34:37], v[152:155], v[212:215], v[34:37]
	v_mfma_f32_16x16x32_bf16 v[26:29], v[160:163], v[212:215], v[26:29]
	v_mfma_f32_16x16x32_bf16 v[18:21], v[152:155], v[220:223], v[18:21]
	v_mfma_f32_16x16x32_bf16 v[10:13], v[160:163], v[220:223], v[10:13]
	s_setprio 0
	s_setprio 3
	v_mfma_f32_16x16x32_bf16 v[54:57], v[176:179], v[192:195], v[54:57]
	v_mfma_f32_16x16x32_bf16 v[46:49], v[184:187], v[192:195], v[46:49]
	v_mfma_f32_16x16x32_bf16 v[38:41], v[176:179], v[200:203], v[38:41]
	v_mfma_f32_16x16x32_bf16 v[30:33], v[184:187], v[200:203], v[30:33]
	v_mfma_f32_16x16x32_bf16 v[22:25], v[176:179], v[208:211], v[22:25]
	v_mfma_f32_16x16x32_bf16 v[14:17], v[184:187], v[208:211], v[14:17]
	v_mfma_f32_16x16x32_bf16 v[6:9], v[176:179], v[216:219], v[6:9]
	v_mfma_f32_16x16x32_bf16 v[2:5], v[184:187], v[216:219], v[2:5]
	v_mfma_f32_16x16x32_bf16 v[54:57], v[180:183], v[196:199], v[54:57]
	v_mfma_f32_16x16x32_bf16 v[46:49], v[188:191], v[196:199], v[46:49]
	v_mfma_f32_16x16x32_bf16 v[38:41], v[180:183], v[204:207], v[38:41]
	v_mfma_f32_16x16x32_bf16 v[30:33], v[188:191], v[204:207], v[30:33]
	v_mfma_f32_16x16x32_bf16 v[22:25], v[180:183], v[212:215], v[22:25]
	v_mfma_f32_16x16x32_bf16 v[14:17], v[188:191], v[212:215], v[14:17]
	v_mfma_f32_16x16x32_bf16 v[6:9], v[180:183], v[220:223], v[6:9]
	v_mfma_f32_16x16x32_bf16 v[2:5], v[188:191], v[220:223], v[2:5]
	s_setprio 0
	s_barrier
	s_add_i32 s58, s58, 2
	s_add_u32 s22, s22, 0x100
	s_addc_u32 s23, s23, 0
	s_add_u32 s56, s56, 0x100
	s_addc_u32 s57, s57, 0
	s_cmp_gt_u32 s58, 13
.LBB0_944:
	ds_read_b128 v[148:151], v170
	ds_read_b128 v[152:155], v170 offset:1024
	ds_read_b128 v[156:159], v170 offset:2048
	ds_read_b128 v[160:163], v170 offset:3072
	ds_read_b128 v[176:179], v171
	ds_read_b128 v[180:183], v171 offset:1024
	ds_read_b128 v[184:187], v171 offset:2048
	ds_read_b128 v[188:191], v171 offset:3072
	s_add_u32 s24, s22, 0xfffc0080
	s_addc_u32 s25, s23, -1
	s_cmp_eq_u32 s58, 12
	s_cselect_b32 s27, s15, s25
	s_cselect_b32 s26, s54, s24
	s_cselect_b32 s25, s13, s57
	s_cselect_b32 s24, s55, s56
	v_lshl_add_u64 v[164:165], s[22:23], 0, v[140:141]
	s_add_i32 m0, s21, 0xc000
	ds_read_b128 v[192:195], v172
	ds_read_b128 v[196:199], v172 offset:1024
	ds_read_b128 v[200:203], v172 offset:2048
	ds_read_b128 v[204:207], v172 offset:3072
	ds_read_b128 v[208:211], v172 offset:4096
	ds_read_b128 v[212:215], v172 offset:5120
	ds_read_b128 v[216:219], v172 offset:6144
	ds_read_b128 v[220:223], v172 offset:7168
	global_load_lds_dwordx4 v[164:165], off
	v_lshl_add_u64 v[164:165], s[22:23], 0, v[142:143]
	s_add_i32 m0, s21, 0xe000
	s_nop 0
	global_load_lds_dwordx4 v[164:165], off
	s_waitcnt vmcnt(8)
	s_waitcnt lgkmcnt(0)
	s_barrier
; #define PG8_STAGE_A(b, h, ptr, NX) do { if constexpr (Sched::GATHER) { unsigned gs_[2]; gs_[0] = ((NX) && last_) ? gN[h][0] : gA[h][0]; gs_[1] = ((NX) && last_) ? gN[h][1] : gA[h][1]; PG8_STAGE(PG8_SA(b, h), ptr, gs_); } \
;         else PG8_STAGE(PG8_SA(b, h), (ptr) + ((h) ? hstep : (size_t)0), voffA); } while (0)
; #define PG8_STAGE(bufoff, gbase, voff) do { _Pragma("unroll") for (int _i = 0; _i < 2; ++_i) \
;         __builtin_amdgcn_global_load_lds((const unsigned*)((const char*)(gbase) + (voff)[_i]), (PG8_LAS unsigned*)(lds + (bufoff) + ldsw + _i * 8192), 16, 0, 0); } while (0)
; #define PG8_LDA(dst, b, h) do { _Pragma("unroll") for (int m = 0; m < 4; ++m) _Pragma("unroll") for (int k = 0; k < 2; ++k) dst[m][k] = *(const PG8_LAS bf16x8*)(lds + PG8_SA(b, h) + aoff + m * 2048 + k * 1024); } while (0)
; #define PG8_MMA(ai, bj, At, Bt) do { __builtin_amdgcn_s_setprio(1); _Pragma("unroll") for (int m = 0; m < 4; ++m) _Pragma("unroll") for (int n = 0; n < 2; ++n) _Pragma("unroll") for (int k = 0; k < 2; ++k) \
;         acc[ai][bj][m][n] = __builtin_amdgcn_mfma_f32_16x16x32_bf16(Bt[n][k], At[m][k], acc[ai][bj][m][n], 0, 0, 0); __builtin_amdgcn_s_setprio(0); } while (0)
; #define PG8_WAIT_V(n) asm volatile("s_waitcnt vmcnt(" #n ")" ::: "memory")
; #define PG8_WAIT_L(n) asm volatile("s_waitcnt lgkmcnt(" #n ")" ::: "memory")
; #define PG8_BAR __builtin_amdgcn_s_barrier()
; #define PG8_SCHED __builtin_amdgcn_sched_barrier(0)
; template <class Epi, class Sched, bool ALIGN_EPI = false, bool SP2 = false>
; __device__ __forceinline__ void gemm_phase(PG8_LAS unsigned char* lds, const Gemm g, const Sched& S, const Epi& E, const bool skip_epi = false) {
;     ...
;             PG8_WAIT_V(8); PG8_WAIT_L(0); PG8_BAR; PG8_MMA(0, 0, At, B0); PG8_MMA(0, 1, At, B1); PG8_BAR; PG8_SCHED;
;             PG8_LDA(At, 0, 1); PG8_STAGE(PG8_SB(0, 0), b2, voffB); PG8_STAGE(PG8_SB(0, 1), b2 + hstep, voffB); PG8_STAGE_A(0, 0, a2, true);
;             PG8_WAIT_V(8); PG8_WAIT_L(0); PG8_BAR; PG8_MMA(1, 0, At, B0); PG8_MMA(1, 1, At, B1); PG8_BAR; PG8_SCHED;
	s_setprio 3
	s_waitcnt lgkmcnt(0)
	v_mfma_f32_16x16x32_bf16 v[126:129], v[148:151], v[192:195], v[126:129]
	v_mfma_f32_16x16x32_bf16 v[122:125], v[156:159], v[192:195], v[122:125]
	v_mfma_f32_16x16x32_bf16 v[114:117], v[148:151], v[200:203], v[114:117]
	v_mfma_f32_16x16x32_bf16 v[106:109], v[156:159], v[200:203], v[106:109]
	v_mfma_f32_16x16x32_bf16 v[98:101], v[148:151], v[208:211], v[98:101]
	v_mfma_f32_16x16x32_bf16 v[90:93], v[156:159], v[208:211], v[90:93]
	v_mfma_f32_16x16x32_bf16 v[82:85], v[148:151], v[216:219], v[82:85]
	v_mfma_f32_16x16x32_bf16 v[74:77], v[156:159], v[216:219], v[74:77]
	v_mfma_f32_16x16x32_bf16 v[126:129], v[152:155], v[196:199], v[126:129]
	v_mfma_f32_16x16x32_bf16 v[122:125], v[160:163], v[196:199], v[122:125]
	v_mfma_f32_16x16x32_bf16 v[114:117], v[152:155], v[204:207], v[114:117]
	v_mfma_f32_16x16x32_bf16 v[106:109], v[160:163], v[204:207], v[106:109]
	v_mfma_f32_16x16x32_bf16 v[98:101], v[152:155], v[212:215], v[98:101]
	v_mfma_f32_16x16x32_bf16 v[90:93], v[160:163], v[212:215], v[90:93]
	v_mfma_f32_16x16x32_bf16 v[82:85], v[152:155], v[220:223], v[82:85]
	v_mfma_f32_16x16x32_bf16 v[74:77], v[160:163], v[220:223], v[74:77]
	s_setprio 0
	s_setprio 3
	v_mfma_f32_16x16x32_bf16 v[118:121], v[176:179], v[192:195], v[118:121]
	v_mfma_f32_16x16x32_bf16 v[110:113], v[184:187], v[192:195], v[110:113]
	v_mfma_f32_16x16x32_bf16 v[102:105], v[176:179], v[200:203], v[102:105]
	v_mfma_f32_16x16x32_bf16 v[94:97], v[184:187], v[200:203], v[94:97]
	v_mfma_f32_16x16x32_bf16 v[86:89], v[176:179], v[208:211], v[86:89]
	v_mfma_f32_16x16x32_bf16 v[78:81], v[184:187], v[208:211], v[78:81]
	v_mfma_f32_16x16x32_bf16 v[70:73], v[176:179], v[216:219], v[70:73]
	v_mfma_f32_16x16x32_bf16 v[66:69], v[184:187], v[216:219], v[66:69]
	v_mfma_f32_16x16x32_bf16 v[118:121], v[180:183], v[196:199], v[118:121]
	v_mfma_f32_16x16x32_bf16 v[110:113], v[188:191], v[196:199], v[110:113]
	v_mfma_f32_16x16x32_bf16 v[102:105], v[180:183], v[204:207], v[102:105]
	v_mfma_f32_16x16x32_bf16 v[94:97], v[188:191], v[204:207], v[94:97]
	v_mfma_f32_16x16x32_bf16 v[86:89], v[180:183], v[212:215], v[86:89]
	v_mfma_f32_16x16x32_bf16 v[78:81], v[188:191], v[212:215], v[78:81]
	v_mfma_f32_16x16x32_bf16 v[70:73], v[180:183], v[220:223], v[70:73]
	v_mfma_f32_16x16x32_bf16 v[66:69], v[188:191], v[220:223], v[66:69]
	s_setprio 0
	s_barrier
	s_add_i32 s59, s48, s28
	v_lshl_add_u64 v[164:165], s[24:25], 0, v[134:135]
	s_mov_b32 m0, s59
	ds_read_b128 v[192:195], v172 offset:16384
	ds_read_b128 v[196:199], v172 offset:17408
	ds_read_b128 v[200:203], v172 offset:18432
	ds_read_b128 v[204:207], v172 offset:19456
	ds_read_b128 v[208:211], v172 offset:20480
	ds_read_b128 v[212:215], v172 offset:21504
	ds_read_b128 v[216:219], v172 offset:22528
	ds_read_b128 v[220:223], v172 offset:23552
	global_load_lds_dwordx4 v[164:165], off
	s_add_i32 m0, s59, 0x2000
	s_add_u32 s60, s24, 0x40000
	v_lshl_add_u64 v[224:225], s[24:25], 0, v[130:131]
	s_addc_u32 s61, s25, 0
	s_add_i32 s59, s49, s28
	global_load_lds_dwordx4 v[224:225], off
	v_lshl_add_u64 v[226:227], s[60:61], 0, v[134:135]
	s_mov_b32 m0, s59
	v_lshl_add_u64 v[230:231], s[26:27], 0, v[132:133]
	global_load_lds_dwordx4 v[226:227], off
	v_lshl_add_u64 v[226:227], s[60:61], 0, v[130:131]
	s_add_i32 m0, s59, 0x2000
	s_nop 0
	global_load_lds_dwordx4 v[226:227], off
	v_lshl_add_u64 v[226:227], s[26:27], 0, v[136:137]
	s_mov_b32 m0, s21
	s_nop 0
	global_load_lds_dwordx4 v[226:227], off
	s_mov_b32 m0, s31
	s_nop 0
	global_load_lds_dwordx4 v[230:231], off
	s_waitcnt vmcnt(8)
	s_waitcnt lgkmcnt(0)
	s_barrier
	s_setprio 3
	s_waitcnt lgkmcnt(0)
	v_mfma_f32_16x16x32_bf16 v[62:65], v[148:151], v[192:195], v[62:65]
	v_mfma_f32_16x16x32_bf16 v[58:61], v[156:159], v[192:195], v[58:61]
	v_mfma_f32_16x16x32_bf16 v[50:53], v[148:151], v[200:203], v[50:53]
	v_mfma_f32_16x16x32_bf16 v[42:45], v[156:159], v[200:203], v[42:45]
	v_mfma_f32_16x16x32_bf16 v[34:37], v[148:151], v[208:211], v[34:37]
	v_mfma_f32_16x16x32_bf16 v[26:29], v[156:159], v[208:211], v[26:29]
	v_mfma_f32_16x16x32_bf16 v[18:21], v[148:151], v[216:219], v[18:21]
	v_mfma_f32_16x16x32_bf16 v[10:13], v[156:159], v[216:219], v[10:13]
	v_mfma_f32_16x16x32_bf16 v[62:65], v[152:155], v[196:199], v[62:65]
	v_mfma_f32_16x16x32_bf16 v[58:61], v[160:163], v[196:199], v[58:61]
	v_mfma_f32_16x16x32_bf16 v[50:53], v[152:155], v[204:207], v[50:53]
	v_mfma_f32_16x16x32_bf16 v[42:45], v[160:163], v[204:207], v[42:45]
	v_mfma_f32_16x16x32_bf16 v[34:37], v[152:155], v[212:215], v[34:37]
	v_mfma_f32_16x16x32_bf16 v[26:29], v[160:163], v[212:215], v[26:29]
	v_mfma_f32_16x16x32_bf16 v[18:21], v[152:155], v[220:223], v[18:21]
	v_mfma_f32_16x16x32_bf16 v[10:13], v[160:163], v[220:223], v[10:13]
	s_setprio 0
	s_setprio 3
	v_mfma_f32_16x16x32_bf16 v[54:57], v[176:179], v[192:195], v[54:57]
	v_mfma_f32_16x16x32_bf16 v[46:49], v[184:187], v[192:195], v[46:49]
	v_mfma_f32_16x16x32_bf16 v[38:41], v[176:179], v[200:203], v[38:41]
	v_mfma_f32_16x16x32_bf16 v[30:33], v[184:187], v[200:203], v[30:33]
	v_mfma_f32_16x16x32_bf16 v[22:25], v[176:179], v[208:211], v[22:25]
	v_mfma_f32_16x16x32_bf16 v[14:17], v[184:187], v[208:211], v[14:17]
	v_mfma_f32_16x16x32_bf16 v[6:9], v[176:179], v[216:219], v[6:9]
	v_mfma_f32_16x16x32_bf16 v[2:5], v[184:187], v[216:219], v[2:5]
	v_mfma_f32_16x16x32_bf16 v[54:57], v[180:183], v[196:199], v[54:57]
	v_mfma_f32_16x16x32_bf16 v[46:49], v[188:191], v[196:199], v[46:49]
	v_mfma_f32_16x16x32_bf16 v[38:41], v[180:183], v[204:207], v[38:41]
	v_mfma_f32_16x16x32_bf16 v[30:33], v[188:191], v[204:207], v[30:33]
	v_mfma_f32_16x16x32_bf16 v[22:25], v[180:183], v[212:215], v[22:25]
	v_mfma_f32_16x16x32_bf16 v[14:17], v[188:191], v[212:215], v[14:17]
	v_mfma_f32_16x16x32_bf16 v[6:9], v[180:183], v[220:223], v[6:9]
	v_mfma_f32_16x16x32_bf16 v[2:5], v[188:191], v[220:223], v[2:5]
	s_setprio 0
	s_barrier
; #define PG8_STAGE_A(b, h, ptr, NX) do { if constexpr (Sched::GATHER) { unsigned gs_[2]; gs_[0] = ((NX) && last_) ? gN[h][0] : gA[h][0]; gs_[1] = ((NX) && last_) ? gN[h][1] : gA[h][1]; PG8_STAGE(PG8_SA(b, h), ptr, gs_); } \
;         else PG8_STAGE(PG8_SA(b, h), (ptr) + ((h) ? hstep : (size_t)0), voffA); } while (0)
; #define PG8_LDA(dst, b, h) do { _Pragma("unroll") for (int m = 0; m < 4; ++m) _Pragma("unroll") for (int k = 0; k < 2; ++k) dst[m][k] = *(const PG8_LAS bf16x8*)(lds + PG8_SA(b, h) + aoff + m * 2048 + k * 1024); } while (0)
; #define PG8_LDB(dst, b, h) do { _Pragma("unroll") for (int n = 0; n < 2; ++n) _Pragma("unroll") for (int k = 0; k < 2; ++k) dst[n][k] = *(const PG8_LAS bf16x8*)(lds + PG8_SB(b, h) + boff + n * 2048 + k * 1024); } while (0)
; #define PG8_MMA(ai, bj, At, Bt) do { __builtin_amdgcn_s_setprio(1); _Pragma("unroll") for (int m = 0; m < 4; ++m) _Pragma("unroll") for (int n = 0; n < 2; ++n) _Pragma("unroll") for (int k = 0; k < 2; ++k) \
;         acc[ai][bj][m][n] = __builtin_amdgcn_mfma_f32_16x16x32_bf16(Bt[n][k], At[m][k], acc[ai][bj][m][n], 0, 0, 0); __builtin_amdgcn_s_setprio(0); } while (0)
; #define PG8_WAIT_V(n) asm volatile("s_waitcnt vmcnt(" #n ")" ::: "memory")
; #define PG8_WAIT_L(n) asm volatile("s_waitcnt lgkmcnt(" #n ")" ::: "memory")
; #define PG8_BAR __builtin_amdgcn_s_barrier()
; #define PG8_SCHED __builtin_amdgcn_sched_barrier(0)
; template <class Epi, class Sched, bool ALIGN_EPI = false, bool SP2 = false>
; __device__ __forceinline__ void gemm_phase(PG8_LAS unsigned char* lds, const Gemm g, const Sched& S, const Epi& E, const bool skip_epi = false) {
;     ...
;             PG8_LDB(B0, 1, 0); PG8_LDB(B1, 1, 1); PG8_SCHED; PG8_LDA(At, 1, 0); PG8_STAGE_A(0, 1, a2, true);
;             PG8_WAIT_V(8); PG8_WAIT_L(0); PG8_BAR; PG8_MMA(0, 0, At, B0); PG8_MMA(0, 1, At, B1); PG8_BAR; PG8_SCHED;
	s_add_i32 s59, 0, 0x18000
	s_add_i32 s60, 0, 0x1c000
	v_add_u32_e32 v160, s59, v1
	v_add_u32_e32 v188, s60, v1
	ds_read_b128 v[148:151], v160
	ds_read_b128 v[152:155], v160 offset:1024
	ds_read_b128 v[156:159], v160 offset:2048
	ds_read_b128 v[160:163], v160 offset:3072
	ds_read_b128 v[176:179], v188
	ds_read_b128 v[180:183], v188 offset:1024
	ds_read_b128 v[184:187], v188 offset:2048
	ds_read_b128 v[188:191], v188 offset:3072
	s_add_u32 s26, s26, 0x40000
	s_addc_u32 s27, s27, 0
	s_mov_b32 m0, s34
	v_lshl_add_u64 v[232:233], s[26:27], 0, v[136:137]
	ds_read_b128 v[192:195], v172 offset:32768
	ds_read_b128 v[196:199], v172 offset:33792
	ds_read_b128 v[200:203], v172 offset:34816
	ds_read_b128 v[204:207], v172 offset:35840
	ds_read_b128 v[208:211], v172 offset:36864
	ds_read_b128 v[212:215], v172 offset:37888
	ds_read_b128 v[216:219], v172 offset:38912
	ds_read_b128 v[220:223], v172 offset:39936
	global_load_lds_dwordx4 v[232:233], off
	v_lshl_add_u64 v[232:233], s[26:27], 0, v[132:133]
	s_mov_b32 m0, s35
	s_nop 0
	global_load_lds_dwordx4 v[232:233], off
	s_waitcnt vmcnt(8)
	s_waitcnt lgkmcnt(0)
	s_barrier
	s_setprio 3
	s_waitcnt lgkmcnt(0)
	v_mfma_f32_16x16x32_bf16 v[126:129], v[148:151], v[192:195], v[126:129]
	v_mfma_f32_16x16x32_bf16 v[122:125], v[156:159], v[192:195], v[122:125]
	v_mfma_f32_16x16x32_bf16 v[114:117], v[148:151], v[200:203], v[114:117]
	v_mfma_f32_16x16x32_bf16 v[106:109], v[156:159], v[200:203], v[106:109]
	v_mfma_f32_16x16x32_bf16 v[98:101], v[148:151], v[208:211], v[98:101]
	v_mfma_f32_16x16x32_bf16 v[90:93], v[156:159], v[208:211], v[90:93]
	v_mfma_f32_16x16x32_bf16 v[82:85], v[148:151], v[216:219], v[82:85]
	v_mfma_f32_16x16x32_bf16 v[74:77], v[156:159], v[216:219], v[74:77]
	v_mfma_f32_16x16x32_bf16 v[126:129], v[152:155], v[196:199], v[126:129]
	v_mfma_f32_16x16x32_bf16 v[122:125], v[160:163], v[196:199], v[122:125]
	v_mfma_f32_16x16x32_bf16 v[114:117], v[152:155], v[204:207], v[114:117]
	v_mfma_f32_16x16x32_bf16 v[106:109], v[160:163], v[204:207], v[106:109]
	v_mfma_f32_16x16x32_bf16 v[98:101], v[152:155], v[212:215], v[98:101]
	v_mfma_f32_16x16x32_bf16 v[90:93], v[160:163], v[212:215], v[90:93]
	v_mfma_f32_16x16x32_bf16 v[82:85], v[152:155], v[220:223], v[82:85]
	v_mfma_f32_16x16x32_bf16 v[74:77], v[160:163], v[220:223], v[74:77]
	s_setprio 0
	s_setprio 3
	v_mfma_f32_16x16x32_bf16 v[118:121], v[176:179], v[192:195], v[118:121]
	v_mfma_f32_16x16x32_bf16 v[110:113], v[184:187], v[192:195], v[110:113]
	v_mfma_f32_16x16x32_bf16 v[102:105], v[176:179], v[200:203], v[102:105]
	v_mfma_f32_16x16x32_bf16 v[94:97], v[184:187], v[200:203], v[94:97]
	v_mfma_f32_16x16x32_bf16 v[86:89], v[176:179], v[208:211], v[86:89]
	v_mfma_f32_16x16x32_bf16 v[78:81], v[184:187], v[208:211], v[78:81]
	v_mfma_f32_16x16x32_bf16 v[70:73], v[176:179], v[216:219], v[70:73]
	v_mfma_f32_16x16x32_bf16 v[66:69], v[184:187], v[216:219], v[66:69]
	v_mfma_f32_16x16x32_bf16 v[118:121], v[180:183], v[196:199], v[118:121]
	v_mfma_f32_16x16x32_bf16 v[110:113], v[188:191], v[196:199], v[110:113]
	v_mfma_f32_16x16x32_bf16 v[102:105], v[180:183], v[204:207], v[102:105]
	v_mfma_f32_16x16x32_bf16 v[94:97], v[188:191], v[204:207], v[94:97]
	v_mfma_f32_16x16x32_bf16 v[86:89], v[180:183], v[212:215], v[86:89]
	v_mfma_f32_16x16x32_bf16 v[78:81], v[188:191], v[212:215], v[78:81]
	v_mfma_f32_16x16x32_bf16 v[70:73], v[180:183], v[220:223], v[70:73]
	v_mfma_f32_16x16x32_bf16 v[66:69], v[188:191], v[220:223], v[66:69]
	s_setprio 0
	s_barrier
; #define PG8_STAGE_A(b, h, ptr, NX) do { if constexpr (Sched::GATHER) { unsigned gs_[2]; gs_[0] = ((NX) && last_) ? gN[h][0] : gA[h][0]; gs_[1] = ((NX) && last_) ? gN[h][1] : gA[h][1]; PG8_STAGE(PG8_SA(b, h), ptr, gs_); } \
;         else PG8_STAGE(PG8_SA(b, h), (ptr) + ((h) ? hstep : (size_t)0), voffA); } while (0)
; #define PG8_STAGE(bufoff, gbase, voff) do { _Pragma("unroll") for (int _i = 0; _i < 2; ++_i) \
;         __builtin_amdgcn_global_load_lds((const unsigned*)((const char*)(gbase) + (voff)[_i]), (PG8_LAS unsigned*)(lds + (bufoff) + ldsw + _i * 8192), 16, 0, 0); } while (0)
; #define PG8_LDA(dst, b, h) do { _Pragma("unroll") for (int m = 0; m < 4; ++m) _Pragma("unroll") for (int k = 0; k < 2; ++k) dst[m][k] = *(const PG8_LAS bf16x8*)(lds + PG8_SA(b, h) + aoff + m * 2048 + k * 1024); } while (0)
; #define PG8_MMA(ai, bj, At, Bt) do { __builtin_amdgcn_s_setprio(1); _Pragma("unroll") for (int m = 0; m < 4; ++m) _Pragma("unroll") for (int n = 0; n < 2; ++n) _Pragma("unroll") for (int k = 0; k < 2; ++k) \
;         acc[ai][bj][m][n] = __builtin_amdgcn_mfma_f32_16x16x32_bf16(Bt[n][k], At[m][k], acc[ai][bj][m][n], 0, 0, 0); __builtin_amdgcn_s_setprio(0); } while (0)
; #define PG8_WAIT_V(n) asm volatile("s_waitcnt vmcnt(" #n ")" ::: "memory")
; #define PG8_WAIT_L(n) asm volatile("s_waitcnt lgkmcnt(" #n ")" ::: "memory")
; #define PG8_BAR __builtin_amdgcn_s_barrier()
; #define PG8_SCHED __builtin_amdgcn_sched_barrier(0)
; __device__ __forceinline__ void rstd8(const float* SS, int rowb, int lane, float (&rs)[2][4]) {
;     ...
;     for (int ai = 0; ai < 2; ++ai)
; #pragma unroll
;         for (int m = 0; m < 4; ++m) p[ai][m] = *(const f32x4*)(SS + (size_t)(rowb + HALF * ai + 16 * m + (lane >> 2)) * 16 + 4 * (lane & 3));
;     asm volatile("" : "+v"(p[0][0]), "+v"(p[0][1]), "+v"(p[0][2]), "+v"(p[0][3]), "+v"(p[1][0]), "+v"(p[1][1]), "+v"(p[1][2]), "+v"(p[1][3]));
; template <class Epi, class Sched, bool ALIGN_EPI = false, bool SP2 = false>
; __device__ __forceinline__ void gemm_phase(PG8_LAS unsigned char* lds, const Gemm g, const Sched& S, const Epi& E, const bool skip_epi = false) {
;     ...
;             PG8_LDA(At, 1, 1); PG8_STAGE(PG8_SB(1, 0), b3, voffB); PG8_STAGE(PG8_SB(1, 1), b3 + hstep, voffB); PG8_STAGE_A(1, 0, a3, true);
;             PG8_WAIT_V(8); PG8_WAIT_L(0); PG8_BAR; PG8_MMA(1, 0, At, B0); PG8_MMA(1, 1, At, B1); PG8_BAR; PG8_SCHED;
	s_add_i32 s26, s59, s28
	v_lshl_add_u64 v[164:165], v[164:165], 0, s[8:9]
	s_mov_b32 m0, s26
	ds_read_b128 v[192:195], v172 offset:49152
	ds_read_b128 v[196:199], v172 offset:50176
	ds_read_b128 v[200:203], v172 offset:51200
	ds_read_b128 v[204:207], v172 offset:52224
	ds_read_b128 v[208:211], v172 offset:53248
	ds_read_b128 v[212:215], v172 offset:54272
	ds_read_b128 v[216:219], v172 offset:55296
	ds_read_b128 v[220:223], v172 offset:56320
	global_load_lds_dwordx4 v[164:165], off
	s_add_i32 m0, s26, 0x2000
	s_add_u32 s24, s24, 0x40080
	v_lshl_add_u64 v[164:165], v[224:225], 0, s[8:9]
	s_addc_u32 s25, s25, 0
	s_add_i32 s26, s60, s28
	global_load_lds_dwordx4 v[164:165], off
	v_lshl_add_u64 v[164:165], s[24:25], 0, v[134:135]
	s_mov_b32 m0, s26
	s_nop 0
	global_load_lds_dwordx4 v[164:165], off
	v_lshl_add_u64 v[164:165], s[24:25], 0, v[130:131]
	s_add_i32 m0, s26, 0x2000
	s_nop 0
	global_load_lds_dwordx4 v[164:165], off
	v_lshl_add_u64 v[164:165], v[226:227], 0, s[8:9]
	s_mov_b32 m0, s37
	s_nop 0
	global_load_lds_dwordx4 v[164:165], off
	v_lshl_add_u64 v[164:165], v[230:231], 0, s[8:9]
	s_mov_b32 m0, s38
	s_nop 0
	global_load_lds_dwordx4 v[164:165], off
	s_waitcnt vmcnt(8)
	s_waitcnt lgkmcnt(0)
	s_barrier
	s_setprio 3
	s_waitcnt lgkmcnt(0)
	v_mfma_f32_16x16x32_bf16 v[62:65], v[148:151], v[192:195], v[62:65]
	v_mfma_f32_16x16x32_bf16 v[58:61], v[156:159], v[192:195], v[58:61]
	v_mfma_f32_16x16x32_bf16 v[50:53], v[148:151], v[200:203], v[50:53]
	v_mfma_f32_16x16x32_bf16 v[42:45], v[156:159], v[200:203], v[42:45]
	v_mfma_f32_16x16x32_bf16 v[34:37], v[148:151], v[208:211], v[34:37]
	v_mfma_f32_16x16x32_bf16 v[26:29], v[156:159], v[208:211], v[26:29]
	v_mfma_f32_16x16x32_bf16 v[18:21], v[148:151], v[216:219], v[18:21]
	v_mfma_f32_16x16x32_bf16 v[10:13], v[156:159], v[216:219], v[10:13]
	v_mfma_f32_16x16x32_bf16 v[62:65], v[152:155], v[196:199], v[62:65]
	v_mfma_f32_16x16x32_bf16 v[58:61], v[160:163], v[196:199], v[58:61]
	v_mfma_f32_16x16x32_bf16 v[50:53], v[152:155], v[204:207], v[50:53]
	v_mfma_f32_16x16x32_bf16 v[42:45], v[160:163], v[204:207], v[42:45]
	v_mfma_f32_16x16x32_bf16 v[34:37], v[152:155], v[212:215], v[34:37]
	v_mfma_f32_16x16x32_bf16 v[26:29], v[160:163], v[212:215], v[26:29]
	v_mfma_f32_16x16x32_bf16 v[18:21], v[152:155], v[220:223], v[18:21]
	v_mfma_f32_16x16x32_bf16 v[10:13], v[160:163], v[220:223], v[10:13]
	s_setprio 0
	s_setprio 3
	v_mfma_f32_16x16x32_bf16 v[54:57], v[176:179], v[192:195], v[54:57]
	v_mfma_f32_16x16x32_bf16 v[46:49], v[184:187], v[192:195], v[46:49]
	v_mfma_f32_16x16x32_bf16 v[38:41], v[176:179], v[200:203], v[38:41]
	v_mfma_f32_16x16x32_bf16 v[30:33], v[184:187], v[200:203], v[30:33]
	v_mfma_f32_16x16x32_bf16 v[22:25], v[176:179], v[208:211], v[22:25]
	v_mfma_f32_16x16x32_bf16 v[14:17], v[184:187], v[208:211], v[14:17]
	v_mfma_f32_16x16x32_bf16 v[6:9], v[176:179], v[216:219], v[6:9]
	v_mfma_f32_16x16x32_bf16 v[2:5], v[184:187], v[216:219], v[2:5]
	v_mfma_f32_16x16x32_bf16 v[54:57], v[180:183], v[196:199], v[54:57]
	v_mfma_f32_16x16x32_bf16 v[46:49], v[188:191], v[196:199], v[46:49]
	v_mfma_f32_16x16x32_bf16 v[38:41], v[180:183], v[204:207], v[38:41]
	v_mfma_f32_16x16x32_bf16 v[30:33], v[188:191], v[204:207], v[30:33]
	v_mfma_f32_16x16x32_bf16 v[22:25], v[180:183], v[212:215], v[22:25]
	v_mfma_f32_16x16x32_bf16 v[14:17], v[188:191], v[212:215], v[14:17]
	v_mfma_f32_16x16x32_bf16 v[6:9], v[180:183], v[220:223], v[6:9]
	v_mfma_f32_16x16x32_bf16 v[2:5], v[188:191], v[220:223], v[2:5]
	s_setprio 0
	s_barrier
	s_add_i32 s58, s58, 2
	s_add_u32 s22, s22, 0x100
	s_addc_u32 s23, s23, 0
	s_add_u32 s56, s56, 0x100
	s_addc_u32 s57, s57, 0
	s_cmp_gt_u32 s58, 13
	s_cbranch_scc0 .LBB0_944
	v_lshl_add_u32 v164, s20, 8, v167
	v_ashrrev_i32_e32 v165, 31, v164
	v_lshlrev_b64 v[148:149], 6, v[164:165]
	v_lshl_add_u64 v[148:149], v[138:139], 0, v[148:149]
	v_add_co_u32_e32 v150, vcc, 0x2000, v148
	v_addc_co_u32_e32 v151, vcc, 0, v149, vcc
	global_load_dwordx4 v[176:179], v[148:149], off
	global_load_dwordx4 v[180:183], v[148:149], off offset:1024
	global_load_dwordx4 v[184:187], v[148:149], off offset:2048
	global_load_dwordx4 v[188:191], v[148:149], off offset:3072
	global_load_dwordx4 v[192:195], v[150:151], off
	global_load_dwordx4 v[196:199], v[150:151], off offset:1024
	global_load_dwordx4 v[200:203], v[150:151], off offset:2048
	global_load_dwordx4 v[204:207], v[150:151], off offset:3072
	s_and_b64 vcc, exec, s[10:11]
	s_cbranch_vccz .LBB0_947
	s_barrier

; #define PG8_STAGE_A(b, h, ptr, NX) do { if constexpr (Sched::GATHER) { unsigned gs_[2]; gs_[0] = ((NX) && last_) ? gN[h][0] : gA[h][0]; gs_[1] = ((NX) && last_) ? gN[h][1] : gA[h][1]; PG8_STAGE(PG8_SA(b, h), ptr, gs_); } \
;         else PG8_STAGE(PG8_SA(b, h), (ptr) + ((h) ? hstep : (size_t)0), voffA); } while (0)
; #define PG8_STAGE(bufoff, gbase, voff) do { _Pragma("unroll") for (int _i = 0; _i < 2; ++_i) \
;         __builtin_amdgcn_global_load_lds((const unsigned*)((const char*)(gbase) + (voff)[_i]), (PG8_LAS unsigned*)(lds + (bufoff) + ldsw + _i * 8192), 16, 0, 0); } while (0)
; #define PG8_LDA(dst, b, h) do { _Pragma("unroll") for (int m = 0; m < 4; ++m) _Pragma("unroll") for (int k = 0; k < 2; ++k) dst[m][k] = *(const PG8_LAS bf16x8*)(lds + PG8_SA(b, h) + aoff + m * 2048 + k * 1024); } while (0)
; #define PG8_LDB(dst, b, h) do { _Pragma("unroll") for (int n = 0; n < 2; ++n) _Pragma("unroll") for (int k = 0; k < 2; ++k) dst[n][k] = *(const PG8_LAS bf16x8*)(lds + PG8_SB(b, h) + boff + n * 2048 + k * 1024); } while (0)
; #define PG8_WAIT_V(n) asm volatile("s_waitcnt vmcnt(" #n ")" ::: "memory")
; template <class Epi, class Sched, bool ALIGN_EPI = false, bool SP2 = false>
; __device__ __forceinline__ void gemm_phase(PG8_LAS unsigned char* lds, const Gemm g, const Sched& S, const Epi& E, const bool skip_epi = false) {
;     ...
;         const char* nA = has_next ? (const char*)g.A + (size_t)nxt.pm * pmstepA + nxt.ko : cA; const char* nB = has_next ? (const char*)g.Bt + (size_t)nxt.pn * tstep + nxt.ko : cB;
;         for (int t = 0; t < nt; t += 2) {
;             const bool last = (t == nt - 2); last_ = last && has_next;
;             const char* a1 = cA + (size_t)(t + 1) * kstep;
;             const char* a2 = last ? nA : cA + (size_t)(t + 2) * kstep; const char* b2 = last ? nB : cB + (size_t)(t + 2) * kstep;
;             const char* a3 = a2 + kstep; const char* b3 = b2 + kstep;
;             if (last && has_next) S.a_ready(nxt);
;             if constexpr (SP2) {
;             PG8_LDB(B0, 0, 0); PG8_LDB(B1, 0, 1); PG8_SCHED; PG8_LDA(At, 0, 0); PG8_STAGE_A(1, 1, a1, false);
;             PG8_WAIT_V(8); PG8_WAIT_L(0); PG8_BAR; PG8_MMA(0, 0, At, B0); PG8_MMA(0, 1, At, B1); PG8_BAR; PG8_SCHED;
;             PG8_LDA(At, 0, 1); PG8_STAGE(PG8_SB(0, 0), b2, voffB); PG8_STAGE(PG8_SB(0, 1), b2 + hstep, voffB); PG8_STAGE_A(0, 0, a2, true);
.LBB0_1323:
	s_ashr_i32 s25, s24, 31
	s_lshl_b64 s[26:27], s[24:25], 19
	s_add_u32 s26, s46, s26
	s_addc_u32 s27, s47, s27
	s_and_b64 s[28:29], s[6:7], exec
	s_cselect_b32 s25, s27, s35
	s_cselect_b32 s31, s26, s34
	s_ashr_i32 s23, s22, 31
	s_lshl_b64 s[28:29], s[22:23], 19
	s_add_u32 s28, s2, s28
	s_addc_u32 s29, s3, s29
	s_and_b64 s[38:39], s[6:7], exec
	s_cselect_b32 s23, s29, s37
	s_cselect_b32 s60, s28, s36
	s_add_u32 s34, s34, 0x40080
	s_addc_u32 s35, s35, 0
	s_add_u32 s61, s36, 0x100
	s_addc_u32 s62, s37, 0
	s_mov_b32 s63, -2
	s_waitcnt vmcnt(0)
	s_waitcnt lgkmcnt(0)
	ds_read_b128 v[98:101], v225
	ds_read_b128 v[110:113], v225 offset:1024
	ds_read_b128 v[122:125], v225 offset:2048
	ds_read_b128 v[130:133], v225 offset:3072
	ds_read_b128 v[146:149], v226
	ds_read_b128 v[150:153], v226 offset:1024
	ds_read_b128 v[154:157], v226 offset:2048
	ds_read_b128 v[158:161], v226 offset:3072
	s_add_u32 s36, s34, 0xfffc0080
	s_addc_u32 s37, s35, -1
	s_cmp_eq_u32 s63, 12
	s_cselect_b32 s39, s25, s37
	s_cselect_b32 s38, s31, s36
	s_cselect_b32 s37, s23, s62
	s_cselect_b32 s36, s60, s61
	v_lshl_add_u64 v[210:211], s[34:35], 0, v[194:195]
	s_add_i32 m0, s41, 0xc000
	ds_read_b128 v[162:165], v227
	ds_read_b128 v[166:169], v227 offset:1024
	ds_read_b128 v[170:173], v227 offset:2048
	ds_read_b128 v[174:177], v227 offset:3072
	ds_read_b128 v[178:181], v227 offset:4096
	ds_read_b128 v[182:185], v227 offset:5120
	ds_read_b128 v[202:205], v227 offset:6144
	ds_read_b128 v[206:209], v227 offset:7168
	global_load_lds_dwordx4 v[210:211], off
	v_lshl_add_u64 v[210:211], s[34:35], 0, v[196:197]
	s_add_i32 m0, s41, 0xe000
	s_nop 0
	global_load_lds_dwordx4 v[210:211], off
	s_waitcnt vmcnt(8)
	s_waitcnt lgkmcnt(0)
	s_barrier
	s_setprio 3
	s_waitcnt lgkmcnt(0)
	v_mfma_f32_16x16x32_bf16 v[142:145], v[98:101], v[162:165], 0
	v_mfma_f32_16x16x32_bf16 v[138:141], v[122:125], v[162:165], 0
	v_mfma_f32_16x16x32_bf16 v[118:121], v[98:101], v[170:173], 0
	v_mfma_f32_16x16x32_bf16 v[114:117], v[122:125], v[170:173], 0
	v_mfma_f32_16x16x32_bf16 v[94:97], v[98:101], v[178:181], 0
	v_mfma_f32_16x16x32_bf16 v[90:93], v[122:125], v[178:181], 0
	v_mfma_f32_16x16x32_bf16 v[78:81], v[98:101], v[202:205], 0
	v_mfma_f32_16x16x32_bf16 v[74:77], v[122:125], v[202:205], 0
	v_mfma_f32_16x16x32_bf16 v[142:145], v[110:113], v[166:169], v[142:145]
	v_mfma_f32_16x16x32_bf16 v[138:141], v[130:133], v[166:169], v[138:141]
	v_mfma_f32_16x16x32_bf16 v[118:121], v[110:113], v[174:177], v[118:121]
	v_mfma_f32_16x16x32_bf16 v[114:117], v[130:133], v[174:177], v[114:117]
	v_mfma_f32_16x16x32_bf16 v[94:97], v[110:113], v[182:185], v[94:97]
	v_mfma_f32_16x16x32_bf16 v[90:93], v[130:133], v[182:185], v[90:93]
	v_mfma_f32_16x16x32_bf16 v[78:81], v[110:113], v[206:209], v[78:81]
	v_mfma_f32_16x16x32_bf16 v[74:77], v[130:133], v[206:209], v[74:77]
	s_setprio 0
	s_setprio 3
	v_mfma_f32_16x16x32_bf16 v[134:137], v[146:149], v[162:165], 0
	v_mfma_f32_16x16x32_bf16 v[126:129], v[154:157], v[162:165], 0
	v_mfma_f32_16x16x32_bf16 v[106:109], v[146:149], v[170:173], 0
	v_mfma_f32_16x16x32_bf16 v[102:105], v[154:157], v[170:173], 0
	v_mfma_f32_16x16x32_bf16 v[86:89], v[146:149], v[178:181], 0
	v_mfma_f32_16x16x32_bf16 v[82:85], v[154:157], v[178:181], 0
	v_mfma_f32_16x16x32_bf16 v[70:73], v[146:149], v[202:205], 0
	v_mfma_f32_16x16x32_bf16 v[66:69], v[154:157], v[202:205], 0
	v_mfma_f32_16x16x32_bf16 v[134:137], v[150:153], v[166:169], v[134:137]
	v_mfma_f32_16x16x32_bf16 v[126:129], v[158:161], v[166:169], v[126:129]
	v_mfma_f32_16x16x32_bf16 v[106:109], v[150:153], v[174:177], v[106:109]
	v_mfma_f32_16x16x32_bf16 v[102:105], v[158:161], v[174:177], v[102:105]
	v_mfma_f32_16x16x32_bf16 v[86:89], v[150:153], v[182:185], v[86:89]
	v_mfma_f32_16x16x32_bf16 v[82:85], v[158:161], v[182:185], v[82:85]
	v_mfma_f32_16x16x32_bf16 v[70:73], v[150:153], v[206:209], v[70:73]
	v_mfma_f32_16x16x32_bf16 v[66:69], v[158:161], v[206:209], v[66:69]
	s_setprio 0
	s_barrier
	s_add_i32 s64, s57, s40
	v_lshl_add_u64 v[210:211], s[36:37], 0, v[188:189]
	s_mov_b32 m0, s64
	ds_read_b128 v[162:165], v227 offset:16384
	ds_read_b128 v[166:169], v227 offset:17408
	ds_read_b128 v[170:173], v227 offset:18432
	ds_read_b128 v[174:177], v227 offset:19456
	ds_read_b128 v[178:181], v227 offset:20480
	ds_read_b128 v[182:185], v227 offset:21504
	ds_read_b128 v[202:205], v227 offset:22528
	ds_read_b128 v[206:209], v227 offset:23552
	global_load_lds_dwordx4 v[210:211], off
	s_add_i32 m0, s64, 0x2000
	s_add_u32 s64, s36, 0x40000
	v_lshl_add_u64 v[212:213], s[36:37], 0, v[192:193]
	s_addc_u32 s65, s37, 0
	s_add_i32 s66, s58, s40
	global_load_lds_dwordx4 v[212:213], off
	v_lshl_add_u64 v[214:215], s[64:65], 0, v[188:189]
	s_mov_b32 m0, s66
	v_lshl_add_u64 v[216:217], s[38:39], 0, v[190:191]
	global_load_lds_dwordx4 v[214:215], off
	v_lshl_add_u64 v[214:215], s[64:65], 0, v[192:193]
	s_add_i32 m0, s66, 0x2000
	s_nop 0
	global_load_lds_dwordx4 v[214:215], off
	v_lshl_add_u64 v[214:215], s[38:39], 0, v[186:187]
	s_mov_b32 m0, s41
	s_nop 0
	global_load_lds_dwordx4 v[214:215], off
	s_mov_b32 m0, s44
	s_nop 0
	global_load_lds_dwordx4 v[216:217], off
	s_waitcnt vmcnt(8)
	s_waitcnt lgkmcnt(0)
	s_barrier
; #define PG8_STAGE_A(b, h, ptr, NX) do { if constexpr (Sched::GATHER) { unsigned gs_[2]; gs_[0] = ((NX) && last_) ? gN[h][0] : gA[h][0]; gs_[1] = ((NX) && last_) ? gN[h][1] : gA[h][1]; PG8_STAGE(PG8_SA(b, h), ptr, gs_); } \
;         else PG8_STAGE(PG8_SA(b, h), (ptr) + ((h) ? hstep : (size_t)0), voffA); } while (0)
; #define PG8_LDA(dst, b, h) do { _Pragma("unroll") for (int m = 0; m < 4; ++m) _Pragma("unroll") for (int k = 0; k < 2; ++k) dst[m][k] = *(const PG8_LAS bf16x8*)(lds + PG8_SA(b, h) + aoff + m * 2048 + k * 1024); } while (0)
; #define PG8_LDB(dst, b, h) do { _Pragma("unroll") for (int n = 0; n < 2; ++n) _Pragma("unroll") for (int k = 0; k < 2; ++k) dst[n][k] = *(const PG8_LAS bf16x8*)(lds + PG8_SB(b, h) + boff + n * 2048 + k * 1024); } while (0)
; #define PG8_MMA(ai, bj, At, Bt) do { __builtin_amdgcn_s_setprio(1); _Pragma("unroll") for (int m = 0; m < 4; ++m) _Pragma("unroll") for (int n = 0; n < 2; ++n) _Pragma("unroll") for (int k = 0; k < 2; ++k) \
;         acc[ai][bj][m][n] = __builtin_amdgcn_mfma_f32_16x16x32_bf16(Bt[n][k], At[m][k], acc[ai][bj][m][n], 0, 0, 0); __builtin_amdgcn_s_setprio(0); } while (0)
; #define PG8_WAIT_V(n) asm volatile("s_waitcnt vmcnt(" #n ")" ::: "memory")
; #define PG8_WAIT_L(n) asm volatile("s_waitcnt lgkmcnt(" #n ")" ::: "memory")
; #define PG8_BAR __builtin_amdgcn_s_barrier()
; #define PG8_SCHED __builtin_amdgcn_sched_barrier(0)
; template <class Epi, class Sched, bool ALIGN_EPI = false, bool SP2 = false>
; __device__ __forceinline__ void gemm_phase(PG8_LAS unsigned char* lds, const Gemm g, const Sched& S, const Epi& E, const bool skip_epi = false) {
;     ...
;             PG8_WAIT_V(8); PG8_WAIT_L(0); PG8_BAR; PG8_MMA(1, 0, At, B0); PG8_MMA(1, 1, At, B1); PG8_BAR; PG8_SCHED;
;             PG8_LDB(B0, 1, 0); PG8_LDB(B1, 1, 1); PG8_SCHED; PG8_LDA(At, 1, 0); PG8_STAGE_A(0, 1, a2, true);
;             PG8_WAIT_V(8); PG8_WAIT_L(0); PG8_BAR; PG8_MMA(0, 0, At, B0); PG8_MMA(0, 1, At, B1); PG8_BAR; PG8_SCHED;
	s_setprio 3
	s_waitcnt lgkmcnt(0)
	v_mfma_f32_16x16x32_bf16 v[62:65], v[98:101], v[162:165], 0
	v_mfma_f32_16x16x32_bf16 v[58:61], v[122:125], v[162:165], 0
	v_mfma_f32_16x16x32_bf16 v[46:49], v[98:101], v[170:173], 0
	v_mfma_f32_16x16x32_bf16 v[42:45], v[122:125], v[170:173], 0
	v_mfma_f32_16x16x32_bf16 v[30:33], v[98:101], v[178:181], 0
	v_mfma_f32_16x16x32_bf16 v[26:29], v[122:125], v[178:181], 0
	v_mfma_f32_16x16x32_bf16 v[14:17], v[98:101], v[202:205], 0
	v_mfma_f32_16x16x32_bf16 v[10:13], v[122:125], v[202:205], 0
	v_mfma_f32_16x16x32_bf16 v[62:65], v[110:113], v[166:169], v[62:65]
	v_mfma_f32_16x16x32_bf16 v[58:61], v[130:133], v[166:169], v[58:61]
	v_mfma_f32_16x16x32_bf16 v[46:49], v[110:113], v[174:177], v[46:49]
	v_mfma_f32_16x16x32_bf16 v[42:45], v[130:133], v[174:177], v[42:45]
	v_mfma_f32_16x16x32_bf16 v[30:33], v[110:113], v[182:185], v[30:33]
	v_mfma_f32_16x16x32_bf16 v[26:29], v[130:133], v[182:185], v[26:29]
	v_mfma_f32_16x16x32_bf16 v[14:17], v[110:113], v[206:209], v[14:17]
	v_mfma_f32_16x16x32_bf16 v[10:13], v[130:133], v[206:209], v[10:13]
	s_setprio 0
	s_setprio 3
	v_mfma_f32_16x16x32_bf16 v[54:57], v[146:149], v[162:165], 0
	v_mfma_f32_16x16x32_bf16 v[50:53], v[154:157], v[162:165], 0
	v_mfma_f32_16x16x32_bf16 v[38:41], v[146:149], v[170:173], 0
	v_mfma_f32_16x16x32_bf16 v[34:37], v[154:157], v[170:173], 0
	v_mfma_f32_16x16x32_bf16 v[22:25], v[146:149], v[178:181], 0
	v_mfma_f32_16x16x32_bf16 v[18:21], v[154:157], v[178:181], 0
	v_mfma_f32_16x16x32_bf16 v[6:9], v[146:149], v[202:205], 0
	v_mfma_f32_16x16x32_bf16 v[2:5], v[154:157], v[202:205], 0
	v_mfma_f32_16x16x32_bf16 v[54:57], v[150:153], v[166:169], v[54:57]
	v_mfma_f32_16x16x32_bf16 v[50:53], v[158:161], v[166:169], v[50:53]
	v_mfma_f32_16x16x32_bf16 v[38:41], v[150:153], v[174:177], v[38:41]
	v_mfma_f32_16x16x32_bf16 v[34:37], v[158:161], v[174:177], v[34:37]
	v_mfma_f32_16x16x32_bf16 v[22:25], v[150:153], v[182:185], v[22:25]
	v_mfma_f32_16x16x32_bf16 v[18:21], v[158:161], v[182:185], v[18:21]
	v_mfma_f32_16x16x32_bf16 v[6:9], v[150:153], v[206:209], v[6:9]
	v_mfma_f32_16x16x32_bf16 v[2:5], v[158:161], v[206:209], v[2:5]
	s_setprio 0
	s_barrier
	s_add_i32 s64, 0, 0x18000
	s_add_i32 s65, 0, 0x1c000
	v_add_u32_e32 v130, s64, v220
	v_add_u32_e32 v158, s65, v220
	ds_read_b128 v[98:101], v130
	ds_read_b128 v[110:113], v130 offset:1024
	ds_read_b128 v[122:125], v130 offset:2048
	ds_read_b128 v[130:133], v130 offset:3072
	ds_read_b128 v[146:149], v158
	ds_read_b128 v[150:153], v158 offset:1024
	ds_read_b128 v[154:157], v158 offset:2048
	ds_read_b128 v[158:161], v158 offset:3072
	s_add_u32 s38, s38, 0x40000
	s_addc_u32 s39, s39, 0
	s_mov_b32 m0, s45
	v_lshl_add_u64 v[218:219], s[38:39], 0, v[186:187]
	ds_read_b128 v[162:165], v227 offset:32768
	ds_read_b128 v[166:169], v227 offset:33792
	ds_read_b128 v[170:173], v227 offset:34816
	ds_read_b128 v[174:177], v227 offset:35840
	ds_read_b128 v[178:181], v227 offset:36864
	ds_read_b128 v[182:185], v227 offset:37888
	ds_read_b128 v[202:205], v227 offset:38912
	ds_read_b128 v[206:209], v227 offset:39936
	global_load_lds_dwordx4 v[218:219], off
	v_lshl_add_u64 v[218:219], s[38:39], 0, v[190:191]
	s_mov_b32 m0, s48
	s_nop 0
	global_load_lds_dwordx4 v[218:219], off
	s_waitcnt vmcnt(8)
	s_waitcnt lgkmcnt(0)
	s_barrier
	s_setprio 3
	s_waitcnt lgkmcnt(0)
	v_mfma_f32_16x16x32_bf16 v[142:145], v[98:101], v[162:165], v[142:145]
	v_mfma_f32_16x16x32_bf16 v[138:141], v[122:125], v[162:165], v[138:141]
	v_mfma_f32_16x16x32_bf16 v[118:121], v[98:101], v[170:173], v[118:121]
	v_mfma_f32_16x16x32_bf16 v[114:117], v[122:125], v[170:173], v[114:117]
	v_mfma_f32_16x16x32_bf16 v[94:97], v[98:101], v[178:181], v[94:97]
	v_mfma_f32_16x16x32_bf16 v[90:93], v[122:125], v[178:181], v[90:93]
	v_mfma_f32_16x16x32_bf16 v[78:81], v[98:101], v[202:205], v[78:81]
	v_mfma_f32_16x16x32_bf16 v[74:77], v[122:125], v[202:205], v[74:77]
	v_mfma_f32_16x16x32_bf16 v[142:145], v[110:113], v[166:169], v[142:145]
	v_mfma_f32_16x16x32_bf16 v[138:141], v[130:133], v[166:169], v[138:141]
	v_mfma_f32_16x16x32_bf16 v[118:121], v[110:113], v[174:177], v[118:121]
	v_mfma_f32_16x16x32_bf16 v[114:117], v[130:133], v[174:177], v[114:117]
	v_mfma_f32_16x16x32_bf16 v[94:97], v[110:113], v[182:185], v[94:97]
	v_mfma_f32_16x16x32_bf16 v[90:93], v[130:133], v[182:185], v[90:93]
	v_mfma_f32_16x16x32_bf16 v[78:81], v[110:113], v[206:209], v[78:81]
	v_mfma_f32_16x16x32_bf16 v[74:77], v[130:133], v[206:209], v[74:77]
	s_setprio 0
	s_setprio 3
	v_mfma_f32_16x16x32_bf16 v[134:137], v[146:149], v[162:165], v[134:137]
	v_mfma_f32_16x16x32_bf16 v[126:129], v[154:157], v[162:165], v[126:129]
	v_mfma_f32_16x16x32_bf16 v[106:109], v[146:149], v[170:173], v[106:109]
	v_mfma_f32_16x16x32_bf16 v[102:105], v[154:157], v[170:173], v[102:105]
	v_mfma_f32_16x16x32_bf16 v[86:89], v[146:149], v[178:181], v[86:89]
	v_mfma_f32_16x16x32_bf16 v[82:85], v[154:157], v[178:181], v[82:85]
	v_mfma_f32_16x16x32_bf16 v[70:73], v[146:149], v[202:205], v[70:73]
	v_mfma_f32_16x16x32_bf16 v[66:69], v[154:157], v[202:205], v[66:69]
	v_mfma_f32_16x16x32_bf16 v[134:137], v[150:153], v[166:169], v[134:137]
	v_mfma_f32_16x16x32_bf16 v[126:129], v[158:161], v[166:169], v[126:129]
	v_mfma_f32_16x16x32_bf16 v[106:109], v[150:153], v[174:177], v[106:109]
	v_mfma_f32_16x16x32_bf16 v[102:105], v[158:161], v[174:177], v[102:105]
	v_mfma_f32_16x16x32_bf16 v[86:89], v[150:153], v[182:185], v[86:89]
	v_mfma_f32_16x16x32_bf16 v[82:85], v[158:161], v[182:185], v[82:85]
	v_mfma_f32_16x16x32_bf16 v[70:73], v[150:153], v[206:209], v[70:73]
	v_mfma_f32_16x16x32_bf16 v[66:69], v[158:161], v[206:209], v[66:69]
	s_setprio 0
	s_barrier
; #define PG8_STAGE_A(b, h, ptr, NX) do { if constexpr (Sched::GATHER) { unsigned gs_[2]; gs_[0] = ((NX) && last_) ? gN[h][0] : gA[h][0]; gs_[1] = ((NX) && last_) ? gN[h][1] : gA[h][1]; PG8_STAGE(PG8_SA(b, h), ptr, gs_); } \
;         else PG8_STAGE(PG8_SA(b, h), (ptr) + ((h) ? hstep : (size_t)0), voffA); } while (0)
; #define PG8_STAGE(bufoff, gbase, voff) do { _Pragma("unroll") for (int _i = 0; _i < 2; ++_i) \
;         __builtin_amdgcn_global_load_lds((const unsigned*)((const char*)(gbase) + (voff)[_i]), (PG8_LAS unsigned*)(lds + (bufoff) + ldsw + _i * 8192), 16, 0, 0); } while (0)
; #define PG8_LDA(dst, b, h) do { _Pragma("unroll") for (int m = 0; m < 4; ++m) _Pragma("unroll") for (int k = 0; k < 2; ++k) dst[m][k] = *(const PG8_LAS bf16x8*)(lds + PG8_SA(b, h) + aoff + m * 2048 + k * 1024); } while (0)
; #define PG8_LDB(dst, b, h) do { _Pragma("unroll") for (int n = 0; n < 2; ++n) _Pragma("unroll") for (int k = 0; k < 2; ++k) dst[n][k] = *(const PG8_LAS bf16x8*)(lds + PG8_SB(b, h) + boff + n * 2048 + k * 1024); } while (0)
; #define PG8_WAIT_V(n) asm volatile("s_waitcnt vmcnt(" #n ")" ::: "memory")
; #define PG8_BAR __builtin_amdgcn_s_barrier()
; template <class Epi, class Sched, bool ALIGN_EPI = false, bool SP2 = false>
; __device__ __forceinline__ void gemm_phase(PG8_LAS unsigned char* lds, const Gemm g, const Sched& S, const Epi& E, const bool skip_epi = false) {
;     ...
;             PG8_LDB(B0, 0, 0); PG8_LDB(B1, 0, 1); PG8_SCHED; PG8_LDA(At, 0, 0); PG8_STAGE_A(1, 1, a1, false);
;             PG8_WAIT_V(8); PG8_WAIT_L(0); PG8_BAR; PG8_MMA(0, 0, At, B0); PG8_MMA(0, 1, At, B1); PG8_BAR; PG8_SCHED;
;             PG8_LDA(At, 0, 1); PG8_STAGE(PG8_SB(0, 0), b2, voffB); PG8_STAGE(PG8_SB(0, 1), b2 + hstep, voffB); PG8_STAGE_A(0, 0, a2, true);
;             PG8_WAIT_V(8); PG8_WAIT_L(0); PG8_BAR; PG8_MMA(1, 0, At, B0); PG8_MMA(1, 1, At, B1); PG8_BAR; PG8_SCHED;
;             PG8_LDB(B0, 1, 0); PG8_LDB(B1, 1, 1); PG8_SCHED; PG8_LDA(At, 1, 0); PG8_STAGE_A(0, 1, a2, true);
;             PG8_WAIT_V(8); PG8_WAIT_L(0); PG8_BAR; PG8_MMA(0, 0, At, B0); PG8_MMA(0, 1, At, B1); PG8_BAR; PG8_SCHED;
;             PG8_LDA(At, 1, 1); PG8_STAGE(PG8_SB(1, 0), b3, voffB); PG8_STAGE(PG8_SB(1, 1), b3 + hstep, voffB); PG8_STAGE_A(1, 0, a3, true);
;             PG8_WAIT_V(8); PG8_WAIT_L(0); PG8_BAR; PG8_MMA(1, 0, At, B0); PG8_MMA(1, 1, At, B1); PG8_BAR; PG8_SCHED;
	s_add_i32 s38, s64, s40
	v_lshl_add_u64 v[210:211], v[210:211], 0, s[12:13]
	s_mov_b32 m0, s38
	ds_read_b128 v[162:165], v227 offset:49152
	ds_read_b128 v[166:169], v227 offset:50176
	ds_read_b128 v[170:173], v227 offset:51200
	ds_read_b128 v[174:177], v227 offset:52224
	ds_read_b128 v[178:181], v227 offset:53248
	ds_read_b128 v[182:185], v227 offset:54272
	ds_read_b128 v[202:205], v227 offset:55296
	ds_read_b128 v[206:209], v227 offset:56320
	global_load_lds_dwordx4 v[210:211], off
	s_add_i32 m0, s38, 0x2000
	s_add_u32 s36, s36, 0x40080
	v_lshl_add_u64 v[210:211], v[212:213], 0, s[12:13]
	s_addc_u32 s37, s37, 0
	s_add_i32 s38, s65, s40
	global_load_lds_dwordx4 v[210:211], off
	v_lshl_add_u64 v[210:211], s[36:37], 0, v[188:189]
	s_mov_b32 m0, s38
	s_nop 0
	global_load_lds_dwordx4 v[210:211], off
	v_lshl_add_u64 v[210:211], s[36:37], 0, v[192:193]
	s_add_i32 m0, s38, 0x2000
	s_nop 0
	global_load_lds_dwordx4 v[210:211], off
	v_lshl_add_u64 v[210:211], v[214:215], 0, s[12:13]
	s_mov_b32 m0, s53
	s_nop 0
	global_load_lds_dwordx4 v[210:211], off
	v_lshl_add_u64 v[210:211], v[216:217], 0, s[12:13]
	s_mov_b32 m0, s54
	s_nop 0
	global_load_lds_dwordx4 v[210:211], off
	s_waitcnt vmcnt(8)
	s_waitcnt lgkmcnt(0)
	s_barrier
	s_setprio 3
	s_waitcnt lgkmcnt(0)
	v_mfma_f32_16x16x32_bf16 v[62:65], v[98:101], v[162:165], v[62:65]
	v_mfma_f32_16x16x32_bf16 v[58:61], v[122:125], v[162:165], v[58:61]
	v_mfma_f32_16x16x32_bf16 v[46:49], v[98:101], v[170:173], v[46:49]
	v_mfma_f32_16x16x32_bf16 v[42:45], v[122:125], v[170:173], v[42:45]
	v_mfma_f32_16x16x32_bf16 v[30:33], v[98:101], v[178:181], v[30:33]
	v_mfma_f32_16x16x32_bf16 v[26:29], v[122:125], v[178:181], v[26:29]
	v_mfma_f32_16x16x32_bf16 v[14:17], v[98:101], v[202:205], v[14:17]
	v_mfma_f32_16x16x32_bf16 v[10:13], v[122:125], v[202:205], v[10:13]
	v_mfma_f32_16x16x32_bf16 v[62:65], v[110:113], v[166:169], v[62:65]
	v_mfma_f32_16x16x32_bf16 v[58:61], v[130:133], v[166:169], v[58:61]
	v_mfma_f32_16x16x32_bf16 v[46:49], v[110:113], v[174:177], v[46:49]
	v_mfma_f32_16x16x32_bf16 v[42:45], v[130:133], v[174:177], v[42:45]
	v_mfma_f32_16x16x32_bf16 v[30:33], v[110:113], v[182:185], v[30:33]
	v_mfma_f32_16x16x32_bf16 v[26:29], v[130:133], v[182:185], v[26:29]
	v_mfma_f32_16x16x32_bf16 v[14:17], v[110:113], v[206:209], v[14:17]
	v_mfma_f32_16x16x32_bf16 v[10:13], v[130:133], v[206:209], v[10:13]
	s_setprio 0
	s_setprio 3
	v_mfma_f32_16x16x32_bf16 v[54:57], v[146:149], v[162:165], v[54:57]
	v_mfma_f32_16x16x32_bf16 v[50:53], v[154:157], v[162:165], v[50:53]
	v_mfma_f32_16x16x32_bf16 v[38:41], v[146:149], v[170:173], v[38:41]
	v_mfma_f32_16x16x32_bf16 v[34:37], v[154:157], v[170:173], v[34:37]
	v_mfma_f32_16x16x32_bf16 v[22:25], v[146:149], v[178:181], v[22:25]
	v_mfma_f32_16x16x32_bf16 v[18:21], v[154:157], v[178:181], v[18:21]
	v_mfma_f32_16x16x32_bf16 v[6:9], v[146:149], v[202:205], v[6:9]
	v_mfma_f32_16x16x32_bf16 v[2:5], v[154:157], v[202:205], v[2:5]
	v_mfma_f32_16x16x32_bf16 v[54:57], v[150:153], v[166:169], v[54:57]
	v_mfma_f32_16x16x32_bf16 v[50:53], v[158:161], v[166:169], v[50:53]
	v_mfma_f32_16x16x32_bf16 v[38:41], v[150:153], v[174:177], v[38:41]
	v_mfma_f32_16x16x32_bf16 v[34:37], v[158:161], v[174:177], v[34:37]
	v_mfma_f32_16x16x32_bf16 v[22:25], v[150:153], v[182:185], v[22:25]
	v_mfma_f32_16x16x32_bf16 v[18:21], v[158:161], v[182:185], v[18:21]
	v_mfma_f32_16x16x32_bf16 v[6:9], v[150:153], v[206:209], v[6:9]
	v_mfma_f32_16x16x32_bf16 v[2:5], v[158:161], v[206:209], v[2:5]
	s_setprio 0
	s_barrier
	s_add_i32 s63, s63, 2
	s_add_u32 s34, s34, 0x100
	s_addc_u32 s35, s35, 0
	s_add_u32 s61, s61, 0x100
	s_addc_u32 s62, s62, 0
	s_cmp_gt_u32 s63, 13
.LBB0_1324:
	ds_read_b128 v[98:101], v225
	ds_read_b128 v[110:113], v225 offset:1024
	ds_read_b128 v[122:125], v225 offset:2048
	ds_read_b128 v[130:133], v225 offset:3072
	ds_read_b128 v[146:149], v226
	ds_read_b128 v[150:153], v226 offset:1024
	ds_read_b128 v[154:157], v226 offset:2048
	ds_read_b128 v[158:161], v226 offset:3072
	s_add_u32 s36, s34, 0xfffc0080
	s_addc_u32 s37, s35, -1
	s_cmp_eq_u32 s63, 12
	s_cselect_b32 s39, s25, s37
	s_cselect_b32 s38, s31, s36
	s_cselect_b32 s37, s23, s62
	s_cselect_b32 s36, s60, s61
	v_lshl_add_u64 v[210:211], s[34:35], 0, v[194:195]
	s_add_i32 m0, s41, 0xc000
	ds_read_b128 v[162:165], v227
	ds_read_b128 v[166:169], v227 offset:1024
	ds_read_b128 v[170:173], v227 offset:2048
	ds_read_b128 v[174:177], v227 offset:3072
	ds_read_b128 v[178:181], v227 offset:4096
	ds_read_b128 v[182:185], v227 offset:5120
	ds_read_b128 v[202:205], v227 offset:6144
	ds_read_b128 v[206:209], v227 offset:7168
	global_load_lds_dwordx4 v[210:211], off
	v_lshl_add_u64 v[210:211], s[34:35], 0, v[196:197]
	s_add_i32 m0, s41, 0xe000
	s_nop 0
	global_load_lds_dwordx4 v[210:211], off
	s_waitcnt vmcnt(8)
	s_waitcnt lgkmcnt(0)
	s_barrier
; #define PG8_STAGE_A(b, h, ptr, NX) do { if constexpr (Sched::GATHER) { unsigned gs_[2]; gs_[0] = ((NX) && last_) ? gN[h][0] : gA[h][0]; gs_[1] = ((NX) && last_) ? gN[h][1] : gA[h][1]; PG8_STAGE(PG8_SA(b, h), ptr, gs_); } \
;         else PG8_STAGE(PG8_SA(b, h), (ptr) + ((h) ? hstep : (size_t)0), voffA); } while (0)
; #define PG8_STAGE(bufoff, gbase, voff) do { _Pragma("unroll") for (int _i = 0; _i < 2; ++_i) \
;         __builtin_amdgcn_global_load_lds((const unsigned*)((const char*)(gbase) + (voff)[_i]), (PG8_LAS unsigned*)(lds + (bufoff) + ldsw + _i * 8192), 16, 0, 0); } while (0)
; #define PG8_LDA(dst, b, h) do { _Pragma("unroll") for (int m = 0; m < 4; ++m) _Pragma("unroll") for (int k = 0; k < 2; ++k) dst[m][k] = *(const PG8_LAS bf16x8*)(lds + PG8_SA(b, h) + aoff + m * 2048 + k * 1024); } while (0)
; #define PG8_MMA(ai, bj, At, Bt) do { __builtin_amdgcn_s_setprio(1); _Pragma("unroll") for (int m = 0; m < 4; ++m) _Pragma("unroll") for (int n = 0; n < 2; ++n) _Pragma("unroll") for (int k = 0; k < 2; ++k) \
;         acc[ai][bj][m][n] = __builtin_amdgcn_mfma_f32_16x16x32_bf16(Bt[n][k], At[m][k], acc[ai][bj][m][n], 0, 0, 0); __builtin_amdgcn_s_setprio(0); } while (0)
; #define PG8_WAIT_V(n) asm volatile("s_waitcnt vmcnt(" #n ")" ::: "memory")
; #define PG8_WAIT_L(n) asm volatile("s_waitcnt lgkmcnt(" #n ")" ::: "memory")
; #define PG8_BAR __builtin_amdgcn_s_barrier()
; #define PG8_SCHED __builtin_amdgcn_sched_barrier(0)
; template <class Epi, class Sched, bool ALIGN_EPI = false, bool SP2 = false>
; __device__ __forceinline__ void gemm_phase(PG8_LAS unsigned char* lds, const Gemm g, const Sched& S, const Epi& E, const bool skip_epi = false) {
;     ...
;             PG8_WAIT_V(8); PG8_WAIT_L(0); PG8_BAR; PG8_MMA(0, 0, At, B0); PG8_MMA(0, 1, At, B1); PG8_BAR; PG8_SCHED;
;             PG8_LDA(At, 0, 1); PG8_STAGE(PG8_SB(0, 0), b2, voffB); PG8_STAGE(PG8_SB(0, 1), b2 + hstep, voffB); PG8_STAGE_A(0, 0, a2, true);
;             PG8_WAIT_V(8); PG8_WAIT_L(0); PG8_BAR; PG8_MMA(1, 0, At, B0); PG8_MMA(1, 1, At, B1); PG8_BAR; PG8_SCHED;
	s_setprio 3
	s_waitcnt lgkmcnt(0)
	v_mfma_f32_16x16x32_bf16 v[142:145], v[98:101], v[162:165], v[142:145]
	v_mfma_f32_16x16x32_bf16 v[138:141], v[122:125], v[162:165], v[138:141]
	v_mfma_f32_16x16x32_bf16 v[118:121], v[98:101], v[170:173], v[118:121]
	v_mfma_f32_16x16x32_bf16 v[114:117], v[122:125], v[170:173], v[114:117]
	v_mfma_f32_16x16x32_bf16 v[94:97], v[98:101], v[178:181], v[94:97]
	v_mfma_f32_16x16x32_bf16 v[90:93], v[122:125], v[178:181], v[90:93]
	v_mfma_f32_16x16x32_bf16 v[78:81], v[98:101], v[202:205], v[78:81]
	v_mfma_f32_16x16x32_bf16 v[74:77], v[122:125], v[202:205], v[74:77]
	v_mfma_f32_16x16x32_bf16 v[142:145], v[110:113], v[166:169], v[142:145]
	v_mfma_f32_16x16x32_bf16 v[138:141], v[130:133], v[166:169], v[138:141]
	v_mfma_f32_16x16x32_bf16 v[118:121], v[110:113], v[174:177], v[118:121]
	v_mfma_f32_16x16x32_bf16 v[114:117], v[130:133], v[174:177], v[114:117]
	v_mfma_f32_16x16x32_bf16 v[94:97], v[110:113], v[182:185], v[94:97]
	v_mfma_f32_16x16x32_bf16 v[90:93], v[130:133], v[182:185], v[90:93]
	v_mfma_f32_16x16x32_bf16 v[78:81], v[110:113], v[206:209], v[78:81]
	v_mfma_f32_16x16x32_bf16 v[74:77], v[130:133], v[206:209], v[74:77]
	s_setprio 0
	s_setprio 3
	v_mfma_f32_16x16x32_bf16 v[134:137], v[146:149], v[162:165], v[134:137]
	v_mfma_f32_16x16x32_bf16 v[126:129], v[154:157], v[162:165], v[126:129]
	v_mfma_f32_16x16x32_bf16 v[106:109], v[146:149], v[170:173], v[106:109]
	v_mfma_f32_16x16x32_bf16 v[102:105], v[154:157], v[170:173], v[102:105]
	v_mfma_f32_16x16x32_bf16 v[86:89], v[146:149], v[178:181], v[86:89]
	v_mfma_f32_16x16x32_bf16 v[82:85], v[154:157], v[178:181], v[82:85]
	v_mfma_f32_16x16x32_bf16 v[70:73], v[146:149], v[202:205], v[70:73]
	v_mfma_f32_16x16x32_bf16 v[66:69], v[154:157], v[202:205], v[66:69]
	v_mfma_f32_16x16x32_bf16 v[134:137], v[150:153], v[166:169], v[134:137]
	v_mfma_f32_16x16x32_bf16 v[126:129], v[158:161], v[166:169], v[126:129]
	v_mfma_f32_16x16x32_bf16 v[106:109], v[150:153], v[174:177], v[106:109]
	v_mfma_f32_16x16x32_bf16 v[102:105], v[158:161], v[174:177], v[102:105]
	v_mfma_f32_16x16x32_bf16 v[86:89], v[150:153], v[182:185], v[86:89]
	v_mfma_f32_16x16x32_bf16 v[82:85], v[158:161], v[182:185], v[82:85]
	v_mfma_f32_16x16x32_bf16 v[70:73], v[150:153], v[206:209], v[70:73]
	v_mfma_f32_16x16x32_bf16 v[66:69], v[158:161], v[206:209], v[66:69]
	s_setprio 0
	s_barrier
	s_add_i32 s64, s57, s40
	v_lshl_add_u64 v[210:211], s[36:37], 0, v[188:189]
	s_mov_b32 m0, s64
	ds_read_b128 v[162:165], v227 offset:16384
	ds_read_b128 v[166:169], v227 offset:17408
	ds_read_b128 v[170:173], v227 offset:18432
	ds_read_b128 v[174:177], v227 offset:19456
	ds_read_b128 v[178:181], v227 offset:20480
	ds_read_b128 v[182:185], v227 offset:21504
	ds_read_b128 v[202:205], v227 offset:22528
	ds_read_b128 v[206:209], v227 offset:23552
	global_load_lds_dwordx4 v[210:211], off
	s_add_i32 m0, s64, 0x2000
	s_add_u32 s64, s36, 0x40000
	v_lshl_add_u64 v[212:213], s[36:37], 0, v[192:193]
	s_addc_u32 s65, s37, 0
	s_add_i32 s66, s58, s40
	global_load_lds_dwordx4 v[212:213], off
	v_lshl_add_u64 v[214:215], s[64:65], 0, v[188:189]
	s_mov_b32 m0, s66
	v_lshl_add_u64 v[216:217], s[38:39], 0, v[190:191]
	global_load_lds_dwordx4 v[214:215], off
	v_lshl_add_u64 v[214:215], s[64:65], 0, v[192:193]
	s_add_i32 m0, s66, 0x2000
	s_nop 0
	global_load_lds_dwordx4 v[214:215], off
	v_lshl_add_u64 v[214:215], s[38:39], 0, v[186:187]
	s_mov_b32 m0, s41
	s_nop 0
	global_load_lds_dwordx4 v[214:215], off
	s_mov_b32 m0, s44
	s_nop 0
	global_load_lds_dwordx4 v[216:217], off
	s_waitcnt vmcnt(8)
	s_waitcnt lgkmcnt(0)
	s_barrier
	s_setprio 3
	s_waitcnt lgkmcnt(0)
	v_mfma_f32_16x16x32_bf16 v[62:65], v[98:101], v[162:165], v[62:65]
	v_mfma_f32_16x16x32_bf16 v[58:61], v[122:125], v[162:165], v[58:61]
	v_mfma_f32_16x16x32_bf16 v[46:49], v[98:101], v[170:173], v[46:49]
	v_mfma_f32_16x16x32_bf16 v[42:45], v[122:125], v[170:173], v[42:45]
	v_mfma_f32_16x16x32_bf16 v[30:33], v[98:101], v[178:181], v[30:33]
	v_mfma_f32_16x16x32_bf16 v[26:29], v[122:125], v[178:181], v[26:29]
	v_mfma_f32_16x16x32_bf16 v[14:17], v[98:101], v[202:205], v[14:17]
	v_mfma_f32_16x16x32_bf16 v[10:13], v[122:125], v[202:205], v[10:13]
	v_mfma_f32_16x16x32_bf16 v[62:65], v[110:113], v[166:169], v[62:65]
	v_mfma_f32_16x16x32_bf16 v[58:61], v[130:133], v[166:169], v[58:61]
	v_mfma_f32_16x16x32_bf16 v[46:49], v[110:113], v[174:177], v[46:49]
	v_mfma_f32_16x16x32_bf16 v[42:45], v[130:133], v[174:177], v[42:45]
	v_mfma_f32_16x16x32_bf16 v[30:33], v[110:113], v[182:185], v[30:33]
	v_mfma_f32_16x16x32_bf16 v[26:29], v[130:133], v[182:185], v[26:29]
	v_mfma_f32_16x16x32_bf16 v[14:17], v[110:113], v[206:209], v[14:17]
	v_mfma_f32_16x16x32_bf16 v[10:13], v[130:133], v[206:209], v[10:13]
	s_setprio 0
	s_setprio 3
	v_mfma_f32_16x16x32_bf16 v[54:57], v[146:149], v[162:165], v[54:57]
	v_mfma_f32_16x16x32_bf16 v[50:53], v[154:157], v[162:165], v[50:53]
	v_mfma_f32_16x16x32_bf16 v[38:41], v[146:149], v[170:173], v[38:41]
	v_mfma_f32_16x16x32_bf16 v[34:37], v[154:157], v[170:173], v[34:37]
	v_mfma_f32_16x16x32_bf16 v[22:25], v[146:149], v[178:181], v[22:25]
	v_mfma_f32_16x16x32_bf16 v[18:21], v[154:157], v[178:181], v[18:21]
	v_mfma_f32_16x16x32_bf16 v[6:9], v[146:149], v[202:205], v[6:9]
	v_mfma_f32_16x16x32_bf16 v[2:5], v[154:157], v[202:205], v[2:5]
	v_mfma_f32_16x16x32_bf16 v[54:57], v[150:153], v[166:169], v[54:57]
	v_mfma_f32_16x16x32_bf16 v[50:53], v[158:161], v[166:169], v[50:53]
	v_mfma_f32_16x16x32_bf16 v[38:41], v[150:153], v[174:177], v[38:41]
	v_mfma_f32_16x16x32_bf16 v[34:37], v[158:161], v[174:177], v[34:37]
	v_mfma_f32_16x16x32_bf16 v[22:25], v[150:153], v[182:185], v[22:25]
	v_mfma_f32_16x16x32_bf16 v[18:21], v[158:161], v[182:185], v[18:21]
	v_mfma_f32_16x16x32_bf16 v[6:9], v[150:153], v[206:209], v[6:9]
	v_mfma_f32_16x16x32_bf16 v[2:5], v[158:161], v[206:209], v[2:5]
	s_setprio 0
	s_barrier
; #define PG8_STAGE_A(b, h, ptr, NX) do { if constexpr (Sched::GATHER) { unsigned gs_[2]; gs_[0] = ((NX) && last_) ? gN[h][0] : gA[h][0]; gs_[1] = ((NX) && last_) ? gN[h][1] : gA[h][1]; PG8_STAGE(PG8_SA(b, h), ptr, gs_); } \
;         else PG8_STAGE(PG8_SA(b, h), (ptr) + ((h) ? hstep : (size_t)0), voffA); } while (0)
; #define PG8_LDA(dst, b, h) do { _Pragma("unroll") for (int m = 0; m < 4; ++m) _Pragma("unroll") for (int k = 0; k < 2; ++k) dst[m][k] = *(const PG8_LAS bf16x8*)(lds + PG8_SA(b, h) + aoff + m * 2048 + k * 1024); } while (0)
; #define PG8_LDB(dst, b, h) do { _Pragma("unroll") for (int n = 0; n < 2; ++n) _Pragma("unroll") for (int k = 0; k < 2; ++k) dst[n][k] = *(const PG8_LAS bf16x8*)(lds + PG8_SB(b, h) + boff + n * 2048 + k * 1024); } while (0)
; #define PG8_MMA(ai, bj, At, Bt) do { __builtin_amdgcn_s_setprio(1); _Pragma("unroll") for (int m = 0; m < 4; ++m) _Pragma("unroll") for (int n = 0; n < 2; ++n) _Pragma("unroll") for (int k = 0; k < 2; ++k) \
;         acc[ai][bj][m][n] = __builtin_amdgcn_mfma_f32_16x16x32_bf16(Bt[n][k], At[m][k], acc[ai][bj][m][n], 0, 0, 0); __builtin_amdgcn_s_setprio(0); } while (0)
; #define PG8_WAIT_V(n) asm volatile("s_waitcnt vmcnt(" #n ")" ::: "memory")
; #define PG8_WAIT_L(n) asm volatile("s_waitcnt lgkmcnt(" #n ")" ::: "memory")
; #define PG8_BAR __builtin_amdgcn_s_barrier()
; #define PG8_SCHED __builtin_amdgcn_sched_barrier(0)
; template <class Epi, class Sched, bool ALIGN_EPI = false, bool SP2 = false>
; __device__ __forceinline__ void gemm_phase(PG8_LAS unsigned char* lds, const Gemm g, const Sched& S, const Epi& E, const bool skip_epi = false) {
;     ...
;             PG8_LDB(B0, 1, 0); PG8_LDB(B1, 1, 1); PG8_SCHED; PG8_LDA(At, 1, 0); PG8_STAGE_A(0, 1, a2, true);
;             PG8_WAIT_V(8); PG8_WAIT_L(0); PG8_BAR; PG8_MMA(0, 0, At, B0); PG8_MMA(0, 1, At, B1); PG8_BAR; PG8_SCHED;
	s_add_i32 s64, 0, 0x18000
	s_add_i32 s65, 0, 0x1c000
	v_add_u32_e32 v130, s64, v220
	v_add_u32_e32 v158, s65, v220
	ds_read_b128 v[98:101], v130
	ds_read_b128 v[110:113], v130 offset:1024
	ds_read_b128 v[122:125], v130 offset:2048
	ds_read_b128 v[130:133], v130 offset:3072
	ds_read_b128 v[146:149], v158
	ds_read_b128 v[150:153], v158 offset:1024
	ds_read_b128 v[154:157], v158 offset:2048
	ds_read_b128 v[158:161], v158 offset:3072
	s_add_u32 s38, s38, 0x40000
	s_addc_u32 s39, s39, 0
	s_mov_b32 m0, s45
	v_lshl_add_u64 v[218:219], s[38:39], 0, v[186:187]
	ds_read_b128 v[162:165], v227 offset:32768
	ds_read_b128 v[166:169], v227 offset:33792
	ds_read_b128 v[170:173], v227 offset:34816
	ds_read_b128 v[174:177], v227 offset:35840
	ds_read_b128 v[178:181], v227 offset:36864
	ds_read_b128 v[182:185], v227 offset:37888
	ds_read_b128 v[202:205], v227 offset:38912
	ds_read_b128 v[206:209], v227 offset:39936
	global_load_lds_dwordx4 v[218:219], off
	v_lshl_add_u64 v[218:219], s[38:39], 0, v[190:191]
	s_mov_b32 m0, s48
	s_nop 0
	global_load_lds_dwordx4 v[218:219], off
	s_waitcnt vmcnt(8)
	s_waitcnt lgkmcnt(0)
	s_barrier
	s_setprio 3
	s_waitcnt lgkmcnt(0)
	v_mfma_f32_16x16x32_bf16 v[142:145], v[98:101], v[162:165], v[142:145]
	v_mfma_f32_16x16x32_bf16 v[138:141], v[122:125], v[162:165], v[138:141]
	v_mfma_f32_16x16x32_bf16 v[118:121], v[98:101], v[170:173], v[118:121]
	v_mfma_f32_16x16x32_bf16 v[114:117], v[122:125], v[170:173], v[114:117]
	v_mfma_f32_16x16x32_bf16 v[94:97], v[98:101], v[178:181], v[94:97]
	v_mfma_f32_16x16x32_bf16 v[90:93], v[122:125], v[178:181], v[90:93]
	v_mfma_f32_16x16x32_bf16 v[78:81], v[98:101], v[202:205], v[78:81]
	v_mfma_f32_16x16x32_bf16 v[74:77], v[122:125], v[202:205], v[74:77]
	v_mfma_f32_16x16x32_bf16 v[142:145], v[110:113], v[166:169], v[142:145]
	v_mfma_f32_16x16x32_bf16 v[138:141], v[130:133], v[166:169], v[138:141]
	v_mfma_f32_16x16x32_bf16 v[118:121], v[110:113], v[174:177], v[118:121]
	v_mfma_f32_16x16x32_bf16 v[114:117], v[130:133], v[174:177], v[114:117]
	v_mfma_f32_16x16x32_bf16 v[94:97], v[110:113], v[182:185], v[94:97]
	v_mfma_f32_16x16x32_bf16 v[90:93], v[130:133], v[182:185], v[90:93]
	v_mfma_f32_16x16x32_bf16 v[78:81], v[110:113], v[206:209], v[78:81]
	v_mfma_f32_16x16x32_bf16 v[74:77], v[130:133], v[206:209], v[74:77]
	s_setprio 0
	s_setprio 3
	v_mfma_f32_16x16x32_bf16 v[134:137], v[146:149], v[162:165], v[134:137]
	v_mfma_f32_16x16x32_bf16 v[126:129], v[154:157], v[162:165], v[126:129]
	v_mfma_f32_16x16x32_bf16 v[106:109], v[146:149], v[170:173], v[106:109]
	v_mfma_f32_16x16x32_bf16 v[102:105], v[154:157], v[170:173], v[102:105]
	v_mfma_f32_16x16x32_bf16 v[86:89], v[146:149], v[178:181], v[86:89]
	v_mfma_f32_16x16x32_bf16 v[82:85], v[154:157], v[178:181], v[82:85]
	v_mfma_f32_16x16x32_bf16 v[70:73], v[146:149], v[202:205], v[70:73]
	v_mfma_f32_16x16x32_bf16 v[66:69], v[154:157], v[202:205], v[66:69]
	v_mfma_f32_16x16x32_bf16 v[134:137], v[150:153], v[166:169], v[134:137]
	v_mfma_f32_16x16x32_bf16 v[126:129], v[158:161], v[166:169], v[126:129]
	v_mfma_f32_16x16x32_bf16 v[106:109], v[150:153], v[174:177], v[106:109]
	v_mfma_f32_16x16x32_bf16 v[102:105], v[158:161], v[174:177], v[102:105]
	v_mfma_f32_16x16x32_bf16 v[86:89], v[150:153], v[182:185], v[86:89]
	v_mfma_f32_16x16x32_bf16 v[82:85], v[158:161], v[182:185], v[82:85]
	v_mfma_f32_16x16x32_bf16 v[70:73], v[150:153], v[206:209], v[70:73]
	v_mfma_f32_16x16x32_bf16 v[66:69], v[158:161], v[206:209], v[66:69]
	s_setprio 0
	s_barrier
; #define PG8_STAGE_A(b, h, ptr, NX) do { if constexpr (Sched::GATHER) { unsigned gs_[2]; gs_[0] = ((NX) && last_) ? gN[h][0] : gA[h][0]; gs_[1] = ((NX) && last_) ? gN[h][1] : gA[h][1]; PG8_STAGE(PG8_SA(b, h), ptr, gs_); } \
;         else PG8_STAGE(PG8_SA(b, h), (ptr) + ((h) ? hstep : (size_t)0), voffA); } while (0)
; #define PG8_STAGE(bufoff, gbase, voff) do { _Pragma("unroll") for (int _i = 0; _i < 2; ++_i) \
;         __builtin_amdgcn_global_load_lds((const unsigned*)((const char*)(gbase) + (voff)[_i]), (PG8_LAS unsigned*)(lds + (bufoff) + ldsw + _i * 8192), 16, 0, 0); } while (0)
; #define PG8_LDA(dst, b, h) do { _Pragma("unroll") for (int m = 0; m < 4; ++m) _Pragma("unroll") for (int k = 0; k < 2; ++k) dst[m][k] = *(const PG8_LAS bf16x8*)(lds + PG8_SA(b, h) + aoff + m * 2048 + k * 1024); } while (0)
; #define PG8_MMA(ai, bj, At, Bt) do { __builtin_amdgcn_s_setprio(1); _Pragma("unroll") for (int m = 0; m < 4; ++m) _Pragma("unroll") for (int n = 0; n < 2; ++n) _Pragma("unroll") for (int k = 0; k < 2; ++k) \
;         acc[ai][bj][m][n] = __builtin_amdgcn_mfma_f32_16x16x32_bf16(Bt[n][k], At[m][k], acc[ai][bj][m][n], 0, 0, 0); __builtin_amdgcn_s_setprio(0); } while (0)
; #define PG8_WAIT_V(n) asm volatile("s_waitcnt vmcnt(" #n ")" ::: "memory")
; #define PG8_WAIT_L(n) asm volatile("s_waitcnt lgkmcnt(" #n ")" ::: "memory")
; #define PG8_BAR __builtin_amdgcn_s_barrier()
; #define PG8_SCHED __builtin_amdgcn_sched_barrier(0)
; template <class Epi, class Sched, bool ALIGN_EPI = false, bool SP2 = false>
; __device__ __forceinline__ void gemm_phase(PG8_LAS unsigned char* lds, const Gemm g, const Sched& S, const Epi& E, const bool skip_epi = false) {
;     ...
;             PG8_LDA(At, 1, 1); PG8_STAGE(PG8_SB(1, 0), b3, voffB); PG8_STAGE(PG8_SB(1, 1), b3 + hstep, voffB); PG8_STAGE_A(1, 0, a3, true);
;             PG8_WAIT_V(8); PG8_WAIT_L(0); PG8_BAR; PG8_MMA(1, 0, At, B0); PG8_MMA(1, 1, At, B1); PG8_BAR; PG8_SCHED;
;     ...
;         if constexpr (ALIGN_EPI) { if (wr == 0) PG8_BAR; }
	s_add_i32 s38, s64, s40
	v_lshl_add_u64 v[210:211], v[210:211], 0, s[12:13]
	s_mov_b32 m0, s38
	ds_read_b128 v[162:165], v227 offset:49152
	ds_read_b128 v[166:169], v227 offset:50176
	ds_read_b128 v[170:173], v227 offset:51200
	ds_read_b128 v[174:177], v227 offset:52224
	ds_read_b128 v[178:181], v227 offset:53248
	ds_read_b128 v[182:185], v227 offset:54272
	ds_read_b128 v[202:205], v227 offset:55296
	ds_read_b128 v[206:209], v227 offset:56320
	global_load_lds_dwordx4 v[210:211], off
	s_add_i32 m0, s38, 0x2000
	s_add_u32 s36, s36, 0x40080
	v_lshl_add_u64 v[210:211], v[212:213], 0, s[12:13]
	s_addc_u32 s37, s37, 0
	s_add_i32 s38, s65, s40
	global_load_lds_dwordx4 v[210:211], off
	v_lshl_add_u64 v[210:211], s[36:37], 0, v[188:189]
	s_mov_b32 m0, s38
	s_nop 0
	global_load_lds_dwordx4 v[210:211], off
	v_lshl_add_u64 v[210:211], s[36:37], 0, v[192:193]
	s_add_i32 m0, s38, 0x2000
	s_nop 0
	global_load_lds_dwordx4 v[210:211], off
	v_lshl_add_u64 v[210:211], v[214:215], 0, s[12:13]
	s_mov_b32 m0, s53
	s_nop 0
	global_load_lds_dwordx4 v[210:211], off
	v_lshl_add_u64 v[210:211], v[216:217], 0, s[12:13]
	s_mov_b32 m0, s54
	s_nop 0
	global_load_lds_dwordx4 v[210:211], off
	s_waitcnt vmcnt(8)
	s_waitcnt lgkmcnt(0)
	s_barrier
	s_setprio 3
	s_waitcnt lgkmcnt(0)
	v_mfma_f32_16x16x32_bf16 v[62:65], v[98:101], v[162:165], v[62:65]
	v_mfma_f32_16x16x32_bf16 v[58:61], v[122:125], v[162:165], v[58:61]
	v_mfma_f32_16x16x32_bf16 v[46:49], v[98:101], v[170:173], v[46:49]
	v_mfma_f32_16x16x32_bf16 v[42:45], v[122:125], v[170:173], v[42:45]
	v_mfma_f32_16x16x32_bf16 v[30:33], v[98:101], v[178:181], v[30:33]
	v_mfma_f32_16x16x32_bf16 v[26:29], v[122:125], v[178:181], v[26:29]
	v_mfma_f32_16x16x32_bf16 v[14:17], v[98:101], v[202:205], v[14:17]
	v_mfma_f32_16x16x32_bf16 v[10:13], v[122:125], v[202:205], v[10:13]
	v_mfma_f32_16x16x32_bf16 v[62:65], v[110:113], v[166:169], v[62:65]
	v_mfma_f32_16x16x32_bf16 v[58:61], v[130:133], v[166:169], v[58:61]
	v_mfma_f32_16x16x32_bf16 v[46:49], v[110:113], v[174:177], v[46:49]
	v_mfma_f32_16x16x32_bf16 v[42:45], v[130:133], v[174:177], v[42:45]
	v_mfma_f32_16x16x32_bf16 v[30:33], v[110:113], v[182:185], v[30:33]
	v_mfma_f32_16x16x32_bf16 v[26:29], v[130:133], v[182:185], v[26:29]
	v_mfma_f32_16x16x32_bf16 v[14:17], v[110:113], v[206:209], v[14:17]
	v_mfma_f32_16x16x32_bf16 v[10:13], v[130:133], v[206:209], v[10:13]
	s_setprio 0
	s_setprio 3
	v_mfma_f32_16x16x32_bf16 v[54:57], v[146:149], v[162:165], v[54:57]
	v_mfma_f32_16x16x32_bf16 v[50:53], v[154:157], v[162:165], v[50:53]
	v_mfma_f32_16x16x32_bf16 v[38:41], v[146:149], v[170:173], v[38:41]
	v_mfma_f32_16x16x32_bf16 v[34:37], v[154:157], v[170:173], v[34:37]
	v_mfma_f32_16x16x32_bf16 v[22:25], v[146:149], v[178:181], v[22:25]
	v_mfma_f32_16x16x32_bf16 v[18:21], v[154:157], v[178:181], v[18:21]
	v_mfma_f32_16x16x32_bf16 v[6:9], v[146:149], v[202:205], v[6:9]
	v_mfma_f32_16x16x32_bf16 v[2:5], v[154:157], v[202:205], v[2:5]
	v_mfma_f32_16x16x32_bf16 v[54:57], v[150:153], v[166:169], v[54:57]
	v_mfma_f32_16x16x32_bf16 v[50:53], v[158:161], v[166:169], v[50:53]
	v_mfma_f32_16x16x32_bf16 v[38:41], v[150:153], v[174:177], v[38:41]
	v_mfma_f32_16x16x32_bf16 v[34:37], v[158:161], v[174:177], v[34:37]
	v_mfma_f32_16x16x32_bf16 v[22:25], v[150:153], v[182:185], v[22:25]
	v_mfma_f32_16x16x32_bf16 v[18:21], v[158:161], v[182:185], v[18:21]
	v_mfma_f32_16x16x32_bf16 v[6:9], v[150:153], v[206:209], v[6:9]
	v_mfma_f32_16x16x32_bf16 v[2:5], v[158:161], v[206:209], v[2:5]
	s_setprio 0
	s_barrier
	s_add_i32 s63, s63, 2
	s_add_u32 s34, s34, 0x100
	s_addc_u32 s35, s35, 0
	s_add_u32 s61, s61, 0x100
	s_addc_u32 s62, s62, 0
	s_cmp_gt_u32 s63, 13
	s_cbranch_scc0 .LBB0_1324
	s_and_b64 vcc, exec, s[14:15]
	s_cbranch_vccz .LBB0_1327
	s_barrier

; #define PG8_STAGE_A(b, h, ptr, NX) do { if constexpr (Sched::GATHER) { unsigned gs_[2]; gs_[0] = ((NX) && last_) ? gN[h][0] : gA[h][0]; gs_[1] = ((NX) && last_) ? gN[h][1] : gA[h][1]; PG8_STAGE(PG8_SA(b, h), ptr, gs_); } \
;         else PG8_STAGE(PG8_SA(b, h), (ptr) + ((h) ? hstep : (size_t)0), voffA); } while (0)
; #define PG8_STAGE(bufoff, gbase, voff) do { _Pragma("unroll") for (int _i = 0; _i < 2; ++_i) \
;         __builtin_amdgcn_global_load_lds((const unsigned*)((const char*)(gbase) + (voff)[_i]), (PG8_LAS unsigned*)(lds + (bufoff) + ldsw + _i * 8192), 16, 0, 0); } while (0)
; #define PG8_LDA(dst, b, h) do { _Pragma("unroll") for (int m = 0; m < 4; ++m) _Pragma("unroll") for (int k = 0; k < 2; ++k) dst[m][k] = *(const PG8_LAS bf16x8*)(lds + PG8_SA(b, h) + aoff + m * 2048 + k * 1024); } while (0)
; #define PG8_LDB(dst, b, h) do { _Pragma("unroll") for (int n = 0; n < 2; ++n) _Pragma("unroll") for (int k = 0; k < 2; ++k) dst[n][k] = *(const PG8_LAS bf16x8*)(lds + PG8_SB(b, h) + boff + n * 2048 + k * 1024); } while (0)
; #define PG8_WAIT_V(n) asm volatile("s_waitcnt vmcnt(" #n ")" ::: "memory")
; template <class Epi, class Sched, bool ALIGN_EPI = false, bool SP2 = false>
; __device__ __forceinline__ void gemm_phase(PG8_LAS unsigned char* lds, const Gemm g, const Sched& S, const Epi& E, const bool skip_epi = false) {
;     ...
;         const char* nA = has_next ? (const char*)g.A + (size_t)nxt.pm * pmstepA + nxt.ko : cA; const char* nB = has_next ? (const char*)g.Bt + (size_t)nxt.pn * tstep + nxt.ko : cB;
;         for (int t = 0; t < nt; t += 2) {
;             const bool last = (t == nt - 2); last_ = last && has_next;
;             const char* a1 = cA + (size_t)(t + 1) * kstep;
;             const char* a2 = last ? nA : cA + (size_t)(t + 2) * kstep; const char* b2 = last ? nB : cB + (size_t)(t + 2) * kstep;
;             const char* a3 = a2 + kstep; const char* b3 = b2 + kstep;
;             if (last && has_next) S.a_ready(nxt);
;             if constexpr (SP2) {
;             PG8_LDB(B0, 0, 0); PG8_LDB(B1, 0, 1); PG8_SCHED; PG8_LDA(At, 0, 0); PG8_STAGE_A(1, 1, a1, false);
;             PG8_WAIT_V(8); PG8_WAIT_L(0); PG8_BAR; PG8_MMA(0, 0, At, B0); PG8_MMA(0, 1, At, B1); PG8_BAR; PG8_SCHED;
;             PG8_LDA(At, 0, 1); PG8_STAGE(PG8_SB(0, 0), b2, voffB); PG8_STAGE(PG8_SB(0, 1), b2 + hstep, voffB); PG8_STAGE_A(0, 0, a2, true);
.Lg5_zero:
.LBB0_1727:
	s_mov_b32 s29, s41
	s_mov_b32 s31, s40
	v_mov_b32_e32 v143, v133
	v_mov_b32_e32 v141, v133
	s_add_u32 s61, s40, 0x100
	v_lshl_add_u64 v[146:147], s[24:25], 0, v[140:141]
	v_lshl_add_u64 v[148:149], s[24:25], 0, v[142:143]
	s_addc_u32 s62, s41, 0
	s_mov_b32 s63, -2
	s_mov_b64 s[40:41], 0
	ds_read_b128 v[166:169], v158
	ds_read_b128 v[170:173], v158 offset:1024
	ds_read_b128 v[174:177], v158 offset:2048
	ds_read_b128 v[178:181], v158 offset:3072
	ds_read_b128 v[182:185], v159
	ds_read_b128 v[186:189], v159 offset:1024
	ds_read_b128 v[190:193], v159 offset:2048
	ds_read_b128 v[194:197], v159 offset:3072
	s_add_u32 s42, s78, s40
	s_addc_u32 s43, s79, s41
	s_add_u32 s44, s42, 0x1aa00100
	s_addc_u32 s45, s43, 0
	s_add_u32 s66, s61, s40
	s_addc_u32 s67, s62, s41
	s_cmpk_eq_i32 s40, 0x700
	s_cselect_b64 s[64:65], -1, 0
	s_and_b64 s[42:43], s[64:65], exec
	s_cselect_b32 s45, s87, s45
	s_cselect_b32 s44, s86, s44
	s_cselect_b32 s42, s31, s66
	s_cselect_b32 s43, s29, s67
	s_and_b64 vcc, s[6:7], s[64:65]
	v_lshl_add_u64 v[226:227], v[148:149], 0, s[40:41]
	s_add_i32 m0, s37, 0xc000
	ds_read_b128 v[198:201], v160
	ds_read_b128 v[202:205], v160 offset:1024
	ds_read_b128 v[206:209], v160 offset:2048
	ds_read_b128 v[210:213], v160 offset:3072
	ds_read_b128 v[214:217], v160 offset:4096
	ds_read_b128 v[218:221], v160 offset:5120
	ds_read_b128 v[222:225], v160 offset:6144
	ds_read_b128 v[230:233], v160 offset:7168
	global_load_lds_dwordx4 v[226:227], off
	v_lshl_add_u64 v[226:227], v[146:147], 0, s[40:41]
	s_add_i32 m0, s37, 0xe000
	s_nop 0
	global_load_lds_dwordx4 v[226:227], off
	s_waitcnt vmcnt(8)
	s_waitcnt lgkmcnt(0)
	s_barrier
	s_setprio 3
	s_waitcnt lgkmcnt(0)
	v_mfma_f32_16x16x32_bf16 v[126:129], v[166:169], v[198:201], 0
	v_mfma_f32_16x16x32_bf16 v[122:125], v[174:177], v[198:201], 0
	v_mfma_f32_16x16x32_bf16 v[110:113], v[166:169], v[206:209], 0
	v_mfma_f32_16x16x32_bf16 v[106:109], v[174:177], v[206:209], 0
	v_mfma_f32_16x16x32_bf16 v[94:97], v[166:169], v[214:217], 0
	v_mfma_f32_16x16x32_bf16 v[90:93], v[174:177], v[214:217], 0
	v_mfma_f32_16x16x32_bf16 v[78:81], v[166:169], v[222:225], 0
	v_mfma_f32_16x16x32_bf16 v[74:77], v[174:177], v[222:225], 0
	v_mfma_f32_16x16x32_bf16 v[126:129], v[170:173], v[202:205], v[126:129]
	v_mfma_f32_16x16x32_bf16 v[122:125], v[178:181], v[202:205], v[122:125]
	v_mfma_f32_16x16x32_bf16 v[110:113], v[170:173], v[210:213], v[110:113]
	v_mfma_f32_16x16x32_bf16 v[106:109], v[178:181], v[210:213], v[106:109]
	v_mfma_f32_16x16x32_bf16 v[94:97], v[170:173], v[218:221], v[94:97]
	v_mfma_f32_16x16x32_bf16 v[90:93], v[178:181], v[218:221], v[90:93]
	v_mfma_f32_16x16x32_bf16 v[78:81], v[170:173], v[230:233], v[78:81]
	v_mfma_f32_16x16x32_bf16 v[74:77], v[178:181], v[230:233], v[74:77]
	s_setprio 0
	s_setprio 3
	v_mfma_f32_16x16x32_bf16 v[118:121], v[182:185], v[198:201], 0
	v_mfma_f32_16x16x32_bf16 v[114:117], v[190:193], v[198:201], 0
	v_mfma_f32_16x16x32_bf16 v[102:105], v[182:185], v[206:209], 0
	v_mfma_f32_16x16x32_bf16 v[98:101], v[190:193], v[206:209], 0
	v_mfma_f32_16x16x32_bf16 v[86:89], v[182:185], v[214:217], 0
	v_mfma_f32_16x16x32_bf16 v[82:85], v[190:193], v[214:217], 0
	v_mfma_f32_16x16x32_bf16 v[70:73], v[182:185], v[222:225], 0
	v_mfma_f32_16x16x32_bf16 v[66:69], v[190:193], v[222:225], 0
	v_mfma_f32_16x16x32_bf16 v[118:121], v[186:189], v[202:205], v[118:121]
	v_mfma_f32_16x16x32_bf16 v[114:117], v[194:197], v[202:205], v[114:117]
	v_mfma_f32_16x16x32_bf16 v[102:105], v[186:189], v[210:213], v[102:105]
	v_mfma_f32_16x16x32_bf16 v[98:101], v[194:197], v[210:213], v[98:101]
	v_mfma_f32_16x16x32_bf16 v[86:89], v[186:189], v[218:221], v[86:89]
	v_mfma_f32_16x16x32_bf16 v[82:85], v[194:197], v[218:221], v[82:85]
	v_mfma_f32_16x16x32_bf16 v[70:73], v[186:189], v[230:233], v[70:73]
	v_mfma_f32_16x16x32_bf16 v[66:69], v[194:197], v[230:233], v[66:69]
	s_setprio 0
	s_barrier
	s_add_i32 s64, s58, s50
	v_lshl_add_u64 v[226:227], s[42:43], 0, v[134:135]
	s_mov_b32 m0, s64
	ds_read_b128 v[198:201], v160 offset:16384
	ds_read_b128 v[202:205], v160 offset:17408
	ds_read_b128 v[206:209], v160 offset:18432
	ds_read_b128 v[210:213], v160 offset:19456
	ds_read_b128 v[214:217], v160 offset:20480
	ds_read_b128 v[218:221], v160 offset:21504
	ds_read_b128 v[222:225], v160 offset:22528
	ds_read_b128 v[230:233], v160 offset:23552
	global_load_lds_dwordx4 v[226:227], off
	s_add_i32 m0, s64, 0x2000
	s_add_u32 s64, s42, 0x40000
	v_lshl_add_u64 v[234:235], s[42:43], 0, v[136:137]
	s_addc_u32 s65, s43, 0
	s_add_i32 s66, s59, s50
	global_load_lds_dwordx4 v[234:235], off
	v_lshl_add_u64 v[236:237], s[64:65], 0, v[134:135]
	s_mov_b32 m0, s66
	v_cndmask_b32_e32 v132, v130, v164, vcc
	global_load_lds_dwordx4 v[236:237], off
	v_lshl_add_u64 v[236:237], s[64:65], 0, v[136:137]
	s_add_i32 m0, s66, 0x2000
	v_lshl_add_u64 v[238:239], s[44:45], 0, v[132:133]
	global_load_lds_dwordx4 v[236:237], off
	s_mov_b32 m0, s37
	v_cndmask_b32_e32 v236, v144, v163, vcc
	global_load_lds_dwordx4 v132, s[44:45]
	s_mov_b32 m0, s39
	v_mov_b32_e32 v237, v133
	global_load_lds_dwordx4 v236, s[44:45]
	s_waitcnt vmcnt(8)
	s_waitcnt lgkmcnt(0)
	v_lshl_add_u64 v[236:237], s[44:45], 0, v[236:237]
	s_barrier
; #define PG8_STAGE_A(b, h, ptr, NX) do { if constexpr (Sched::GATHER) { unsigned gs_[2]; gs_[0] = ((NX) && last_) ? gN[h][0] : gA[h][0]; gs_[1] = ((NX) && last_) ? gN[h][1] : gA[h][1]; PG8_STAGE(PG8_SA(b, h), ptr, gs_); } \
;         else PG8_STAGE(PG8_SA(b, h), (ptr) + ((h) ? hstep : (size_t)0), voffA); } while (0)
; #define PG8_LDA(dst, b, h) do { _Pragma("unroll") for (int m = 0; m < 4; ++m) _Pragma("unroll") for (int k = 0; k < 2; ++k) dst[m][k] = *(const PG8_LAS bf16x8*)(lds + PG8_SA(b, h) + aoff + m * 2048 + k * 1024); } while (0)
; #define PG8_LDB(dst, b, h) do { _Pragma("unroll") for (int n = 0; n < 2; ++n) _Pragma("unroll") for (int k = 0; k < 2; ++k) dst[n][k] = *(const PG8_LAS bf16x8*)(lds + PG8_SB(b, h) + boff + n * 2048 + k * 1024); } while (0)
; #define PG8_MMA(ai, bj, At, Bt) do { __builtin_amdgcn_s_setprio(1); _Pragma("unroll") for (int m = 0; m < 4; ++m) _Pragma("unroll") for (int n = 0; n < 2; ++n) _Pragma("unroll") for (int k = 0; k < 2; ++k) \
;         acc[ai][bj][m][n] = __builtin_amdgcn_mfma_f32_16x16x32_bf16(Bt[n][k], At[m][k], acc[ai][bj][m][n], 0, 0, 0); __builtin_amdgcn_s_setprio(0); } while (0)
; #define PG8_WAIT_V(n) asm volatile("s_waitcnt vmcnt(" #n ")" ::: "memory")
; #define PG8_WAIT_L(n) asm volatile("s_waitcnt lgkmcnt(" #n ")" ::: "memory")
; #define PG8_BAR __builtin_amdgcn_s_barrier()
; #define PG8_SCHED __builtin_amdgcn_sched_barrier(0)
; template <class Epi, class Sched, bool ALIGN_EPI = false, bool SP2 = false>
; __device__ __forceinline__ void gemm_phase(PG8_LAS unsigned char* lds, const Gemm g, const Sched& S, const Epi& E, const bool skip_epi = false) {
;     ...
;             PG8_WAIT_V(8); PG8_WAIT_L(0); PG8_BAR; PG8_MMA(1, 0, At, B0); PG8_MMA(1, 1, At, B1); PG8_BAR; PG8_SCHED;
;             PG8_LDB(B0, 1, 0); PG8_LDB(B1, 1, 1); PG8_SCHED; PG8_LDA(At, 1, 0); PG8_STAGE_A(0, 1, a2, true);
;             PG8_WAIT_V(8); PG8_WAIT_L(0); PG8_BAR; PG8_MMA(0, 0, At, B0); PG8_MMA(0, 1, At, B1); PG8_BAR; PG8_SCHED;
	s_setprio 3
	s_waitcnt lgkmcnt(0)
	v_mfma_f32_16x16x32_bf16 v[62:65], v[166:169], v[198:201], 0
	v_mfma_f32_16x16x32_bf16 v[58:61], v[174:177], v[198:201], 0
	v_mfma_f32_16x16x32_bf16 v[38:41], v[166:169], v[206:209], 0
	v_mfma_f32_16x16x32_bf16 v[34:37], v[174:177], v[206:209], 0
	v_mfma_f32_16x16x32_bf16 v[22:25], v[166:169], v[214:217], 0
	v_mfma_f32_16x16x32_bf16 v[18:21], v[174:177], v[214:217], 0
	v_mfma_f32_16x16x32_bf16 v[6:9], v[166:169], v[222:225], 0
	v_mfma_f32_16x16x32_bf16 v[2:5], v[174:177], v[222:225], 0
	v_mfma_f32_16x16x32_bf16 v[62:65], v[170:173], v[202:205], v[62:65]
	v_mfma_f32_16x16x32_bf16 v[58:61], v[178:181], v[202:205], v[58:61]
	v_mfma_f32_16x16x32_bf16 v[38:41], v[170:173], v[210:213], v[38:41]
	v_mfma_f32_16x16x32_bf16 v[34:37], v[178:181], v[210:213], v[34:37]
	v_mfma_f32_16x16x32_bf16 v[22:25], v[170:173], v[218:221], v[22:25]
	v_mfma_f32_16x16x32_bf16 v[18:21], v[178:181], v[218:221], v[18:21]
	v_mfma_f32_16x16x32_bf16 v[6:9], v[170:173], v[230:233], v[6:9]
	v_mfma_f32_16x16x32_bf16 v[2:5], v[178:181], v[230:233], v[2:5]
	s_setprio 0
	s_setprio 3
	v_mfma_f32_16x16x32_bf16 v[50:53], v[182:185], v[198:201], 0
	v_mfma_f32_16x16x32_bf16 v[42:45], v[190:193], v[198:201], 0
	v_mfma_f32_16x16x32_bf16 v[54:57], v[182:185], v[206:209], 0
	v_mfma_f32_16x16x32_bf16 v[46:49], v[190:193], v[206:209], 0
	v_mfma_f32_16x16x32_bf16 v[30:33], v[182:185], v[214:217], 0
	v_mfma_f32_16x16x32_bf16 v[26:29], v[190:193], v[214:217], 0
	v_mfma_f32_16x16x32_bf16 v[14:17], v[182:185], v[222:225], 0
	v_mfma_f32_16x16x32_bf16 v[10:13], v[190:193], v[222:225], 0
	v_mfma_f32_16x16x32_bf16 v[50:53], v[186:189], v[202:205], v[50:53]
	v_mfma_f32_16x16x32_bf16 v[42:45], v[194:197], v[202:205], v[42:45]
	v_mfma_f32_16x16x32_bf16 v[54:57], v[186:189], v[210:213], v[54:57]
	v_mfma_f32_16x16x32_bf16 v[46:49], v[194:197], v[210:213], v[46:49]
	v_mfma_f32_16x16x32_bf16 v[30:33], v[186:189], v[218:221], v[30:33]
	v_mfma_f32_16x16x32_bf16 v[26:29], v[194:197], v[218:221], v[26:29]
	v_mfma_f32_16x16x32_bf16 v[14:17], v[186:189], v[230:233], v[14:17]
	v_mfma_f32_16x16x32_bf16 v[10:13], v[194:197], v[230:233], v[10:13]
	s_setprio 0
	s_barrier
	s_add_i32 s64, 0, 0x18000
	v_add_u32_e32 v132, s64, v154
	s_add_i32 s65, 0, 0x1c000
	ds_read_b128 v[166:169], v132
	ds_read_b128 v[170:173], v132 offset:1024
	ds_read_b128 v[174:177], v132 offset:2048
	ds_read_b128 v[178:181], v132 offset:3072
	v_add_u32_e32 v132, s65, v154
	ds_read_b128 v[182:185], v132
	ds_read_b128 v[186:189], v132 offset:1024
	ds_read_b128 v[190:193], v132 offset:2048
	ds_read_b128 v[194:197], v132 offset:3072
	s_mov_b32 m0, s51
	v_cndmask_b32_e32 v132, v142, v162, vcc
	ds_read_b128 v[198:201], v160 offset:32768
	ds_read_b128 v[202:205], v160 offset:33792
	ds_read_b128 v[206:209], v160 offset:34816
	ds_read_b128 v[210:213], v160 offset:35840
	ds_read_b128 v[214:217], v160 offset:36864
	ds_read_b128 v[218:221], v160 offset:37888
	ds_read_b128 v[222:225], v160 offset:38912
	ds_read_b128 v[230:233], v160 offset:39936
	v_cndmask_b32_e32 v141, v140, v161, vcc
	global_load_lds_dwordx4 v132, s[44:45]
	s_mov_b32 m0, s52
	s_nop 0
	global_load_lds_dwordx4 v141, s[44:45]
	s_waitcnt vmcnt(8)
	s_waitcnt lgkmcnt(0)
	s_barrier
	s_setprio 3
	s_waitcnt lgkmcnt(0)
	v_mfma_f32_16x16x32_bf16 v[126:129], v[166:169], v[198:201], v[126:129]
	v_mfma_f32_16x16x32_bf16 v[122:125], v[174:177], v[198:201], v[122:125]
	v_mfma_f32_16x16x32_bf16 v[110:113], v[166:169], v[206:209], v[110:113]
	v_mfma_f32_16x16x32_bf16 v[106:109], v[174:177], v[206:209], v[106:109]
	v_mfma_f32_16x16x32_bf16 v[94:97], v[166:169], v[214:217], v[94:97]
	v_mfma_f32_16x16x32_bf16 v[90:93], v[174:177], v[214:217], v[90:93]
	v_mfma_f32_16x16x32_bf16 v[78:81], v[166:169], v[222:225], v[78:81]
	v_mfma_f32_16x16x32_bf16 v[74:77], v[174:177], v[222:225], v[74:77]
	v_mfma_f32_16x16x32_bf16 v[126:129], v[170:173], v[202:205], v[126:129]
	v_mfma_f32_16x16x32_bf16 v[122:125], v[178:181], v[202:205], v[122:125]
	v_mfma_f32_16x16x32_bf16 v[110:113], v[170:173], v[210:213], v[110:113]
	v_mfma_f32_16x16x32_bf16 v[106:109], v[178:181], v[210:213], v[106:109]
	v_mfma_f32_16x16x32_bf16 v[94:97], v[170:173], v[218:221], v[94:97]
	v_mfma_f32_16x16x32_bf16 v[90:93], v[178:181], v[218:221], v[90:93]
	v_mfma_f32_16x16x32_bf16 v[78:81], v[170:173], v[230:233], v[78:81]
	v_mfma_f32_16x16x32_bf16 v[74:77], v[178:181], v[230:233], v[74:77]
	s_setprio 0
	s_setprio 3
	v_mfma_f32_16x16x32_bf16 v[118:121], v[182:185], v[198:201], v[118:121]
	v_mfma_f32_16x16x32_bf16 v[114:117], v[190:193], v[198:201], v[114:117]
	v_mfma_f32_16x16x32_bf16 v[102:105], v[182:185], v[206:209], v[102:105]
	v_mfma_f32_16x16x32_bf16 v[98:101], v[190:193], v[206:209], v[98:101]
	v_mfma_f32_16x16x32_bf16 v[86:89], v[182:185], v[214:217], v[86:89]
	v_mfma_f32_16x16x32_bf16 v[82:85], v[190:193], v[214:217], v[82:85]
	v_mfma_f32_16x16x32_bf16 v[70:73], v[182:185], v[222:225], v[70:73]
	v_mfma_f32_16x16x32_bf16 v[66:69], v[190:193], v[222:225], v[66:69]
	v_mfma_f32_16x16x32_bf16 v[118:121], v[186:189], v[202:205], v[118:121]
	v_mfma_f32_16x16x32_bf16 v[114:117], v[194:197], v[202:205], v[114:117]
	v_mfma_f32_16x16x32_bf16 v[102:105], v[186:189], v[210:213], v[102:105]
	v_mfma_f32_16x16x32_bf16 v[98:101], v[194:197], v[210:213], v[98:101]
	v_mfma_f32_16x16x32_bf16 v[86:89], v[186:189], v[218:221], v[86:89]
	v_mfma_f32_16x16x32_bf16 v[82:85], v[194:197], v[218:221], v[82:85]
	v_mfma_f32_16x16x32_bf16 v[70:73], v[186:189], v[230:233], v[70:73]
	v_mfma_f32_16x16x32_bf16 v[66:69], v[194:197], v[230:233], v[66:69]
	s_setprio 0
	s_barrier
; #define PG8_STAGE_A(b, h, ptr, NX) do { if constexpr (Sched::GATHER) { unsigned gs_[2]; gs_[0] = ((NX) && last_) ? gN[h][0] : gA[h][0]; gs_[1] = ((NX) && last_) ? gN[h][1] : gA[h][1]; PG8_STAGE(PG8_SA(b, h), ptr, gs_); } \
;         else PG8_STAGE(PG8_SA(b, h), (ptr) + ((h) ? hstep : (size_t)0), voffA); } while (0)
; #define PG8_STAGE(bufoff, gbase, voff) do { _Pragma("unroll") for (int _i = 0; _i < 2; ++_i) \
;         __builtin_amdgcn_global_load_lds((const unsigned*)((const char*)(gbase) + (voff)[_i]), (PG8_LAS unsigned*)(lds + (bufoff) + ldsw + _i * 8192), 16, 0, 0); } while (0)
; #define PG8_LDA(dst, b, h) do { _Pragma("unroll") for (int m = 0; m < 4; ++m) _Pragma("unroll") for (int k = 0; k < 2; ++k) dst[m][k] = *(const PG8_LAS bf16x8*)(lds + PG8_SA(b, h) + aoff + m * 2048 + k * 1024); } while (0)
; #define PG8_LDB(dst, b, h) do { _Pragma("unroll") for (int n = 0; n < 2; ++n) _Pragma("unroll") for (int k = 0; k < 2; ++k) dst[n][k] = *(const PG8_LAS bf16x8*)(lds + PG8_SB(b, h) + boff + n * 2048 + k * 1024); } while (0)
; #define PG8_WAIT_V(n) asm volatile("s_waitcnt vmcnt(" #n ")" ::: "memory")
; #define PG8_BAR __builtin_amdgcn_s_barrier()
; template <class Epi, class Sched, bool ALIGN_EPI = false, bool SP2 = false>
; __device__ __forceinline__ void gemm_phase(PG8_LAS unsigned char* lds, const Gemm g, const Sched& S, const Epi& E, const bool skip_epi = false) {
;     ...
;             PG8_LDB(B0, 0, 0); PG8_LDB(B1, 0, 1); PG8_SCHED; PG8_LDA(At, 0, 0); PG8_STAGE_A(1, 1, a1, false);
;             PG8_WAIT_V(8); PG8_WAIT_L(0); PG8_BAR; PG8_MMA(0, 0, At, B0); PG8_MMA(0, 1, At, B1); PG8_BAR; PG8_SCHED;
;             PG8_LDA(At, 0, 1); PG8_STAGE(PG8_SB(0, 0), b2, voffB); PG8_STAGE(PG8_SB(0, 1), b2 + hstep, voffB); PG8_STAGE_A(0, 0, a2, true);
;             PG8_WAIT_V(8); PG8_WAIT_L(0); PG8_BAR; PG8_MMA(1, 0, At, B0); PG8_MMA(1, 1, At, B1); PG8_BAR; PG8_SCHED;
;             PG8_LDB(B0, 1, 0); PG8_LDB(B1, 1, 1); PG8_SCHED; PG8_LDA(At, 1, 0); PG8_STAGE_A(0, 1, a2, true);
;             PG8_WAIT_V(8); PG8_WAIT_L(0); PG8_BAR; PG8_MMA(0, 0, At, B0); PG8_MMA(0, 1, At, B1); PG8_BAR; PG8_SCHED;
;             PG8_LDA(At, 1, 1); PG8_STAGE(PG8_SB(1, 0), b3, voffB); PG8_STAGE(PG8_SB(1, 1), b3 + hstep, voffB); PG8_STAGE_A(1, 0, a3, true);
;             PG8_WAIT_V(8); PG8_WAIT_L(0); PG8_BAR; PG8_MMA(1, 0, At, B0); PG8_MMA(1, 1, At, B1); PG8_BAR; PG8_SCHED;
	s_add_i32 s44, s64, s50
	v_lshl_add_u64 v[226:227], v[226:227], 0, s[22:23]
	s_mov_b32 m0, s44
	ds_read_b128 v[198:201], v160 offset:49152
	ds_read_b128 v[202:205], v160 offset:50176
	ds_read_b128 v[206:209], v160 offset:51200
	ds_read_b128 v[210:213], v160 offset:52224
	ds_read_b128 v[214:217], v160 offset:53248
	ds_read_b128 v[218:221], v160 offset:54272
	ds_read_b128 v[222:225], v160 offset:55296
	ds_read_b128 v[230:233], v160 offset:56320
	global_load_lds_dwordx4 v[226:227], off
	s_add_i32 m0, s44, 0x2000
	s_add_u32 s42, s42, 0x40080
	v_lshl_add_u64 v[226:227], v[234:235], 0, s[22:23]
	s_addc_u32 s43, s43, 0
	s_add_i32 s44, s65, s50
	global_load_lds_dwordx4 v[226:227], off
	v_lshl_add_u64 v[226:227], s[42:43], 0, v[134:135]
	s_mov_b32 m0, s44
	s_nop 0
	global_load_lds_dwordx4 v[226:227], off
	v_lshl_add_u64 v[226:227], s[42:43], 0, v[136:137]
	s_add_i32 m0, s44, 0x2000
	s_nop 0
	global_load_lds_dwordx4 v[226:227], off
	v_lshl_add_u64 v[226:227], v[238:239], 0, s[22:23]
	s_mov_b32 m0, s55
	s_nop 0
	global_load_lds_dwordx4 v[226:227], off
	v_lshl_add_u64 v[226:227], v[236:237], 0, s[22:23]
	s_mov_b32 m0, s56
	s_nop 0
	global_load_lds_dwordx4 v[226:227], off
	s_waitcnt vmcnt(8)
	s_waitcnt lgkmcnt(0)
	s_barrier
	s_setprio 3
	s_waitcnt lgkmcnt(0)
	v_mfma_f32_16x16x32_bf16 v[62:65], v[166:169], v[198:201], v[62:65]
	v_mfma_f32_16x16x32_bf16 v[58:61], v[174:177], v[198:201], v[58:61]
	v_mfma_f32_16x16x32_bf16 v[38:41], v[166:169], v[206:209], v[38:41]
	v_mfma_f32_16x16x32_bf16 v[34:37], v[174:177], v[206:209], v[34:37]
	v_mfma_f32_16x16x32_bf16 v[22:25], v[166:169], v[214:217], v[22:25]
	v_mfma_f32_16x16x32_bf16 v[18:21], v[174:177], v[214:217], v[18:21]
	v_mfma_f32_16x16x32_bf16 v[6:9], v[166:169], v[222:225], v[6:9]
	v_mfma_f32_16x16x32_bf16 v[2:5], v[174:177], v[222:225], v[2:5]
	v_mfma_f32_16x16x32_bf16 v[62:65], v[170:173], v[202:205], v[62:65]
	v_mfma_f32_16x16x32_bf16 v[58:61], v[178:181], v[202:205], v[58:61]
	v_mfma_f32_16x16x32_bf16 v[38:41], v[170:173], v[210:213], v[38:41]
	v_mfma_f32_16x16x32_bf16 v[34:37], v[178:181], v[210:213], v[34:37]
	v_mfma_f32_16x16x32_bf16 v[22:25], v[170:173], v[218:221], v[22:25]
	v_mfma_f32_16x16x32_bf16 v[18:21], v[178:181], v[218:221], v[18:21]
	v_mfma_f32_16x16x32_bf16 v[6:9], v[170:173], v[230:233], v[6:9]
	v_mfma_f32_16x16x32_bf16 v[2:5], v[178:181], v[230:233], v[2:5]
	s_setprio 0
	s_setprio 3
	v_mfma_f32_16x16x32_bf16 v[50:53], v[182:185], v[198:201], v[50:53]
	v_mfma_f32_16x16x32_bf16 v[42:45], v[190:193], v[198:201], v[42:45]
	v_mfma_f32_16x16x32_bf16 v[54:57], v[182:185], v[206:209], v[54:57]
	v_mfma_f32_16x16x32_bf16 v[46:49], v[190:193], v[206:209], v[46:49]
	v_mfma_f32_16x16x32_bf16 v[30:33], v[182:185], v[214:217], v[30:33]
	v_mfma_f32_16x16x32_bf16 v[26:29], v[190:193], v[214:217], v[26:29]
	v_mfma_f32_16x16x32_bf16 v[14:17], v[182:185], v[222:225], v[14:17]
	v_mfma_f32_16x16x32_bf16 v[10:13], v[190:193], v[222:225], v[10:13]
	v_mfma_f32_16x16x32_bf16 v[50:53], v[186:189], v[202:205], v[50:53]
	v_mfma_f32_16x16x32_bf16 v[42:45], v[194:197], v[202:205], v[42:45]
	v_mfma_f32_16x16x32_bf16 v[54:57], v[186:189], v[210:213], v[54:57]
	v_mfma_f32_16x16x32_bf16 v[46:49], v[194:197], v[210:213], v[46:49]
	v_mfma_f32_16x16x32_bf16 v[30:33], v[186:189], v[218:221], v[30:33]
	v_mfma_f32_16x16x32_bf16 v[26:29], v[194:197], v[218:221], v[26:29]
	v_mfma_f32_16x16x32_bf16 v[14:17], v[186:189], v[230:233], v[14:17]
	v_mfma_f32_16x16x32_bf16 v[10:13], v[194:197], v[230:233], v[10:13]
	s_setprio 0
	s_barrier
	s_add_i32 s63, s63, 2
	s_add_u32 s40, s40, 0x100
	s_addc_u32 s41, s41, 0
	s_cmp_gt_u32 s63, 13
	s_andn2_b64 vcc, exec, s[6:7]
	s_cbranch_vccnz .Lg5_nonext
	s_waitcnt vmcnt(8)
	v_readfirstlane_b32 s34, v250
	v_lshl_add_u32 v164, v229, 11, v152
	v_lshl_add_u32 v163, v251, 11, v153
	v_lshl_add_u32 v162, v252, 11, v152
	v_lshl_add_u32 v161, v253, 11, v153
	s_mul_i32 s34, s34, 28
	s_add_i32 s30, s34, s30
	s_ashr_i32 s31, s30, 31
	s_lshl_b64 s[34:35], s[30:31], 19
	v_readlane_b32 s42, v254, 29
	v_readlane_b32 s43, v254, 30
	s_add_u32 s34, s42, s34
	s_addc_u32 s35, s43, s35
	s_mov_b32 s29, s35
	s_mov_b32 s31, s34
.Lg5_nonext:
.LBB0_1728:
	ds_read_b128 v[166:169], v158
	ds_read_b128 v[170:173], v158 offset:1024
	ds_read_b128 v[174:177], v158 offset:2048
	ds_read_b128 v[178:181], v158 offset:3072
	ds_read_b128 v[182:185], v159
	ds_read_b128 v[186:189], v159 offset:1024
	ds_read_b128 v[190:193], v159 offset:2048
	ds_read_b128 v[194:197], v159 offset:3072
	s_add_u32 s42, s78, s40
	s_addc_u32 s43, s79, s41
	s_add_u32 s44, s42, 0x1aa00100
	s_addc_u32 s45, s43, 0
	s_add_u32 s66, s61, s40
	s_addc_u32 s67, s62, s41
	s_cmpk_eq_i32 s40, 0x700
	s_cselect_b64 s[64:65], -1, 0
	s_and_b64 s[42:43], s[64:65], exec
	s_cselect_b32 s45, s87, s45
	s_cselect_b32 s44, s86, s44
	s_cselect_b32 s42, s31, s66
	s_cselect_b32 s43, s29, s67
	s_and_b64 vcc, s[6:7], s[64:65]
	v_lshl_add_u64 v[226:227], v[148:149], 0, s[40:41]
	s_add_i32 m0, s37, 0xc000
	ds_read_b128 v[198:201], v160
	ds_read_b128 v[202:205], v160 offset:1024
	ds_read_b128 v[206:209], v160 offset:2048
	ds_read_b128 v[210:213], v160 offset:3072
	ds_read_b128 v[214:217], v160 offset:4096
	ds_read_b128 v[218:221], v160 offset:5120
	ds_read_b128 v[222:225], v160 offset:6144
	ds_read_b128 v[230:233], v160 offset:7168
	global_load_lds_dwordx4 v[226:227], off
	v_lshl_add_u64 v[226:227], v[146:147], 0, s[40:41]
	s_add_i32 m0, s37, 0xe000
	s_nop 0
	global_load_lds_dwordx4 v[226:227], off
	s_waitcnt vmcnt(8)
	s_waitcnt lgkmcnt(0)
	s_barrier
; #define PG8_STAGE_A(b, h, ptr, NX) do { if constexpr (Sched::GATHER) { unsigned gs_[2]; gs_[0] = ((NX) && last_) ? gN[h][0] : gA[h][0]; gs_[1] = ((NX) && last_) ? gN[h][1] : gA[h][1]; PG8_STAGE(PG8_SA(b, h), ptr, gs_); } \
;         else PG8_STAGE(PG8_SA(b, h), (ptr) + ((h) ? hstep : (size_t)0), voffA); } while (0)
; #define PG8_STAGE(bufoff, gbase, voff) do { _Pragma("unroll") for (int _i = 0; _i < 2; ++_i) \
;         __builtin_amdgcn_global_load_lds((const unsigned*)((const char*)(gbase) + (voff)[_i]), (PG8_LAS unsigned*)(lds + (bufoff) + ldsw + _i * 8192), 16, 0, 0); } while (0)
; #define PG8_LDA(dst, b, h) do { _Pragma("unroll") for (int m = 0; m < 4; ++m) _Pragma("unroll") for (int k = 0; k < 2; ++k) dst[m][k] = *(const PG8_LAS bf16x8*)(lds + PG8_SA(b, h) + aoff + m * 2048 + k * 1024); } while (0)
; #define PG8_MMA(ai, bj, At, Bt) do { __builtin_amdgcn_s_setprio(1); _Pragma("unroll") for (int m = 0; m < 4; ++m) _Pragma("unroll") for (int n = 0; n < 2; ++n) _Pragma("unroll") for (int k = 0; k < 2; ++k) \
;         acc[ai][bj][m][n] = __builtin_amdgcn_mfma_f32_16x16x32_bf16(Bt[n][k], At[m][k], acc[ai][bj][m][n], 0, 0, 0); __builtin_amdgcn_s_setprio(0); } while (0)
; #define PG8_WAIT_V(n) asm volatile("s_waitcnt vmcnt(" #n ")" ::: "memory")
; #define PG8_WAIT_L(n) asm volatile("s_waitcnt lgkmcnt(" #n ")" ::: "memory")
; #define PG8_BAR __builtin_amdgcn_s_barrier()
; #define PG8_SCHED __builtin_amdgcn_sched_barrier(0)
; template <class Epi, class Sched, bool ALIGN_EPI = false, bool SP2 = false>
; __device__ __forceinline__ void gemm_phase(PG8_LAS unsigned char* lds, const Gemm g, const Sched& S, const Epi& E, const bool skip_epi = false) {
;     ...
;             PG8_WAIT_V(8); PG8_WAIT_L(0); PG8_BAR; PG8_MMA(0, 0, At, B0); PG8_MMA(0, 1, At, B1); PG8_BAR; PG8_SCHED;
;             PG8_LDA(At, 0, 1); PG8_STAGE(PG8_SB(0, 0), b2, voffB); PG8_STAGE(PG8_SB(0, 1), b2 + hstep, voffB); PG8_STAGE_A(0, 0, a2, true);
;             PG8_WAIT_V(8); PG8_WAIT_L(0); PG8_BAR; PG8_MMA(1, 0, At, B0); PG8_MMA(1, 1, At, B1); PG8_BAR; PG8_SCHED;
	s_setprio 3
	s_waitcnt lgkmcnt(0)
	v_mfma_f32_16x16x32_bf16 v[126:129], v[166:169], v[198:201], v[126:129]
	v_mfma_f32_16x16x32_bf16 v[122:125], v[174:177], v[198:201], v[122:125]
	v_mfma_f32_16x16x32_bf16 v[110:113], v[166:169], v[206:209], v[110:113]
	v_mfma_f32_16x16x32_bf16 v[106:109], v[174:177], v[206:209], v[106:109]
	v_mfma_f32_16x16x32_bf16 v[94:97], v[166:169], v[214:217], v[94:97]
	v_mfma_f32_16x16x32_bf16 v[90:93], v[174:177], v[214:217], v[90:93]
	v_mfma_f32_16x16x32_bf16 v[78:81], v[166:169], v[222:225], v[78:81]
	v_mfma_f32_16x16x32_bf16 v[74:77], v[174:177], v[222:225], v[74:77]
	v_mfma_f32_16x16x32_bf16 v[126:129], v[170:173], v[202:205], v[126:129]
	v_mfma_f32_16x16x32_bf16 v[122:125], v[178:181], v[202:205], v[122:125]
	v_mfma_f32_16x16x32_bf16 v[110:113], v[170:173], v[210:213], v[110:113]
	v_mfma_f32_16x16x32_bf16 v[106:109], v[178:181], v[210:213], v[106:109]
	v_mfma_f32_16x16x32_bf16 v[94:97], v[170:173], v[218:221], v[94:97]
	v_mfma_f32_16x16x32_bf16 v[90:93], v[178:181], v[218:221], v[90:93]
	v_mfma_f32_16x16x32_bf16 v[78:81], v[170:173], v[230:233], v[78:81]
	v_mfma_f32_16x16x32_bf16 v[74:77], v[178:181], v[230:233], v[74:77]
	s_setprio 0
	s_setprio 3
	v_mfma_f32_16x16x32_bf16 v[118:121], v[182:185], v[198:201], v[118:121]
	v_mfma_f32_16x16x32_bf16 v[114:117], v[190:193], v[198:201], v[114:117]
	v_mfma_f32_16x16x32_bf16 v[102:105], v[182:185], v[206:209], v[102:105]
	v_mfma_f32_16x16x32_bf16 v[98:101], v[190:193], v[206:209], v[98:101]
	v_mfma_f32_16x16x32_bf16 v[86:89], v[182:185], v[214:217], v[86:89]
	v_mfma_f32_16x16x32_bf16 v[82:85], v[190:193], v[214:217], v[82:85]
	v_mfma_f32_16x16x32_bf16 v[70:73], v[182:185], v[222:225], v[70:73]
	v_mfma_f32_16x16x32_bf16 v[66:69], v[190:193], v[222:225], v[66:69]
	v_mfma_f32_16x16x32_bf16 v[118:121], v[186:189], v[202:205], v[118:121]
	v_mfma_f32_16x16x32_bf16 v[114:117], v[194:197], v[202:205], v[114:117]
	v_mfma_f32_16x16x32_bf16 v[102:105], v[186:189], v[210:213], v[102:105]
	v_mfma_f32_16x16x32_bf16 v[98:101], v[194:197], v[210:213], v[98:101]
	v_mfma_f32_16x16x32_bf16 v[86:89], v[186:189], v[218:221], v[86:89]
	v_mfma_f32_16x16x32_bf16 v[82:85], v[194:197], v[218:221], v[82:85]
	v_mfma_f32_16x16x32_bf16 v[70:73], v[186:189], v[230:233], v[70:73]
	v_mfma_f32_16x16x32_bf16 v[66:69], v[194:197], v[230:233], v[66:69]
	s_setprio 0
	s_barrier
	s_add_i32 s64, s58, s50
	v_lshl_add_u64 v[226:227], s[42:43], 0, v[134:135]
	s_mov_b32 m0, s64
	ds_read_b128 v[198:201], v160 offset:16384
	ds_read_b128 v[202:205], v160 offset:17408
	ds_read_b128 v[206:209], v160 offset:18432
	ds_read_b128 v[210:213], v160 offset:19456
	ds_read_b128 v[214:217], v160 offset:20480
	ds_read_b128 v[218:221], v160 offset:21504
	ds_read_b128 v[222:225], v160 offset:22528
	ds_read_b128 v[230:233], v160 offset:23552
	global_load_lds_dwordx4 v[226:227], off
	s_add_i32 m0, s64, 0x2000
	s_add_u32 s64, s42, 0x40000
	v_lshl_add_u64 v[234:235], s[42:43], 0, v[136:137]
	s_addc_u32 s65, s43, 0
	s_add_i32 s66, s59, s50
	global_load_lds_dwordx4 v[234:235], off
	v_lshl_add_u64 v[236:237], s[64:65], 0, v[134:135]
	s_mov_b32 m0, s66
	v_cndmask_b32_e32 v132, v130, v164, vcc
	global_load_lds_dwordx4 v[236:237], off
	v_lshl_add_u64 v[236:237], s[64:65], 0, v[136:137]
	s_add_i32 m0, s66, 0x2000
	v_lshl_add_u64 v[238:239], s[44:45], 0, v[132:133]
	global_load_lds_dwordx4 v[236:237], off
	s_mov_b32 m0, s37
	v_cndmask_b32_e32 v236, v144, v163, vcc
	global_load_lds_dwordx4 v132, s[44:45]
	s_mov_b32 m0, s39
	v_mov_b32_e32 v237, v133
	global_load_lds_dwordx4 v236, s[44:45]
	s_waitcnt vmcnt(8)
	s_waitcnt lgkmcnt(0)
	v_lshl_add_u64 v[236:237], s[44:45], 0, v[236:237]
	s_barrier
	s_setprio 3
	s_waitcnt lgkmcnt(0)
	v_mfma_f32_16x16x32_bf16 v[62:65], v[166:169], v[198:201], v[62:65]
	v_mfma_f32_16x16x32_bf16 v[58:61], v[174:177], v[198:201], v[58:61]
	v_mfma_f32_16x16x32_bf16 v[38:41], v[166:169], v[206:209], v[38:41]
	v_mfma_f32_16x16x32_bf16 v[34:37], v[174:177], v[206:209], v[34:37]
	v_mfma_f32_16x16x32_bf16 v[22:25], v[166:169], v[214:217], v[22:25]
	v_mfma_f32_16x16x32_bf16 v[18:21], v[174:177], v[214:217], v[18:21]
	v_mfma_f32_16x16x32_bf16 v[6:9], v[166:169], v[222:225], v[6:9]
	v_mfma_f32_16x16x32_bf16 v[2:5], v[174:177], v[222:225], v[2:5]
	v_mfma_f32_16x16x32_bf16 v[62:65], v[170:173], v[202:205], v[62:65]
	v_mfma_f32_16x16x32_bf16 v[58:61], v[178:181], v[202:205], v[58:61]
	v_mfma_f32_16x16x32_bf16 v[38:41], v[170:173], v[210:213], v[38:41]
	v_mfma_f32_16x16x32_bf16 v[34:37], v[178:181], v[210:213], v[34:37]
	v_mfma_f32_16x16x32_bf16 v[22:25], v[170:173], v[218:221], v[22:25]
	v_mfma_f32_16x16x32_bf16 v[18:21], v[178:181], v[218:221], v[18:21]
	v_mfma_f32_16x16x32_bf16 v[6:9], v[170:173], v[230:233], v[6:9]
	v_mfma_f32_16x16x32_bf16 v[2:5], v[178:181], v[230:233], v[2:5]
	s_setprio 0
	s_setprio 3
	v_mfma_f32_16x16x32_bf16 v[50:53], v[182:185], v[198:201], v[50:53]
	v_mfma_f32_16x16x32_bf16 v[42:45], v[190:193], v[198:201], v[42:45]
	v_mfma_f32_16x16x32_bf16 v[54:57], v[182:185], v[206:209], v[54:57]
	v_mfma_f32_16x16x32_bf16 v[46:49], v[190:193], v[206:209], v[46:49]
	v_mfma_f32_16x16x32_bf16 v[30:33], v[182:185], v[214:217], v[30:33]
	v_mfma_f32_16x16x32_bf16 v[26:29], v[190:193], v[214:217], v[26:29]
	v_mfma_f32_16x16x32_bf16 v[14:17], v[182:185], v[222:225], v[14:17]
	v_mfma_f32_16x16x32_bf16 v[10:13], v[190:193], v[222:225], v[10:13]
	v_mfma_f32_16x16x32_bf16 v[50:53], v[186:189], v[202:205], v[50:53]
	v_mfma_f32_16x16x32_bf16 v[42:45], v[194:197], v[202:205], v[42:45]
	v_mfma_f32_16x16x32_bf16 v[54:57], v[186:189], v[210:213], v[54:57]
	v_mfma_f32_16x16x32_bf16 v[46:49], v[194:197], v[210:213], v[46:49]
	v_mfma_f32_16x16x32_bf16 v[30:33], v[186:189], v[218:221], v[30:33]
	v_mfma_f32_16x16x32_bf16 v[26:29], v[194:197], v[218:221], v[26:29]
	v_mfma_f32_16x16x32_bf16 v[14:17], v[186:189], v[230:233], v[14:17]
	v_mfma_f32_16x16x32_bf16 v[10:13], v[194:197], v[230:233], v[10:13]
	s_setprio 0
	s_barrier
; #define PG8_STAGE_A(b, h, ptr, NX) do { if constexpr (Sched::GATHER) { unsigned gs_[2]; gs_[0] = ((NX) && last_) ? gN[h][0] : gA[h][0]; gs_[1] = ((NX) && last_) ? gN[h][1] : gA[h][1]; PG8_STAGE(PG8_SA(b, h), ptr, gs_); } \
;         else PG8_STAGE(PG8_SA(b, h), (ptr) + ((h) ? hstep : (size_t)0), voffA); } while (0)
; #define PG8_LDA(dst, b, h) do { _Pragma("unroll") for (int m = 0; m < 4; ++m) _Pragma("unroll") for (int k = 0; k < 2; ++k) dst[m][k] = *(const PG8_LAS bf16x8*)(lds + PG8_SA(b, h) + aoff + m * 2048 + k * 1024); } while (0)
; #define PG8_LDB(dst, b, h) do { _Pragma("unroll") for (int n = 0; n < 2; ++n) _Pragma("unroll") for (int k = 0; k < 2; ++k) dst[n][k] = *(const PG8_LAS bf16x8*)(lds + PG8_SB(b, h) + boff + n * 2048 + k * 1024); } while (0)
; #define PG8_MMA(ai, bj, At, Bt) do { __builtin_amdgcn_s_setprio(1); _Pragma("unroll") for (int m = 0; m < 4; ++m) _Pragma("unroll") for (int n = 0; n < 2; ++n) _Pragma("unroll") for (int k = 0; k < 2; ++k) \
;         acc[ai][bj][m][n] = __builtin_amdgcn_mfma_f32_16x16x32_bf16(Bt[n][k], At[m][k], acc[ai][bj][m][n], 0, 0, 0); __builtin_amdgcn_s_setprio(0); } while (0)
; #define PG8_WAIT_V(n) asm volatile("s_waitcnt vmcnt(" #n ")" ::: "memory")
; #define PG8_WAIT_L(n) asm volatile("s_waitcnt lgkmcnt(" #n ")" ::: "memory")
; #define PG8_BAR __builtin_amdgcn_s_barrier()
; #define PG8_SCHED __builtin_amdgcn_sched_barrier(0)
; template <class Epi, class Sched, bool ALIGN_EPI = false, bool SP2 = false>
; __device__ __forceinline__ void gemm_phase(PG8_LAS unsigned char* lds, const Gemm g, const Sched& S, const Epi& E, const bool skip_epi = false) {
;     ...
;             PG8_LDB(B0, 1, 0); PG8_LDB(B1, 1, 1); PG8_SCHED; PG8_LDA(At, 1, 0); PG8_STAGE_A(0, 1, a2, true);
;             PG8_WAIT_V(8); PG8_WAIT_L(0); PG8_BAR; PG8_MMA(0, 0, At, B0); PG8_MMA(0, 1, At, B1); PG8_BAR; PG8_SCHED;
	s_add_i32 s64, 0, 0x18000
	v_add_u32_e32 v132, s64, v154
	s_add_i32 s65, 0, 0x1c000
	ds_read_b128 v[166:169], v132
	ds_read_b128 v[170:173], v132 offset:1024
	ds_read_b128 v[174:177], v132 offset:2048
	ds_read_b128 v[178:181], v132 offset:3072
	v_add_u32_e32 v132, s65, v154
	ds_read_b128 v[182:185], v132
	ds_read_b128 v[186:189], v132 offset:1024
	ds_read_b128 v[190:193], v132 offset:2048
	ds_read_b128 v[194:197], v132 offset:3072
	s_mov_b32 m0, s51
	v_cndmask_b32_e32 v132, v142, v162, vcc
	ds_read_b128 v[198:201], v160 offset:32768
	ds_read_b128 v[202:205], v160 offset:33792
	ds_read_b128 v[206:209], v160 offset:34816
	ds_read_b128 v[210:213], v160 offset:35840
	ds_read_b128 v[214:217], v160 offset:36864
	ds_read_b128 v[218:221], v160 offset:37888
	ds_read_b128 v[222:225], v160 offset:38912
	ds_read_b128 v[230:233], v160 offset:39936
	v_cndmask_b32_e32 v141, v140, v161, vcc
	global_load_lds_dwordx4 v132, s[44:45]
	s_mov_b32 m0, s52
	s_nop 0
	global_load_lds_dwordx4 v141, s[44:45]
	s_waitcnt vmcnt(8)
	s_waitcnt lgkmcnt(0)
	s_barrier
	s_setprio 3
	s_waitcnt lgkmcnt(0)
	v_mfma_f32_16x16x32_bf16 v[126:129], v[166:169], v[198:201], v[126:129]
	v_mfma_f32_16x16x32_bf16 v[122:125], v[174:177], v[198:201], v[122:125]
	v_mfma_f32_16x16x32_bf16 v[110:113], v[166:169], v[206:209], v[110:113]
	v_mfma_f32_16x16x32_bf16 v[106:109], v[174:177], v[206:209], v[106:109]
	v_mfma_f32_16x16x32_bf16 v[94:97], v[166:169], v[214:217], v[94:97]
	v_mfma_f32_16x16x32_bf16 v[90:93], v[174:177], v[214:217], v[90:93]
	v_mfma_f32_16x16x32_bf16 v[78:81], v[166:169], v[222:225], v[78:81]
	v_mfma_f32_16x16x32_bf16 v[74:77], v[174:177], v[222:225], v[74:77]
	v_mfma_f32_16x16x32_bf16 v[126:129], v[170:173], v[202:205], v[126:129]
	v_mfma_f32_16x16x32_bf16 v[122:125], v[178:181], v[202:205], v[122:125]
	v_mfma_f32_16x16x32_bf16 v[110:113], v[170:173], v[210:213], v[110:113]
	v_mfma_f32_16x16x32_bf16 v[106:109], v[178:181], v[210:213], v[106:109]
	v_mfma_f32_16x16x32_bf16 v[94:97], v[170:173], v[218:221], v[94:97]
	v_mfma_f32_16x16x32_bf16 v[90:93], v[178:181], v[218:221], v[90:93]
	v_mfma_f32_16x16x32_bf16 v[78:81], v[170:173], v[230:233], v[78:81]
	v_mfma_f32_16x16x32_bf16 v[74:77], v[178:181], v[230:233], v[74:77]
	s_setprio 0
	s_setprio 3
	v_mfma_f32_16x16x32_bf16 v[118:121], v[182:185], v[198:201], v[118:121]
	v_mfma_f32_16x16x32_bf16 v[114:117], v[190:193], v[198:201], v[114:117]
	v_mfma_f32_16x16x32_bf16 v[102:105], v[182:185], v[206:209], v[102:105]
	v_mfma_f32_16x16x32_bf16 v[98:101], v[190:193], v[206:209], v[98:101]
	v_mfma_f32_16x16x32_bf16 v[86:89], v[182:185], v[214:217], v[86:89]
	v_mfma_f32_16x16x32_bf16 v[82:85], v[190:193], v[214:217], v[82:85]
	v_mfma_f32_16x16x32_bf16 v[70:73], v[182:185], v[222:225], v[70:73]
	v_mfma_f32_16x16x32_bf16 v[66:69], v[190:193], v[222:225], v[66:69]
	v_mfma_f32_16x16x32_bf16 v[118:121], v[186:189], v[202:205], v[118:121]
	v_mfma_f32_16x16x32_bf16 v[114:117], v[194:197], v[202:205], v[114:117]
	v_mfma_f32_16x16x32_bf16 v[102:105], v[186:189], v[210:213], v[102:105]
	v_mfma_f32_16x16x32_bf16 v[98:101], v[194:197], v[210:213], v[98:101]
	v_mfma_f32_16x16x32_bf16 v[86:89], v[186:189], v[218:221], v[86:89]
	v_mfma_f32_16x16x32_bf16 v[82:85], v[194:197], v[218:221], v[82:85]
	v_mfma_f32_16x16x32_bf16 v[70:73], v[186:189], v[230:233], v[70:73]
	v_mfma_f32_16x16x32_bf16 v[66:69], v[194:197], v[230:233], v[66:69]
	s_setprio 0
	s_barrier
; #define PG8_STAGE_A(b, h, ptr, NX) do { if constexpr (Sched::GATHER) { unsigned gs_[2]; gs_[0] = ((NX) && last_) ? gN[h][0] : gA[h][0]; gs_[1] = ((NX) && last_) ? gN[h][1] : gA[h][1]; PG8_STAGE(PG8_SA(b, h), ptr, gs_); } \
;         else PG8_STAGE(PG8_SA(b, h), (ptr) + ((h) ? hstep : (size_t)0), voffA); } while (0)
; #define PG8_STAGE(bufoff, gbase, voff) do { _Pragma("unroll") for (int _i = 0; _i < 2; ++_i) \
;         __builtin_amdgcn_global_load_lds((const unsigned*)((const char*)(gbase) + (voff)[_i]), (PG8_LAS unsigned*)(lds + (bufoff) + ldsw + _i * 8192), 16, 0, 0); } while (0)
; #define PG8_LDA(dst, b, h) do { _Pragma("unroll") for (int m = 0; m < 4; ++m) _Pragma("unroll") for (int k = 0; k < 2; ++k) dst[m][k] = *(const PG8_LAS bf16x8*)(lds + PG8_SA(b, h) + aoff + m * 2048 + k * 1024); } while (0)
; #define PG8_MMA(ai, bj, At, Bt) do { __builtin_amdgcn_s_setprio(1); _Pragma("unroll") for (int m = 0; m < 4; ++m) _Pragma("unroll") for (int n = 0; n < 2; ++n) _Pragma("unroll") for (int k = 0; k < 2; ++k) \
;         acc[ai][bj][m][n] = __builtin_amdgcn_mfma_f32_16x16x32_bf16(Bt[n][k], At[m][k], acc[ai][bj][m][n], 0, 0, 0); __builtin_amdgcn_s_setprio(0); } while (0)
; #define PG8_WAIT_V(n) asm volatile("s_waitcnt vmcnt(" #n ")" ::: "memory")
; #define PG8_WAIT_L(n) asm volatile("s_waitcnt lgkmcnt(" #n ")" ::: "memory")
; #define PG8_BAR __builtin_amdgcn_s_barrier()
; #define PG8_SCHED __builtin_amdgcn_sched_barrier(0)
; template <class Epi, class Sched, bool ALIGN_EPI = false, bool SP2 = false>
; __device__ __forceinline__ void gemm_phase(PG8_LAS unsigned char* lds, const Gemm g, const Sched& S, const Epi& E, const bool skip_epi = false) {
;     ...
;             PG8_LDA(At, 1, 1); PG8_STAGE(PG8_SB(1, 0), b3, voffB); PG8_STAGE(PG8_SB(1, 1), b3 + hstep, voffB); PG8_STAGE_A(1, 0, a3, true);
;             PG8_WAIT_V(8); PG8_WAIT_L(0); PG8_BAR; PG8_MMA(1, 0, At, B0); PG8_MMA(1, 1, At, B1); PG8_BAR; PG8_SCHED;
;     ...
;         if constexpr (ALIGN_EPI) { if (wr == 0) PG8_BAR; }
	s_add_i32 s44, s64, s50
	v_lshl_add_u64 v[226:227], v[226:227], 0, s[22:23]
	s_mov_b32 m0, s44
	ds_read_b128 v[198:201], v160 offset:49152
	ds_read_b128 v[202:205], v160 offset:50176
	ds_read_b128 v[206:209], v160 offset:51200
	ds_read_b128 v[210:213], v160 offset:52224
	ds_read_b128 v[214:217], v160 offset:53248
	ds_read_b128 v[218:221], v160 offset:54272
	ds_read_b128 v[222:225], v160 offset:55296
	ds_read_b128 v[230:233], v160 offset:56320
	global_load_lds_dwordx4 v[226:227], off
	s_add_i32 m0, s44, 0x2000
	s_add_u32 s42, s42, 0x40080
	v_lshl_add_u64 v[226:227], v[234:235], 0, s[22:23]
	s_addc_u32 s43, s43, 0
	s_add_i32 s44, s65, s50
	global_load_lds_dwordx4 v[226:227], off
	v_lshl_add_u64 v[226:227], s[42:43], 0, v[134:135]
	s_mov_b32 m0, s44
	s_nop 0
	global_load_lds_dwordx4 v[226:227], off
	v_lshl_add_u64 v[226:227], s[42:43], 0, v[136:137]
	s_add_i32 m0, s44, 0x2000
	s_nop 0
	global_load_lds_dwordx4 v[226:227], off
	v_lshl_add_u64 v[226:227], v[238:239], 0, s[22:23]
	s_mov_b32 m0, s55
	s_nop 0
	global_load_lds_dwordx4 v[226:227], off
	v_lshl_add_u64 v[226:227], v[236:237], 0, s[22:23]
	s_mov_b32 m0, s56
	s_nop 0
	global_load_lds_dwordx4 v[226:227], off
	s_waitcnt vmcnt(8)
	s_waitcnt lgkmcnt(0)
	s_barrier
	s_setprio 3
	s_waitcnt lgkmcnt(0)
	v_mfma_f32_16x16x32_bf16 v[62:65], v[166:169], v[198:201], v[62:65]
	v_mfma_f32_16x16x32_bf16 v[58:61], v[174:177], v[198:201], v[58:61]
	v_mfma_f32_16x16x32_bf16 v[38:41], v[166:169], v[206:209], v[38:41]
	v_mfma_f32_16x16x32_bf16 v[34:37], v[174:177], v[206:209], v[34:37]
	v_mfma_f32_16x16x32_bf16 v[22:25], v[166:169], v[214:217], v[22:25]
	v_mfma_f32_16x16x32_bf16 v[18:21], v[174:177], v[214:217], v[18:21]
	v_mfma_f32_16x16x32_bf16 v[6:9], v[166:169], v[222:225], v[6:9]
	v_mfma_f32_16x16x32_bf16 v[2:5], v[174:177], v[222:225], v[2:5]
	v_mfma_f32_16x16x32_bf16 v[62:65], v[170:173], v[202:205], v[62:65]
	v_mfma_f32_16x16x32_bf16 v[58:61], v[178:181], v[202:205], v[58:61]
	v_mfma_f32_16x16x32_bf16 v[38:41], v[170:173], v[210:213], v[38:41]
	v_mfma_f32_16x16x32_bf16 v[34:37], v[178:181], v[210:213], v[34:37]
	v_mfma_f32_16x16x32_bf16 v[22:25], v[170:173], v[218:221], v[22:25]
	v_mfma_f32_16x16x32_bf16 v[18:21], v[178:181], v[218:221], v[18:21]
	v_mfma_f32_16x16x32_bf16 v[6:9], v[170:173], v[230:233], v[6:9]
	v_mfma_f32_16x16x32_bf16 v[2:5], v[178:181], v[230:233], v[2:5]
	s_setprio 0
	s_setprio 3
	v_mfma_f32_16x16x32_bf16 v[50:53], v[182:185], v[198:201], v[50:53]
	v_mfma_f32_16x16x32_bf16 v[42:45], v[190:193], v[198:201], v[42:45]
	v_mfma_f32_16x16x32_bf16 v[54:57], v[182:185], v[206:209], v[54:57]
	v_mfma_f32_16x16x32_bf16 v[46:49], v[190:193], v[206:209], v[46:49]
	v_mfma_f32_16x16x32_bf16 v[30:33], v[182:185], v[214:217], v[30:33]
	v_mfma_f32_16x16x32_bf16 v[26:29], v[190:193], v[214:217], v[26:29]
	v_mfma_f32_16x16x32_bf16 v[14:17], v[182:185], v[222:225], v[14:17]
	v_mfma_f32_16x16x32_bf16 v[10:13], v[190:193], v[222:225], v[10:13]
	v_mfma_f32_16x16x32_bf16 v[50:53], v[186:189], v[202:205], v[50:53]
	v_mfma_f32_16x16x32_bf16 v[42:45], v[194:197], v[202:205], v[42:45]
	v_mfma_f32_16x16x32_bf16 v[54:57], v[186:189], v[210:213], v[54:57]
	v_mfma_f32_16x16x32_bf16 v[46:49], v[194:197], v[210:213], v[46:49]
	v_mfma_f32_16x16x32_bf16 v[30:33], v[186:189], v[218:221], v[30:33]
	v_mfma_f32_16x16x32_bf16 v[26:29], v[194:197], v[218:221], v[26:29]
	v_mfma_f32_16x16x32_bf16 v[14:17], v[186:189], v[230:233], v[14:17]
	v_mfma_f32_16x16x32_bf16 v[10:13], v[194:197], v[230:233], v[10:13]
	s_setprio 0
	s_barrier
	s_add_i32 s63, s63, 2
	s_add_u32 s40, s40, 0x100
	s_addc_u32 s41, s41, 0
	s_cmp_gt_u32 s63, 13
	s_cbranch_scc0 .LBB0_1728
	s_and_b64 vcc, exec, s[26:27]
	s_cbranch_vccz .LBB0_1731
	s_barrier

; #define PG8_STAGE_A(b, h, ptr, NX) do { if constexpr (Sched::GATHER) { unsigned gs_[2]; gs_[0] = ((NX) && last_) ? gN[h][0] : gA[h][0]; gs_[1] = ((NX) && last_) ? gN[h][1] : gA[h][1]; PG8_STAGE(PG8_SA(b, h), ptr, gs_); } \
;         else PG8_STAGE(PG8_SA(b, h), (ptr) + ((h) ? hstep : (size_t)0), voffA); } while (0)
; #define PG8_STAGE(bufoff, gbase, voff) do { _Pragma("unroll") for (int _i = 0; _i < 2; ++_i) \
;         __builtin_amdgcn_global_load_lds((const unsigned*)((const char*)(gbase) + (voff)[_i]), (PG8_LAS unsigned*)(lds + (bufoff) + ldsw + _i * 8192), 16, 0, 0); } while (0)
; #define PG8_LDA(dst, b, h) do { _Pragma("unroll") for (int m = 0; m < 4; ++m) _Pragma("unroll") for (int k = 0; k < 2; ++k) dst[m][k] = *(const PG8_LAS bf16x8*)(lds + PG8_SA(b, h) + aoff + m * 2048 + k * 1024); } while (0)
; #define PG8_LDB(dst, b, h) do { _Pragma("unroll") for (int n = 0; n < 2; ++n) _Pragma("unroll") for (int k = 0; k < 2; ++k) dst[n][k] = *(const PG8_LAS bf16x8*)(lds + PG8_SB(b, h) + boff + n * 2048 + k * 1024); } while (0)
; #define PG8_WAIT_V(n) asm volatile("s_waitcnt vmcnt(" #n ")" ::: "memory")
; #define PG8_WAIT_L(n) asm volatile("s_waitcnt lgkmcnt(" #n ")" ::: "memory")
; #define PG8_BAR __builtin_amdgcn_s_barrier()
; #define PG8_SCHED __builtin_amdgcn_sched_barrier(0)
; template <class Epi, class Sched, bool ALIGN_EPI = false, bool SP2 = false>
; __device__ __forceinline__ void gemm_phase(PG8_LAS unsigned char* lds, const Gemm g, const Sched& S, const Epi& E, const bool skip_epi = false) {
;     ...
;         for (int t = 0; t < nt; t += 2) {
;             const bool last = (t == nt - 2); last_ = last && has_next;
;             const char* a1 = cA + (size_t)(t + 1) * kstep;
;             const char* a2 = last ? nA : cA + (size_t)(t + 2) * kstep; const char* b2 = last ? nB : cB + (size_t)(t + 2) * kstep;
;             const char* a3 = a2 + kstep; const char* b3 = b2 + kstep;
;             if (last && has_next) S.a_ready(nxt);
;             if constexpr (SP2) {
;             PG8_LDB(B0, 0, 0); PG8_LDB(B1, 0, 1); PG8_SCHED; PG8_LDA(At, 0, 0); PG8_STAGE_A(1, 1, a1, false);
;             PG8_WAIT_V(8); PG8_WAIT_L(0); PG8_BAR; PG8_MMA(0, 0, At, B0); PG8_MMA(0, 1, At, B1); PG8_BAR; PG8_SCHED;
;             PG8_LDA(At, 0, 1); PG8_STAGE(PG8_SB(0, 0), b2, voffB); PG8_STAGE(PG8_SB(0, 1), b2 + hstep, voffB); PG8_STAGE_A(0, 0, a2, true);
.LBB0_1822:
	s_add_u32 s67, s40, 0x100
	s_addc_u32 s68, s41, 0
	s_mov_b32 s69, -2
	ds_read_b128 v[160:163], v157
	ds_read_b128 v[164:167], v157 offset:1024
	ds_read_b128 v[168:171], v157 offset:2048
	ds_read_b128 v[172:175], v157 offset:3072
	ds_read_b128 v[176:179], v158
	ds_read_b128 v[180:183], v158 offset:1024
	ds_read_b128 v[184:187], v158 offset:2048
	ds_read_b128 v[188:191], v158 offset:3072
	s_add_u32 s40, s38, 0x100
	s_addc_u32 s41, s39, 0
	s_cmp_eq_u32 s69, 52
	s_cselect_b32 s45, s7, s41
	s_cselect_b32 s44, s6, s40
	s_cselect_b32 s43, s35, s68
	s_cselect_b32 s42, s34, s67
	v_lshl_add_u64 v[152:153], s[38:39], 0, v[140:141]
	s_add_i32 m0, s37, 0xc000
	ds_read_b128 v[192:195], v159
	ds_read_b128 v[196:199], v159 offset:1024
	ds_read_b128 v[200:203], v159 offset:2048
	ds_read_b128 v[204:207], v159 offset:3072
	ds_read_b128 v[208:211], v159 offset:4096
	ds_read_b128 v[212:215], v159 offset:5120
	ds_read_b128 v[216:219], v159 offset:6144
	ds_read_b128 v[220:223], v159 offset:7168
	global_load_lds_dwordx4 v[152:153], off
	v_lshl_add_u64 v[152:153], s[38:39], 0, v[142:143]
	s_add_i32 m0, s37, 0xe000
	s_nop 0
	global_load_lds_dwordx4 v[152:153], off
	s_waitcnt vmcnt(8)
	s_waitcnt lgkmcnt(0)
	s_barrier
	s_setprio 3
	s_waitcnt lgkmcnt(0)
	v_mfma_f32_16x16x32_bf16 v[126:129], v[160:163], v[192:195], 0
	v_mfma_f32_16x16x32_bf16 v[122:125], v[168:171], v[192:195], 0
	v_mfma_f32_16x16x32_bf16 v[118:121], v[160:163], v[200:203], 0
	v_mfma_f32_16x16x32_bf16 v[114:117], v[168:171], v[200:203], 0
	v_mfma_f32_16x16x32_bf16 v[106:109], v[160:163], v[208:211], 0
	v_mfma_f32_16x16x32_bf16 v[98:101], v[168:171], v[208:211], 0
	v_mfma_f32_16x16x32_bf16 v[78:81], v[160:163], v[216:219], 0
	v_mfma_f32_16x16x32_bf16 v[74:77], v[168:171], v[216:219], 0
	v_mfma_f32_16x16x32_bf16 v[126:129], v[164:167], v[196:199], v[126:129]
	v_mfma_f32_16x16x32_bf16 v[122:125], v[172:175], v[196:199], v[122:125]
	v_mfma_f32_16x16x32_bf16 v[118:121], v[164:167], v[204:207], v[118:121]
	v_mfma_f32_16x16x32_bf16 v[114:117], v[172:175], v[204:207], v[114:117]
	v_mfma_f32_16x16x32_bf16 v[106:109], v[164:167], v[212:215], v[106:109]
	v_mfma_f32_16x16x32_bf16 v[98:101], v[172:175], v[212:215], v[98:101]
	v_mfma_f32_16x16x32_bf16 v[78:81], v[164:167], v[220:223], v[78:81]
	v_mfma_f32_16x16x32_bf16 v[74:77], v[172:175], v[220:223], v[74:77]
	s_setprio 0
	s_setprio 3
	v_mfma_f32_16x16x32_bf16 v[110:113], v[176:179], v[192:195], 0
	v_mfma_f32_16x16x32_bf16 v[102:105], v[184:187], v[192:195], 0
	v_mfma_f32_16x16x32_bf16 v[94:97], v[176:179], v[200:203], 0
	v_mfma_f32_16x16x32_bf16 v[90:93], v[184:187], v[200:203], 0
	v_mfma_f32_16x16x32_bf16 v[86:89], v[176:179], v[208:211], 0
	v_mfma_f32_16x16x32_bf16 v[82:85], v[184:187], v[208:211], 0
	v_mfma_f32_16x16x32_bf16 v[70:73], v[176:179], v[216:219], 0
	v_mfma_f32_16x16x32_bf16 v[66:69], v[184:187], v[216:219], 0
	v_mfma_f32_16x16x32_bf16 v[110:113], v[180:183], v[196:199], v[110:113]
	v_mfma_f32_16x16x32_bf16 v[102:105], v[188:191], v[196:199], v[102:105]
	v_mfma_f32_16x16x32_bf16 v[94:97], v[180:183], v[204:207], v[94:97]
	v_mfma_f32_16x16x32_bf16 v[90:93], v[188:191], v[204:207], v[90:93]
	v_mfma_f32_16x16x32_bf16 v[86:89], v[180:183], v[212:215], v[86:89]
	v_mfma_f32_16x16x32_bf16 v[82:85], v[188:191], v[212:215], v[82:85]
	v_mfma_f32_16x16x32_bf16 v[70:73], v[180:183], v[220:223], v[70:73]
	v_mfma_f32_16x16x32_bf16 v[66:69], v[188:191], v[220:223], v[66:69]
	s_setprio 0
	s_barrier
	s_add_i32 s38, s60, s51
	v_lshl_add_u64 v[152:153], s[42:43], 0, v[134:135]
	s_mov_b32 m0, s38
	ds_read_b128 v[192:195], v159 offset:16384
	ds_read_b128 v[196:199], v159 offset:17408
	ds_read_b128 v[200:203], v159 offset:18432
	ds_read_b128 v[204:207], v159 offset:19456
	ds_read_b128 v[208:211], v159 offset:20480
	ds_read_b128 v[212:215], v159 offset:21504
	ds_read_b128 v[216:219], v159 offset:22528
	ds_read_b128 v[220:223], v159 offset:23552
	global_load_lds_dwordx4 v[152:153], off
	s_add_i32 m0, s38, 0x2000
	s_add_u32 s38, s42, 0xe0000
	v_lshl_add_u64 v[224:225], s[42:43], 0, v[138:139]
	s_addc_u32 s39, s43, 0
	s_add_i32 s70, s61, s51
	global_load_lds_dwordx4 v[224:225], off
	v_lshl_add_u64 v[226:227], s[38:39], 0, v[134:135]
	s_mov_b32 m0, s70
	v_lshl_add_u64 v[230:231], s[44:45], 0, v[136:137]
	global_load_lds_dwordx4 v[226:227], off
	v_lshl_add_u64 v[226:227], s[38:39], 0, v[138:139]
	s_add_i32 m0, s70, 0x2000
	s_nop 0
	global_load_lds_dwordx4 v[226:227], off
	v_lshl_add_u64 v[226:227], s[44:45], 0, v[132:133]
	s_mov_b32 m0, s37
	s_nop 0
	global_load_lds_dwordx4 v[226:227], off
	s_mov_b32 m0, s52
	s_nop 0
	global_load_lds_dwordx4 v[230:231], off
	s_waitcnt vmcnt(8)
	s_waitcnt lgkmcnt(0)
	s_barrier
; #define PG8_STAGE_A(b, h, ptr, NX) do { if constexpr (Sched::GATHER) { unsigned gs_[2]; gs_[0] = ((NX) && last_) ? gN[h][0] : gA[h][0]; gs_[1] = ((NX) && last_) ? gN[h][1] : gA[h][1]; PG8_STAGE(PG8_SA(b, h), ptr, gs_); } \
;         else PG8_STAGE(PG8_SA(b, h), (ptr) + ((h) ? hstep : (size_t)0), voffA); } while (0)
; #define PG8_LDA(dst, b, h) do { _Pragma("unroll") for (int m = 0; m < 4; ++m) _Pragma("unroll") for (int k = 0; k < 2; ++k) dst[m][k] = *(const PG8_LAS bf16x8*)(lds + PG8_SA(b, h) + aoff + m * 2048 + k * 1024); } while (0)
; #define PG8_LDB(dst, b, h) do { _Pragma("unroll") for (int n = 0; n < 2; ++n) _Pragma("unroll") for (int k = 0; k < 2; ++k) dst[n][k] = *(const PG8_LAS bf16x8*)(lds + PG8_SB(b, h) + boff + n * 2048 + k * 1024); } while (0)
; #define PG8_MMA(ai, bj, At, Bt) do { __builtin_amdgcn_s_setprio(1); _Pragma("unroll") for (int m = 0; m < 4; ++m) _Pragma("unroll") for (int n = 0; n < 2; ++n) _Pragma("unroll") for (int k = 0; k < 2; ++k) \
;         acc[ai][bj][m][n] = __builtin_amdgcn_mfma_f32_16x16x32_bf16(Bt[n][k], At[m][k], acc[ai][bj][m][n], 0, 0, 0); __builtin_amdgcn_s_setprio(0); } while (0)
; #define PG8_WAIT_V(n) asm volatile("s_waitcnt vmcnt(" #n ")" ::: "memory")
; #define PG8_WAIT_L(n) asm volatile("s_waitcnt lgkmcnt(" #n ")" ::: "memory")
; #define PG8_BAR __builtin_amdgcn_s_barrier()
; #define PG8_SCHED __builtin_amdgcn_sched_barrier(0)
; template <class Epi, class Sched, bool ALIGN_EPI = false, bool SP2 = false>
; __device__ __forceinline__ void gemm_phase(PG8_LAS unsigned char* lds, const Gemm g, const Sched& S, const Epi& E, const bool skip_epi = false) {
;     ...
;             PG8_WAIT_V(8); PG8_WAIT_L(0); PG8_BAR; PG8_MMA(1, 0, At, B0); PG8_MMA(1, 1, At, B1); PG8_BAR; PG8_SCHED;
;             PG8_LDB(B0, 1, 0); PG8_LDB(B1, 1, 1); PG8_SCHED; PG8_LDA(At, 1, 0); PG8_STAGE_A(0, 1, a2, true);
;             PG8_WAIT_V(8); PG8_WAIT_L(0); PG8_BAR; PG8_MMA(0, 0, At, B0); PG8_MMA(0, 1, At, B1); PG8_BAR; PG8_SCHED;
	s_setprio 3
	s_waitcnt lgkmcnt(0)
	v_mfma_f32_16x16x32_bf16 v[62:65], v[160:163], v[192:195], 0
	v_mfma_f32_16x16x32_bf16 v[58:61], v[168:171], v[192:195], 0
	v_mfma_f32_16x16x32_bf16 v[50:53], v[160:163], v[200:203], 0
	v_mfma_f32_16x16x32_bf16 v[42:45], v[168:171], v[200:203], 0
	v_mfma_f32_16x16x32_bf16 v[34:37], v[160:163], v[208:211], 0
	v_mfma_f32_16x16x32_bf16 v[26:29], v[168:171], v[208:211], 0
	v_mfma_f32_16x16x32_bf16 v[18:21], v[160:163], v[216:219], 0
	v_mfma_f32_16x16x32_bf16 v[10:13], v[168:171], v[216:219], 0
	v_mfma_f32_16x16x32_bf16 v[62:65], v[164:167], v[196:199], v[62:65]
	v_mfma_f32_16x16x32_bf16 v[58:61], v[172:175], v[196:199], v[58:61]
	v_mfma_f32_16x16x32_bf16 v[50:53], v[164:167], v[204:207], v[50:53]
	v_mfma_f32_16x16x32_bf16 v[42:45], v[172:175], v[204:207], v[42:45]
	v_mfma_f32_16x16x32_bf16 v[34:37], v[164:167], v[212:215], v[34:37]
	v_mfma_f32_16x16x32_bf16 v[26:29], v[172:175], v[212:215], v[26:29]
	v_mfma_f32_16x16x32_bf16 v[18:21], v[164:167], v[220:223], v[18:21]
	v_mfma_f32_16x16x32_bf16 v[10:13], v[172:175], v[220:223], v[10:13]
	s_setprio 0
	s_setprio 3
	v_mfma_f32_16x16x32_bf16 v[54:57], v[176:179], v[192:195], 0
	v_mfma_f32_16x16x32_bf16 v[46:49], v[184:187], v[192:195], 0
	v_mfma_f32_16x16x32_bf16 v[38:41], v[176:179], v[200:203], 0
	v_mfma_f32_16x16x32_bf16 v[30:33], v[184:187], v[200:203], 0
	v_mfma_f32_16x16x32_bf16 v[22:25], v[176:179], v[208:211], 0
	v_mfma_f32_16x16x32_bf16 v[14:17], v[184:187], v[208:211], 0
	v_mfma_f32_16x16x32_bf16 v[6:9], v[176:179], v[216:219], 0
	v_mfma_f32_16x16x32_bf16 v[2:5], v[184:187], v[216:219], 0
	v_mfma_f32_16x16x32_bf16 v[54:57], v[180:183], v[196:199], v[54:57]
	v_mfma_f32_16x16x32_bf16 v[46:49], v[188:191], v[196:199], v[46:49]
	v_mfma_f32_16x16x32_bf16 v[38:41], v[180:183], v[204:207], v[38:41]
	v_mfma_f32_16x16x32_bf16 v[30:33], v[188:191], v[204:207], v[30:33]
	v_mfma_f32_16x16x32_bf16 v[22:25], v[180:183], v[212:215], v[22:25]
	v_mfma_f32_16x16x32_bf16 v[14:17], v[188:191], v[212:215], v[14:17]
	v_mfma_f32_16x16x32_bf16 v[6:9], v[180:183], v[220:223], v[6:9]
	v_mfma_f32_16x16x32_bf16 v[2:5], v[188:191], v[220:223], v[2:5]
	s_setprio 0
	s_barrier
	s_add_i32 s70, 0, 0x18000
	v_add_u32_e32 v130, s70, v147
	s_add_i32 s71, 0, 0x1c000
	ds_read_b128 v[160:163], v130
	ds_read_b128 v[164:167], v130 offset:1024
	ds_read_b128 v[168:171], v130 offset:2048
	ds_read_b128 v[172:175], v130 offset:3072
	v_add_u32_e32 v130, s71, v147
	ds_read_b128 v[176:179], v130
	ds_read_b128 v[180:183], v130 offset:1024
	ds_read_b128 v[184:187], v130 offset:2048
	ds_read_b128 v[188:191], v130 offset:3072
	s_add_u32 s38, s44, 0xe0000
	s_addc_u32 s39, s45, 0
	s_mov_b32 m0, s53
	v_lshl_add_u64 v[232:233], s[38:39], 0, v[132:133]
	ds_read_b128 v[192:195], v159 offset:32768
	ds_read_b128 v[196:199], v159 offset:33792
	ds_read_b128 v[200:203], v159 offset:34816
	ds_read_b128 v[204:207], v159 offset:35840
	ds_read_b128 v[208:211], v159 offset:36864
	ds_read_b128 v[212:215], v159 offset:37888
	ds_read_b128 v[216:219], v159 offset:38912
	ds_read_b128 v[220:223], v159 offset:39936
	global_load_lds_dwordx4 v[232:233], off
	v_lshl_add_u64 v[232:233], s[38:39], 0, v[136:137]
	s_mov_b32 m0, s54
	s_nop 0
	global_load_lds_dwordx4 v[232:233], off
	s_waitcnt vmcnt(8)
	s_waitcnt lgkmcnt(0)
	s_barrier
	s_setprio 3
	s_waitcnt lgkmcnt(0)
	v_mfma_f32_16x16x32_bf16 v[126:129], v[160:163], v[192:195], v[126:129]
	v_mfma_f32_16x16x32_bf16 v[122:125], v[168:171], v[192:195], v[122:125]
	v_mfma_f32_16x16x32_bf16 v[118:121], v[160:163], v[200:203], v[118:121]
	v_mfma_f32_16x16x32_bf16 v[114:117], v[168:171], v[200:203], v[114:117]
	v_mfma_f32_16x16x32_bf16 v[106:109], v[160:163], v[208:211], v[106:109]
	v_mfma_f32_16x16x32_bf16 v[98:101], v[168:171], v[208:211], v[98:101]
	v_mfma_f32_16x16x32_bf16 v[78:81], v[160:163], v[216:219], v[78:81]
	v_mfma_f32_16x16x32_bf16 v[74:77], v[168:171], v[216:219], v[74:77]
	v_mfma_f32_16x16x32_bf16 v[126:129], v[164:167], v[196:199], v[126:129]
	v_mfma_f32_16x16x32_bf16 v[122:125], v[172:175], v[196:199], v[122:125]
	v_mfma_f32_16x16x32_bf16 v[118:121], v[164:167], v[204:207], v[118:121]
	v_mfma_f32_16x16x32_bf16 v[114:117], v[172:175], v[204:207], v[114:117]
	v_mfma_f32_16x16x32_bf16 v[106:109], v[164:167], v[212:215], v[106:109]
	v_mfma_f32_16x16x32_bf16 v[98:101], v[172:175], v[212:215], v[98:101]
	v_mfma_f32_16x16x32_bf16 v[78:81], v[164:167], v[220:223], v[78:81]
	v_mfma_f32_16x16x32_bf16 v[74:77], v[172:175], v[220:223], v[74:77]
	s_setprio 0
	s_setprio 3
	v_mfma_f32_16x16x32_bf16 v[110:113], v[176:179], v[192:195], v[110:113]
	v_mfma_f32_16x16x32_bf16 v[102:105], v[184:187], v[192:195], v[102:105]
	v_mfma_f32_16x16x32_bf16 v[94:97], v[176:179], v[200:203], v[94:97]
	v_mfma_f32_16x16x32_bf16 v[90:93], v[184:187], v[200:203], v[90:93]
	v_mfma_f32_16x16x32_bf16 v[86:89], v[176:179], v[208:211], v[86:89]
	v_mfma_f32_16x16x32_bf16 v[82:85], v[184:187], v[208:211], v[82:85]
	v_mfma_f32_16x16x32_bf16 v[70:73], v[176:179], v[216:219], v[70:73]
	v_mfma_f32_16x16x32_bf16 v[66:69], v[184:187], v[216:219], v[66:69]
	v_mfma_f32_16x16x32_bf16 v[110:113], v[180:183], v[196:199], v[110:113]
	v_mfma_f32_16x16x32_bf16 v[102:105], v[188:191], v[196:199], v[102:105]
	v_mfma_f32_16x16x32_bf16 v[94:97], v[180:183], v[204:207], v[94:97]
	v_mfma_f32_16x16x32_bf16 v[90:93], v[188:191], v[204:207], v[90:93]
	v_mfma_f32_16x16x32_bf16 v[86:89], v[180:183], v[212:215], v[86:89]
	v_mfma_f32_16x16x32_bf16 v[82:85], v[188:191], v[212:215], v[82:85]
	v_mfma_f32_16x16x32_bf16 v[70:73], v[180:183], v[220:223], v[70:73]
	v_mfma_f32_16x16x32_bf16 v[66:69], v[188:191], v[220:223], v[66:69]
	s_setprio 0
	s_barrier
; #define PG8_STAGE_A(b, h, ptr, NX) do { if constexpr (Sched::GATHER) { unsigned gs_[2]; gs_[0] = ((NX) && last_) ? gN[h][0] : gA[h][0]; gs_[1] = ((NX) && last_) ? gN[h][1] : gA[h][1]; PG8_STAGE(PG8_SA(b, h), ptr, gs_); } \
;         else PG8_STAGE(PG8_SA(b, h), (ptr) + ((h) ? hstep : (size_t)0), voffA); } while (0)
; #define PG8_STAGE(bufoff, gbase, voff) do { _Pragma("unroll") for (int _i = 0; _i < 2; ++_i) \
;         __builtin_amdgcn_global_load_lds((const unsigned*)((const char*)(gbase) + (voff)[_i]), (PG8_LAS unsigned*)(lds + (bufoff) + ldsw + _i * 8192), 16, 0, 0); } while (0)
; #define PG8_LDA(dst, b, h) do { _Pragma("unroll") for (int m = 0; m < 4; ++m) _Pragma("unroll") for (int k = 0; k < 2; ++k) dst[m][k] = *(const PG8_LAS bf16x8*)(lds + PG8_SA(b, h) + aoff + m * 2048 + k * 1024); } while (0)
; #define PG8_LDB(dst, b, h) do { _Pragma("unroll") for (int n = 0; n < 2; ++n) _Pragma("unroll") for (int k = 0; k < 2; ++k) dst[n][k] = *(const PG8_LAS bf16x8*)(lds + PG8_SB(b, h) + boff + n * 2048 + k * 1024); } while (0)
; #define PG8_WAIT_V(n) asm volatile("s_waitcnt vmcnt(" #n ")" ::: "memory")
; #define PG8_BAR __builtin_amdgcn_s_barrier()
; template <class Epi, class Sched, bool ALIGN_EPI = false, bool SP2 = false>
; __device__ __forceinline__ void gemm_phase(PG8_LAS unsigned char* lds, const Gemm g, const Sched& S, const Epi& E, const bool skip_epi = false) {
;     ...
;             PG8_LDB(B0, 0, 0); PG8_LDB(B1, 0, 1); PG8_SCHED; PG8_LDA(At, 0, 0); PG8_STAGE_A(1, 1, a1, false);
;             PG8_WAIT_V(8); PG8_WAIT_L(0); PG8_BAR; PG8_MMA(0, 0, At, B0); PG8_MMA(0, 1, At, B1); PG8_BAR; PG8_SCHED;
;             PG8_LDA(At, 0, 1); PG8_STAGE(PG8_SB(0, 0), b2, voffB); PG8_STAGE(PG8_SB(0, 1), b2 + hstep, voffB); PG8_STAGE_A(0, 0, a2, true);
;             PG8_WAIT_V(8); PG8_WAIT_L(0); PG8_BAR; PG8_MMA(1, 0, At, B0); PG8_MMA(1, 1, At, B1); PG8_BAR; PG8_SCHED;
;             PG8_LDB(B0, 1, 0); PG8_LDB(B1, 1, 1); PG8_SCHED; PG8_LDA(At, 1, 0); PG8_STAGE_A(0, 1, a2, true);
;             PG8_WAIT_V(8); PG8_WAIT_L(0); PG8_BAR; PG8_MMA(0, 0, At, B0); PG8_MMA(0, 1, At, B1); PG8_BAR; PG8_SCHED;
;             PG8_LDA(At, 1, 1); PG8_STAGE(PG8_SB(1, 0), b3, voffB); PG8_STAGE(PG8_SB(1, 1), b3 + hstep, voffB); PG8_STAGE_A(1, 0, a3, true);
;             PG8_WAIT_V(8); PG8_WAIT_L(0); PG8_BAR; PG8_MMA(1, 0, At, B0); PG8_MMA(1, 1, At, B1); PG8_BAR; PG8_SCHED;
	s_add_i32 s38, s70, s51
	v_lshl_add_u64 v[152:153], v[152:153], 0, s[18:19]
	s_mov_b32 m0, s38
	ds_read_b128 v[192:195], v159 offset:49152
	ds_read_b128 v[196:199], v159 offset:50176
	ds_read_b128 v[200:203], v159 offset:51200
	ds_read_b128 v[204:207], v159 offset:52224
	ds_read_b128 v[208:211], v159 offset:53248
	ds_read_b128 v[212:215], v159 offset:54272
	ds_read_b128 v[216:219], v159 offset:55296
	ds_read_b128 v[220:223], v159 offset:56320
	global_load_lds_dwordx4 v[152:153], off
	s_add_i32 m0, s38, 0x2000
	s_add_u32 s38, s42, 0xe0080
	v_lshl_add_u64 v[152:153], v[224:225], 0, s[18:19]
	s_addc_u32 s39, s43, 0
	s_add_i32 s42, s71, s51
	global_load_lds_dwordx4 v[152:153], off
	v_lshl_add_u64 v[152:153], s[38:39], 0, v[134:135]
	s_mov_b32 m0, s42
	s_nop 0
	global_load_lds_dwordx4 v[152:153], off
	v_lshl_add_u64 v[152:153], s[38:39], 0, v[138:139]
	s_add_i32 m0, s42, 0x2000
	s_nop 0
	global_load_lds_dwordx4 v[152:153], off
	v_lshl_add_u64 v[152:153], v[226:227], 0, s[18:19]
	s_mov_b32 m0, s57
	s_nop 0
	global_load_lds_dwordx4 v[152:153], off
	v_lshl_add_u64 v[152:153], v[230:231], 0, s[18:19]
	s_mov_b32 m0, s58
	s_nop 0
	global_load_lds_dwordx4 v[152:153], off
	s_waitcnt vmcnt(8)
	s_waitcnt lgkmcnt(0)
	s_barrier
	s_setprio 3
	s_waitcnt lgkmcnt(0)
	v_mfma_f32_16x16x32_bf16 v[62:65], v[160:163], v[192:195], v[62:65]
	v_mfma_f32_16x16x32_bf16 v[58:61], v[168:171], v[192:195], v[58:61]
	v_mfma_f32_16x16x32_bf16 v[50:53], v[160:163], v[200:203], v[50:53]
	v_mfma_f32_16x16x32_bf16 v[42:45], v[168:171], v[200:203], v[42:45]
	v_mfma_f32_16x16x32_bf16 v[34:37], v[160:163], v[208:211], v[34:37]
	v_mfma_f32_16x16x32_bf16 v[26:29], v[168:171], v[208:211], v[26:29]
	v_mfma_f32_16x16x32_bf16 v[18:21], v[160:163], v[216:219], v[18:21]
	v_mfma_f32_16x16x32_bf16 v[10:13], v[168:171], v[216:219], v[10:13]
	v_mfma_f32_16x16x32_bf16 v[62:65], v[164:167], v[196:199], v[62:65]
	v_mfma_f32_16x16x32_bf16 v[58:61], v[172:175], v[196:199], v[58:61]
	v_mfma_f32_16x16x32_bf16 v[50:53], v[164:167], v[204:207], v[50:53]
	v_mfma_f32_16x16x32_bf16 v[42:45], v[172:175], v[204:207], v[42:45]
	v_mfma_f32_16x16x32_bf16 v[34:37], v[164:167], v[212:215], v[34:37]
	v_mfma_f32_16x16x32_bf16 v[26:29], v[172:175], v[212:215], v[26:29]
	v_mfma_f32_16x16x32_bf16 v[18:21], v[164:167], v[220:223], v[18:21]
	v_mfma_f32_16x16x32_bf16 v[10:13], v[172:175], v[220:223], v[10:13]
	s_setprio 0
	s_setprio 3
	v_mfma_f32_16x16x32_bf16 v[54:57], v[176:179], v[192:195], v[54:57]
	v_mfma_f32_16x16x32_bf16 v[46:49], v[184:187], v[192:195], v[46:49]
	v_mfma_f32_16x16x32_bf16 v[38:41], v[176:179], v[200:203], v[38:41]
	v_mfma_f32_16x16x32_bf16 v[30:33], v[184:187], v[200:203], v[30:33]
	v_mfma_f32_16x16x32_bf16 v[22:25], v[176:179], v[208:211], v[22:25]
	v_mfma_f32_16x16x32_bf16 v[14:17], v[184:187], v[208:211], v[14:17]
	v_mfma_f32_16x16x32_bf16 v[6:9], v[176:179], v[216:219], v[6:9]
	v_mfma_f32_16x16x32_bf16 v[2:5], v[184:187], v[216:219], v[2:5]
	v_mfma_f32_16x16x32_bf16 v[54:57], v[180:183], v[196:199], v[54:57]
	v_mfma_f32_16x16x32_bf16 v[46:49], v[188:191], v[196:199], v[46:49]
	v_mfma_f32_16x16x32_bf16 v[38:41], v[180:183], v[204:207], v[38:41]
	v_mfma_f32_16x16x32_bf16 v[30:33], v[188:191], v[204:207], v[30:33]
	v_mfma_f32_16x16x32_bf16 v[22:25], v[180:183], v[212:215], v[22:25]
	v_mfma_f32_16x16x32_bf16 v[14:17], v[188:191], v[212:215], v[14:17]
	v_mfma_f32_16x16x32_bf16 v[6:9], v[180:183], v[220:223], v[6:9]
	v_mfma_f32_16x16x32_bf16 v[2:5], v[188:191], v[220:223], v[2:5]
	s_setprio 0
	s_barrier
	s_add_i32 s69, s69, 2
	s_add_u32 s67, s67, 0x100
	s_addc_u32 s68, s68, 0
	s_cmp_gt_u32 s69, 53
	s_mov_b64 s[38:39], s[40:41]
.LBB0_1823:
	ds_read_b128 v[160:163], v157
	ds_read_b128 v[164:167], v157 offset:1024
	ds_read_b128 v[168:171], v157 offset:2048
	ds_read_b128 v[172:175], v157 offset:3072
	ds_read_b128 v[176:179], v158
	ds_read_b128 v[180:183], v158 offset:1024
	ds_read_b128 v[184:187], v158 offset:2048
	ds_read_b128 v[188:191], v158 offset:3072
	s_add_u32 s40, s38, 0x100
	s_addc_u32 s41, s39, 0
	s_cmp_eq_u32 s69, 52
	s_cselect_b32 s45, s7, s41
	s_cselect_b32 s44, s6, s40
	s_cselect_b32 s43, s35, s68
	s_cselect_b32 s42, s34, s67
	v_lshl_add_u64 v[152:153], s[38:39], 0, v[140:141]
	s_add_i32 m0, s37, 0xc000
	ds_read_b128 v[192:195], v159
	ds_read_b128 v[196:199], v159 offset:1024
	ds_read_b128 v[200:203], v159 offset:2048
	ds_read_b128 v[204:207], v159 offset:3072
	ds_read_b128 v[208:211], v159 offset:4096
	ds_read_b128 v[212:215], v159 offset:5120
	ds_read_b128 v[216:219], v159 offset:6144
	ds_read_b128 v[220:223], v159 offset:7168
	global_load_lds_dwordx4 v[152:153], off
	v_lshl_add_u64 v[152:153], s[38:39], 0, v[142:143]
	s_add_i32 m0, s37, 0xe000
	s_nop 0
	global_load_lds_dwordx4 v[152:153], off
	s_waitcnt vmcnt(8)
	s_waitcnt lgkmcnt(0)
	s_barrier
; #define PG8_STAGE_A(b, h, ptr, NX) do { if constexpr (Sched::GATHER) { unsigned gs_[2]; gs_[0] = ((NX) && last_) ? gN[h][0] : gA[h][0]; gs_[1] = ((NX) && last_) ? gN[h][1] : gA[h][1]; PG8_STAGE(PG8_SA(b, h), ptr, gs_); } \
;         else PG8_STAGE(PG8_SA(b, h), (ptr) + ((h) ? hstep : (size_t)0), voffA); } while (0)
; #define PG8_STAGE(bufoff, gbase, voff) do { _Pragma("unroll") for (int _i = 0; _i < 2; ++_i) \
;         __builtin_amdgcn_global_load_lds((const unsigned*)((const char*)(gbase) + (voff)[_i]), (PG8_LAS unsigned*)(lds + (bufoff) + ldsw + _i * 8192), 16, 0, 0); } while (0)
; #define PG8_LDA(dst, b, h) do { _Pragma("unroll") for (int m = 0; m < 4; ++m) _Pragma("unroll") for (int k = 0; k < 2; ++k) dst[m][k] = *(const PG8_LAS bf16x8*)(lds + PG8_SA(b, h) + aoff + m * 2048 + k * 1024); } while (0)
; #define PG8_LDB(dst, b, h) do { _Pragma("unroll") for (int n = 0; n < 2; ++n) _Pragma("unroll") for (int k = 0; k < 2; ++k) dst[n][k] = *(const PG8_LAS bf16x8*)(lds + PG8_SB(b, h) + boff + n * 2048 + k * 1024); } while (0)
; #define PG8_MMA(ai, bj, At, Bt) do { __builtin_amdgcn_s_setprio(1); _Pragma("unroll") for (int m = 0; m < 4; ++m) _Pragma("unroll") for (int n = 0; n < 2; ++n) _Pragma("unroll") for (int k = 0; k < 2; ++k) \
;         acc[ai][bj][m][n] = __builtin_amdgcn_mfma_f32_16x16x32_bf16(Bt[n][k], At[m][k], acc[ai][bj][m][n], 0, 0, 0); __builtin_amdgcn_s_setprio(0); } while (0)
; #define PG8_WAIT_V(n) asm volatile("s_waitcnt vmcnt(" #n ")" ::: "memory")
; #define PG8_WAIT_L(n) asm volatile("s_waitcnt lgkmcnt(" #n ")" ::: "memory")
; #define PG8_BAR __builtin_amdgcn_s_barrier()
; #define PG8_SCHED __builtin_amdgcn_sched_barrier(0)
; template <class Epi, class Sched, bool ALIGN_EPI = false, bool SP2 = false>
; __device__ __forceinline__ void gemm_phase(PG8_LAS unsigned char* lds, const Gemm g, const Sched& S, const Epi& E, const bool skip_epi = false) {
;     ...
;             PG8_LDB(B0, 0, 0); PG8_LDB(B1, 0, 1); PG8_SCHED; PG8_LDA(At, 0, 0); PG8_STAGE_A(1, 1, a1, false);
;             PG8_WAIT_V(8); PG8_WAIT_L(0); PG8_BAR; PG8_MMA(0, 0, At, B0); PG8_MMA(0, 1, At, B1); PG8_BAR; PG8_SCHED;
;             PG8_LDA(At, 0, 1); PG8_STAGE(PG8_SB(0, 0), b2, voffB); PG8_STAGE(PG8_SB(0, 1), b2 + hstep, voffB); PG8_STAGE_A(0, 0, a2, true);
;             PG8_WAIT_V(8); PG8_WAIT_L(0); PG8_BAR; PG8_MMA(1, 0, At, B0); PG8_MMA(1, 1, At, B1); PG8_BAR; PG8_SCHED;
	s_setprio 3
	s_waitcnt lgkmcnt(0)
	v_mfma_f32_16x16x32_bf16 v[126:129], v[160:163], v[192:195], v[126:129]
	v_mfma_f32_16x16x32_bf16 v[122:125], v[168:171], v[192:195], v[122:125]
	v_mfma_f32_16x16x32_bf16 v[118:121], v[160:163], v[200:203], v[118:121]
	v_mfma_f32_16x16x32_bf16 v[114:117], v[168:171], v[200:203], v[114:117]
	v_mfma_f32_16x16x32_bf16 v[106:109], v[160:163], v[208:211], v[106:109]
	v_mfma_f32_16x16x32_bf16 v[98:101], v[168:171], v[208:211], v[98:101]
	v_mfma_f32_16x16x32_bf16 v[78:81], v[160:163], v[216:219], v[78:81]
	v_mfma_f32_16x16x32_bf16 v[74:77], v[168:171], v[216:219], v[74:77]
	v_mfma_f32_16x16x32_bf16 v[126:129], v[164:167], v[196:199], v[126:129]
	v_mfma_f32_16x16x32_bf16 v[122:125], v[172:175], v[196:199], v[122:125]
	v_mfma_f32_16x16x32_bf16 v[118:121], v[164:167], v[204:207], v[118:121]
	v_mfma_f32_16x16x32_bf16 v[114:117], v[172:175], v[204:207], v[114:117]
	v_mfma_f32_16x16x32_bf16 v[106:109], v[164:167], v[212:215], v[106:109]
	v_mfma_f32_16x16x32_bf16 v[98:101], v[172:175], v[212:215], v[98:101]
	v_mfma_f32_16x16x32_bf16 v[78:81], v[164:167], v[220:223], v[78:81]
	v_mfma_f32_16x16x32_bf16 v[74:77], v[172:175], v[220:223], v[74:77]
	s_setprio 0
	s_setprio 3
	v_mfma_f32_16x16x32_bf16 v[110:113], v[176:179], v[192:195], v[110:113]
	v_mfma_f32_16x16x32_bf16 v[102:105], v[184:187], v[192:195], v[102:105]
	v_mfma_f32_16x16x32_bf16 v[94:97], v[176:179], v[200:203], v[94:97]
	v_mfma_f32_16x16x32_bf16 v[90:93], v[184:187], v[200:203], v[90:93]
	v_mfma_f32_16x16x32_bf16 v[86:89], v[176:179], v[208:211], v[86:89]
	v_mfma_f32_16x16x32_bf16 v[82:85], v[184:187], v[208:211], v[82:85]
	v_mfma_f32_16x16x32_bf16 v[70:73], v[176:179], v[216:219], v[70:73]
	v_mfma_f32_16x16x32_bf16 v[66:69], v[184:187], v[216:219], v[66:69]
	v_mfma_f32_16x16x32_bf16 v[110:113], v[180:183], v[196:199], v[110:113]
	v_mfma_f32_16x16x32_bf16 v[102:105], v[188:191], v[196:199], v[102:105]
	v_mfma_f32_16x16x32_bf16 v[94:97], v[180:183], v[204:207], v[94:97]
	v_mfma_f32_16x16x32_bf16 v[90:93], v[188:191], v[204:207], v[90:93]
	v_mfma_f32_16x16x32_bf16 v[86:89], v[180:183], v[212:215], v[86:89]
	v_mfma_f32_16x16x32_bf16 v[82:85], v[188:191], v[212:215], v[82:85]
	v_mfma_f32_16x16x32_bf16 v[70:73], v[180:183], v[220:223], v[70:73]
	v_mfma_f32_16x16x32_bf16 v[66:69], v[188:191], v[220:223], v[66:69]
	s_setprio 0
	s_barrier
	s_add_i32 s38, s60, s51
	v_lshl_add_u64 v[152:153], s[42:43], 0, v[134:135]
	s_mov_b32 m0, s38
	ds_read_b128 v[192:195], v159 offset:16384
	ds_read_b128 v[196:199], v159 offset:17408
	ds_read_b128 v[200:203], v159 offset:18432
	ds_read_b128 v[204:207], v159 offset:19456
	ds_read_b128 v[208:211], v159 offset:20480
	ds_read_b128 v[212:215], v159 offset:21504
	ds_read_b128 v[216:219], v159 offset:22528
	ds_read_b128 v[220:223], v159 offset:23552
	global_load_lds_dwordx4 v[152:153], off
	s_add_i32 m0, s38, 0x2000
	s_add_u32 s38, s42, 0xe0000
	v_lshl_add_u64 v[224:225], s[42:43], 0, v[138:139]
	s_addc_u32 s39, s43, 0
	s_add_i32 s70, s61, s51
	global_load_lds_dwordx4 v[224:225], off
	v_lshl_add_u64 v[226:227], s[38:39], 0, v[134:135]
	s_mov_b32 m0, s70
	v_lshl_add_u64 v[230:231], s[44:45], 0, v[136:137]
	global_load_lds_dwordx4 v[226:227], off
	v_lshl_add_u64 v[226:227], s[38:39], 0, v[138:139]
	s_add_i32 m0, s70, 0x2000
	s_nop 0
	global_load_lds_dwordx4 v[226:227], off
	v_lshl_add_u64 v[226:227], s[44:45], 0, v[132:133]
	s_mov_b32 m0, s37
	s_nop 0
	global_load_lds_dwordx4 v[226:227], off
	s_mov_b32 m0, s52
	s_nop 0
	global_load_lds_dwordx4 v[230:231], off
	s_waitcnt vmcnt(8)
	s_waitcnt lgkmcnt(0)
	s_barrier
	s_setprio 3
	s_waitcnt lgkmcnt(0)
	v_mfma_f32_16x16x32_bf16 v[62:65], v[160:163], v[192:195], v[62:65]
	v_mfma_f32_16x16x32_bf16 v[58:61], v[168:171], v[192:195], v[58:61]
	v_mfma_f32_16x16x32_bf16 v[50:53], v[160:163], v[200:203], v[50:53]
	v_mfma_f32_16x16x32_bf16 v[42:45], v[168:171], v[200:203], v[42:45]
	v_mfma_f32_16x16x32_bf16 v[34:37], v[160:163], v[208:211], v[34:37]
	v_mfma_f32_16x16x32_bf16 v[26:29], v[168:171], v[208:211], v[26:29]
	v_mfma_f32_16x16x32_bf16 v[18:21], v[160:163], v[216:219], v[18:21]
	v_mfma_f32_16x16x32_bf16 v[10:13], v[168:171], v[216:219], v[10:13]
	v_mfma_f32_16x16x32_bf16 v[62:65], v[164:167], v[196:199], v[62:65]
	v_mfma_f32_16x16x32_bf16 v[58:61], v[172:175], v[196:199], v[58:61]
	v_mfma_f32_16x16x32_bf16 v[50:53], v[164:167], v[204:207], v[50:53]
	v_mfma_f32_16x16x32_bf16 v[42:45], v[172:175], v[204:207], v[42:45]
	v_mfma_f32_16x16x32_bf16 v[34:37], v[164:167], v[212:215], v[34:37]
	v_mfma_f32_16x16x32_bf16 v[26:29], v[172:175], v[212:215], v[26:29]
	v_mfma_f32_16x16x32_bf16 v[18:21], v[164:167], v[220:223], v[18:21]
	v_mfma_f32_16x16x32_bf16 v[10:13], v[172:175], v[220:223], v[10:13]
	s_setprio 0
	s_setprio 3
	v_mfma_f32_16x16x32_bf16 v[54:57], v[176:179], v[192:195], v[54:57]
	v_mfma_f32_16x16x32_bf16 v[46:49], v[184:187], v[192:195], v[46:49]
	v_mfma_f32_16x16x32_bf16 v[38:41], v[176:179], v[200:203], v[38:41]
	v_mfma_f32_16x16x32_bf16 v[30:33], v[184:187], v[200:203], v[30:33]
	v_mfma_f32_16x16x32_bf16 v[22:25], v[176:179], v[208:211], v[22:25]
	v_mfma_f32_16x16x32_bf16 v[14:17], v[184:187], v[208:211], v[14:17]
	v_mfma_f32_16x16x32_bf16 v[6:9], v[176:179], v[216:219], v[6:9]
	v_mfma_f32_16x16x32_bf16 v[2:5], v[184:187], v[216:219], v[2:5]
	v_mfma_f32_16x16x32_bf16 v[54:57], v[180:183], v[196:199], v[54:57]
	v_mfma_f32_16x16x32_bf16 v[46:49], v[188:191], v[196:199], v[46:49]
	v_mfma_f32_16x16x32_bf16 v[38:41], v[180:183], v[204:207], v[38:41]
	v_mfma_f32_16x16x32_bf16 v[30:33], v[188:191], v[204:207], v[30:33]
	v_mfma_f32_16x16x32_bf16 v[22:25], v[180:183], v[212:215], v[22:25]
	v_mfma_f32_16x16x32_bf16 v[14:17], v[188:191], v[212:215], v[14:17]
	v_mfma_f32_16x16x32_bf16 v[6:9], v[180:183], v[220:223], v[6:9]
	v_mfma_f32_16x16x32_bf16 v[2:5], v[188:191], v[220:223], v[2:5]
	s_setprio 0
	s_barrier
; #define PG8_STAGE_A(b, h, ptr, NX) do { if constexpr (Sched::GATHER) { unsigned gs_[2]; gs_[0] = ((NX) && last_) ? gN[h][0] : gA[h][0]; gs_[1] = ((NX) && last_) ? gN[h][1] : gA[h][1]; PG8_STAGE(PG8_SA(b, h), ptr, gs_); } \
;         else PG8_STAGE(PG8_SA(b, h), (ptr) + ((h) ? hstep : (size_t)0), voffA); } while (0)
; #define PG8_LDA(dst, b, h) do { _Pragma("unroll") for (int m = 0; m < 4; ++m) _Pragma("unroll") for (int k = 0; k < 2; ++k) dst[m][k] = *(const PG8_LAS bf16x8*)(lds + PG8_SA(b, h) + aoff + m * 2048 + k * 1024); } while (0)
; #define PG8_LDB(dst, b, h) do { _Pragma("unroll") for (int n = 0; n < 2; ++n) _Pragma("unroll") for (int k = 0; k < 2; ++k) dst[n][k] = *(const PG8_LAS bf16x8*)(lds + PG8_SB(b, h) + boff + n * 2048 + k * 1024); } while (0)
; #define PG8_MMA(ai, bj, At, Bt) do { __builtin_amdgcn_s_setprio(1); _Pragma("unroll") for (int m = 0; m < 4; ++m) _Pragma("unroll") for (int n = 0; n < 2; ++n) _Pragma("unroll") for (int k = 0; k < 2; ++k) \
;         acc[ai][bj][m][n] = __builtin_amdgcn_mfma_f32_16x16x32_bf16(Bt[n][k], At[m][k], acc[ai][bj][m][n], 0, 0, 0); __builtin_amdgcn_s_setprio(0); } while (0)
; #define PG8_WAIT_V(n) asm volatile("s_waitcnt vmcnt(" #n ")" ::: "memory")
; #define PG8_WAIT_L(n) asm volatile("s_waitcnt lgkmcnt(" #n ")" ::: "memory")
; #define PG8_BAR __builtin_amdgcn_s_barrier()
; #define PG8_SCHED __builtin_amdgcn_sched_barrier(0)
; template <class Epi, class Sched, bool ALIGN_EPI = false, bool SP2 = false>
; __device__ __forceinline__ void gemm_phase(PG8_LAS unsigned char* lds, const Gemm g, const Sched& S, const Epi& E, const bool skip_epi = false) {
;     ...
;             PG8_LDB(B0, 1, 0); PG8_LDB(B1, 1, 1); PG8_SCHED; PG8_LDA(At, 1, 0); PG8_STAGE_A(0, 1, a2, true);
;             PG8_WAIT_V(8); PG8_WAIT_L(0); PG8_BAR; PG8_MMA(0, 0, At, B0); PG8_MMA(0, 1, At, B1); PG8_BAR; PG8_SCHED;
	s_add_i32 s70, 0, 0x18000
	v_add_u32_e32 v130, s70, v147
	s_add_i32 s71, 0, 0x1c000
	ds_read_b128 v[160:163], v130
	ds_read_b128 v[164:167], v130 offset:1024
	ds_read_b128 v[168:171], v130 offset:2048
	ds_read_b128 v[172:175], v130 offset:3072
	v_add_u32_e32 v130, s71, v147
	ds_read_b128 v[176:179], v130
	ds_read_b128 v[180:183], v130 offset:1024
	ds_read_b128 v[184:187], v130 offset:2048
	ds_read_b128 v[188:191], v130 offset:3072
	s_add_u32 s38, s44, 0xe0000
	s_addc_u32 s39, s45, 0
	s_mov_b32 m0, s53
	v_lshl_add_u64 v[232:233], s[38:39], 0, v[132:133]
	ds_read_b128 v[192:195], v159 offset:32768
	ds_read_b128 v[196:199], v159 offset:33792
	ds_read_b128 v[200:203], v159 offset:34816
	ds_read_b128 v[204:207], v159 offset:35840
	ds_read_b128 v[208:211], v159 offset:36864
	ds_read_b128 v[212:215], v159 offset:37888
	ds_read_b128 v[216:219], v159 offset:38912
	ds_read_b128 v[220:223], v159 offset:39936
	global_load_lds_dwordx4 v[232:233], off
	v_lshl_add_u64 v[232:233], s[38:39], 0, v[136:137]
	s_mov_b32 m0, s54
	s_nop 0
	global_load_lds_dwordx4 v[232:233], off
	s_waitcnt vmcnt(8)
	s_waitcnt lgkmcnt(0)
	s_barrier
	s_setprio 3
	s_waitcnt lgkmcnt(0)
	v_mfma_f32_16x16x32_bf16 v[126:129], v[160:163], v[192:195], v[126:129]
	v_mfma_f32_16x16x32_bf16 v[122:125], v[168:171], v[192:195], v[122:125]
	v_mfma_f32_16x16x32_bf16 v[118:121], v[160:163], v[200:203], v[118:121]
	v_mfma_f32_16x16x32_bf16 v[114:117], v[168:171], v[200:203], v[114:117]
	v_mfma_f32_16x16x32_bf16 v[106:109], v[160:163], v[208:211], v[106:109]
	v_mfma_f32_16x16x32_bf16 v[98:101], v[168:171], v[208:211], v[98:101]
	v_mfma_f32_16x16x32_bf16 v[78:81], v[160:163], v[216:219], v[78:81]
	v_mfma_f32_16x16x32_bf16 v[74:77], v[168:171], v[216:219], v[74:77]
	v_mfma_f32_16x16x32_bf16 v[126:129], v[164:167], v[196:199], v[126:129]
	v_mfma_f32_16x16x32_bf16 v[122:125], v[172:175], v[196:199], v[122:125]
	v_mfma_f32_16x16x32_bf16 v[118:121], v[164:167], v[204:207], v[118:121]
	v_mfma_f32_16x16x32_bf16 v[114:117], v[172:175], v[204:207], v[114:117]
	v_mfma_f32_16x16x32_bf16 v[106:109], v[164:167], v[212:215], v[106:109]
	v_mfma_f32_16x16x32_bf16 v[98:101], v[172:175], v[212:215], v[98:101]
	v_mfma_f32_16x16x32_bf16 v[78:81], v[164:167], v[220:223], v[78:81]
	v_mfma_f32_16x16x32_bf16 v[74:77], v[172:175], v[220:223], v[74:77]
	s_setprio 0
	s_setprio 3
	v_mfma_f32_16x16x32_bf16 v[110:113], v[176:179], v[192:195], v[110:113]
	v_mfma_f32_16x16x32_bf16 v[102:105], v[184:187], v[192:195], v[102:105]
	v_mfma_f32_16x16x32_bf16 v[94:97], v[176:179], v[200:203], v[94:97]
	v_mfma_f32_16x16x32_bf16 v[90:93], v[184:187], v[200:203], v[90:93]
	v_mfma_f32_16x16x32_bf16 v[86:89], v[176:179], v[208:211], v[86:89]
	v_mfma_f32_16x16x32_bf16 v[82:85], v[184:187], v[208:211], v[82:85]
	v_mfma_f32_16x16x32_bf16 v[70:73], v[176:179], v[216:219], v[70:73]
	v_mfma_f32_16x16x32_bf16 v[66:69], v[184:187], v[216:219], v[66:69]
	v_mfma_f32_16x16x32_bf16 v[110:113], v[180:183], v[196:199], v[110:113]
	v_mfma_f32_16x16x32_bf16 v[102:105], v[188:191], v[196:199], v[102:105]
	v_mfma_f32_16x16x32_bf16 v[94:97], v[180:183], v[204:207], v[94:97]
	v_mfma_f32_16x16x32_bf16 v[90:93], v[188:191], v[204:207], v[90:93]
	v_mfma_f32_16x16x32_bf16 v[86:89], v[180:183], v[212:215], v[86:89]
	v_mfma_f32_16x16x32_bf16 v[82:85], v[188:191], v[212:215], v[82:85]
	v_mfma_f32_16x16x32_bf16 v[70:73], v[180:183], v[220:223], v[70:73]
	v_mfma_f32_16x16x32_bf16 v[66:69], v[188:191], v[220:223], v[66:69]
	s_setprio 0
	s_barrier
; #define PG8_STAGE_A(b, h, ptr, NX) do { if constexpr (Sched::GATHER) { unsigned gs_[2]; gs_[0] = ((NX) && last_) ? gN[h][0] : gA[h][0]; gs_[1] = ((NX) && last_) ? gN[h][1] : gA[h][1]; PG8_STAGE(PG8_SA(b, h), ptr, gs_); } \
;         else PG8_STAGE(PG8_SA(b, h), (ptr) + ((h) ? hstep : (size_t)0), voffA); } while (0)
; #define PG8_STAGE(bufoff, gbase, voff) do { _Pragma("unroll") for (int _i = 0; _i < 2; ++_i) \
;         __builtin_amdgcn_global_load_lds((const unsigned*)((const char*)(gbase) + (voff)[_i]), (PG8_LAS unsigned*)(lds + (bufoff) + ldsw + _i * 8192), 16, 0, 0); } while (0)
; #define PG8_LDA(dst, b, h) do { _Pragma("unroll") for (int m = 0; m < 4; ++m) _Pragma("unroll") for (int k = 0; k < 2; ++k) dst[m][k] = *(const PG8_LAS bf16x8*)(lds + PG8_SA(b, h) + aoff + m * 2048 + k * 1024); } while (0)
; #define PG8_MMA(ai, bj, At, Bt) do { __builtin_amdgcn_s_setprio(1); _Pragma("unroll") for (int m = 0; m < 4; ++m) _Pragma("unroll") for (int n = 0; n < 2; ++n) _Pragma("unroll") for (int k = 0; k < 2; ++k) \
;         acc[ai][bj][m][n] = __builtin_amdgcn_mfma_f32_16x16x32_bf16(Bt[n][k], At[m][k], acc[ai][bj][m][n], 0, 0, 0); __builtin_amdgcn_s_setprio(0); } while (0)
; #define PG8_WAIT_V(n) asm volatile("s_waitcnt vmcnt(" #n ")" ::: "memory")
; #define PG8_WAIT_L(n) asm volatile("s_waitcnt lgkmcnt(" #n ")" ::: "memory")
; #define PG8_BAR __builtin_amdgcn_s_barrier()
; #define PG8_SCHED __builtin_amdgcn_sched_barrier(0)
; template <class Epi, class Sched, bool ALIGN_EPI = false, bool SP2 = false>
; __device__ __forceinline__ void gemm_phase(PG8_LAS unsigned char* lds, const Gemm g, const Sched& S, const Epi& E, const bool skip_epi = false) {
;     ...
;         for (int t = 0; t < nt; t += 2) {
;     ...
;             PG8_LDA(At, 1, 1); PG8_STAGE(PG8_SB(1, 0), b3, voffB); PG8_STAGE(PG8_SB(1, 1), b3 + hstep, voffB); PG8_STAGE_A(1, 0, a3, true);
;             PG8_WAIT_V(8); PG8_WAIT_L(0); PG8_BAR; PG8_MMA(1, 0, At, B0); PG8_MMA(1, 1, At, B1); PG8_BAR; PG8_SCHED;
	s_add_i32 s38, s70, s51
	v_lshl_add_u64 v[152:153], v[152:153], 0, s[18:19]
	s_mov_b32 m0, s38
	ds_read_b128 v[192:195], v159 offset:49152
	ds_read_b128 v[196:199], v159 offset:50176
	ds_read_b128 v[200:203], v159 offset:51200
	ds_read_b128 v[204:207], v159 offset:52224
	ds_read_b128 v[208:211], v159 offset:53248
	ds_read_b128 v[212:215], v159 offset:54272
	ds_read_b128 v[216:219], v159 offset:55296
	ds_read_b128 v[220:223], v159 offset:56320
	global_load_lds_dwordx4 v[152:153], off
	s_add_i32 m0, s38, 0x2000
	s_add_u32 s38, s42, 0xe0080
	v_lshl_add_u64 v[152:153], v[224:225], 0, s[18:19]
	s_addc_u32 s39, s43, 0
	s_add_i32 s42, s71, s51
	global_load_lds_dwordx4 v[152:153], off
	v_lshl_add_u64 v[152:153], s[38:39], 0, v[134:135]
	s_mov_b32 m0, s42
	s_nop 0
	global_load_lds_dwordx4 v[152:153], off
	v_lshl_add_u64 v[152:153], s[38:39], 0, v[138:139]
	s_add_i32 m0, s42, 0x2000
	s_nop 0
	global_load_lds_dwordx4 v[152:153], off
	v_lshl_add_u64 v[152:153], v[226:227], 0, s[18:19]
	s_mov_b32 m0, s57
	s_nop 0
	global_load_lds_dwordx4 v[152:153], off
	v_lshl_add_u64 v[152:153], v[230:231], 0, s[18:19]
	s_mov_b32 m0, s58
	s_nop 0
	global_load_lds_dwordx4 v[152:153], off
	s_waitcnt vmcnt(8)
	s_waitcnt lgkmcnt(0)
	s_barrier
	s_setprio 3
	s_waitcnt lgkmcnt(0)
	v_mfma_f32_16x16x32_bf16 v[62:65], v[160:163], v[192:195], v[62:65]
	v_mfma_f32_16x16x32_bf16 v[58:61], v[168:171], v[192:195], v[58:61]
	v_mfma_f32_16x16x32_bf16 v[50:53], v[160:163], v[200:203], v[50:53]
	v_mfma_f32_16x16x32_bf16 v[42:45], v[168:171], v[200:203], v[42:45]
	v_mfma_f32_16x16x32_bf16 v[34:37], v[160:163], v[208:211], v[34:37]
	v_mfma_f32_16x16x32_bf16 v[26:29], v[168:171], v[208:211], v[26:29]
	v_mfma_f32_16x16x32_bf16 v[18:21], v[160:163], v[216:219], v[18:21]
	v_mfma_f32_16x16x32_bf16 v[10:13], v[168:171], v[216:219], v[10:13]
	v_mfma_f32_16x16x32_bf16 v[62:65], v[164:167], v[196:199], v[62:65]
	v_mfma_f32_16x16x32_bf16 v[58:61], v[172:175], v[196:199], v[58:61]
	v_mfma_f32_16x16x32_bf16 v[50:53], v[164:167], v[204:207], v[50:53]
	v_mfma_f32_16x16x32_bf16 v[42:45], v[172:175], v[204:207], v[42:45]
	v_mfma_f32_16x16x32_bf16 v[34:37], v[164:167], v[212:215], v[34:37]
	v_mfma_f32_16x16x32_bf16 v[26:29], v[172:175], v[212:215], v[26:29]
	v_mfma_f32_16x16x32_bf16 v[18:21], v[164:167], v[220:223], v[18:21]
	v_mfma_f32_16x16x32_bf16 v[10:13], v[172:175], v[220:223], v[10:13]
	s_setprio 0
	s_setprio 3
	v_mfma_f32_16x16x32_bf16 v[54:57], v[176:179], v[192:195], v[54:57]
	v_mfma_f32_16x16x32_bf16 v[46:49], v[184:187], v[192:195], v[46:49]
	v_mfma_f32_16x16x32_bf16 v[38:41], v[176:179], v[200:203], v[38:41]
	v_mfma_f32_16x16x32_bf16 v[30:33], v[184:187], v[200:203], v[30:33]
	v_mfma_f32_16x16x32_bf16 v[22:25], v[176:179], v[208:211], v[22:25]
	v_mfma_f32_16x16x32_bf16 v[14:17], v[184:187], v[208:211], v[14:17]
	v_mfma_f32_16x16x32_bf16 v[6:9], v[176:179], v[216:219], v[6:9]
	v_mfma_f32_16x16x32_bf16 v[2:5], v[184:187], v[216:219], v[2:5]
	v_mfma_f32_16x16x32_bf16 v[54:57], v[180:183], v[196:199], v[54:57]
	v_mfma_f32_16x16x32_bf16 v[46:49], v[188:191], v[196:199], v[46:49]
	v_mfma_f32_16x16x32_bf16 v[38:41], v[180:183], v[204:207], v[38:41]
	v_mfma_f32_16x16x32_bf16 v[30:33], v[188:191], v[204:207], v[30:33]
	v_mfma_f32_16x16x32_bf16 v[22:25], v[180:183], v[212:215], v[22:25]
	v_mfma_f32_16x16x32_bf16 v[14:17], v[188:191], v[212:215], v[14:17]
	v_mfma_f32_16x16x32_bf16 v[6:9], v[180:183], v[220:223], v[6:9]
	v_mfma_f32_16x16x32_bf16 v[2:5], v[188:191], v[220:223], v[2:5]
	s_setprio 0
	s_barrier
	s_add_i32 s69, s69, 2
	s_add_u32 s67, s67, 0x100
	s_addc_u32 s68, s68, 0
	s_cmp_gt_u32 s69, 53
	s_mov_b64 s[38:39], s[40:41]
	s_cbranch_scc0 .LBB0_1823
	s_and_b64 vcc, exec, s[20:21]
	s_cbranch_vccz .LBB0_1826
	s_barrier

; #define PG8_STAGE_A(b, h, ptr, NX) do { if constexpr (Sched::GATHER) { unsigned gs_[2]; gs_[0] = ((NX) && last_) ? gN[h][0] : gA[h][0]; gs_[1] = ((NX) && last_) ? gN[h][1] : gA[h][1]; PG8_STAGE(PG8_SA(b, h), ptr, gs_); } \
;         else PG8_STAGE(PG8_SA(b, h), (ptr) + ((h) ? hstep : (size_t)0), voffA); } while (0)
; #define PG8_STAGE(bufoff, gbase, voff) do { _Pragma("unroll") for (int _i = 0; _i < 2; ++_i) \
;         __builtin_amdgcn_global_load_lds((const unsigned*)((const char*)(gbase) + (voff)[_i]), (PG8_LAS unsigned*)(lds + (bufoff) + ldsw + _i * 8192), 16, 0, 0); } while (0)
; #define PG8_LDA(dst, b, h) do { _Pragma("unroll") for (int m = 0; m < 4; ++m) _Pragma("unroll") for (int k = 0; k < 2; ++k) dst[m][k] = *(const PG8_LAS bf16x8*)(lds + PG8_SA(b, h) + aoff + m * 2048 + k * 1024); } while (0)
; #define PG8_LDB(dst, b, h) do { _Pragma("unroll") for (int n = 0; n < 2; ++n) _Pragma("unroll") for (int k = 0; k < 2; ++k) dst[n][k] = *(const PG8_LAS bf16x8*)(lds + PG8_SB(b, h) + boff + n * 2048 + k * 1024); } while (0)
; #define PG8_MMA(ai, bj, At, Bt) do { __builtin_amdgcn_s_setprio(1); _Pragma("unroll") for (int m = 0; m < 4; ++m) _Pragma("unroll") for (int n = 0; n < 2; ++n) _Pragma("unroll") for (int k = 0; k < 2; ++k) \
;         acc[ai][bj][m][n] = __builtin_amdgcn_mfma_f32_16x16x32_bf16(Bt[n][k], At[m][k], acc[ai][bj][m][n], 0, 0, 0); __builtin_amdgcn_s_setprio(0); } while (0)
; #define PG8_WAIT_V(n) asm volatile("s_waitcnt vmcnt(" #n ")" ::: "memory")
; #define PG8_WAIT_L(n) asm volatile("s_waitcnt lgkmcnt(" #n ")" ::: "memory")
; template <class Epi, class Sched, bool ALIGN_EPI = false, bool SP2 = false>
; __device__ __forceinline__ void gemm_phase(PG8_LAS unsigned char* lds, const Gemm g, const Sched& S, const Epi& E, const bool skip_epi = false) {
;     ...
;                 for (int n = 0; n < 2; ++n) acc[a][b][m][n] = (f32x4){0.f, 0.f, 0.f, 0.f};
;     ...
;             PG8_LDB(B0, 0, 0); PG8_LDB(B1, 0, 1); PG8_SCHED; PG8_LDA(At, 0, 0); PG8_STAGE_A(1, 1, a1, false);
;             PG8_WAIT_V(8); PG8_WAIT_L(0); PG8_BAR; PG8_MMA(0, 0, At, B0); PG8_MMA(0, 1, At, B1); PG8_BAR; PG8_SCHED;
;             PG8_LDA(At, 0, 1); PG8_STAGE(PG8_SB(0, 0), b2, voffB); PG8_STAGE(PG8_SB(0, 1), b2 + hstep, voffB); PG8_STAGE_A(0, 0, a2, true);
;             PG8_WAIT_V(8); PG8_WAIT_L(0); PG8_BAR; PG8_MMA(1, 0, At, B0); PG8_MMA(1, 1, At, B1); PG8_BAR; PG8_SCHED;
.LBB0_1843:
	s_add_u32 s54, s30, 0x100
	s_addc_u32 s55, s31, 0
	s_mov_b32 s56, -2
	ds_read_b128 v[142:145], v150
	ds_read_b128 v[154:157], v150 offset:1024
	ds_read_b128 v[158:161], v150 offset:2048
	ds_read_b128 v[162:165], v150 offset:3072
	ds_read_b128 v[166:169], v151
	ds_read_b128 v[170:173], v151 offset:1024
	ds_read_b128 v[174:177], v151 offset:2048
	ds_read_b128 v[178:181], v151 offset:3072
	s_add_u32 s30, s28, 0x100
	s_addc_u32 s31, s29, 0
	s_cmp_eq_u32 s56, 10
	s_cselect_b32 s37, s7, s31
	s_cselect_b32 s36, s6, s30
	s_cselect_b32 s35, s25, s55
	s_cselect_b32 s34, s24, s54
	v_lshl_add_u64 v[214:215], s[28:29], 0, v[136:137]
	s_add_i32 m0, s38, 0xc000
	ds_read_b128 v[182:185], v152
	ds_read_b128 v[186:189], v152 offset:1024
	ds_read_b128 v[190:193], v152 offset:2048
	ds_read_b128 v[194:197], v152 offset:3072
	ds_read_b128 v[198:201], v152 offset:4096
	ds_read_b128 v[202:205], v152 offset:5120
	ds_read_b128 v[206:209], v152 offset:6144
	ds_read_b128 v[210:213], v152 offset:7168
	global_load_lds_dwordx4 v[214:215], off
	v_lshl_add_u64 v[214:215], s[28:29], 0, v[138:139]
	s_add_i32 m0, s38, 0xe000
	s_nop 0
	global_load_lds_dwordx4 v[214:215], off
	s_waitcnt vmcnt(8)
	s_waitcnt lgkmcnt(0)
	s_barrier
	s_setprio 3
	s_waitcnt lgkmcnt(0)
	v_mfma_f32_16x16x32_bf16 v[126:129], v[142:145], v[182:185], 0
	v_mfma_f32_16x16x32_bf16 v[122:125], v[158:161], v[182:185], 0
	v_mfma_f32_16x16x32_bf16 v[110:113], v[142:145], v[190:193], 0
	v_mfma_f32_16x16x32_bf16 v[106:109], v[158:161], v[190:193], 0
	v_mfma_f32_16x16x32_bf16 v[94:97], v[142:145], v[198:201], 0
	v_mfma_f32_16x16x32_bf16 v[90:93], v[158:161], v[198:201], 0
	v_mfma_f32_16x16x32_bf16 v[78:81], v[142:145], v[206:209], 0
	v_mfma_f32_16x16x32_bf16 v[74:77], v[158:161], v[206:209], 0
	v_mfma_f32_16x16x32_bf16 v[126:129], v[154:157], v[186:189], v[126:129]
	v_mfma_f32_16x16x32_bf16 v[122:125], v[162:165], v[186:189], v[122:125]
	v_mfma_f32_16x16x32_bf16 v[110:113], v[154:157], v[194:197], v[110:113]
	v_mfma_f32_16x16x32_bf16 v[106:109], v[162:165], v[194:197], v[106:109]
	v_mfma_f32_16x16x32_bf16 v[94:97], v[154:157], v[202:205], v[94:97]
	v_mfma_f32_16x16x32_bf16 v[90:93], v[162:165], v[202:205], v[90:93]
	v_mfma_f32_16x16x32_bf16 v[78:81], v[154:157], v[210:213], v[78:81]
	v_mfma_f32_16x16x32_bf16 v[74:77], v[162:165], v[210:213], v[74:77]
	s_setprio 0
	s_setprio 3
	v_mfma_f32_16x16x32_bf16 v[118:121], v[166:169], v[182:185], 0
	v_mfma_f32_16x16x32_bf16 v[114:117], v[174:177], v[182:185], 0
	v_mfma_f32_16x16x32_bf16 v[102:105], v[166:169], v[190:193], 0
	v_mfma_f32_16x16x32_bf16 v[98:101], v[174:177], v[190:193], 0
	v_mfma_f32_16x16x32_bf16 v[86:89], v[166:169], v[198:201], 0
	v_mfma_f32_16x16x32_bf16 v[82:85], v[174:177], v[198:201], 0
	v_mfma_f32_16x16x32_bf16 v[70:73], v[166:169], v[206:209], 0
	v_mfma_f32_16x16x32_bf16 v[66:69], v[174:177], v[206:209], 0
	v_mfma_f32_16x16x32_bf16 v[118:121], v[170:173], v[186:189], v[118:121]
	v_mfma_f32_16x16x32_bf16 v[114:117], v[178:181], v[186:189], v[114:117]
	v_mfma_f32_16x16x32_bf16 v[102:105], v[170:173], v[194:197], v[102:105]
	v_mfma_f32_16x16x32_bf16 v[98:101], v[178:181], v[194:197], v[98:101]
	v_mfma_f32_16x16x32_bf16 v[86:89], v[170:173], v[202:205], v[86:89]
	v_mfma_f32_16x16x32_bf16 v[82:85], v[178:181], v[202:205], v[82:85]
	v_mfma_f32_16x16x32_bf16 v[70:73], v[170:173], v[210:213], v[70:73]
	v_mfma_f32_16x16x32_bf16 v[66:69], v[178:181], v[210:213], v[66:69]
	s_setprio 0
	s_barrier
	s_add_i32 s28, s50, s3
	v_lshl_add_u64 v[214:215], s[34:35], 0, v[132:133]
	s_mov_b32 m0, s28
	ds_read_b128 v[182:185], v152 offset:16384
	ds_read_b128 v[186:189], v152 offset:17408
	ds_read_b128 v[190:193], v152 offset:18432
	ds_read_b128 v[194:197], v152 offset:19456
	ds_read_b128 v[198:201], v152 offset:20480
	ds_read_b128 v[202:205], v152 offset:21504
	ds_read_b128 v[206:209], v152 offset:22528
	ds_read_b128 v[210:213], v152 offset:23552
	global_load_lds_dwordx4 v[214:215], off
	s_add_i32 m0, s28, 0x2000
	s_add_u32 s28, s34, 0xe0000
	v_lshl_add_u64 v[216:217], s[34:35], 0, v[134:135]
	s_addc_u32 s29, s35, 0
	s_add_i32 s57, s51, s3
	global_load_lds_dwordx4 v[216:217], off
	v_lshl_add_u64 v[218:219], s[28:29], 0, v[132:133]
	s_mov_b32 m0, s57
	v_lshl_add_u64 v[220:221], s[36:37], 0, v[134:135]
	global_load_lds_dwordx4 v[218:219], off
	v_lshl_add_u64 v[218:219], s[28:29], 0, v[134:135]
	s_add_i32 m0, s57, 0x2000
	s_nop 0
	global_load_lds_dwordx4 v[218:219], off
	v_lshl_add_u64 v[218:219], s[36:37], 0, v[132:133]
	s_mov_b32 m0, s38
	s_nop 0
	global_load_lds_dwordx4 v[218:219], off
	s_mov_b32 m0, s39
	s_nop 0
	global_load_lds_dwordx4 v[220:221], off
	s_waitcnt vmcnt(8)
	s_waitcnt lgkmcnt(0)
	s_barrier
; #define PG8_STAGE_A(b, h, ptr, NX) do { if constexpr (Sched::GATHER) { unsigned gs_[2]; gs_[0] = ((NX) && last_) ? gN[h][0] : gA[h][0]; gs_[1] = ((NX) && last_) ? gN[h][1] : gA[h][1]; PG8_STAGE(PG8_SA(b, h), ptr, gs_); } \
;         else PG8_STAGE(PG8_SA(b, h), (ptr) + ((h) ? hstep : (size_t)0), voffA); } while (0)
; #define PG8_LDA(dst, b, h) do { _Pragma("unroll") for (int m = 0; m < 4; ++m) _Pragma("unroll") for (int k = 0; k < 2; ++k) dst[m][k] = *(const PG8_LAS bf16x8*)(lds + PG8_SA(b, h) + aoff + m * 2048 + k * 1024); } while (0)
; #define PG8_LDB(dst, b, h) do { _Pragma("unroll") for (int n = 0; n < 2; ++n) _Pragma("unroll") for (int k = 0; k < 2; ++k) dst[n][k] = *(const PG8_LAS bf16x8*)(lds + PG8_SB(b, h) + boff + n * 2048 + k * 1024); } while (0)
; #define PG8_MMA(ai, bj, At, Bt) do { __builtin_amdgcn_s_setprio(1); _Pragma("unroll") for (int m = 0; m < 4; ++m) _Pragma("unroll") for (int n = 0; n < 2; ++n) _Pragma("unroll") for (int k = 0; k < 2; ++k) \
;         acc[ai][bj][m][n] = __builtin_amdgcn_mfma_f32_16x16x32_bf16(Bt[n][k], At[m][k], acc[ai][bj][m][n], 0, 0, 0); __builtin_amdgcn_s_setprio(0); } while (0)
; #define PG8_WAIT_V(n) asm volatile("s_waitcnt vmcnt(" #n ")" ::: "memory")
; #define PG8_WAIT_L(n) asm volatile("s_waitcnt lgkmcnt(" #n ")" ::: "memory")
; #define PG8_BAR __builtin_amdgcn_s_barrier()
; #define PG8_SCHED __builtin_amdgcn_sched_barrier(0)
; template <class Epi, class Sched, bool ALIGN_EPI = false, bool SP2 = false>
; __device__ __forceinline__ void gemm_phase(PG8_LAS unsigned char* lds, const Gemm g, const Sched& S, const Epi& E, const bool skip_epi = false) {
;     ...
;             PG8_WAIT_V(8); PG8_WAIT_L(0); PG8_BAR; PG8_MMA(1, 0, At, B0); PG8_MMA(1, 1, At, B1); PG8_BAR; PG8_SCHED;
;             PG8_LDB(B0, 1, 0); PG8_LDB(B1, 1, 1); PG8_SCHED; PG8_LDA(At, 1, 0); PG8_STAGE_A(0, 1, a2, true);
;             PG8_WAIT_V(8); PG8_WAIT_L(0); PG8_BAR; PG8_MMA(0, 0, At, B0); PG8_MMA(0, 1, At, B1); PG8_BAR; PG8_SCHED;
	s_setprio 3
	s_waitcnt lgkmcnt(0)
	v_mfma_f32_16x16x32_bf16 v[62:65], v[142:145], v[182:185], 0
	v_mfma_f32_16x16x32_bf16 v[58:61], v[158:161], v[182:185], 0
	v_mfma_f32_16x16x32_bf16 v[46:49], v[142:145], v[190:193], 0
	v_mfma_f32_16x16x32_bf16 v[42:45], v[158:161], v[190:193], 0
	v_mfma_f32_16x16x32_bf16 v[30:33], v[142:145], v[198:201], 0
	v_mfma_f32_16x16x32_bf16 v[26:29], v[158:161], v[198:201], 0
	v_mfma_f32_16x16x32_bf16 v[14:17], v[142:145], v[206:209], 0
	v_mfma_f32_16x16x32_bf16 v[10:13], v[158:161], v[206:209], 0
	v_mfma_f32_16x16x32_bf16 v[62:65], v[154:157], v[186:189], v[62:65]
	v_mfma_f32_16x16x32_bf16 v[58:61], v[162:165], v[186:189], v[58:61]
	v_mfma_f32_16x16x32_bf16 v[46:49], v[154:157], v[194:197], v[46:49]
	v_mfma_f32_16x16x32_bf16 v[42:45], v[162:165], v[194:197], v[42:45]
	v_mfma_f32_16x16x32_bf16 v[30:33], v[154:157], v[202:205], v[30:33]
	v_mfma_f32_16x16x32_bf16 v[26:29], v[162:165], v[202:205], v[26:29]
	v_mfma_f32_16x16x32_bf16 v[14:17], v[154:157], v[210:213], v[14:17]
	v_mfma_f32_16x16x32_bf16 v[10:13], v[162:165], v[210:213], v[10:13]
	s_setprio 0
	s_setprio 3
	v_mfma_f32_16x16x32_bf16 v[54:57], v[166:169], v[182:185], 0
	v_mfma_f32_16x16x32_bf16 v[50:53], v[174:177], v[182:185], 0
	v_mfma_f32_16x16x32_bf16 v[38:41], v[166:169], v[190:193], 0
	v_mfma_f32_16x16x32_bf16 v[34:37], v[174:177], v[190:193], 0
	v_mfma_f32_16x16x32_bf16 v[22:25], v[166:169], v[198:201], 0
	v_mfma_f32_16x16x32_bf16 v[18:21], v[174:177], v[198:201], 0
	v_mfma_f32_16x16x32_bf16 v[6:9], v[166:169], v[206:209], 0
	v_mfma_f32_16x16x32_bf16 v[2:5], v[174:177], v[206:209], 0
	v_mfma_f32_16x16x32_bf16 v[54:57], v[170:173], v[186:189], v[54:57]
	v_mfma_f32_16x16x32_bf16 v[50:53], v[178:181], v[186:189], v[50:53]
	v_mfma_f32_16x16x32_bf16 v[38:41], v[170:173], v[194:197], v[38:41]
	v_mfma_f32_16x16x32_bf16 v[34:37], v[178:181], v[194:197], v[34:37]
	v_mfma_f32_16x16x32_bf16 v[22:25], v[170:173], v[202:205], v[22:25]
	v_mfma_f32_16x16x32_bf16 v[18:21], v[178:181], v[202:205], v[18:21]
	v_mfma_f32_16x16x32_bf16 v[6:9], v[170:173], v[210:213], v[6:9]
	v_mfma_f32_16x16x32_bf16 v[2:5], v[178:181], v[210:213], v[2:5]
	s_setprio 0
	s_barrier
	s_add_i32 s57, 0, 0x18000
	v_add_u32_e32 v130, s57, v146
	s_add_i32 s58, 0, 0x1c000
	ds_read_b128 v[142:145], v130
	ds_read_b128 v[154:157], v130 offset:1024
	ds_read_b128 v[158:161], v130 offset:2048
	ds_read_b128 v[162:165], v130 offset:3072
	v_add_u32_e32 v130, s58, v146
	ds_read_b128 v[166:169], v130
	ds_read_b128 v[170:173], v130 offset:1024
	ds_read_b128 v[174:177], v130 offset:2048
	ds_read_b128 v[178:181], v130 offset:3072
	s_add_u32 s28, s36, 0xe0000
	s_addc_u32 s29, s37, 0
	s_mov_b32 m0, s40
	v_lshl_add_u64 v[222:223], s[28:29], 0, v[132:133]
	ds_read_b128 v[182:185], v152 offset:32768
	ds_read_b128 v[186:189], v152 offset:33792
	ds_read_b128 v[190:193], v152 offset:34816
	ds_read_b128 v[194:197], v152 offset:35840
	ds_read_b128 v[198:201], v152 offset:36864
	ds_read_b128 v[202:205], v152 offset:37888
	ds_read_b128 v[206:209], v152 offset:38912
	ds_read_b128 v[210:213], v152 offset:39936
	global_load_lds_dwordx4 v[222:223], off
	v_lshl_add_u64 v[222:223], s[28:29], 0, v[134:135]
	s_mov_b32 m0, s41
	s_nop 0
	global_load_lds_dwordx4 v[222:223], off
	s_waitcnt vmcnt(8)
	s_waitcnt lgkmcnt(0)
	s_barrier
	s_setprio 3
	s_waitcnt lgkmcnt(0)
	v_mfma_f32_16x16x32_bf16 v[126:129], v[142:145], v[182:185], v[126:129]
	v_mfma_f32_16x16x32_bf16 v[122:125], v[158:161], v[182:185], v[122:125]
	v_mfma_f32_16x16x32_bf16 v[110:113], v[142:145], v[190:193], v[110:113]
	v_mfma_f32_16x16x32_bf16 v[106:109], v[158:161], v[190:193], v[106:109]
	v_mfma_f32_16x16x32_bf16 v[94:97], v[142:145], v[198:201], v[94:97]
	v_mfma_f32_16x16x32_bf16 v[90:93], v[158:161], v[198:201], v[90:93]
	v_mfma_f32_16x16x32_bf16 v[78:81], v[142:145], v[206:209], v[78:81]
	v_mfma_f32_16x16x32_bf16 v[74:77], v[158:161], v[206:209], v[74:77]
	v_mfma_f32_16x16x32_bf16 v[126:129], v[154:157], v[186:189], v[126:129]
	v_mfma_f32_16x16x32_bf16 v[122:125], v[162:165], v[186:189], v[122:125]
	v_mfma_f32_16x16x32_bf16 v[110:113], v[154:157], v[194:197], v[110:113]
	v_mfma_f32_16x16x32_bf16 v[106:109], v[162:165], v[194:197], v[106:109]
	v_mfma_f32_16x16x32_bf16 v[94:97], v[154:157], v[202:205], v[94:97]
	v_mfma_f32_16x16x32_bf16 v[90:93], v[162:165], v[202:205], v[90:93]
	v_mfma_f32_16x16x32_bf16 v[78:81], v[154:157], v[210:213], v[78:81]
	v_mfma_f32_16x16x32_bf16 v[74:77], v[162:165], v[210:213], v[74:77]
	s_setprio 0
	s_setprio 3
	v_mfma_f32_16x16x32_bf16 v[118:121], v[166:169], v[182:185], v[118:121]
	v_mfma_f32_16x16x32_bf16 v[114:117], v[174:177], v[182:185], v[114:117]
	v_mfma_f32_16x16x32_bf16 v[102:105], v[166:169], v[190:193], v[102:105]
	v_mfma_f32_16x16x32_bf16 v[98:101], v[174:177], v[190:193], v[98:101]
	v_mfma_f32_16x16x32_bf16 v[86:89], v[166:169], v[198:201], v[86:89]
	v_mfma_f32_16x16x32_bf16 v[82:85], v[174:177], v[198:201], v[82:85]
	v_mfma_f32_16x16x32_bf16 v[70:73], v[166:169], v[206:209], v[70:73]
	v_mfma_f32_16x16x32_bf16 v[66:69], v[174:177], v[206:209], v[66:69]
	v_mfma_f32_16x16x32_bf16 v[118:121], v[170:173], v[186:189], v[118:121]
	v_mfma_f32_16x16x32_bf16 v[114:117], v[178:181], v[186:189], v[114:117]
	v_mfma_f32_16x16x32_bf16 v[102:105], v[170:173], v[194:197], v[102:105]
	v_mfma_f32_16x16x32_bf16 v[98:101], v[178:181], v[194:197], v[98:101]
	v_mfma_f32_16x16x32_bf16 v[86:89], v[170:173], v[202:205], v[86:89]
	v_mfma_f32_16x16x32_bf16 v[82:85], v[178:181], v[202:205], v[82:85]
	v_mfma_f32_16x16x32_bf16 v[70:73], v[170:173], v[210:213], v[70:73]
	v_mfma_f32_16x16x32_bf16 v[66:69], v[178:181], v[210:213], v[66:69]
	s_setprio 0
	s_barrier
; #define PG8_STAGE_A(b, h, ptr, NX) do { if constexpr (Sched::GATHER) { unsigned gs_[2]; gs_[0] = ((NX) && last_) ? gN[h][0] : gA[h][0]; gs_[1] = ((NX) && last_) ? gN[h][1] : gA[h][1]; PG8_STAGE(PG8_SA(b, h), ptr, gs_); } \
;         else PG8_STAGE(PG8_SA(b, h), (ptr) + ((h) ? hstep : (size_t)0), voffA); } while (0)
; #define PG8_STAGE(bufoff, gbase, voff) do { _Pragma("unroll") for (int _i = 0; _i < 2; ++_i) \
;         __builtin_amdgcn_global_load_lds((const unsigned*)((const char*)(gbase) + (voff)[_i]), (PG8_LAS unsigned*)(lds + (bufoff) + ldsw + _i * 8192), 16, 0, 0); } while (0)
; #define PG8_LDA(dst, b, h) do { _Pragma("unroll") for (int m = 0; m < 4; ++m) _Pragma("unroll") for (int k = 0; k < 2; ++k) dst[m][k] = *(const PG8_LAS bf16x8*)(lds + PG8_SA(b, h) + aoff + m * 2048 + k * 1024); } while (0)
; #define PG8_LDB(dst, b, h) do { _Pragma("unroll") for (int n = 0; n < 2; ++n) _Pragma("unroll") for (int k = 0; k < 2; ++k) dst[n][k] = *(const PG8_LAS bf16x8*)(lds + PG8_SB(b, h) + boff + n * 2048 + k * 1024); } while (0)
; #define PG8_WAIT_V(n) asm volatile("s_waitcnt vmcnt(" #n ")" ::: "memory")
; #define PG8_WAIT_L(n) asm volatile("s_waitcnt lgkmcnt(" #n ")" ::: "memory")
; #define PG8_BAR __builtin_amdgcn_s_barrier()
; #define PG8_SCHED __builtin_amdgcn_sched_barrier(0)
; template <class Epi, class Sched, bool ALIGN_EPI = false, bool SP2 = false>
; __device__ __forceinline__ void gemm_phase(PG8_LAS unsigned char* lds, const Gemm g, const Sched& S, const Epi& E, const bool skip_epi = false) {
;     ...
;         for (int t = 0; t < nt; t += 2) {
;             const bool last = (t == nt - 2); last_ = last && has_next;
;             const char* a1 = cA + (size_t)(t + 1) * kstep;
;             const char* a2 = last ? nA : cA + (size_t)(t + 2) * kstep; const char* b2 = last ? nB : cB + (size_t)(t + 2) * kstep;
;             const char* a3 = a2 + kstep; const char* b3 = b2 + kstep;
;             if (last && has_next) S.a_ready(nxt);
;             if constexpr (SP2) {
;             PG8_LDB(B0, 0, 0); PG8_LDB(B1, 0, 1); PG8_SCHED; PG8_LDA(At, 0, 0); PG8_STAGE_A(1, 1, a1, false);
;     ...
;             PG8_LDA(At, 1, 1); PG8_STAGE(PG8_SB(1, 0), b3, voffB); PG8_STAGE(PG8_SB(1, 1), b3 + hstep, voffB); PG8_STAGE_A(1, 0, a3, true);
;             PG8_WAIT_V(8); PG8_WAIT_L(0); PG8_BAR; PG8_MMA(1, 0, At, B0); PG8_MMA(1, 1, At, B1); PG8_BAR; PG8_SCHED;
	s_add_i32 s28, s57, s3
	v_lshl_add_u64 v[214:215], v[214:215], 0, s[18:19]
	s_mov_b32 m0, s28
	ds_read_b128 v[182:185], v152 offset:49152
	ds_read_b128 v[186:189], v152 offset:50176
	ds_read_b128 v[190:193], v152 offset:51200
	ds_read_b128 v[194:197], v152 offset:52224
	ds_read_b128 v[198:201], v152 offset:53248
	ds_read_b128 v[202:205], v152 offset:54272
	ds_read_b128 v[206:209], v152 offset:55296
	ds_read_b128 v[210:213], v152 offset:56320
	global_load_lds_dwordx4 v[214:215], off
	s_add_i32 m0, s28, 0x2000
	s_add_u32 s28, s34, 0xe0080
	v_lshl_add_u64 v[214:215], v[216:217], 0, s[18:19]
	s_addc_u32 s29, s35, 0
	s_add_i32 s34, s58, s3
	global_load_lds_dwordx4 v[214:215], off
	v_lshl_add_u64 v[214:215], s[28:29], 0, v[132:133]
	s_mov_b32 m0, s34
	s_nop 0
	global_load_lds_dwordx4 v[214:215], off
	v_lshl_add_u64 v[214:215], s[28:29], 0, v[134:135]
	s_add_i32 m0, s34, 0x2000
	s_nop 0
	global_load_lds_dwordx4 v[214:215], off
	v_lshl_add_u64 v[214:215], v[218:219], 0, s[18:19]
	s_mov_b32 m0, s46
	s_nop 0
	global_load_lds_dwordx4 v[214:215], off
	v_lshl_add_u64 v[214:215], v[220:221], 0, s[18:19]
	s_mov_b32 m0, s47
	s_nop 0
	global_load_lds_dwordx4 v[214:215], off
	s_waitcnt vmcnt(8)
	s_waitcnt lgkmcnt(0)
	s_barrier
	s_setprio 3
	s_waitcnt lgkmcnt(0)
	v_mfma_f32_16x16x32_bf16 v[62:65], v[142:145], v[182:185], v[62:65]
	v_mfma_f32_16x16x32_bf16 v[58:61], v[158:161], v[182:185], v[58:61]
	v_mfma_f32_16x16x32_bf16 v[46:49], v[142:145], v[190:193], v[46:49]
	v_mfma_f32_16x16x32_bf16 v[42:45], v[158:161], v[190:193], v[42:45]
	v_mfma_f32_16x16x32_bf16 v[30:33], v[142:145], v[198:201], v[30:33]
	v_mfma_f32_16x16x32_bf16 v[26:29], v[158:161], v[198:201], v[26:29]
	v_mfma_f32_16x16x32_bf16 v[14:17], v[142:145], v[206:209], v[14:17]
	v_mfma_f32_16x16x32_bf16 v[10:13], v[158:161], v[206:209], v[10:13]
	v_mfma_f32_16x16x32_bf16 v[62:65], v[154:157], v[186:189], v[62:65]
	v_mfma_f32_16x16x32_bf16 v[58:61], v[162:165], v[186:189], v[58:61]
	v_mfma_f32_16x16x32_bf16 v[46:49], v[154:157], v[194:197], v[46:49]
	v_mfma_f32_16x16x32_bf16 v[42:45], v[162:165], v[194:197], v[42:45]
	v_mfma_f32_16x16x32_bf16 v[30:33], v[154:157], v[202:205], v[30:33]
	v_mfma_f32_16x16x32_bf16 v[26:29], v[162:165], v[202:205], v[26:29]
	v_mfma_f32_16x16x32_bf16 v[14:17], v[154:157], v[210:213], v[14:17]
	v_mfma_f32_16x16x32_bf16 v[10:13], v[162:165], v[210:213], v[10:13]
	s_setprio 0
	s_setprio 3
	v_mfma_f32_16x16x32_bf16 v[54:57], v[166:169], v[182:185], v[54:57]
	v_mfma_f32_16x16x32_bf16 v[50:53], v[174:177], v[182:185], v[50:53]
	v_mfma_f32_16x16x32_bf16 v[38:41], v[166:169], v[190:193], v[38:41]
	v_mfma_f32_16x16x32_bf16 v[34:37], v[174:177], v[190:193], v[34:37]
	v_mfma_f32_16x16x32_bf16 v[22:25], v[166:169], v[198:201], v[22:25]
	v_mfma_f32_16x16x32_bf16 v[18:21], v[174:177], v[198:201], v[18:21]
	v_mfma_f32_16x16x32_bf16 v[6:9], v[166:169], v[206:209], v[6:9]
	v_mfma_f32_16x16x32_bf16 v[2:5], v[174:177], v[206:209], v[2:5]
	v_mfma_f32_16x16x32_bf16 v[54:57], v[170:173], v[186:189], v[54:57]
	v_mfma_f32_16x16x32_bf16 v[50:53], v[178:181], v[186:189], v[50:53]
	v_mfma_f32_16x16x32_bf16 v[38:41], v[170:173], v[194:197], v[38:41]
	v_mfma_f32_16x16x32_bf16 v[34:37], v[178:181], v[194:197], v[34:37]
	v_mfma_f32_16x16x32_bf16 v[22:25], v[170:173], v[202:205], v[22:25]
	v_mfma_f32_16x16x32_bf16 v[18:21], v[178:181], v[202:205], v[18:21]
	v_mfma_f32_16x16x32_bf16 v[6:9], v[170:173], v[210:213], v[6:9]
	v_mfma_f32_16x16x32_bf16 v[2:5], v[178:181], v[210:213], v[2:5]
	s_setprio 0
	s_barrier
	s_add_i32 s56, s56, 2
	s_add_u32 s54, s54, 0x100
	s_addc_u32 s55, s55, 0
	s_cmp_gt_u32 s56, 11
	s_mov_b64 s[28:29], s[30:31]
.LBB0_1844:
	ds_read_b128 v[142:145], v150
	ds_read_b128 v[154:157], v150 offset:1024
	ds_read_b128 v[158:161], v150 offset:2048
	ds_read_b128 v[162:165], v150 offset:3072
	ds_read_b128 v[166:169], v151
	ds_read_b128 v[170:173], v151 offset:1024
	ds_read_b128 v[174:177], v151 offset:2048
	ds_read_b128 v[178:181], v151 offset:3072
	s_add_u32 s30, s28, 0x100
	s_addc_u32 s31, s29, 0
	s_cmp_eq_u32 s56, 10
	s_cselect_b32 s37, s7, s31
	s_cselect_b32 s36, s6, s30
	s_cselect_b32 s35, s25, s55
	s_cselect_b32 s34, s24, s54
	v_lshl_add_u64 v[214:215], s[28:29], 0, v[136:137]
	s_add_i32 m0, s38, 0xc000
	ds_read_b128 v[182:185], v152
	ds_read_b128 v[186:189], v152 offset:1024
	ds_read_b128 v[190:193], v152 offset:2048
	ds_read_b128 v[194:197], v152 offset:3072
	ds_read_b128 v[198:201], v152 offset:4096
	ds_read_b128 v[202:205], v152 offset:5120
	ds_read_b128 v[206:209], v152 offset:6144
	ds_read_b128 v[210:213], v152 offset:7168
	global_load_lds_dwordx4 v[214:215], off
	v_lshl_add_u64 v[214:215], s[28:29], 0, v[138:139]
	s_add_i32 m0, s38, 0xe000
	s_nop 0
	global_load_lds_dwordx4 v[214:215], off
	s_waitcnt vmcnt(8)
	s_waitcnt lgkmcnt(0)
	s_barrier
; #define PG8_STAGE_A(b, h, ptr, NX) do { if constexpr (Sched::GATHER) { unsigned gs_[2]; gs_[0] = ((NX) && last_) ? gN[h][0] : gA[h][0]; gs_[1] = ((NX) && last_) ? gN[h][1] : gA[h][1]; PG8_STAGE(PG8_SA(b, h), ptr, gs_); } \
;         else PG8_STAGE(PG8_SA(b, h), (ptr) + ((h) ? hstep : (size_t)0), voffA); } while (0)
; #define PG8_STAGE(bufoff, gbase, voff) do { _Pragma("unroll") for (int _i = 0; _i < 2; ++_i) \
;         __builtin_amdgcn_global_load_lds((const unsigned*)((const char*)(gbase) + (voff)[_i]), (PG8_LAS unsigned*)(lds + (bufoff) + ldsw + _i * 8192), 16, 0, 0); } while (0)
; #define PG8_LDA(dst, b, h) do { _Pragma("unroll") for (int m = 0; m < 4; ++m) _Pragma("unroll") for (int k = 0; k < 2; ++k) dst[m][k] = *(const PG8_LAS bf16x8*)(lds + PG8_SA(b, h) + aoff + m * 2048 + k * 1024); } while (0)
; #define PG8_MMA(ai, bj, At, Bt) do { __builtin_amdgcn_s_setprio(1); _Pragma("unroll") for (int m = 0; m < 4; ++m) _Pragma("unroll") for (int n = 0; n < 2; ++n) _Pragma("unroll") for (int k = 0; k < 2; ++k) \
;         acc[ai][bj][m][n] = __builtin_amdgcn_mfma_f32_16x16x32_bf16(Bt[n][k], At[m][k], acc[ai][bj][m][n], 0, 0, 0); __builtin_amdgcn_s_setprio(0); } while (0)
; #define PG8_WAIT_V(n) asm volatile("s_waitcnt vmcnt(" #n ")" ::: "memory")
; #define PG8_WAIT_L(n) asm volatile("s_waitcnt lgkmcnt(" #n ")" ::: "memory")
; #define PG8_BAR __builtin_amdgcn_s_barrier()
; #define PG8_SCHED __builtin_amdgcn_sched_barrier(0)
; template <class Epi, class Sched, bool ALIGN_EPI = false, bool SP2 = false>
; __device__ __forceinline__ void gemm_phase(PG8_LAS unsigned char* lds, const Gemm g, const Sched& S, const Epi& E, const bool skip_epi = false) {
;     ...
;             PG8_WAIT_V(8); PG8_WAIT_L(0); PG8_BAR; PG8_MMA(0, 0, At, B0); PG8_MMA(0, 1, At, B1); PG8_BAR; PG8_SCHED;
;             PG8_LDA(At, 0, 1); PG8_STAGE(PG8_SB(0, 0), b2, voffB); PG8_STAGE(PG8_SB(0, 1), b2 + hstep, voffB); PG8_STAGE_A(0, 0, a2, true);
;             PG8_WAIT_V(8); PG8_WAIT_L(0); PG8_BAR; PG8_MMA(1, 0, At, B0); PG8_MMA(1, 1, At, B1); PG8_BAR; PG8_SCHED;
	s_setprio 3
	s_waitcnt lgkmcnt(0)
	v_mfma_f32_16x16x32_bf16 v[126:129], v[142:145], v[182:185], v[126:129]
	v_mfma_f32_16x16x32_bf16 v[122:125], v[158:161], v[182:185], v[122:125]
	v_mfma_f32_16x16x32_bf16 v[110:113], v[142:145], v[190:193], v[110:113]
	v_mfma_f32_16x16x32_bf16 v[106:109], v[158:161], v[190:193], v[106:109]
	v_mfma_f32_16x16x32_bf16 v[94:97], v[142:145], v[198:201], v[94:97]
	v_mfma_f32_16x16x32_bf16 v[90:93], v[158:161], v[198:201], v[90:93]
	v_mfma_f32_16x16x32_bf16 v[78:81], v[142:145], v[206:209], v[78:81]
	v_mfma_f32_16x16x32_bf16 v[74:77], v[158:161], v[206:209], v[74:77]
	v_mfma_f32_16x16x32_bf16 v[126:129], v[154:157], v[186:189], v[126:129]
	v_mfma_f32_16x16x32_bf16 v[122:125], v[162:165], v[186:189], v[122:125]
	v_mfma_f32_16x16x32_bf16 v[110:113], v[154:157], v[194:197], v[110:113]
	v_mfma_f32_16x16x32_bf16 v[106:109], v[162:165], v[194:197], v[106:109]
	v_mfma_f32_16x16x32_bf16 v[94:97], v[154:157], v[202:205], v[94:97]
	v_mfma_f32_16x16x32_bf16 v[90:93], v[162:165], v[202:205], v[90:93]
	v_mfma_f32_16x16x32_bf16 v[78:81], v[154:157], v[210:213], v[78:81]
	v_mfma_f32_16x16x32_bf16 v[74:77], v[162:165], v[210:213], v[74:77]
	s_setprio 0
	s_setprio 3
	v_mfma_f32_16x16x32_bf16 v[118:121], v[166:169], v[182:185], v[118:121]
	v_mfma_f32_16x16x32_bf16 v[114:117], v[174:177], v[182:185], v[114:117]
	v_mfma_f32_16x16x32_bf16 v[102:105], v[166:169], v[190:193], v[102:105]
	v_mfma_f32_16x16x32_bf16 v[98:101], v[174:177], v[190:193], v[98:101]
	v_mfma_f32_16x16x32_bf16 v[86:89], v[166:169], v[198:201], v[86:89]
	v_mfma_f32_16x16x32_bf16 v[82:85], v[174:177], v[198:201], v[82:85]
	v_mfma_f32_16x16x32_bf16 v[70:73], v[166:169], v[206:209], v[70:73]
	v_mfma_f32_16x16x32_bf16 v[66:69], v[174:177], v[206:209], v[66:69]
	v_mfma_f32_16x16x32_bf16 v[118:121], v[170:173], v[186:189], v[118:121]
	v_mfma_f32_16x16x32_bf16 v[114:117], v[178:181], v[186:189], v[114:117]
	v_mfma_f32_16x16x32_bf16 v[102:105], v[170:173], v[194:197], v[102:105]
	v_mfma_f32_16x16x32_bf16 v[98:101], v[178:181], v[194:197], v[98:101]
	v_mfma_f32_16x16x32_bf16 v[86:89], v[170:173], v[202:205], v[86:89]
	v_mfma_f32_16x16x32_bf16 v[82:85], v[178:181], v[202:205], v[82:85]
	v_mfma_f32_16x16x32_bf16 v[70:73], v[170:173], v[210:213], v[70:73]
	v_mfma_f32_16x16x32_bf16 v[66:69], v[178:181], v[210:213], v[66:69]
	s_setprio 0
	s_barrier
	s_add_i32 s28, s50, s3
	v_lshl_add_u64 v[214:215], s[34:35], 0, v[132:133]
	s_mov_b32 m0, s28
	ds_read_b128 v[182:185], v152 offset:16384
	ds_read_b128 v[186:189], v152 offset:17408
	ds_read_b128 v[190:193], v152 offset:18432
	ds_read_b128 v[194:197], v152 offset:19456
	ds_read_b128 v[198:201], v152 offset:20480
	ds_read_b128 v[202:205], v152 offset:21504
	ds_read_b128 v[206:209], v152 offset:22528
	ds_read_b128 v[210:213], v152 offset:23552
	global_load_lds_dwordx4 v[214:215], off
	s_add_i32 m0, s28, 0x2000
	s_add_u32 s28, s34, 0xe0000
	v_lshl_add_u64 v[216:217], s[34:35], 0, v[134:135]
	s_addc_u32 s29, s35, 0
	s_add_i32 s57, s51, s3
	global_load_lds_dwordx4 v[216:217], off
	v_lshl_add_u64 v[218:219], s[28:29], 0, v[132:133]
	s_mov_b32 m0, s57
	v_lshl_add_u64 v[220:221], s[36:37], 0, v[134:135]
	global_load_lds_dwordx4 v[218:219], off
	v_lshl_add_u64 v[218:219], s[28:29], 0, v[134:135]
	s_add_i32 m0, s57, 0x2000
	s_nop 0
	global_load_lds_dwordx4 v[218:219], off
	v_lshl_add_u64 v[218:219], s[36:37], 0, v[132:133]
	s_mov_b32 m0, s38
	s_nop 0
	global_load_lds_dwordx4 v[218:219], off
	s_mov_b32 m0, s39
	s_nop 0
	global_load_lds_dwordx4 v[220:221], off
	s_waitcnt vmcnt(8)
	s_waitcnt lgkmcnt(0)
	s_barrier
	s_setprio 3
	s_waitcnt lgkmcnt(0)
	v_mfma_f32_16x16x32_bf16 v[62:65], v[142:145], v[182:185], v[62:65]
	v_mfma_f32_16x16x32_bf16 v[58:61], v[158:161], v[182:185], v[58:61]
	v_mfma_f32_16x16x32_bf16 v[46:49], v[142:145], v[190:193], v[46:49]
	v_mfma_f32_16x16x32_bf16 v[42:45], v[158:161], v[190:193], v[42:45]
	v_mfma_f32_16x16x32_bf16 v[30:33], v[142:145], v[198:201], v[30:33]
	v_mfma_f32_16x16x32_bf16 v[26:29], v[158:161], v[198:201], v[26:29]
	v_mfma_f32_16x16x32_bf16 v[14:17], v[142:145], v[206:209], v[14:17]
	v_mfma_f32_16x16x32_bf16 v[10:13], v[158:161], v[206:209], v[10:13]
	v_mfma_f32_16x16x32_bf16 v[62:65], v[154:157], v[186:189], v[62:65]
	v_mfma_f32_16x16x32_bf16 v[58:61], v[162:165], v[186:189], v[58:61]
	v_mfma_f32_16x16x32_bf16 v[46:49], v[154:157], v[194:197], v[46:49]
	v_mfma_f32_16x16x32_bf16 v[42:45], v[162:165], v[194:197], v[42:45]
	v_mfma_f32_16x16x32_bf16 v[30:33], v[154:157], v[202:205], v[30:33]
	v_mfma_f32_16x16x32_bf16 v[26:29], v[162:165], v[202:205], v[26:29]
	v_mfma_f32_16x16x32_bf16 v[14:17], v[154:157], v[210:213], v[14:17]
	v_mfma_f32_16x16x32_bf16 v[10:13], v[162:165], v[210:213], v[10:13]
	s_setprio 0
	s_setprio 3
	v_mfma_f32_16x16x32_bf16 v[54:57], v[166:169], v[182:185], v[54:57]
	v_mfma_f32_16x16x32_bf16 v[50:53], v[174:177], v[182:185], v[50:53]
	v_mfma_f32_16x16x32_bf16 v[38:41], v[166:169], v[190:193], v[38:41]
	v_mfma_f32_16x16x32_bf16 v[34:37], v[174:177], v[190:193], v[34:37]
	v_mfma_f32_16x16x32_bf16 v[22:25], v[166:169], v[198:201], v[22:25]
	v_mfma_f32_16x16x32_bf16 v[18:21], v[174:177], v[198:201], v[18:21]
	v_mfma_f32_16x16x32_bf16 v[6:9], v[166:169], v[206:209], v[6:9]
	v_mfma_f32_16x16x32_bf16 v[2:5], v[174:177], v[206:209], v[2:5]
	v_mfma_f32_16x16x32_bf16 v[54:57], v[170:173], v[186:189], v[54:57]
	v_mfma_f32_16x16x32_bf16 v[50:53], v[178:181], v[186:189], v[50:53]
	v_mfma_f32_16x16x32_bf16 v[38:41], v[170:173], v[194:197], v[38:41]
	v_mfma_f32_16x16x32_bf16 v[34:37], v[178:181], v[194:197], v[34:37]
	v_mfma_f32_16x16x32_bf16 v[22:25], v[170:173], v[202:205], v[22:25]
	v_mfma_f32_16x16x32_bf16 v[18:21], v[178:181], v[202:205], v[18:21]
	v_mfma_f32_16x16x32_bf16 v[6:9], v[170:173], v[210:213], v[6:9]
	v_mfma_f32_16x16x32_bf16 v[2:5], v[178:181], v[210:213], v[2:5]
	s_setprio 0
	s_barrier
; #define PG8_STAGE_A(b, h, ptr, NX) do { if constexpr (Sched::GATHER) { unsigned gs_[2]; gs_[0] = ((NX) && last_) ? gN[h][0] : gA[h][0]; gs_[1] = ((NX) && last_) ? gN[h][1] : gA[h][1]; PG8_STAGE(PG8_SA(b, h), ptr, gs_); } \
;         else PG8_STAGE(PG8_SA(b, h), (ptr) + ((h) ? hstep : (size_t)0), voffA); } while (0)
; #define PG8_LDA(dst, b, h) do { _Pragma("unroll") for (int m = 0; m < 4; ++m) _Pragma("unroll") for (int k = 0; k < 2; ++k) dst[m][k] = *(const PG8_LAS bf16x8*)(lds + PG8_SA(b, h) + aoff + m * 2048 + k * 1024); } while (0)
; #define PG8_LDB(dst, b, h) do { _Pragma("unroll") for (int n = 0; n < 2; ++n) _Pragma("unroll") for (int k = 0; k < 2; ++k) dst[n][k] = *(const PG8_LAS bf16x8*)(lds + PG8_SB(b, h) + boff + n * 2048 + k * 1024); } while (0)
; #define PG8_MMA(ai, bj, At, Bt) do { __builtin_amdgcn_s_setprio(1); _Pragma("unroll") for (int m = 0; m < 4; ++m) _Pragma("unroll") for (int n = 0; n < 2; ++n) _Pragma("unroll") for (int k = 0; k < 2; ++k) \
;         acc[ai][bj][m][n] = __builtin_amdgcn_mfma_f32_16x16x32_bf16(Bt[n][k], At[m][k], acc[ai][bj][m][n], 0, 0, 0); __builtin_amdgcn_s_setprio(0); } while (0)
; #define PG8_WAIT_V(n) asm volatile("s_waitcnt vmcnt(" #n ")" ::: "memory")
; #define PG8_WAIT_L(n) asm volatile("s_waitcnt lgkmcnt(" #n ")" ::: "memory")
; #define PG8_BAR __builtin_amdgcn_s_barrier()
; #define PG8_SCHED __builtin_amdgcn_sched_barrier(0)
; template <class Epi, class Sched, bool ALIGN_EPI = false, bool SP2 = false>
; __device__ __forceinline__ void gemm_phase(PG8_LAS unsigned char* lds, const Gemm g, const Sched& S, const Epi& E, const bool skip_epi = false) {
;     ...
;             PG8_LDB(B0, 1, 0); PG8_LDB(B1, 1, 1); PG8_SCHED; PG8_LDA(At, 1, 0); PG8_STAGE_A(0, 1, a2, true);
;             PG8_WAIT_V(8); PG8_WAIT_L(0); PG8_BAR; PG8_MMA(0, 0, At, B0); PG8_MMA(0, 1, At, B1); PG8_BAR; PG8_SCHED;
	s_add_i32 s57, 0, 0x18000
	v_add_u32_e32 v130, s57, v146
	s_add_i32 s58, 0, 0x1c000
	ds_read_b128 v[142:145], v130
	ds_read_b128 v[154:157], v130 offset:1024
	ds_read_b128 v[158:161], v130 offset:2048
	ds_read_b128 v[162:165], v130 offset:3072
	v_add_u32_e32 v130, s58, v146
	ds_read_b128 v[166:169], v130
	ds_read_b128 v[170:173], v130 offset:1024
	ds_read_b128 v[174:177], v130 offset:2048
	ds_read_b128 v[178:181], v130 offset:3072
	s_add_u32 s28, s36, 0xe0000
	s_addc_u32 s29, s37, 0
	s_mov_b32 m0, s40
	v_lshl_add_u64 v[222:223], s[28:29], 0, v[132:133]
	ds_read_b128 v[182:185], v152 offset:32768
	ds_read_b128 v[186:189], v152 offset:33792
	ds_read_b128 v[190:193], v152 offset:34816
	ds_read_b128 v[194:197], v152 offset:35840
	ds_read_b128 v[198:201], v152 offset:36864
	ds_read_b128 v[202:205], v152 offset:37888
	ds_read_b128 v[206:209], v152 offset:38912
	ds_read_b128 v[210:213], v152 offset:39936
	global_load_lds_dwordx4 v[222:223], off
	v_lshl_add_u64 v[222:223], s[28:29], 0, v[134:135]
	s_mov_b32 m0, s41
	s_nop 0
	global_load_lds_dwordx4 v[222:223], off
	s_waitcnt vmcnt(8)
	s_waitcnt lgkmcnt(0)
	s_barrier
	s_setprio 3
	s_waitcnt lgkmcnt(0)
	v_mfma_f32_16x16x32_bf16 v[126:129], v[142:145], v[182:185], v[126:129]
	v_mfma_f32_16x16x32_bf16 v[122:125], v[158:161], v[182:185], v[122:125]
	v_mfma_f32_16x16x32_bf16 v[110:113], v[142:145], v[190:193], v[110:113]
	v_mfma_f32_16x16x32_bf16 v[106:109], v[158:161], v[190:193], v[106:109]
	v_mfma_f32_16x16x32_bf16 v[94:97], v[142:145], v[198:201], v[94:97]
	v_mfma_f32_16x16x32_bf16 v[90:93], v[158:161], v[198:201], v[90:93]
	v_mfma_f32_16x16x32_bf16 v[78:81], v[142:145], v[206:209], v[78:81]
	v_mfma_f32_16x16x32_bf16 v[74:77], v[158:161], v[206:209], v[74:77]
	v_mfma_f32_16x16x32_bf16 v[126:129], v[154:157], v[186:189], v[126:129]
	v_mfma_f32_16x16x32_bf16 v[122:125], v[162:165], v[186:189], v[122:125]
	v_mfma_f32_16x16x32_bf16 v[110:113], v[154:157], v[194:197], v[110:113]
	v_mfma_f32_16x16x32_bf16 v[106:109], v[162:165], v[194:197], v[106:109]
	v_mfma_f32_16x16x32_bf16 v[94:97], v[154:157], v[202:205], v[94:97]
	v_mfma_f32_16x16x32_bf16 v[90:93], v[162:165], v[202:205], v[90:93]
	v_mfma_f32_16x16x32_bf16 v[78:81], v[154:157], v[210:213], v[78:81]
	v_mfma_f32_16x16x32_bf16 v[74:77], v[162:165], v[210:213], v[74:77]
	s_setprio 0
	s_setprio 3
	v_mfma_f32_16x16x32_bf16 v[118:121], v[166:169], v[182:185], v[118:121]
	v_mfma_f32_16x16x32_bf16 v[114:117], v[174:177], v[182:185], v[114:117]
	v_mfma_f32_16x16x32_bf16 v[102:105], v[166:169], v[190:193], v[102:105]
	v_mfma_f32_16x16x32_bf16 v[98:101], v[174:177], v[190:193], v[98:101]
	v_mfma_f32_16x16x32_bf16 v[86:89], v[166:169], v[198:201], v[86:89]
	v_mfma_f32_16x16x32_bf16 v[82:85], v[174:177], v[198:201], v[82:85]
	v_mfma_f32_16x16x32_bf16 v[70:73], v[166:169], v[206:209], v[70:73]
	v_mfma_f32_16x16x32_bf16 v[66:69], v[174:177], v[206:209], v[66:69]
	v_mfma_f32_16x16x32_bf16 v[118:121], v[170:173], v[186:189], v[118:121]
	v_mfma_f32_16x16x32_bf16 v[114:117], v[178:181], v[186:189], v[114:117]
	v_mfma_f32_16x16x32_bf16 v[102:105], v[170:173], v[194:197], v[102:105]
	v_mfma_f32_16x16x32_bf16 v[98:101], v[178:181], v[194:197], v[98:101]
	v_mfma_f32_16x16x32_bf16 v[86:89], v[170:173], v[202:205], v[86:89]
	v_mfma_f32_16x16x32_bf16 v[82:85], v[178:181], v[202:205], v[82:85]
	v_mfma_f32_16x16x32_bf16 v[70:73], v[170:173], v[210:213], v[70:73]
	v_mfma_f32_16x16x32_bf16 v[66:69], v[178:181], v[210:213], v[66:69]
	s_setprio 0
	s_barrier
; #define PG8_STAGE_A(b, h, ptr, NX) do { if constexpr (Sched::GATHER) { unsigned gs_[2]; gs_[0] = ((NX) && last_) ? gN[h][0] : gA[h][0]; gs_[1] = ((NX) && last_) ? gN[h][1] : gA[h][1]; PG8_STAGE(PG8_SA(b, h), ptr, gs_); } \
;         else PG8_STAGE(PG8_SA(b, h), (ptr) + ((h) ? hstep : (size_t)0), voffA); } while (0)
; #define PG8_STAGE(bufoff, gbase, voff) do { _Pragma("unroll") for (int _i = 0; _i < 2; ++_i) \
;         __builtin_amdgcn_global_load_lds((const unsigned*)((const char*)(gbase) + (voff)[_i]), (PG8_LAS unsigned*)(lds + (bufoff) + ldsw + _i * 8192), 16, 0, 0); } while (0)
; #define PG8_LDA(dst, b, h) do { _Pragma("unroll") for (int m = 0; m < 4; ++m) _Pragma("unroll") for (int k = 0; k < 2; ++k) dst[m][k] = *(const PG8_LAS bf16x8*)(lds + PG8_SA(b, h) + aoff + m * 2048 + k * 1024); } while (0)
; #define PG8_MMA(ai, bj, At, Bt) do { __builtin_amdgcn_s_setprio(1); _Pragma("unroll") for (int m = 0; m < 4; ++m) _Pragma("unroll") for (int n = 0; n < 2; ++n) _Pragma("unroll") for (int k = 0; k < 2; ++k) \
;         acc[ai][bj][m][n] = __builtin_amdgcn_mfma_f32_16x16x32_bf16(Bt[n][k], At[m][k], acc[ai][bj][m][n], 0, 0, 0); __builtin_amdgcn_s_setprio(0); } while (0)
; #define PG8_WAIT_V(n) asm volatile("s_waitcnt vmcnt(" #n ")" ::: "memory")
; #define PG8_WAIT_L(n) asm volatile("s_waitcnt lgkmcnt(" #n ")" ::: "memory")
; #define PG8_BAR __builtin_amdgcn_s_barrier()
; #define PG8_SCHED __builtin_amdgcn_sched_barrier(0)
; template <class Epi, class Sched, bool ALIGN_EPI = false, bool SP2 = false>
; __device__ __forceinline__ void gemm_phase(PG8_LAS unsigned char* lds, const Gemm g, const Sched& S, const Epi& E, const bool skip_epi = false) {
;     ...
;         for (int t = 0; t < nt; t += 2) {
;     ...
;             PG8_LDA(At, 1, 1); PG8_STAGE(PG8_SB(1, 0), b3, voffB); PG8_STAGE(PG8_SB(1, 1), b3 + hstep, voffB); PG8_STAGE_A(1, 0, a3, true);
;             PG8_WAIT_V(8); PG8_WAIT_L(0); PG8_BAR; PG8_MMA(1, 0, At, B0); PG8_MMA(1, 1, At, B1); PG8_BAR; PG8_SCHED;
	s_add_i32 s28, s57, s3
	v_lshl_add_u64 v[214:215], v[214:215], 0, s[18:19]
	s_mov_b32 m0, s28
	ds_read_b128 v[182:185], v152 offset:49152
	ds_read_b128 v[186:189], v152 offset:50176
	ds_read_b128 v[190:193], v152 offset:51200
	ds_read_b128 v[194:197], v152 offset:52224
	ds_read_b128 v[198:201], v152 offset:53248
	ds_read_b128 v[202:205], v152 offset:54272
	ds_read_b128 v[206:209], v152 offset:55296
	ds_read_b128 v[210:213], v152 offset:56320
	global_load_lds_dwordx4 v[214:215], off
	s_add_i32 m0, s28, 0x2000
	s_add_u32 s28, s34, 0xe0080
	v_lshl_add_u64 v[214:215], v[216:217], 0, s[18:19]
	s_addc_u32 s29, s35, 0
	s_add_i32 s34, s58, s3
	global_load_lds_dwordx4 v[214:215], off
	v_lshl_add_u64 v[214:215], s[28:29], 0, v[132:133]
	s_mov_b32 m0, s34
	s_nop 0
	global_load_lds_dwordx4 v[214:215], off
	v_lshl_add_u64 v[214:215], s[28:29], 0, v[134:135]
	s_add_i32 m0, s34, 0x2000
	s_nop 0
	global_load_lds_dwordx4 v[214:215], off
	v_lshl_add_u64 v[214:215], v[218:219], 0, s[18:19]
	s_mov_b32 m0, s46
	s_nop 0
	global_load_lds_dwordx4 v[214:215], off
	v_lshl_add_u64 v[214:215], v[220:221], 0, s[18:19]
	s_mov_b32 m0, s47
	s_nop 0
	global_load_lds_dwordx4 v[214:215], off
	s_waitcnt vmcnt(8)
	s_waitcnt lgkmcnt(0)
	s_barrier
	s_setprio 3
	s_waitcnt lgkmcnt(0)
	v_mfma_f32_16x16x32_bf16 v[62:65], v[142:145], v[182:185], v[62:65]
	v_mfma_f32_16x16x32_bf16 v[58:61], v[158:161], v[182:185], v[58:61]
	v_mfma_f32_16x16x32_bf16 v[46:49], v[142:145], v[190:193], v[46:49]
	v_mfma_f32_16x16x32_bf16 v[42:45], v[158:161], v[190:193], v[42:45]
	v_mfma_f32_16x16x32_bf16 v[30:33], v[142:145], v[198:201], v[30:33]
	v_mfma_f32_16x16x32_bf16 v[26:29], v[158:161], v[198:201], v[26:29]
	v_mfma_f32_16x16x32_bf16 v[14:17], v[142:145], v[206:209], v[14:17]
	v_mfma_f32_16x16x32_bf16 v[10:13], v[158:161], v[206:209], v[10:13]
	v_mfma_f32_16x16x32_bf16 v[62:65], v[154:157], v[186:189], v[62:65]
	v_mfma_f32_16x16x32_bf16 v[58:61], v[162:165], v[186:189], v[58:61]
	v_mfma_f32_16x16x32_bf16 v[46:49], v[154:157], v[194:197], v[46:49]
	v_mfma_f32_16x16x32_bf16 v[42:45], v[162:165], v[194:197], v[42:45]
	v_mfma_f32_16x16x32_bf16 v[30:33], v[154:157], v[202:205], v[30:33]
	v_mfma_f32_16x16x32_bf16 v[26:29], v[162:165], v[202:205], v[26:29]
	v_mfma_f32_16x16x32_bf16 v[14:17], v[154:157], v[210:213], v[14:17]
	v_mfma_f32_16x16x32_bf16 v[10:13], v[162:165], v[210:213], v[10:13]
	s_setprio 0
	s_setprio 3
	v_mfma_f32_16x16x32_bf16 v[54:57], v[166:169], v[182:185], v[54:57]
	v_mfma_f32_16x16x32_bf16 v[50:53], v[174:177], v[182:185], v[50:53]
	v_mfma_f32_16x16x32_bf16 v[38:41], v[166:169], v[190:193], v[38:41]
	v_mfma_f32_16x16x32_bf16 v[34:37], v[174:177], v[190:193], v[34:37]
	v_mfma_f32_16x16x32_bf16 v[22:25], v[166:169], v[198:201], v[22:25]
	v_mfma_f32_16x16x32_bf16 v[18:21], v[174:177], v[198:201], v[18:21]
	v_mfma_f32_16x16x32_bf16 v[6:9], v[166:169], v[206:209], v[6:9]
	v_mfma_f32_16x16x32_bf16 v[2:5], v[174:177], v[206:209], v[2:5]
	v_mfma_f32_16x16x32_bf16 v[54:57], v[170:173], v[186:189], v[54:57]
	v_mfma_f32_16x16x32_bf16 v[50:53], v[178:181], v[186:189], v[50:53]
	v_mfma_f32_16x16x32_bf16 v[38:41], v[170:173], v[194:197], v[38:41]
	v_mfma_f32_16x16x32_bf16 v[34:37], v[178:181], v[194:197], v[34:37]
	v_mfma_f32_16x16x32_bf16 v[22:25], v[170:173], v[202:205], v[22:25]
	v_mfma_f32_16x16x32_bf16 v[18:21], v[178:181], v[202:205], v[18:21]
	v_mfma_f32_16x16x32_bf16 v[6:9], v[170:173], v[210:213], v[6:9]
	v_mfma_f32_16x16x32_bf16 v[2:5], v[178:181], v[210:213], v[2:5]
	s_setprio 0
	s_barrier
	s_add_i32 s56, s56, 2
	s_add_u32 s54, s54, 0x100
	s_addc_u32 s55, s55, 0
	s_cmp_gt_u32 s56, 11
	s_mov_b64 s[28:29], s[30:31]
	s_cbranch_scc0 .LBB0_1844
	s_and_b64 vcc, exec, s[20:21]
	s_cbranch_vccz .LBB0_1847
	s_barrier
